# fp8 weight-copy loops: LDS read-out remapped (row=lane>>2, 16 k per lane, two row groups) so each global store writes 16 rows x 64 contiguous bytes instead of 32 rows x 2 separate 16-byte pieces
# speedup vs baseline: 1.0086x; 1.0086x over previous
.LBB6_901:
	s_lshl_b32 s84, s0, 3
	s_or_b32 s1, s84, s59
	s_mul_hi_i32 s3, s63, s1
	s_mul_i32 s2, s63, s1
	s_lshr_b64 s[2:3], s[2:3], 9
	s_add_i32 s1, s1, 1
	s_and_b32 s90, s2, 0xffffffe0
	s_mul_hi_i32 s3, s63, s1
	s_mul_i32 s2, s63, s1
	s_lshr_b64 s[2:3], s[2:3], 9
	s_and_b32 s91, s2, 0xffffffe0
	s_bitcmp0_b32 s0, 0
	s_cselect_b64 s[22:23], -1, 0
	s_and_b64 vcc, exec, s[22:23]
	s_cbranch_vccnz .LBB6_1210
	v_readlane_b32 s6, v254, 13
	v_readlane_b32 s7, v254, 14
	s_waitcnt vmcnt(0)
	v_mov_b32_e32 v167, v0
	s_max_i32 s64, s90, 0
	v_readfirstlane_b32 s0, v167
	s_ashr_i32 s95, s0, 6
	v_readlane_b32 s0, v254, 60
	s_lshl_b32 s81, s95, 14
	v_readlane_b32 s1, v254, 61
	v_and_b32_e32 v166, 63, v167
	s_add_i32 s94, s81, 0
	s_mov_b64 s[2:3], -1
	s_and_b64 vcc, exec, s[0:1]
	s_cbranch_vccz .LBB6_915
	s_min_i32 s30, s91, 0xdc00
	s_cmp_le_i32 s30, s64
	s_cbranch_scc1 .LBB6_908
	s_sub_i32 s0, s30, s64
	s_mov_b32 s2, 18
	s_cmp_lt_i32 s0, 32
	s_cbranch_scc1 .LBB6_908
	s_add_i32 s31, s95, s64
	s_cmp_ge_i32 s31, s30
	s_cbranch_scc1 .LBB6_908
	s_ashr_i32 s3, s2, 31
	s_lshl_b64 s[0:1], s[2:3], 3
	s_add_u32 s0, s76, s0
	s_addc_u32 s1, s77, s1
	s_load_dwordx2 s[0:1], s[0:1], 0x0
	v_lshrrev_b32_e32 v4, 3, v166
	v_lshlrev_b32_e32 v2, 2, v166
	v_mul_u32_u24_e32 v5, 0x2c00, v4
	v_and_b32_e32 v6, 28, v2
	s_waitcnt lgkmcnt(0)
	s_add_u32 s34, s0, 0x10800000
	v_or_b32_e32 v2, v5, v6
	v_lshl_add_u32 v5, v6, 2, s94
	v_lshlrev_b32_e32 v6, 5, v166
	s_addc_u32 s35, s1, 0
	v_lshrrev_b32_e32 v135, 2, v166
	v_lshlrev_b32_e32 v132, 4, v166
	v_and_b32_e32 v132, 48, v132
	s_add_u32 s36, s6, 0x85280000
	v_mul_u32_u24_e32 v4, 0x84, v4
	v_mul_u32_u24_e32 v6, 0x84, v132
	v_lshlrev_b32_e32 v7, 2, v135
	v_and_b32_e32 v134, 31, v167
	s_addc_u32 s37, s7, 0
	v_lshlrev_b32_e32 v2, 2, v2
	v_add3_u32 v136, s94, v6, v7
	v_mov_b32_e32 v133, v3
	v_add_u32_e32 v137, v5, v4
.LBB6_907:
	s_mul_hi_i32 s0, s31, 0x2e8ba2e9
	s_lshr_b32 s1, s0, 31
	s_ashr_i32 s28, s0, 11
	s_add_i32 s28, s28, s1
	s_mul_i32 s0, s28, 0xffffd400
	s_add_i32 s0, s0, s31
	s_ashr_i32 s0, s0, 1
	s_and_b32 s1, s0, -8
	s_and_b32 s0, s31, 7
	s_or_b32 s1, s1, s0
	s_mul_hi_i32 s2, s1, 0x2e8ba2e9
	s_lshr_b32 s3, s2, 31
	s_ashr_i32 s2, s2, 6
	s_add_i32 s2, s2, s3
	s_mul_i32 s3, s2, 0xfffffea0
	s_add_i32 s3, s3, s1
	s_lshl_b32 s1, s2, 7
	s_lshl_b32 s2, s31, 3
	s_and_b32 s12, s2, 64
	s_lshl_b32 s62, s3, 5
	s_or_b32 s26, s1, s12
	s_mul_i32 s2, s28, 0x5800000
	s_mul_hi_i32 s1, s28, 0x5800000
	s_add_u32 s4, s34, s2
	s_addc_u32 s1, s35, s1
	s_and_b32 s2, s62, 0xe0
	s_cmpk_lt_u32 s2, 0x80
	v_or_b32_e32 v4, s2, v134
	s_cselect_b64 vcc, -1, 0
	s_lshl_b32 s2, s3, 4
	s_and_b32 s2, s2, 0xffffff80
	v_or_b32_e32 v5, s2, v4
	s_addk_i32 s2, 0x1580
	v_add_u32_e32 v4, s2, v4
	v_cndmask_b32_e32 v4, v4, v5, vcc
	s_ashr_i32 s27, s26, 31
	v_readfirstlane_b32 s2, v4
	s_andn2_b32 s2, s2, 31
	s_mul_i32 s5, s26, 0xb000
	s_mul_hi_i32 s3, s26, 0xb000
	s_add_u32 s4, s4, s5
	s_addc_u32 s1, s1, s3
	s_ashr_i32 s3, s2, 31
	s_lshl_b64 s[2:3], s[2:3], 2
	s_add_u32 s2, s4, s2
	s_addc_u32 s3, s1, s3
	s_mov_b64 s[4:5], s[2:3]
	v_mov_b32_e32 v138, v3
	v_lshl_add_u64 v[4:5], s[4:5], 0, v[2:3]
	s_add_u32 s4, s2, 0x58000
	s_addc_u32 s5, s3, 0
	global_load_dwordx4 v[128:131], v[4:5], off nt
	v_mov_b32_e32 v139, v3
	v_lshl_add_u64 v[4:5], s[4:5], 0, v[2:3]
	s_add_u32 s4, s2, 0xb0000
	s_addc_u32 s5, s3, 0
	global_load_dwordx4 v[124:127], v[4:5], off nt
	s_nop 0
	v_lshl_add_u64 v[4:5], s[4:5], 0, v[2:3]
	s_add_u32 s4, s2, 0x108000
	s_addc_u32 s5, s3, 0
	global_load_dwordx4 v[120:123], v[4:5], off nt
	s_nop 0
	v_lshl_add_u64 v[4:5], s[4:5], 0, v[2:3]
	s_add_u32 s4, s2, 0x160000
	s_addc_u32 s5, s3, 0
	global_load_dwordx4 v[116:119], v[4:5], off nt
	s_nop 0
	v_lshl_add_u64 v[4:5], s[4:5], 0, v[2:3]
	s_add_u32 s4, s2, 0x1b8000
	s_addc_u32 s5, s3, 0
	global_load_dwordx4 v[112:115], v[4:5], off nt
	s_nop 0
	v_lshl_add_u64 v[4:5], s[4:5], 0, v[2:3]
	s_add_u32 s4, s2, 0x210000
	s_addc_u32 s5, s3, 0
	s_add_u32 s2, s2, 0x268000
	global_load_dwordx4 v[108:111], v[4:5], off nt
	s_addc_u32 s3, s3, 0
	v_lshl_add_u64 v[4:5], s[4:5], 0, v[2:3]
	global_load_dwordx4 v[104:107], v[4:5], off nt
	s_add_i32 s1, s31, 8
	v_lshl_add_u64 v[4:5], s[2:3], 0, v[2:3]
	s_mul_hi_i32 s2, s1, 0x2e8ba2e9
	s_lshr_b32 s3, s2, 31
	s_ashr_i32 s51, s2, 11
	s_add_i32 s51, s51, s3
	s_mul_i32 s2, s51, 0xffffd400
	s_add_i32 s2, s2, s1
	s_ashr_i32 s2, s2, 1
	s_and_b32 s2, s2, -8
	s_or_b32 s2, s2, s0
	s_mul_hi_i32 s3, s2, 0x2e8ba2e9
	s_lshr_b32 s4, s3, 31
	s_ashr_i32 s3, s3, 6
	s_add_i32 s3, s3, s4
	s_mul_i32 s4, s3, 0xfffffea0
	s_lshl_b32 s1, s1, 3
	s_add_i32 s4, s4, s2
	s_lshl_b32 s2, s3, 7
	s_and_b32 s1, s1, 64
	s_lshl_b32 s58, s4, 5
	s_or_b32 s24, s2, s1
	s_mul_i32 s2, s51, 0x5800000
	s_mul_hi_i32 s1, s51, 0x5800000
	s_add_u32 s3, s34, s2
	s_addc_u32 s1, s35, s1
	s_and_b32 s2, s58, 0xe0
	s_cmpk_lt_u32 s2, 0x80
	global_load_dwordx4 v[100:103], v[4:5], off nt
	v_or_b32_e32 v4, s2, v134
	s_cselect_b64 vcc, -1, 0
	s_lshl_b32 s2, s4, 4
	s_and_b32 s2, s2, 0xffffff80
	v_or_b32_e32 v5, s2, v4
	s_addk_i32 s2, 0x1580
	v_add_u32_e32 v4, s2, v4
	v_cndmask_b32_e32 v4, v4, v5, vcc
	s_ashr_i32 s25, s24, 31
	v_readfirstlane_b32 s2, v4
	s_andn2_b32 s2, s2, 31
	s_mul_i32 s5, s24, 0xb000
	s_mul_hi_i32 s4, s24, 0xb000
	s_add_u32 s5, s3, s5
	s_addc_u32 s1, s1, s4
	s_ashr_i32 s3, s2, 31
	s_lshl_b64 s[2:3], s[2:3], 2
	s_add_u32 s2, s5, s2
	s_addc_u32 s3, s1, s3
	s_mov_b64 s[4:5], s[2:3]
	s_nop 0
	v_lshl_add_u64 v[4:5], s[4:5], 0, v[2:3]
	s_add_u32 s4, s2, 0x58000
	s_addc_u32 s5, s3, 0
	global_load_dwordx4 v[68:71], v[4:5], off nt
	s_nop 0
	v_lshl_add_u64 v[4:5], s[4:5], 0, v[2:3]
	s_add_u32 s4, s2, 0xb0000
	s_addc_u32 s5, s3, 0
	global_load_dwordx4 v[72:75], v[4:5], off nt
	s_nop 0
	v_lshl_add_u64 v[4:5], s[4:5], 0, v[2:3]
	s_add_u32 s4, s2, 0x108000
	s_addc_u32 s5, s3, 0
	global_load_dwordx4 v[76:79], v[4:5], off nt
	s_nop 0
	v_lshl_add_u64 v[4:5], s[4:5], 0, v[2:3]
	s_add_u32 s4, s2, 0x160000
	s_addc_u32 s5, s3, 0
	global_load_dwordx4 v[80:83], v[4:5], off nt
	s_nop 0
	v_lshl_add_u64 v[4:5], s[4:5], 0, v[2:3]
	s_add_u32 s4, s2, 0x1b8000
	s_addc_u32 s5, s3, 0
	global_load_dwordx4 v[84:87], v[4:5], off nt
	s_nop 0
	v_lshl_add_u64 v[4:5], s[4:5], 0, v[2:3]
	s_add_u32 s4, s2, 0x210000
	s_addc_u32 s5, s3, 0
	s_add_u32 s2, s2, 0x268000
	global_load_dwordx4 v[88:91], v[4:5], off nt
	s_addc_u32 s3, s3, 0
	v_lshl_add_u64 v[4:5], s[4:5], 0, v[2:3]
	global_load_dwordx4 v[92:95], v[4:5], off nt
	s_add_i32 s1, s31, 16
	v_lshl_add_u64 v[4:5], s[2:3], 0, v[2:3]
	s_mul_hi_i32 s2, s1, 0x2e8ba2e9
	s_lshr_b32 s3, s2, 31
	s_ashr_i32 s49, s2, 11
	s_add_i32 s49, s49, s3
	s_mul_i32 s2, s49, 0xffffd400
	s_add_i32 s2, s2, s1
	s_ashr_i32 s1, s2, 1
	s_and_b32 s1, s1, -8
	s_or_b32 s1, s1, s0
	s_mul_hi_i32 s2, s1, 0x2e8ba2e9
	s_lshr_b32 s3, s2, 31
	s_ashr_i32 s2, s2, 6
	s_add_i32 s2, s2, s3
	s_mul_i32 s3, s2, 0xfffffea0
	s_add_i32 s3, s3, s1
	s_lshl_b32 s1, s2, 7
	s_lshl_b32 s50, s3, 5
	s_or_b32 s4, s1, s12
	s_mul_i32 s2, s49, 0x5800000
	s_mul_hi_i32 s1, s49, 0x5800000
	s_add_u32 s12, s34, s2
	s_addc_u32 s1, s35, s1
	s_and_b32 s2, s50, 0xe0
	s_cmpk_lt_u32 s2, 0x80
	global_load_dwordx4 v[96:99], v[4:5], off nt
	v_or_b32_e32 v4, s2, v134
	s_cselect_b64 vcc, -1, 0
	s_lshl_b32 s2, s3, 4
	s_and_b32 s2, s2, 0xffffff80
	v_or_b32_e32 v5, s2, v4
	s_addk_i32 s2, 0x1580
	v_add_u32_e32 v4, s2, v4
	v_cndmask_b32_e32 v4, v4, v5, vcc
	s_ashr_i32 s5, s4, 31
	v_readfirstlane_b32 s2, v4
	s_andn2_b32 s2, s2, 31
	s_mul_i32 s13, s4, 0xb000
	s_mul_hi_i32 s3, s4, 0xb000
	s_add_u32 s12, s12, s13
	s_addc_u32 s1, s1, s3
	s_ashr_i32 s3, s2, 31
	s_lshl_b64 s[2:3], s[2:3], 2
	s_add_u32 s2, s12, s2
	s_addc_u32 s3, s1, s3
	s_mov_b64 s[12:13], s[2:3]
	s_nop 0
	v_lshl_add_u64 v[4:5], s[12:13], 0, v[2:3]
	s_add_u32 s12, s2, 0x58000
	s_addc_u32 s13, s3, 0
	global_load_dwordx4 v[36:39], v[4:5], off nt
	s_nop 0
	v_lshl_add_u64 v[4:5], s[12:13], 0, v[2:3]
	s_add_u32 s12, s2, 0xb0000
	s_addc_u32 s13, s3, 0
	global_load_dwordx4 v[40:43], v[4:5], off nt
	s_nop 0
	v_lshl_add_u64 v[4:5], s[12:13], 0, v[2:3]
	s_add_u32 s12, s2, 0x108000
	s_addc_u32 s13, s3, 0
	global_load_dwordx4 v[44:47], v[4:5], off nt
	s_nop 0
	v_lshl_add_u64 v[4:5], s[12:13], 0, v[2:3]
	s_add_u32 s12, s2, 0x160000
	s_addc_u32 s13, s3, 0
	global_load_dwordx4 v[48:51], v[4:5], off nt
	s_nop 0
	v_lshl_add_u64 v[4:5], s[12:13], 0, v[2:3]
	s_add_u32 s12, s2, 0x1b8000
	s_addc_u32 s13, s3, 0
	global_load_dwordx4 v[52:55], v[4:5], off nt
	s_nop 0
	v_lshl_add_u64 v[4:5], s[12:13], 0, v[2:3]
	s_add_u32 s12, s2, 0x210000
	s_addc_u32 s13, s3, 0
	s_add_u32 s2, s2, 0x268000
	global_load_dwordx4 v[56:59], v[4:5], off nt
	s_addc_u32 s3, s3, 0
	v_lshl_add_u64 v[4:5], s[12:13], 0, v[2:3]
	global_load_dwordx4 v[60:63], v[4:5], off nt
	s_add_i32 s1, s31, 24
	v_lshl_add_u64 v[4:5], s[2:3], 0, v[2:3]
	s_mul_hi_i32 s2, s1, 0x2e8ba2e9
	s_lshr_b32 s3, s2, 31
	s_ashr_i32 s47, s2, 11
	s_add_i32 s47, s47, s3
	s_mul_i32 s2, s47, 0xffffd400
	s_add_i32 s2, s2, s1
	s_ashr_i32 s2, s2, 1
	s_and_b32 s2, s2, -8
	s_or_b32 s0, s2, s0
	s_mul_hi_i32 s2, s0, 0x2e8ba2e9
	s_lshr_b32 s3, s2, 31
	s_ashr_i32 s2, s2, 6
	s_add_i32 s2, s2, s3
	s_mul_i32 s3, s2, 0xfffffea0
	s_lshl_b32 s1, s1, 3
	s_add_i32 s3, s3, s0
	s_lshl_b32 s0, s2, 7
	s_and_b32 s1, s1, 64
	s_lshl_b32 s48, s3, 5
	s_or_b32 s2, s0, s1
	s_mul_i32 s1, s47, 0x5800000
	s_mul_hi_i32 s0, s47, 0x5800000
	s_add_u32 s1, s34, s1
	s_addc_u32 s12, s35, s0
	s_and_b32 s0, s48, 0xe0
	s_cmpk_lt_u32 s0, 0x80
	global_load_dwordx4 v[64:67], v[4:5], off nt
	v_or_b32_e32 v4, s0, v134
	s_cselect_b64 vcc, -1, 0
	s_lshl_b32 s0, s3, 4
	s_and_b32 s0, s0, 0xffffff80
	v_or_b32_e32 v5, s0, v4
	s_addk_i32 s0, 0x1580
	v_add_u32_e32 v4, s0, v4
	v_cndmask_b32_e32 v4, v4, v5, vcc
	s_ashr_i32 s3, s2, 31
	v_readfirstlane_b32 s0, v4
	s_andn2_b32 s0, s0, 31
	s_mul_i32 s29, s2, 0xb000
	s_mul_hi_i32 s13, s2, 0xb000
	s_add_u32 s29, s1, s29
	s_addc_u32 s12, s12, s13
	s_ashr_i32 s1, s0, 31
	s_lshl_b64 s[0:1], s[0:1], 2
	s_add_u32 s0, s29, s0
	s_addc_u32 s1, s12, s1
	s_mov_b64 s[12:13], s[0:1]
	s_nop 0
	v_lshl_add_u64 v[4:5], s[12:13], 0, v[2:3]
	s_add_u32 s12, s0, 0x58000
	s_addc_u32 s13, s1, 0
	global_load_dwordx4 v[4:7], v[4:5], off nt
	s_nop 0
	v_lshl_add_u64 v[8:9], s[12:13], 0, v[2:3]
	s_add_u32 s12, s0, 0xb0000
	s_addc_u32 s13, s1, 0
	global_load_dwordx4 v[8:11], v[8:9], off nt
	s_nop 0
	v_lshl_add_u64 v[12:13], s[12:13], 0, v[2:3]
	s_add_u32 s12, s0, 0x108000
	s_addc_u32 s13, s1, 0
	global_load_dwordx4 v[12:15], v[12:13], off nt
	s_nop 0
	v_lshl_add_u64 v[16:17], s[12:13], 0, v[2:3]
	s_add_u32 s12, s0, 0x160000
	s_addc_u32 s13, s1, 0
	global_load_dwordx4 v[16:19], v[16:17], off nt
	s_nop 0
	v_lshl_add_u64 v[20:21], s[12:13], 0, v[2:3]
	s_add_u32 s12, s0, 0x1b8000
	s_addc_u32 s13, s1, 0
	global_load_dwordx4 v[20:23], v[20:21], off nt
	s_nop 0
	v_lshl_add_u64 v[24:25], s[12:13], 0, v[2:3]
	s_add_u32 s12, s0, 0x210000
	s_addc_u32 s13, s1, 0
	s_add_u32 s0, s0, 0x268000
	global_load_dwordx4 v[24:27], v[24:25], off nt
	s_addc_u32 s1, s1, 0
	v_lshl_add_u64 v[28:29], s[12:13], 0, v[2:3]
	global_load_dwordx4 v[28:31], v[28:29], off nt
	s_nop 0
	v_lshl_add_u64 v[32:33], s[0:1], 0, v[2:3]
	global_load_dwordx4 v[32:35], v[32:33], off nt
	s_waitcnt vmcnt(0)
	ds_write2_b32 v137, v128, v129 offset1:1
	ds_write2_b32 v137, v130, v131 offset0:2 offset1:3
	v_add_u32_e32 v128, 0x420, v137
	ds_write2_b32 v128, v124, v125 offset1:1
	v_add_u32_e32 v125, 0x840, v137
	ds_write2_b32 v125, v120, v121 offset1:1
	v_add_u32_e32 v121, 0xc60, v137
	ds_write2_b32 v121, v116, v117 offset1:1
	v_add_u32_e32 v117, 0x1080, v137
	ds_write2_b32 v117, v112, v113 offset1:1
	v_add_u32_e32 v113, 0x14a0, v137
	ds_write2_b32 v113, v108, v109 offset1:1
	v_add_u32_e32 v109, 0x18c0, v137
	ds_write2_b32 v109, v104, v105 offset1:1
	v_add_u32_e32 v104, 0x18c8, v137
	v_add_u32_e32 v124, 0x428, v137
	v_add_u32_e32 v120, 0x848, v137
	v_add_u32_e32 v116, 0xc68, v137
	v_add_u32_e32 v112, 0x1088, v137
	v_add_u32_e32 v108, 0x14a8, v137
	ds_write2_b32 v104, v106, v107 offset1:1
	v_add_u32_e32 v105, 0x1ce0, v137
	v_add_u32_e32 v106, 0x1ce8, v137
	ds_write2_b32 v124, v126, v127 offset1:1
	ds_write2_b32 v120, v122, v123 offset1:1
	ds_write2_b32 v116, v118, v119 offset1:1
	ds_write2_b32 v112, v114, v115 offset1:1
	ds_write2_b32 v108, v110, v111 offset1:1
	ds_write2_b32 v105, v100, v101 offset1:1
	ds_write2_b32 v106, v102, v103 offset1:1
	ds_read2_b32 v[110:111], v136 offset1:33
	ds_read2_b32 v[114:115], v136 offset0:66 offset1:99
	ds_read2_b32 v[118:119], v136 offset0:132 offset1:165
	ds_read2_b32 v[122:123], v136 offset0:198 offset1:231
	v_add_u32_e32 v102, 0x400, v136
	s_waitcnt lgkmcnt(3)
	v_mul_f32_e32 v101, 0x42800000, v110
	v_mul_f32_e32 v110, 0x42800000, v111
	v_mov_b32_e32 v103, v136
	v_cvt_pk_fp8_f32 v138, v101, v110
	ds_read2_b32 v[126:127], v102 offset0:8 offset1:41
	ds_read2_b32 v[130:131], v102 offset0:74 offset1:107
	ds_read2_b32 v[146:147], v102 offset0:140 offset1:173
	ds_read2_b32 v[148:149], v102 offset0:206 offset1:239
	ds_read2_b32 v[140:141], v103 offset0:16 offset1:49
	ds_read2_b32 v[142:143], v103 offset0:82 offset1:115
	ds_read2_b32 v[144:145], v103 offset0:148 offset1:181
	ds_read2_b32 v[150:151], v103 offset0:214 offset1:247
	s_waitcnt lgkmcnt(10)
	v_mul_f32_e32 v111, 0x42800000, v114
	v_mul_f32_e32 v114, 0x42800000, v115
	v_cvt_pk_fp8_f32 v138, v111, v114 op_sel:[0,0,1]
	s_waitcnt lgkmcnt(3)
	v_mul_f32_e32 v101, 0x42800000, v140
	v_mul_f32_e32 v110, 0x42800000, v141
	s_waitcnt lgkmcnt(2)
	v_mul_f32_e32 v111, 0x42800000, v142
	v_mov_b32_e32 v142, v3
	v_add_u32_e32 v107, 0x400, v136
	v_cvt_pk_fp8_f32 v142, v101, v110
	v_mul_f32_e32 v101, 0x42800000, v118
	v_mul_f32_e32 v110, 0x42800000, v119
	ds_read2_b32 v[152:153], v107 offset0:24 offset1:57
	ds_read2_b32 v[154:155], v107 offset0:90 offset1:123
	ds_read2_b32 v[156:157], v107 offset0:156 offset1:189
	ds_read2_b32 v[158:159], v107 offset0:222 offset1:255
	v_mul_f32_e32 v114, 0x42800000, v143
	v_cvt_pk_fp8_f32 v139, v101, v110
	s_waitcnt lgkmcnt(5)
	v_mul_f32_e32 v101, 0x42800000, v144
	v_mul_f32_e32 v110, 0x42800000, v145
	v_mov_b32_e32 v143, v3
	v_cvt_pk_fp8_f32 v143, v101, v110
	v_mul_f32_e32 v101, 0x42800000, v126
	v_mul_f32_e32 v110, 0x42800000, v127
	v_mov_b32_e32 v140, v3
	v_cvt_pk_fp8_f32 v140, v101, v110
	s_waitcnt lgkmcnt(3)
	v_mul_f32_e32 v101, 0x42800000, v152
	v_mul_f32_e32 v110, 0x42800000, v153
	v_mov_b32_e32 v144, v3
	v_cvt_pk_fp8_f32 v142, v111, v114 op_sel:[0,0,1]
	v_mul_f32_e32 v111, 0x42800000, v122
	v_mul_f32_e32 v114, 0x42800000, v123
	v_cvt_pk_fp8_f32 v144, v101, v110
	v_mul_f32_e32 v101, 0x42800000, v146
	v_mul_f32_e32 v110, 0x42800000, v147
	v_mov_b32_e32 v141, v3
	v_cvt_pk_fp8_f32 v139, v111, v114 op_sel:[0,0,1]
	v_mul_f32_e32 v111, 0x42800000, v150
	v_mul_f32_e32 v114, 0x42800000, v151
	v_cvt_pk_fp8_f32 v141, v101, v110
	s_waitcnt lgkmcnt(1)
	v_mul_f32_e32 v101, 0x42800000, v156
	v_mul_f32_e32 v110, 0x42800000, v157
	v_mov_b32_e32 v145, v3
	v_cvt_pk_fp8_f32 v143, v111, v114 op_sel:[0,0,1]
	v_mul_f32_e32 v111, 0x42800000, v130
	v_mul_f32_e32 v114, 0x42800000, v131
	v_cvt_pk_fp8_f32 v145, v101, v110
	s_mul_hi_i32 s0, s28, 0x1600000
	s_mul_i32 s28, s28, 0x1600000
	v_or_b32_e32 v100, s62, v135
	v_cvt_pk_fp8_f32 v140, v111, v114 op_sel:[0,0,1]
	v_mul_f32_e32 v111, 0x42800000, v154
	v_mul_f32_e32 v114, 0x42800000, v155
	s_add_u32 s28, s36, s28
	v_cvt_pk_fp8_f32 v144, v111, v114 op_sel:[0,0,1]
	v_mul_f32_e32 v111, 0x42800000, v148
	v_mul_f32_e32 v114, 0x42800000, v149
	v_ashrrev_i32_e32 v101, 31, v100
	s_addc_u32 s29, s37, s0
	v_cvt_pk_fp8_f32 v141, v111, v114 op_sel:[0,0,1]
	s_waitcnt lgkmcnt(0)
	v_mul_f32_e32 v111, 0x42800000, v158
	v_mul_f32_e32 v114, 0x42800000, v159
	v_lshlrev_b64 v[100:101], 11, v[100:101]
	v_cvt_pk_fp8_f32 v145, v111, v114 op_sel:[0,0,1]
	v_lshl_add_u64 v[100:101], s[28:29], 0, v[100:101]
	v_lshl_add_u64 v[100:101], v[100:101], 0, s[26:27]
	v_lshl_add_u64 v[100:101], v[100:101], 0, v[132:133]
	global_store_dwordx4 v[100:101], v[138:141], off
	s_nop 1
	v_add_co_u32_e32 v100, vcc, 0x8000, v100
	s_nop 1
	v_addc_co_u32_e32 v101, vcc, 0, v101, vcc
	global_store_dwordx4 v[100:101], v[142:145], off
	ds_write2_b32 v137, v68, v69 offset1:1
	ds_write2_b32 v137, v70, v71 offset0:2 offset1:3
	ds_write2_b32 v128, v72, v73 offset1:1
	ds_write2_b32 v124, v74, v75 offset1:1
	ds_write2_b32 v125, v76, v77 offset1:1
	ds_write2_b32 v120, v78, v79 offset1:1
	ds_write2_b32 v121, v80, v81 offset1:1
	ds_write2_b32 v116, v82, v83 offset1:1
	ds_write2_b32 v117, v84, v85 offset1:1
	ds_write2_b32 v112, v86, v87 offset1:1
	ds_write2_b32 v113, v88, v89 offset1:1
	ds_write2_b32 v108, v90, v91 offset1:1
	ds_write2_b32 v109, v92, v93 offset1:1
	ds_write2_b32 v104, v94, v95 offset1:1
	ds_write2_b32 v105, v96, v97 offset1:1
	ds_write2_b32 v106, v98, v99 offset1:1
	ds_read2_b32 v[94:95], v136 offset1:33
	ds_read2_b32 v[96:97], v136 offset0:66 offset1:99
	ds_read2_b32 v[92:93], v136 offset0:132 offset1:165
	ds_read2_b32 v[90:91], v136 offset0:198 offset1:231
	ds_read2_b32 v[84:85], v102 offset0:8 offset1:41
	ds_read2_b32 v[82:83], v102 offset0:74 offset1:107
	ds_read2_b32 v[76:77], v102 offset0:140 offset1:173
	ds_read2_b32 v[74:75], v102 offset0:206 offset1:239
	ds_read2_b32 v[98:99], v103 offset0:16 offset1:49
	ds_read2_b32 v[100:101], v103 offset0:82 offset1:115
	ds_read2_b32 v[88:89], v103 offset0:148 offset1:181
	ds_read2_b32 v[86:87], v103 offset0:214 offset1:247
	ds_read2_b32 v[80:81], v107 offset0:24 offset1:57
	ds_read2_b32 v[78:79], v107 offset0:90 offset1:123
	ds_read2_b32 v[72:73], v107 offset0:156 offset1:189
	ds_read2_b32 v[70:71], v107 offset0:222 offset1:255
	s_waitcnt lgkmcnt(14)
	v_mul_f32_e32 v69, 0x42800000, v94
	v_mul_f32_e32 v95, 0x42800000, v95
	v_mov_b32_e32 v94, v3
	v_cvt_pk_fp8_f32 v94, v69, v95
	s_waitcnt lgkmcnt(7)
	v_mul_f32_e32 v69, 0x42800000, v98
	v_mul_f32_e32 v95, 0x42800000, v99
	v_mov_b32_e32 v98, v3
	v_cvt_pk_fp8_f32 v98, v69, v95
	v_mul_f32_e32 v96, 0x42800000, v96
	v_mul_f32_e32 v97, 0x42800000, v97
	v_mul_f32_e32 v69, 0x42800000, v92
	v_mul_f32_e32 v92, 0x42800000, v93
	v_mov_b32_e32 v95, v3
	v_cvt_pk_fp8_f32 v94, v96, v97 op_sel:[0,0,1]
	s_waitcnt lgkmcnt(6)
	v_mul_f32_e32 v96, 0x42800000, v100
	v_mul_f32_e32 v97, 0x42800000, v101
	v_cvt_pk_fp8_f32 v95, v69, v92
	s_waitcnt lgkmcnt(5)
	v_mul_f32_e32 v69, 0x42800000, v88
	v_mul_f32_e32 v88, 0x42800000, v89
	v_mov_b32_e32 v99, v3
	v_cvt_pk_fp8_f32 v98, v96, v97 op_sel:[0,0,1]
	v_cvt_pk_fp8_f32 v99, v69, v88
	v_mul_f32_e32 v69, 0x42800000, v84
	v_mul_f32_e32 v84, 0x42800000, v85
	v_mov_b32_e32 v96, v3
	v_cvt_pk_fp8_f32 v96, v69, v84
	s_waitcnt lgkmcnt(3)
	v_mul_f32_e32 v69, 0x42800000, v80
	v_mul_f32_e32 v80, 0x42800000, v81
	v_mov_b32_e32 v100, v3
	v_cvt_pk_fp8_f32 v100, v69, v80
	v_mul_f32_e32 v69, 0x42800000, v76
	v_mul_f32_e32 v76, 0x42800000, v77
	v_mov_b32_e32 v97, v3
	v_cvt_pk_fp8_f32 v97, v69, v76
	s_waitcnt lgkmcnt(1)
	v_mul_f32_e32 v69, 0x42800000, v72
	v_mul_f32_e32 v72, 0x42800000, v73
	v_mov_b32_e32 v101, v3
	v_cvt_pk_fp8_f32 v101, v69, v72
	s_mul_hi_i32 s0, s51, 0x1600000
	s_mul_i32 s51, s51, 0x1600000
	v_or_b32_e32 v68, s58, v135
	s_add_u32 s26, s36, s51
	v_mul_f32_e32 v90, 0x42800000, v90
	v_mul_f32_e32 v91, 0x42800000, v91
	v_mul_f32_e32 v82, 0x42800000, v82
	v_mul_f32_e32 v83, 0x42800000, v83
	v_mul_f32_e32 v74, 0x42800000, v74
	v_mul_f32_e32 v75, 0x42800000, v75
	v_ashrrev_i32_e32 v69, 31, v68
	s_addc_u32 s27, s37, s0
	v_cvt_pk_fp8_f32 v95, v90, v91 op_sel:[0,0,1]
	v_mul_f32_e32 v86, 0x42800000, v86
	v_mul_f32_e32 v87, 0x42800000, v87
	v_cvt_pk_fp8_f32 v96, v82, v83 op_sel:[0,0,1]
	v_mul_f32_e32 v78, 0x42800000, v78
	v_mul_f32_e32 v79, 0x42800000, v79
	v_cvt_pk_fp8_f32 v97, v74, v75 op_sel:[0,0,1]
	s_waitcnt lgkmcnt(0)
	v_mul_f32_e32 v70, 0x42800000, v70
	v_mul_f32_e32 v71, 0x42800000, v71
	v_lshlrev_b64 v[68:69], 11, v[68:69]
	v_cvt_pk_fp8_f32 v99, v86, v87 op_sel:[0,0,1]
	v_cvt_pk_fp8_f32 v100, v78, v79 op_sel:[0,0,1]
	v_cvt_pk_fp8_f32 v101, v70, v71 op_sel:[0,0,1]
	v_lshl_add_u64 v[68:69], s[26:27], 0, v[68:69]
	v_lshl_add_u64 v[68:69], v[68:69], 0, s[24:25]
	v_lshl_add_u64 v[68:69], v[68:69], 0, v[132:133]
	global_store_dwordx4 v[68:69], v[94:97], off
	s_nop 1
	v_add_co_u32_e32 v68, vcc, 0x8000, v68
	s_nop 1
	v_addc_co_u32_e32 v69, vcc, 0, v69, vcc
	global_store_dwordx4 v[68:69], v[98:101], off
	ds_write2_b32 v137, v36, v37 offset1:1
	ds_write2_b32 v137, v38, v39 offset0:2 offset1:3
	ds_write2_b32 v128, v40, v41 offset1:1
	ds_write2_b32 v124, v42, v43 offset1:1
	ds_write2_b32 v125, v44, v45 offset1:1
	ds_write2_b32 v120, v46, v47 offset1:1
	ds_write2_b32 v121, v48, v49 offset1:1
	ds_write2_b32 v116, v50, v51 offset1:1
	ds_write2_b32 v117, v52, v53 offset1:1
	ds_write2_b32 v112, v54, v55 offset1:1
	ds_write2_b32 v113, v56, v57 offset1:1
	ds_write2_b32 v108, v58, v59 offset1:1
	ds_write2_b32 v109, v60, v61 offset1:1
	ds_write2_b32 v104, v62, v63 offset1:1
	ds_write2_b32 v105, v64, v65 offset1:1
	ds_write2_b32 v106, v66, v67 offset1:1
	ds_read2_b32 v[62:63], v136 offset1:33
	ds_read2_b32 v[64:65], v136 offset0:66 offset1:99
	ds_read2_b32 v[60:61], v136 offset0:132 offset1:165
	ds_read2_b32 v[58:59], v136 offset0:198 offset1:231
	ds_read2_b32 v[52:53], v102 offset0:8 offset1:41
	ds_read2_b32 v[50:51], v102 offset0:74 offset1:107
	ds_read2_b32 v[44:45], v102 offset0:140 offset1:173
	ds_read2_b32 v[42:43], v102 offset0:206 offset1:239
	ds_read2_b32 v[66:67], v103 offset0:16 offset1:49
	ds_read2_b32 v[68:69], v103 offset0:82 offset1:115
	ds_read2_b32 v[56:57], v103 offset0:148 offset1:181
	ds_read2_b32 v[54:55], v103 offset0:214 offset1:247
	ds_read2_b32 v[48:49], v107 offset0:24 offset1:57
	ds_read2_b32 v[46:47], v107 offset0:90 offset1:123
	ds_read2_b32 v[40:41], v107 offset0:156 offset1:189
	ds_read2_b32 v[38:39], v107 offset0:222 offset1:255
	s_waitcnt lgkmcnt(14)
	v_mul_f32_e32 v37, 0x42800000, v62
	v_mul_f32_e32 v63, 0x42800000, v63
	v_mov_b32_e32 v62, v3
	v_cvt_pk_fp8_f32 v62, v37, v63
	s_waitcnt lgkmcnt(7)
	v_mul_f32_e32 v37, 0x42800000, v66
	v_mul_f32_e32 v63, 0x42800000, v67
	v_mov_b32_e32 v66, v3
	v_cvt_pk_fp8_f32 v66, v37, v63
	v_mul_f32_e32 v64, 0x42800000, v64
	v_mul_f32_e32 v65, 0x42800000, v65
	v_mul_f32_e32 v37, 0x42800000, v60
	v_mul_f32_e32 v60, 0x42800000, v61
	v_mov_b32_e32 v63, v3
	v_cvt_pk_fp8_f32 v62, v64, v65 op_sel:[0,0,1]
	s_waitcnt lgkmcnt(6)
	v_mul_f32_e32 v64, 0x42800000, v68
	v_mul_f32_e32 v65, 0x42800000, v69
	v_cvt_pk_fp8_f32 v63, v37, v60
	s_waitcnt lgkmcnt(5)
	v_mul_f32_e32 v37, 0x42800000, v56
	v_mul_f32_e32 v56, 0x42800000, v57
	v_mov_b32_e32 v67, v3
	v_cvt_pk_fp8_f32 v66, v64, v65 op_sel:[0,0,1]
	v_cvt_pk_fp8_f32 v67, v37, v56
	v_mul_f32_e32 v37, 0x42800000, v52
	v_mul_f32_e32 v52, 0x42800000, v53
	v_mov_b32_e32 v64, v3
	v_cvt_pk_fp8_f32 v64, v37, v52
	s_waitcnt lgkmcnt(3)
	v_mul_f32_e32 v37, 0x42800000, v48
	v_mul_f32_e32 v48, 0x42800000, v49
	v_mov_b32_e32 v68, v3
	v_cvt_pk_fp8_f32 v68, v37, v48
	v_mul_f32_e32 v37, 0x42800000, v44
	v_mul_f32_e32 v44, 0x42800000, v45
	v_mov_b32_e32 v65, v3
	v_cvt_pk_fp8_f32 v65, v37, v44
	s_waitcnt lgkmcnt(1)
	v_mul_f32_e32 v37, 0x42800000, v40
	v_mul_f32_e32 v40, 0x42800000, v41
	v_mov_b32_e32 v69, v3
	v_cvt_pk_fp8_f32 v69, v37, v40
	s_mul_hi_i32 s0, s49, 0x1600000
	s_mul_i32 s49, s49, 0x1600000
	v_or_b32_e32 v36, s50, v135
	s_add_u32 s24, s36, s49
	v_mul_f32_e32 v58, 0x42800000, v58
	v_mul_f32_e32 v59, 0x42800000, v59
	v_mul_f32_e32 v50, 0x42800000, v50
	v_mul_f32_e32 v51, 0x42800000, v51
	v_mul_f32_e32 v42, 0x42800000, v42
	v_mul_f32_e32 v43, 0x42800000, v43
	v_ashrrev_i32_e32 v37, 31, v36
	s_addc_u32 s25, s37, s0
	v_cvt_pk_fp8_f32 v63, v58, v59 op_sel:[0,0,1]
	v_mul_f32_e32 v54, 0x42800000, v54
	v_mul_f32_e32 v55, 0x42800000, v55
	v_cvt_pk_fp8_f32 v64, v50, v51 op_sel:[0,0,1]
	v_mul_f32_e32 v46, 0x42800000, v46
	v_mul_f32_e32 v47, 0x42800000, v47
	v_cvt_pk_fp8_f32 v65, v42, v43 op_sel:[0,0,1]
	s_waitcnt lgkmcnt(0)
	v_mul_f32_e32 v38, 0x42800000, v38
	v_mul_f32_e32 v39, 0x42800000, v39
	v_lshlrev_b64 v[36:37], 11, v[36:37]
	v_cvt_pk_fp8_f32 v67, v54, v55 op_sel:[0,0,1]
	v_cvt_pk_fp8_f32 v68, v46, v47 op_sel:[0,0,1]
	v_cvt_pk_fp8_f32 v69, v38, v39 op_sel:[0,0,1]
	v_lshl_add_u64 v[36:37], s[24:25], 0, v[36:37]
	v_lshl_add_u64 v[36:37], v[36:37], 0, s[4:5]
	v_lshl_add_u64 v[36:37], v[36:37], 0, v[132:133]
	global_store_dwordx4 v[36:37], v[62:65], off
	s_nop 1
	v_add_co_u32_e32 v36, vcc, 0x8000, v36
	s_nop 1
	v_addc_co_u32_e32 v37, vcc, 0, v37, vcc
	global_store_dwordx4 v[36:37], v[66:69], off
	ds_write2_b32 v137, v4, v5 offset1:1
	ds_write2_b32 v137, v6, v7 offset0:2 offset1:3
	ds_write2_b32 v128, v8, v9 offset1:1
	ds_write2_b32 v124, v10, v11 offset1:1
	ds_write2_b32 v125, v12, v13 offset1:1
	ds_write2_b32 v120, v14, v15 offset1:1
	ds_write2_b32 v121, v16, v17 offset1:1
	ds_write2_b32 v116, v18, v19 offset1:1
	ds_write2_b32 v117, v20, v21 offset1:1
	ds_write2_b32 v112, v22, v23 offset1:1
	ds_write2_b32 v113, v24, v25 offset1:1
	ds_write2_b32 v108, v26, v27 offset1:1
	ds_write2_b32 v109, v28, v29 offset1:1
	ds_write2_b32 v104, v30, v31 offset1:1
	ds_write2_b32 v105, v32, v33 offset1:1
	ds_write2_b32 v106, v34, v35 offset1:1
	ds_read2_b32 v[4:5], v136 offset1:33
	ds_read2_b32 v[8:9], v136 offset0:66 offset1:99
	ds_read2_b32 v[32:33], v136 offset0:132 offset1:165
	ds_read2_b32 v[30:31], v136 offset0:198 offset1:231
	ds_read2_b32 v[24:25], v102 offset0:8 offset1:41
	ds_read2_b32 v[6:7], v102 offset0:74 offset1:107
	ds_read2_b32 v[20:21], v102 offset0:140 offset1:173
	ds_read2_b32 v[18:19], v102 offset0:206 offset1:239
	ds_read2_b32 v[34:35], v103 offset0:16 offset1:49
	ds_read2_b32 v[36:37], v103 offset0:82 offset1:115
	ds_read2_b32 v[28:29], v103 offset0:148 offset1:181
	ds_read2_b32 v[26:27], v103 offset0:214 offset1:247
	ds_read2_b32 v[22:23], v107 offset0:24 offset1:57
	ds_read2_b32 v[10:11], v107 offset0:90 offset1:123
	ds_read2_b32 v[16:17], v107 offset0:156 offset1:189
	ds_read2_b32 v[14:15], v107 offset0:222 offset1:255
	s_waitcnt lgkmcnt(14)
	v_mul_f32_e32 v13, 0x42800000, v4
	v_mul_f32_e32 v5, 0x42800000, v5
	v_mov_b32_e32 v4, v3
	v_cvt_pk_fp8_f32 v4, v13, v5
	v_mul_f32_e32 v8, 0x42800000, v8
	v_mul_f32_e32 v9, 0x42800000, v9
	s_waitcnt lgkmcnt(7)
	v_mul_f32_e32 v5, 0x42800000, v34
	v_cvt_pk_fp8_f32 v4, v8, v9 op_sel:[0,0,1]
	v_mul_f32_e32 v9, 0x42800000, v35
	v_mov_b32_e32 v8, v3
	v_cvt_pk_fp8_f32 v8, v5, v9
	s_waitcnt lgkmcnt(6)
	v_mul_f32_e32 v13, 0x42800000, v36
	v_mul_f32_e32 v34, 0x42800000, v37
	v_mul_f32_e32 v9, 0x42800000, v32
	v_cvt_pk_fp8_f32 v8, v13, v34 op_sel:[0,0,1]
	v_mul_f32_e32 v13, 0x42800000, v33
	v_mov_b32_e32 v5, v3
	v_cvt_pk_fp8_f32 v5, v9, v13
	s_waitcnt lgkmcnt(5)
	v_mul_f32_e32 v13, 0x42800000, v28
	v_mul_f32_e32 v28, 0x42800000, v29
	v_mov_b32_e32 v9, v3
	v_cvt_pk_fp8_f32 v9, v13, v28
	v_mul_f32_e32 v13, 0x42800000, v24
	v_mul_f32_e32 v24, 0x42800000, v25
	v_mul_f32_e32 v25, 0x42800000, v6
	v_mov_b32_e32 v6, v3
	v_cvt_pk_fp8_f32 v6, v13, v24
	v_mul_f32_e32 v7, 0x42800000, v7
	s_waitcnt lgkmcnt(3)
	v_mul_f32_e32 v13, 0x42800000, v23
	s_waitcnt lgkmcnt(2)
	v_mul_f32_e32 v11, 0x42800000, v11
	v_cvt_pk_fp8_f32 v6, v25, v7 op_sel:[0,0,1]
	v_mul_f32_e32 v7, 0x42800000, v22
	v_mul_f32_e32 v22, 0x42800000, v10
	v_mov_b32_e32 v10, v3
	v_cvt_pk_fp8_f32 v10, v7, v13
	v_mul_f32_e32 v13, 0x42800000, v21
	v_mov_b32_e32 v7, v3
	s_mul_hi_i32 s0, s47, 0x1600000
	v_cvt_pk_fp8_f32 v10, v22, v11 op_sel:[0,0,1]
	v_mul_f32_e32 v11, 0x42800000, v20
	v_cvt_pk_fp8_f32 v7, v11, v13
	s_waitcnt lgkmcnt(1)
	v_mul_f32_e32 v13, 0x42800000, v16
	v_mul_f32_e32 v16, 0x42800000, v17
	v_mov_b32_e32 v11, v3
	v_cvt_pk_fp8_f32 v11, v13, v16
	s_mul_i32 s47, s47, 0x1600000
	v_or_b32_e32 v12, s48, v135
	s_add_u32 s4, s36, s47
	v_mul_f32_e32 v30, 0x42800000, v30
	v_mul_f32_e32 v31, 0x42800000, v31
	v_mul_f32_e32 v18, 0x42800000, v18
	v_mul_f32_e32 v19, 0x42800000, v19
	v_ashrrev_i32_e32 v13, 31, v12
	s_addc_u32 s5, s37, s0
	v_cvt_pk_fp8_f32 v5, v30, v31 op_sel:[0,0,1]
	v_mul_f32_e32 v26, 0x42800000, v26
	v_mul_f32_e32 v27, 0x42800000, v27
	v_cvt_pk_fp8_f32 v7, v18, v19 op_sel:[0,0,1]
	s_waitcnt lgkmcnt(0)
	v_mul_f32_e32 v14, 0x42800000, v14
	v_mul_f32_e32 v15, 0x42800000, v15
	v_lshlrev_b64 v[12:13], 11, v[12:13]
	v_cvt_pk_fp8_f32 v9, v26, v27 op_sel:[0,0,1]
	v_cvt_pk_fp8_f32 v11, v14, v15 op_sel:[0,0,1]
	v_lshl_add_u64 v[12:13], s[4:5], 0, v[12:13]
	v_lshl_add_u64 v[12:13], v[12:13], 0, s[2:3]
	v_lshl_add_u64 v[12:13], v[12:13], 0, v[132:133]
	global_store_dwordx4 v[12:13], v[4:7], off
	s_nop 1
	v_add_co_u32_e32 v12, vcc, 0x8000, v12
	s_nop 1
	v_addc_co_u32_e32 v13, vcc, 0, v13, vcc
	global_store_dwordx4 v[12:13], v[8:11], off
	s_add_i32 s31, s31, 32
	s_cmp_lt_i32 s31, s30
	s_cbranch_scc1 .LBB6_907
.LBB6_908:
	s_max_i32 s0, s90, 0xdc00
	s_min_i32 s12, s91, 0x14a00
	s_cmp_le_i32 s12, s0
	s_mov_b32 s58, 0x800000
	s_cbranch_scc1 .LBB6_914
	s_sub_i32 s1, s12, s0
	s_mov_b32 s2, 19
	s_cmp_lt_i32 s1, 32
	s_cbranch_scc1 .LBB6_914
	s_add_i32 s0, s0, s95
	s_add_i32 s12, s12, 0xffff2400
	s_add_i32 s13, s0, 0xffff2400
	s_cmp_ge_i32 s13, s12
	s_cbranch_scc1 .LBB6_914
	s_ashr_i32 s3, s2, 31
	s_lshl_b64 s[0:1], s[2:3], 3
	s_add_u32 s0, s76, s0
	s_addc_u32 s1, s77, s1
	s_load_dwordx2 s[0:1], s[0:1], 0x0
	v_lshlrev_b32_e32 v2, 4, v166
	v_lshlrev_b32_e32 v6, 5, v166
	v_lshrrev_b32_e32 v4, 3, v166
	v_and_b32_e32 v5, 0x70, v2
	s_waitcnt lgkmcnt(0)
	s_add_u32 s47, s0, 0x8400000
	s_addc_u32 s48, s1, 0
	v_lshrrev_b32_e32 v147, 2, v166
	v_lshlrev_b32_e32 v144, 4, v166
	v_and_b32_e32 v144, 48, v144
	s_add_u32 s49, s6, 0x99180000
	v_lshl_or_b32 v2, v4, 13, v5
	v_add_u32_e32 v5, s94, v5
	v_mul_u32_u24_e32 v4, 0x84, v4
	v_mul_u32_u24_e32 v6, 0x84, v144
	v_lshlrev_b32_e32 v7, 2, v147
	v_and_b32_e32 v146, 31, v167
	s_addc_u32 s50, s7, 0
	v_mov_b32_e32 v145, v3
	v_add3_u32 v148, s94, v6, v7
	v_add_u32_e32 v149, v5, v4
.LBB6_912:
	s_mul_hi_i32 s1, s13, 0x2e8ba2e9
	s_lshr_b32 s3, s1, 31
	s_ashr_i32 s1, s1, 10
	s_lshl_b32 s2, s13, 3
	s_add_i32 s1, s1, s3
	s_and_b32 s33, s2, 64
	s_mul_i32 s2, s1, 0xffffea00
	s_add_i32 s2, s2, s13
	s_mul_hi_i32 s5, s1, 0xb00000
	s_mul_i32 s4, s1, 0xb00000
	s_ashr_i32 s1, s2, 1
	s_and_b32 s0, s13, 7
	s_ashr_i32 s2, s2, 31
	s_and_b32 s1, s1, -8
	s_lshr_b32 s2, s2, 26
	s_or_b32 s1, s1, s0
	s_add_i32 s2, s1, s2
	s_ashr_i32 s2, s2, 6
	s_lshl_b32 s1, s1, 5
	s_lshl_b32 s3, s2, 11
	s_lshl_b32 s2, s2, 7
	s_lshl_b64 s[24:25], s[4:5], 2
	s_sub_i32 s1, s1, s3
	s_or_b32 s2, s2, s33
	s_add_u32 s28, s47, s24
	v_or_b32_e32 v36, s1, v146
	v_or_b32_e32 v169, s1, v147
	s_addc_u32 s1, s48, s25
	v_readfirstlane_b32 s24, v36
	s_ashr_i32 s3, s2, 31
	s_andn2_b32 s24, s24, 31
	s_lshl_b64 s[26:27], s[2:3], 13
	s_add_u32 s26, s28, s26
	s_addc_u32 s1, s1, s27
	s_ashr_i32 s25, s24, 31
	s_lshl_b64 s[24:25], s[24:25], 2
	s_add_u32 s24, s26, s24
	s_addc_u32 s25, s1, s25
	s_mov_b64 s[26:27], s[24:25]
	s_add_u32 s28, s24, 0x10000
	s_addc_u32 s29, s25, 0
	v_lshl_add_u64 v[36:37], s[26:27], 0, v[2:3]
	s_add_u32 s26, s24, 0x20000
	global_load_dwordx4 v[124:127], v[36:37], off nt
	s_addc_u32 s27, s25, 0
	v_lshl_add_u64 v[36:37], s[28:29], 0, v[2:3]
	s_add_u32 s28, s24, 0x30000
	global_load_dwordx4 v[132:135], v[36:37], off nt
	s_addc_u32 s29, s25, 0
	v_lshl_add_u64 v[36:37], s[26:27], 0, v[2:3]
	s_add_u32 s26, s24, 0x40000
	global_load_dwordx4 v[136:139], v[36:37], off nt
	s_addc_u32 s27, s25, 0
	v_lshl_add_u64 v[36:37], s[28:29], 0, v[2:3]
	s_add_u32 s28, s24, 0x50000
	global_load_dwordx4 v[140:143], v[36:37], off nt
	s_addc_u32 s29, s25, 0
	v_lshl_add_u64 v[36:37], s[26:27], 0, v[2:3]
	s_add_u32 s26, s24, 0x60000
	s_addc_u32 s27, s25, 0
	global_load_dwordx4 v[170:173], v[36:37], off nt
	s_add_u32 s24, s24, 0x70000
	v_lshl_add_u64 v[36:37], s[28:29], 0, v[2:3]
	global_load_dwordx4 v[174:177], v[36:37], off nt
	s_addc_u32 s25, s25, 0
	s_add_i32 s1, s13, 8
	v_lshl_add_u64 v[36:37], s[26:27], 0, v[2:3]
	s_mul_hi_i32 s26, s1, 0x2e8ba2e9
	global_load_dwordx4 v[184:187], v[36:37], off nt
	s_lshr_b32 s28, s26, 31
	s_ashr_i32 s26, s26, 10
	v_lshl_add_u64 v[36:37], s[24:25], 0, v[2:3]
	s_add_i32 s24, s26, s28
	s_mul_i32 s25, s24, 0xffffea00
	s_add_i32 s25, s25, s1
	s_lshl_b32 s27, s1, 3
	s_ashr_i32 s1, s25, 1
	s_and_b32 s30, s27, 64
	s_mul_hi_i32 s27, s24, 0xb00000
	s_mul_i32 s26, s24, 0xb00000
	s_ashr_i32 s24, s25, 31
	s_and_b32 s1, s1, -8
	s_lshr_b32 s24, s24, 26
	s_or_b32 s1, s1, s0
	s_add_i32 s24, s1, s24
	s_ashr_i32 s24, s24, 6
	s_lshl_b32 s1, s1, 5
	s_lshl_b32 s25, s24, 11
	s_lshl_b32 s24, s24, 7
	s_lshl_b64 s[28:29], s[26:27], 2
	s_sub_i32 s1, s1, s25
	s_or_b32 s24, s24, s30
	global_load_dwordx4 v[188:191], v[36:37], off nt
	s_add_u32 s34, s47, s28
	v_or_b32_e32 v36, s1, v146
	v_or_b32_e32 v183, s1, v147
	s_addc_u32 s1, s48, s29
	v_readfirstlane_b32 s28, v36
	s_ashr_i32 s25, s24, 31
	s_andn2_b32 s28, s28, 31
	s_lshl_b64 s[30:31], s[24:25], 13
	s_add_u32 s30, s34, s30
	s_addc_u32 s1, s1, s31
	s_ashr_i32 s29, s28, 31
	s_lshl_b64 s[28:29], s[28:29], 2
	s_add_u32 s28, s30, s28
	s_addc_u32 s29, s1, s29
	s_mov_b64 s[30:31], s[28:29]
	s_add_u32 s34, s28, 0x10000
	s_addc_u32 s35, s29, 0
	v_lshl_add_u64 v[36:37], s[30:31], 0, v[2:3]
	s_add_u32 s30, s28, 0x20000
	global_load_dwordx4 v[76:79], v[36:37], off nt
	s_addc_u32 s31, s29, 0
	v_lshl_add_u64 v[36:37], s[34:35], 0, v[2:3]
	s_add_u32 s34, s28, 0x30000
	global_load_dwordx4 v[88:91], v[36:37], off nt
	s_addc_u32 s35, s29, 0
	v_lshl_add_u64 v[36:37], s[30:31], 0, v[2:3]
	s_add_u32 s30, s28, 0x40000
	global_load_dwordx4 v[96:99], v[36:37], off nt
	s_addc_u32 s31, s29, 0
	v_lshl_add_u64 v[36:37], s[34:35], 0, v[2:3]
	s_add_u32 s34, s28, 0x50000
	global_load_dwordx4 v[100:103], v[36:37], off nt
	s_addc_u32 s35, s29, 0
	v_lshl_add_u64 v[36:37], s[30:31], 0, v[2:3]
	s_add_u32 s30, s28, 0x60000
	s_addc_u32 s31, s29, 0
	global_load_dwordx4 v[108:111], v[36:37], off nt
	s_add_u32 s28, s28, 0x70000
	v_lshl_add_u64 v[36:37], s[34:35], 0, v[2:3]
	global_load_dwordx4 v[112:115], v[36:37], off nt
	s_addc_u32 s29, s29, 0
	s_add_i32 s1, s13, 16
	v_lshl_add_u64 v[36:37], s[30:31], 0, v[2:3]
	s_mul_hi_i32 s30, s1, 0x2e8ba2e9
	global_load_dwordx4 v[120:123], v[36:37], off nt
	s_lshr_b32 s31, s30, 31
	s_ashr_i32 s30, s30, 10
	v_lshl_add_u64 v[36:37], s[28:29], 0, v[2:3]
	s_add_i32 s28, s30, s31
	s_mul_i32 s30, s28, 0xffffea00
	s_add_i32 s30, s30, s1
	s_ashr_i32 s1, s30, 1
	s_ashr_i32 s30, s30, 31
	s_and_b32 s1, s1, -8
	s_lshr_b32 s30, s30, 26
	s_or_b32 s1, s1, s0
	s_add_i32 s30, s1, s30
	s_ashr_i32 s30, s30, 6
	s_mul_hi_i32 s29, s28, 0xb00000
	s_mul_i32 s28, s28, 0xb00000
	s_lshl_b32 s1, s1, 5
	s_lshl_b32 s31, s30, 11
	s_lshl_b32 s30, s30, 7
	s_lshl_b64 s[34:35], s[28:29], 2
	s_sub_i32 s1, s1, s31
	s_or_b32 s30, s30, s33
	global_load_dwordx4 v[128:131], v[36:37], off nt
	s_add_u32 s33, s47, s34
	v_or_b32_e32 v36, s1, v146
	v_or_b32_e32 v202, s1, v147
	s_addc_u32 s1, s48, s35
	v_readfirstlane_b32 s34, v36
	s_ashr_i32 s31, s30, 31
	s_andn2_b32 s34, s34, 31
	s_lshl_b64 s[36:37], s[30:31], 13
	s_add_u32 s33, s33, s36
	s_addc_u32 s1, s1, s37
	s_ashr_i32 s35, s34, 31
	s_lshl_b64 s[34:35], s[34:35], 2
	s_add_u32 s34, s33, s34
	s_addc_u32 s35, s1, s35
	s_mov_b64 s[36:37], s[34:35]
	s_add_u32 s66, s34, 0x10000
	s_addc_u32 s67, s35, 0
	v_lshl_add_u64 v[36:37], s[36:37], 0, v[2:3]
	s_add_u32 s36, s34, 0x20000
	global_load_dwordx4 v[48:51], v[36:37], off nt
	s_addc_u32 s37, s35, 0
	v_lshl_add_u64 v[36:37], s[66:67], 0, v[2:3]
	s_add_u32 s66, s34, 0x30000
	global_load_dwordx4 v[56:59], v[36:37], off nt
	s_addc_u32 s67, s35, 0
	v_lshl_add_u64 v[36:37], s[36:37], 0, v[2:3]
	s_add_u32 s36, s34, 0x40000
	global_load_dwordx4 v[64:67], v[36:37], off nt
	s_addc_u32 s37, s35, 0
	v_lshl_add_u64 v[36:37], s[66:67], 0, v[2:3]
	s_add_u32 s66, s34, 0x50000
	global_load_dwordx4 v[72:75], v[36:37], off nt
	s_addc_u32 s67, s35, 0
	v_lshl_add_u64 v[36:37], s[36:37], 0, v[2:3]
	s_add_u32 s36, s34, 0x60000
	s_addc_u32 s37, s35, 0
	s_add_u32 s34, s34, 0x70000
	global_load_dwordx4 v[84:87], v[36:37], off nt
	s_addc_u32 s35, s35, 0
	v_lshl_add_u64 v[36:37], s[66:67], 0, v[2:3]
	s_add_i32 s1, s13, 24
	global_load_dwordx4 v[92:95], v[36:37], off nt
	s_mul_hi_i32 s33, s1, 0x2e8ba2e9
	v_lshl_add_u64 v[36:37], s[36:37], 0, v[2:3]
	s_lshr_b32 s37, s33, 31
	s_ashr_i32 s33, s33, 10
	global_load_dwordx4 v[104:107], v[36:37], off nt
	s_add_i32 s33, s33, s37
	v_lshl_add_u64 v[36:37], s[34:35], 0, v[2:3]
	s_mul_i32 s34, s33, 0xffffea00
	s_add_i32 s34, s34, s1
	s_lshl_b32 s36, s1, 3
	s_ashr_i32 s1, s34, 1
	s_and_b32 s45, s36, 64
	s_mul_hi_i32 s37, s33, 0xb00000
	s_mul_i32 s36, s33, 0xb00000
	s_ashr_i32 s33, s34, 31
	s_and_b32 s1, s1, -8
	s_lshr_b32 s33, s33, 26
	s_or_b32 s0, s1, s0
	s_add_i32 s1, s0, s33
	s_ashr_i32 s1, s1, 6
	s_lshl_b32 s0, s0, 5
	s_lshl_b32 s33, s1, 11
	s_lshl_b32 s1, s1, 7
	s_lshl_b64 s[66:67], s[36:37], 2
	s_sub_i32 s0, s0, s33
	s_or_b32 s34, s1, s45
	global_load_dwordx4 v[116:119], v[36:37], off nt
	s_add_u32 s1, s47, s66
	v_or_b32_e32 v36, s0, v146
	v_or_b32_e32 v203, s0, v147
	s_addc_u32 s33, s48, s67
	v_readfirstlane_b32 s0, v36
	s_ashr_i32 s35, s34, 31
	s_andn2_b32 s0, s0, 31
	s_lshl_b64 s[66:67], s[34:35], 13
	s_add_u32 s45, s1, s66
	s_addc_u32 s33, s33, s67
	s_ashr_i32 s1, s0, 31
	s_lshl_b64 s[0:1], s[0:1], 2
	s_add_u32 s0, s45, s0
	s_addc_u32 s1, s33, s1
	s_mov_b64 s[66:67], s[0:1]
	s_add_u32 s68, s0, 0x10000
	s_addc_u32 s69, s1, 0
	v_lshl_add_u64 v[36:37], s[66:67], 0, v[2:3]
	global_load_dwordx4 v[36:39], v[36:37], off nt
	s_add_u32 s66, s0, 0x20000
	s_addc_u32 s67, s1, 0
	v_lshl_add_u64 v[40:41], s[68:69], 0, v[2:3]
	global_load_dwordx4 v[40:43], v[40:41], off nt
	s_add_u32 s68, s0, 0x30000
	s_addc_u32 s69, s1, 0
	v_lshl_add_u64 v[44:45], s[66:67], 0, v[2:3]
	global_load_dwordx4 v[44:47], v[44:45], off nt
	s_add_u32 s66, s0, 0x40000
	s_addc_u32 s67, s1, 0
	v_lshl_add_u64 v[52:53], s[68:69], 0, v[2:3]
	global_load_dwordx4 v[52:55], v[52:53], off nt
	s_add_u32 s68, s0, 0x50000
	s_addc_u32 s69, s1, 0
	v_lshl_add_u64 v[60:61], s[66:67], 0, v[2:3]
	global_load_dwordx4 v[60:63], v[60:61], off nt
	s_add_u32 s66, s0, 0x60000
	s_addc_u32 s67, s1, 0
	v_lshl_add_u64 v[68:69], s[68:69], 0, v[2:3]
	global_load_dwordx4 v[68:71], v[68:69], off nt
	s_add_u32 s0, s0, 0x70000
	s_addc_u32 s1, s1, 0
	v_lshl_add_u64 v[80:81], s[66:67], 0, v[2:3]
	global_load_dwordx4 v[80:83], v[80:81], off nt
	v_add_u32_e32 v150, 0x420, v149
	v_add_u32_e32 v151, 0x428, v149
	v_add_u32_e32 v152, 0x840, v149
	v_add_u32_e32 v153, 0x848, v149
	v_add_u32_e32 v154, 0xc60, v149
	v_add_u32_e32 v155, 0xc68, v149
	v_add_u32_e32 v156, 0x1080, v149
	v_add_u32_e32 v157, 0x1088, v149
	v_add_u32_e32 v158, 0x14a0, v149
	v_add_u32_e32 v159, 0x14a8, v149
	v_add_u32_e32 v160, 0x18c0, v149
	v_add_u32_e32 v161, 0x18c8, v149
	v_add_u32_e32 v162, 0x1ce0, v149
	v_add_u32_e32 v163, 0x1ce8, v149
	s_waitcnt vmcnt(0)
	ds_write2_b32 v149, v124, v125 offset1:1
	ds_write2_b32 v149, v126, v127 offset0:2 offset1:3
	ds_write2_b32 v150, v132, v133 offset1:1
	ds_write2_b32 v151, v134, v135 offset1:1
	ds_write2_b32 v152, v136, v137 offset1:1
	ds_write2_b32 v153, v138, v139 offset1:1
	ds_write2_b32 v154, v140, v141 offset1:1
	ds_write2_b32 v155, v142, v143 offset1:1
	ds_write2_b32 v156, v170, v171 offset1:1
	ds_write2_b32 v157, v172, v173 offset1:1
	ds_write2_b32 v158, v174, v175 offset1:1
	ds_write2_b32 v159, v176, v177 offset1:1
	ds_write2_b32 v160, v184, v185 offset1:1
	ds_write2_b32 v161, v186, v187 offset1:1
	ds_write2_b32 v162, v188, v189 offset1:1
	ds_write2_b32 v163, v190, v191 offset1:1
	v_lshl_add_u64 v[124:125], s[0:1], 0, v[2:3]
	global_load_dwordx4 v[124:127], v[124:125], off nt
	s_add_u32 s4, s49, s4
	s_addc_u32 s5, s50, s5
	v_add_u32_e32 v164, 0x400, v148
	v_mov_b32_e32 v165, v148
	v_add_u32_e32 v168, 0x400, v148
	v_mov_b64_e32 v[132:133], s[4:5]
	s_add_u32 s0, s49, s26
	ds_read2_b32 v[134:135], v148 offset1:33
	ds_read2_b32 v[136:137], v148 offset0:66 offset1:99
	ds_read2_b32 v[138:139], v148 offset0:132 offset1:165
	ds_read2_b32 v[140:141], v148 offset0:198 offset1:231
	ds_read2_b32 v[142:143], v164 offset0:8 offset1:41
	ds_read2_b32 v[170:171], v164 offset0:74 offset1:107
	ds_read2_b32 v[172:173], v164 offset0:140 offset1:173
	ds_read2_b32 v[174:175], v164 offset0:206 offset1:239
	ds_read2_b32 v[176:177], v165 offset0:16 offset1:49
	ds_read2_b32 v[178:179], v165 offset0:82 offset1:115
	ds_read2_b32 v[184:185], v165 offset0:148 offset1:181
	ds_read2_b32 v[186:187], v165 offset0:214 offset1:247
	ds_read2_b32 v[188:189], v168 offset0:24 offset1:57
	ds_read2_b32 v[190:191], v168 offset0:90 offset1:123
	ds_read2_b32 v[192:193], v168 offset0:156 offset1:189
	ds_read2_b32 v[194:195], v168 offset0:222 offset1:255
	v_mad_i64_i32 v[132:133], s[4:5], v169, s82, v[132:133]
	s_addc_u32 s1, s50, s27
	v_lshl_add_u64 v[132:133], v[132:133], 0, s[2:3]
	v_mov_b64_e32 v[196:197], s[0:1]
	v_mov_b32_e32 v4, v3
	v_mov_b32_e32 v5, v3
	v_mov_b32_e32 v6, v3
	v_mov_b32_e32 v7, v3
	v_lshl_add_u64 v[198:199], v[132:133], 0, v[144:145]
	v_mad_i64_i32 v[132:133], s[2:3], v183, s82, v[196:197]
	s_waitcnt lgkmcnt(14)
	v_mul_f32_e32 v169, 0x42800000, v134
	v_mul_f32_e32 v183, 0x42800000, v135
	s_waitcnt lgkmcnt(13)
	v_mul_f32_e32 v138, 0x42800000, v138
	v_mul_f32_e32 v139, 0x42800000, v139
	s_waitcnt lgkmcnt(11)
	v_mul_f32_e32 v142, 0x42800000, v142
	v_mul_f32_e32 v143, 0x42800000, v143
	s_waitcnt lgkmcnt(9)
	v_mul_f32_e32 v172, 0x42800000, v172
	v_mul_f32_e32 v173, 0x42800000, v173
	v_mov_b32_e32 v8, v3
	v_mov_b32_e32 v9, v3
	v_mov_b32_e32 v10, v3
	v_mov_b32_e32 v11, v3
	s_waitcnt lgkmcnt(7)
	v_mul_f32_e32 v176, 0x42800000, v176
	v_mul_f32_e32 v177, 0x42800000, v177
	s_waitcnt lgkmcnt(5)
	v_mul_f32_e32 v184, 0x42800000, v184
	v_mul_f32_e32 v185, 0x42800000, v185
	s_waitcnt lgkmcnt(3)
	v_mul_f32_e32 v188, 0x42800000, v188
	v_mul_f32_e32 v189, 0x42800000, v189
	s_waitcnt lgkmcnt(1)
	v_mul_f32_e32 v192, 0x42800000, v192
	v_mul_f32_e32 v193, 0x42800000, v193
	v_cvt_pk_fp8_f32 v4, v169, v183
	v_cvt_pk_fp8_f32 v5, v138, v139
	v_cvt_pk_fp8_f32 v6, v142, v143
	v_cvt_pk_fp8_f32 v7, v172, v173
	v_cvt_pk_fp8_f32 v8, v176, v177
	v_cvt_pk_fp8_f32 v9, v184, v185
	v_cvt_pk_fp8_f32 v10, v188, v189
	v_cvt_pk_fp8_f32 v11, v192, v193
	v_mul_f32_e32 v136, 0x42800000, v136
	v_mul_f32_e32 v137, 0x42800000, v137
	v_mul_f32_e32 v140, 0x42800000, v140
	v_mul_f32_e32 v141, 0x42800000, v141
	v_mul_f32_e32 v170, 0x42800000, v170
	v_mul_f32_e32 v171, 0x42800000, v171
	v_mul_f32_e32 v174, 0x42800000, v174
	v_mul_f32_e32 v175, 0x42800000, v175
	v_mul_f32_e32 v178, 0x42800000, v178
	v_mul_f32_e32 v179, 0x42800000, v179
	v_mul_f32_e32 v186, 0x42800000, v186
	v_mul_f32_e32 v187, 0x42800000, v187
	v_mul_f32_e32 v190, 0x42800000, v190
	v_mul_f32_e32 v191, 0x42800000, v191
	s_waitcnt lgkmcnt(0)
	v_mul_f32_e32 v194, 0x42800000, v194
	v_mul_f32_e32 v195, 0x42800000, v195
	v_cvt_pk_fp8_f32 v4, v136, v137 op_sel:[0,0,1]
	v_cvt_pk_fp8_f32 v5, v140, v141 op_sel:[0,0,1]
	v_cvt_pk_fp8_f32 v6, v170, v171 op_sel:[0,0,1]
	v_cvt_pk_fp8_f32 v7, v174, v175 op_sel:[0,0,1]
	v_cvt_pk_fp8_f32 v8, v178, v179 op_sel:[0,0,1]
	v_cvt_pk_fp8_f32 v9, v186, v187 op_sel:[0,0,1]
	v_cvt_pk_fp8_f32 v10, v190, v191 op_sel:[0,0,1]
	v_cvt_pk_fp8_f32 v11, v194, v195 op_sel:[0,0,1]
	global_store_dwordx4 v[198:199], v[4:7], off
	s_nop 1
	v_add_co_u32_e32 v198, vcc, 0x16000, v198
	s_nop 1
	v_addc_co_u32_e32 v199, vcc, 0, v199, vcc
	global_store_dwordx4 v[198:199], v[8:11], off
	ds_write2_b32 v149, v76, v77 offset1:1
	ds_write2_b32 v149, v78, v79 offset0:2 offset1:3
	ds_write2_b32 v150, v88, v89 offset1:1
	ds_write2_b32 v151, v90, v91 offset1:1
	ds_write2_b32 v152, v96, v97 offset1:1
	ds_write2_b32 v153, v98, v99 offset1:1
	ds_write2_b32 v154, v100, v101 offset1:1
	ds_write2_b32 v155, v102, v103 offset1:1
	ds_write2_b32 v156, v108, v109 offset1:1
	ds_write2_b32 v157, v110, v111 offset1:1
	ds_write2_b32 v158, v112, v113 offset1:1
	ds_write2_b32 v159, v114, v115 offset1:1
	ds_write2_b32 v160, v120, v121 offset1:1
	ds_write2_b32 v161, v122, v123 offset1:1
	ds_write2_b32 v162, v128, v129 offset1:1
	ds_write2_b32 v163, v130, v131 offset1:1
	ds_read2_b32 v[4:5], v148 offset1:33
	ds_read2_b32 v[6:7], v148 offset0:66 offset1:99
	ds_read2_b32 v[8:9], v148 offset0:132 offset1:165
	ds_read2_b32 v[10:11], v148 offset0:198 offset1:231
	ds_read2_b32 v[76:77], v164 offset0:8 offset1:41
	ds_read2_b32 v[78:79], v164 offset0:74 offset1:107
	ds_read2_b32 v[88:89], v164 offset0:140 offset1:173
	ds_read2_b32 v[90:91], v164 offset0:206 offset1:239
	ds_read2_b32 v[96:97], v165 offset0:16 offset1:49
	ds_read2_b32 v[98:99], v165 offset0:82 offset1:115
	ds_read2_b32 v[100:101], v165 offset0:148 offset1:181
	ds_read2_b32 v[102:103], v165 offset0:214 offset1:247
	ds_read2_b32 v[108:109], v168 offset0:24 offset1:57
	ds_read2_b32 v[110:111], v168 offset0:90 offset1:123
	ds_read2_b32 v[112:113], v168 offset0:156 offset1:189
	ds_read2_b32 v[114:115], v168 offset0:222 offset1:255
	v_mov_b32_e32 v12, v3
	v_mov_b32_e32 v13, v3
	v_mov_b32_e32 v14, v3
	v_mov_b32_e32 v15, v3
	s_waitcnt lgkmcnt(14)
	v_mul_f32_e32 v4, 0x42800000, v4
	v_mul_f32_e32 v5, 0x42800000, v5
	s_waitcnt lgkmcnt(13)
	v_mul_f32_e32 v8, 0x42800000, v8
	v_mul_f32_e32 v9, 0x42800000, v9
	s_waitcnt lgkmcnt(11)
	v_mul_f32_e32 v76, 0x42800000, v76
	v_mul_f32_e32 v77, 0x42800000, v77
	s_waitcnt lgkmcnt(9)
	v_mul_f32_e32 v88, 0x42800000, v88
	v_mul_f32_e32 v89, 0x42800000, v89
	v_mov_b32_e32 v16, v3
	v_mov_b32_e32 v17, v3
	v_mov_b32_e32 v18, v3
	v_mov_b32_e32 v19, v3
	s_waitcnt lgkmcnt(7)
	v_mul_f32_e32 v96, 0x42800000, v96
	v_mul_f32_e32 v97, 0x42800000, v97
	s_waitcnt lgkmcnt(5)
	v_mul_f32_e32 v100, 0x42800000, v100
	v_mul_f32_e32 v101, 0x42800000, v101
	s_waitcnt lgkmcnt(3)
	v_mul_f32_e32 v108, 0x42800000, v108
	v_mul_f32_e32 v109, 0x42800000, v109
	s_waitcnt lgkmcnt(1)
	v_mul_f32_e32 v112, 0x42800000, v112
	v_mul_f32_e32 v113, 0x42800000, v113
	v_cvt_pk_fp8_f32 v12, v4, v5
	v_cvt_pk_fp8_f32 v13, v8, v9
	v_cvt_pk_fp8_f32 v14, v76, v77
	v_cvt_pk_fp8_f32 v15, v88, v89
	v_cvt_pk_fp8_f32 v16, v96, v97
	v_cvt_pk_fp8_f32 v17, v100, v101
	v_cvt_pk_fp8_f32 v18, v108, v109
	v_cvt_pk_fp8_f32 v19, v112, v113
	v_mul_f32_e32 v6, 0x42800000, v6
	v_mul_f32_e32 v7, 0x42800000, v7
	v_mul_f32_e32 v10, 0x42800000, v10
	v_mul_f32_e32 v11, 0x42800000, v11
	v_mul_f32_e32 v78, 0x42800000, v78
	v_mul_f32_e32 v79, 0x42800000, v79
	v_mul_f32_e32 v90, 0x42800000, v90
	v_mul_f32_e32 v91, 0x42800000, v91
	v_mul_f32_e32 v98, 0x42800000, v98
	v_mul_f32_e32 v99, 0x42800000, v99
	v_mul_f32_e32 v102, 0x42800000, v102
	v_mul_f32_e32 v103, 0x42800000, v103
	v_mul_f32_e32 v110, 0x42800000, v110
	v_mul_f32_e32 v111, 0x42800000, v111
	s_waitcnt lgkmcnt(0)
	v_mul_f32_e32 v114, 0x42800000, v114
	v_mul_f32_e32 v115, 0x42800000, v115
	v_cvt_pk_fp8_f32 v12, v6, v7 op_sel:[0,0,1]
	v_cvt_pk_fp8_f32 v13, v10, v11 op_sel:[0,0,1]
	v_cvt_pk_fp8_f32 v14, v78, v79 op_sel:[0,0,1]
	v_cvt_pk_fp8_f32 v15, v90, v91 op_sel:[0,0,1]
	v_cvt_pk_fp8_f32 v16, v98, v99 op_sel:[0,0,1]
	v_cvt_pk_fp8_f32 v17, v102, v103 op_sel:[0,0,1]
	v_cvt_pk_fp8_f32 v18, v110, v111 op_sel:[0,0,1]
	v_cvt_pk_fp8_f32 v19, v114, v115 op_sel:[0,0,1]
	v_lshl_add_u64 v[132:133], v[132:133], 0, s[24:25]
	v_lshl_add_u64 v[200:201], v[132:133], 0, v[144:145]
	global_store_dwordx4 v[200:201], v[12:15], off
	s_nop 1
	v_add_co_u32_e32 v200, vcc, 0x16000, v200
	s_nop 1
	v_addc_co_u32_e32 v201, vcc, 0, v201, vcc
	global_store_dwordx4 v[200:201], v[16:19], off
	ds_write2_b32 v149, v48, v49 offset1:1
	ds_write2_b32 v149, v50, v51 offset0:2 offset1:3
	ds_write2_b32 v150, v56, v57 offset1:1
	ds_write2_b32 v151, v58, v59 offset1:1
	ds_write2_b32 v152, v64, v65 offset1:1
	ds_write2_b32 v153, v66, v67 offset1:1
	ds_write2_b32 v154, v72, v73 offset1:1
	ds_write2_b32 v155, v74, v75 offset1:1
	ds_write2_b32 v156, v84, v85 offset1:1
	ds_write2_b32 v157, v86, v87 offset1:1
	ds_write2_b32 v158, v92, v93 offset1:1
	ds_write2_b32 v159, v94, v95 offset1:1
	ds_write2_b32 v160, v104, v105 offset1:1
	ds_write2_b32 v161, v106, v107 offset1:1
	ds_write2_b32 v162, v116, v117 offset1:1
	ds_write2_b32 v163, v118, v119 offset1:1
	ds_read2_b32 v[4:5], v148 offset1:33
	ds_read2_b32 v[6:7], v148 offset0:66 offset1:99
	ds_read2_b32 v[8:9], v148 offset0:132 offset1:165
	ds_read2_b32 v[10:11], v148 offset0:198 offset1:231
	ds_read2_b32 v[12:13], v164 offset0:8 offset1:41
	ds_read2_b32 v[14:15], v164 offset0:74 offset1:107
	ds_read2_b32 v[16:17], v164 offset0:140 offset1:173
	ds_read2_b32 v[18:19], v164 offset0:206 offset1:239
	ds_read2_b32 v[48:49], v165 offset0:16 offset1:49
	ds_read2_b32 v[50:51], v165 offset0:82 offset1:115
	ds_read2_b32 v[56:57], v165 offset0:148 offset1:181
	ds_read2_b32 v[58:59], v165 offset0:214 offset1:247
	ds_read2_b32 v[64:65], v168 offset0:24 offset1:57
	ds_read2_b32 v[66:67], v168 offset0:90 offset1:123
	ds_read2_b32 v[72:73], v168 offset0:156 offset1:189
	ds_read2_b32 v[74:75], v168 offset0:222 offset1:255
	v_mov_b32_e32 v20, v3
	v_mov_b32_e32 v21, v3
	v_mov_b32_e32 v22, v3
	v_mov_b32_e32 v23, v3
	s_waitcnt lgkmcnt(14)
	v_mul_f32_e32 v4, 0x42800000, v4
	v_mul_f32_e32 v5, 0x42800000, v5
	s_waitcnt lgkmcnt(13)
	v_mul_f32_e32 v8, 0x42800000, v8
	v_mul_f32_e32 v9, 0x42800000, v9
	s_waitcnt lgkmcnt(11)
	v_mul_f32_e32 v12, 0x42800000, v12
	v_mul_f32_e32 v13, 0x42800000, v13
	s_waitcnt lgkmcnt(9)
	v_mul_f32_e32 v16, 0x42800000, v16
	v_mul_f32_e32 v17, 0x42800000, v17
	v_mov_b32_e32 v24, v3
	v_mov_b32_e32 v25, v3
	v_mov_b32_e32 v26, v3
	v_mov_b32_e32 v27, v3
	s_waitcnt lgkmcnt(7)
	v_mul_f32_e32 v48, 0x42800000, v48
	v_mul_f32_e32 v49, 0x42800000, v49
	s_waitcnt lgkmcnt(5)
	v_mul_f32_e32 v56, 0x42800000, v56
	v_mul_f32_e32 v57, 0x42800000, v57
	s_waitcnt lgkmcnt(3)
	v_mul_f32_e32 v64, 0x42800000, v64
	v_mul_f32_e32 v65, 0x42800000, v65
	s_waitcnt lgkmcnt(1)
	v_mul_f32_e32 v72, 0x42800000, v72
	v_mul_f32_e32 v73, 0x42800000, v73
	v_cvt_pk_fp8_f32 v20, v4, v5
	v_cvt_pk_fp8_f32 v21, v8, v9
	v_cvt_pk_fp8_f32 v22, v12, v13
	v_cvt_pk_fp8_f32 v23, v16, v17
	v_cvt_pk_fp8_f32 v24, v48, v49
	v_cvt_pk_fp8_f32 v25, v56, v57
	v_cvt_pk_fp8_f32 v26, v64, v65
	v_cvt_pk_fp8_f32 v27, v72, v73
	s_add_u32 s0, s49, s28
	s_addc_u32 s1, s50, s29
	v_mul_f32_e32 v6, 0x42800000, v6
	v_mul_f32_e32 v7, 0x42800000, v7
	v_mul_f32_e32 v10, 0x42800000, v10
	v_mul_f32_e32 v11, 0x42800000, v11
	v_mul_f32_e32 v14, 0x42800000, v14
	v_mul_f32_e32 v15, 0x42800000, v15
	v_mul_f32_e32 v18, 0x42800000, v18
	v_mul_f32_e32 v19, 0x42800000, v19
	v_mov_b64_e32 v[196:197], s[0:1]
	v_mul_f32_e32 v50, 0x42800000, v50
	v_mul_f32_e32 v51, 0x42800000, v51
	v_mul_f32_e32 v58, 0x42800000, v58
	v_mul_f32_e32 v59, 0x42800000, v59
	v_mul_f32_e32 v66, 0x42800000, v66
	v_mul_f32_e32 v67, 0x42800000, v67
	s_waitcnt lgkmcnt(0)
	v_mul_f32_e32 v74, 0x42800000, v74
	v_mul_f32_e32 v75, 0x42800000, v75
	v_cvt_pk_fp8_f32 v20, v6, v7 op_sel:[0,0,1]
	v_cvt_pk_fp8_f32 v21, v10, v11 op_sel:[0,0,1]
	v_cvt_pk_fp8_f32 v22, v14, v15 op_sel:[0,0,1]
	v_cvt_pk_fp8_f32 v23, v18, v19 op_sel:[0,0,1]
	v_mad_i64_i32 v[132:133], s[2:3], v202, s82, v[196:197]
	v_cvt_pk_fp8_f32 v24, v50, v51 op_sel:[0,0,1]
	v_cvt_pk_fp8_f32 v25, v58, v59 op_sel:[0,0,1]
	v_cvt_pk_fp8_f32 v26, v66, v67 op_sel:[0,0,1]
	v_cvt_pk_fp8_f32 v27, v74, v75 op_sel:[0,0,1]
	v_lshl_add_u64 v[132:133], v[132:133], 0, s[30:31]
	v_lshl_add_u64 v[134:135], v[132:133], 0, v[144:145]
	global_store_dwordx4 v[134:135], v[20:23], off
	s_nop 1
	v_add_co_u32_e32 v134, vcc, 0x16000, v134
	s_nop 1
	v_addc_co_u32_e32 v135, vcc, 0, v135, vcc
	global_store_dwordx4 v[134:135], v[24:27], off
	ds_write2_b32 v149, v36, v37 offset1:1
	ds_write2_b32 v149, v38, v39 offset0:2 offset1:3
	ds_write2_b32 v150, v40, v41 offset1:1
	ds_write2_b32 v151, v42, v43 offset1:1
	ds_write2_b32 v152, v44, v45 offset1:1
	ds_write2_b32 v153, v46, v47 offset1:1
	ds_write2_b32 v154, v52, v53 offset1:1
	ds_write2_b32 v155, v54, v55 offset1:1
	ds_write2_b32 v156, v60, v61 offset1:1
	ds_write2_b32 v157, v62, v63 offset1:1
	ds_write2_b32 v158, v68, v69 offset1:1
	ds_write2_b32 v159, v70, v71 offset1:1
	ds_write2_b32 v160, v80, v81 offset1:1
	ds_write2_b32 v161, v82, v83 offset1:1
	s_waitcnt vmcnt(6)
	ds_write2_b32 v162, v124, v125 offset1:1
	ds_write2_b32 v163, v126, v127 offset1:1
	ds_read2_b32 v[4:5], v148 offset1:33
	ds_read2_b32 v[6:7], v148 offset0:66 offset1:99
	ds_read2_b32 v[8:9], v148 offset0:132 offset1:165
	ds_read2_b32 v[10:11], v148 offset0:198 offset1:231
	ds_read2_b32 v[12:13], v164 offset0:8 offset1:41
	ds_read2_b32 v[14:15], v164 offset0:74 offset1:107
	ds_read2_b32 v[16:17], v164 offset0:140 offset1:173
	ds_read2_b32 v[18:19], v164 offset0:206 offset1:239
	ds_read2_b32 v[20:21], v165 offset0:16 offset1:49
	ds_read2_b32 v[22:23], v165 offset0:82 offset1:115
	ds_read2_b32 v[24:25], v165 offset0:148 offset1:181
	ds_read2_b32 v[26:27], v165 offset0:214 offset1:247
	ds_read2_b32 v[36:37], v168 offset0:24 offset1:57
	ds_read2_b32 v[38:39], v168 offset0:90 offset1:123
	ds_read2_b32 v[40:41], v168 offset0:156 offset1:189
	ds_read2_b32 v[42:43], v168 offset0:222 offset1:255
	v_mov_b32_e32 v28, v3
	v_mov_b32_e32 v29, v3
	v_mov_b32_e32 v30, v3
	v_mov_b32_e32 v31, v3
	s_waitcnt lgkmcnt(14)
	v_mul_f32_e32 v4, 0x42800000, v4
	v_mul_f32_e32 v5, 0x42800000, v5
	s_waitcnt lgkmcnt(13)
	v_mul_f32_e32 v8, 0x42800000, v8
	v_mul_f32_e32 v9, 0x42800000, v9
	s_waitcnt lgkmcnt(11)
	v_mul_f32_e32 v12, 0x42800000, v12
	v_mul_f32_e32 v13, 0x42800000, v13
	s_waitcnt lgkmcnt(9)
	v_mul_f32_e32 v16, 0x42800000, v16
	v_mul_f32_e32 v17, 0x42800000, v17
	v_mov_b32_e32 v32, v3
	v_mov_b32_e32 v33, v3
	v_mov_b32_e32 v34, v3
	v_mov_b32_e32 v35, v3
	s_waitcnt lgkmcnt(7)
	v_mul_f32_e32 v20, 0x42800000, v20
	v_mul_f32_e32 v21, 0x42800000, v21
	s_waitcnt lgkmcnt(5)
	v_mul_f32_e32 v24, 0x42800000, v24
	v_mul_f32_e32 v25, 0x42800000, v25
	s_waitcnt lgkmcnt(3)
	v_mul_f32_e32 v36, 0x42800000, v36
	v_mul_f32_e32 v37, 0x42800000, v37
	s_waitcnt lgkmcnt(1)
	v_mul_f32_e32 v40, 0x42800000, v40
	v_mul_f32_e32 v41, 0x42800000, v41
	v_cvt_pk_fp8_f32 v28, v4, v5
	v_cvt_pk_fp8_f32 v29, v8, v9
	v_cvt_pk_fp8_f32 v30, v12, v13
	v_cvt_pk_fp8_f32 v31, v16, v17
	v_cvt_pk_fp8_f32 v32, v20, v21
	v_cvt_pk_fp8_f32 v33, v24, v25
	v_cvt_pk_fp8_f32 v34, v36, v37
	v_cvt_pk_fp8_f32 v35, v40, v41
	s_add_u32 s0, s49, s36
	s_addc_u32 s1, s50, s37
	v_mul_f32_e32 v6, 0x42800000, v6
	v_mul_f32_e32 v7, 0x42800000, v7
	v_mul_f32_e32 v10, 0x42800000, v10
	v_mul_f32_e32 v11, 0x42800000, v11
	v_mul_f32_e32 v14, 0x42800000, v14
	v_mul_f32_e32 v15, 0x42800000, v15
	v_mul_f32_e32 v18, 0x42800000, v18
	v_mul_f32_e32 v19, 0x42800000, v19
	v_mov_b64_e32 v[196:197], s[0:1]
	v_mul_f32_e32 v22, 0x42800000, v22
	v_mul_f32_e32 v23, 0x42800000, v23
	v_mul_f32_e32 v26, 0x42800000, v26
	v_mul_f32_e32 v27, 0x42800000, v27
	v_mul_f32_e32 v38, 0x42800000, v38
	v_mul_f32_e32 v39, 0x42800000, v39
	s_waitcnt lgkmcnt(0)
	v_mul_f32_e32 v42, 0x42800000, v42
	v_mul_f32_e32 v43, 0x42800000, v43
	v_cvt_pk_fp8_f32 v28, v6, v7 op_sel:[0,0,1]
	v_cvt_pk_fp8_f32 v29, v10, v11 op_sel:[0,0,1]
	v_cvt_pk_fp8_f32 v30, v14, v15 op_sel:[0,0,1]
	v_cvt_pk_fp8_f32 v31, v18, v19 op_sel:[0,0,1]
	v_mad_i64_i32 v[132:133], s[0:1], v203, s82, v[196:197]
	v_cvt_pk_fp8_f32 v32, v22, v23 op_sel:[0,0,1]
	v_cvt_pk_fp8_f32 v33, v26, v27 op_sel:[0,0,1]
	v_cvt_pk_fp8_f32 v34, v38, v39 op_sel:[0,0,1]
	v_cvt_pk_fp8_f32 v35, v42, v43 op_sel:[0,0,1]
	v_lshl_add_u64 v[132:133], v[132:133], 0, s[34:35]
	v_lshl_add_u64 v[4:5], v[132:133], 0, v[144:145]
	global_store_dwordx4 v[4:5], v[28:31], off
	s_nop 1
	v_add_co_u32_e32 v4, vcc, 0x16000, v4
	s_nop 1
	v_addc_co_u32_e32 v5, vcc, 0, v5, vcc
	global_store_dwordx4 v[4:5], v[32:35], off
	s_add_i32 s13, s13, 32
	s_cmp_lt_i32 s13, s12
	s_cbranch_scc1 .LBB6_912
	v_readlane_b32 s68, v254, 58
	v_readlane_b32 s69, v254, 59

.LBB6_1067:
	s_max_i32 s0, s90, 0x7b00
	s_min_i32 s4, s91, 0x9b00
	s_cmp_le_i32 s4, s0
	s_cbranch_scc1 .LBB6_1072
	s_sub_i32 s1, s4, s0
	s_mov_b32 s2, 2
	s_cmp_lt_i32 s1, 32
	s_cbranch_scc1 .LBB6_1072
	s_add_i32 s0, s0, s95
	s_addk_i32 s4, 0x8500
	s_add_i32 s5, s0, 0xffff8500
	s_cmp_ge_i32 s5, s4
	s_cbranch_scc1 .LBB6_1072
	s_ashr_i32 s3, s2, 31
	s_lshl_b64 s[0:1], s[2:3], 3
	s_add_u32 s0, s76, s0
	s_addc_u32 s1, s77, s1
	s_load_dwordx2 s[0:1], s[0:1], 0x0
	s_waitcnt vmcnt(0)
	v_lshrrev_b32_e32 v4, 3, v166
	v_lshlrev_b32_e32 v2, 2, v166
	v_mul_u32_u24_e32 v5, 0x4240, v4
	v_and_b32_e32 v6, 28, v2
	s_waitcnt lgkmcnt(0)
	s_add_u32 s12, s0, 0x8480000
	v_or_b32_e32 v2, v5, v6
	v_lshl_add_u32 v5, v6, 2, s94
	v_lshlrev_b32_e32 v6, 5, v166
	s_addc_u32 s13, s1, 0
	v_lshrrev_b32_e32 v168, 2, v166
	v_lshlrev_b32_e32 v156, 4, v166
	v_and_b32_e32 v156, 48, v156
	v_mov_b32_e32 v7, 0x2240
	s_add_u32 s2, s6, 0x8d080000
	v_mul_u32_u24_e32 v4, 0x84, v4
	v_mul_u32_u24_e32 v6, 0x84, v156
	v_and_or_b32 v169, v167, 31, v7
	v_lshlrev_b32_e32 v7, 2, v168
	s_addc_u32 s3, s7, 0
	v_lshlrev_b32_e32 v2, 2, v2
	v_mov_b32_e32 v157, v3
	v_add3_u32 v170, s94, v6, v7
	v_add_u32_e32 v171, v5, v4
.LBB6_1071:
	s_ashr_i32 s0, s5, 31
	s_lshr_b32 s0, s0, 19
	s_add_i32 s0, s5, s0
	s_and_b32 s0, s0, 0xffffe000
	s_sub_i32 s0, s5, s0
	s_ashr_i32 s1, s0, 1
	s_and_b32 s24, s0, 7
	s_ashr_i32 s25, s0, 31
	s_and_b32 s1, s1, -8
	s_lshr_b32 s25, s25, 24
	s_or_b32 s1, s1, s24
	s_add_i32 s24, s1, s25
	s_ashr_i32 s24, s24, 8
	s_lshl_b32 s1, s1, 5
	s_lshl_b32 s25, s24, 13
	s_lshl_b32 s0, s0, 3
	s_sub_i32 s25, s1, s25
	s_and_b32 s0, s0, 64
	s_lshl_b32 s24, s24, 7
	v_add_u32_e32 v37, s25, v169
	s_or_b32 s0, s24, s0
	v_or_b32_e32 v36, s25, v168
	v_readfirstlane_b32 s24, v37
	s_ashr_i32 s1, s0, 31
	s_mul_i32 s27, s0, 0x10900
	v_ashrrev_i32_e32 v37, 31, v36
	s_andn2_b32 s24, s24, 31
	s_mul_hi_i32 s26, s0, 0x10900
	v_lshlrev_b64 v[36:37], 11, v[36:37]
	s_add_u32 s27, s12, s27
	v_lshl_add_u64 v[36:37], s[2:3], 0, v[36:37]
	s_addc_u32 s26, s13, s26
	s_ashr_i32 s25, s24, 31
	v_lshl_add_u64 v[36:37], v[36:37], 0, s[0:1]
	s_lshl_b64 s[0:1], s[24:25], 2
	s_add_u32 s0, s27, s0
	s_addc_u32 s1, s26, s1
	s_mov_b64 s[24:25], s[0:1]
	s_add_u32 s26, s0, 0x84800
	s_addc_u32 s27, s1, 0
	v_lshl_add_u64 v[164:165], v[36:37], 0, v[156:157]
	v_lshl_add_u64 v[36:37], s[24:25], 0, v[2:3]
	s_add_u32 s24, s0, 0x109000
	global_load_dwordx4 v[92:95], v[36:37], off nt
	s_addc_u32 s25, s1, 0
	v_lshl_add_u64 v[36:37], s[26:27], 0, v[2:3]
	s_add_u32 s26, s0, 0x18d800
	global_load_dwordx4 v[108:111], v[36:37], off nt
	s_addc_u32 s27, s1, 0
	v_lshl_add_u64 v[36:37], s[24:25], 0, v[2:3]
	s_add_u32 s24, s0, 0x212000
	global_load_dwordx4 v[120:123], v[36:37], off nt
	s_addc_u32 s25, s1, 0
	v_lshl_add_u64 v[36:37], s[26:27], 0, v[2:3]
	s_add_u32 s26, s0, 0x296800
	global_load_dwordx4 v[132:135], v[36:37], off nt
	s_addc_u32 s27, s1, 0
	v_lshl_add_u64 v[36:37], s[24:25], 0, v[2:3]
	s_add_u32 s24, s0, 0x31b000
	s_addc_u32 s25, s1, 0
	global_load_dwordx4 v[140:143], v[36:37], off nt
	s_add_u32 s0, s0, 0x39f800
	v_lshl_add_u64 v[36:37], s[26:27], 0, v[2:3]
	global_load_dwordx4 v[148:151], v[36:37], off nt
	s_addc_u32 s1, s1, 0
	s_add_i32 s26, s5, 8
	v_lshl_add_u64 v[36:37], s[24:25], 0, v[2:3]
	s_ashr_i32 s24, s26, 31
	global_load_dwordx4 v[152:155], v[36:37], off nt
	s_lshr_b32 s24, s24, 19
	v_lshl_add_u64 v[36:37], s[0:1], 0, v[2:3]
	s_add_i32 s0, s26, s24
	s_and_b32 s0, s0, 0xffffe000
	s_sub_i32 s0, s26, s0
	s_ashr_i32 s1, s0, 1
	s_and_b32 s24, s0, 7
	s_ashr_i32 s25, s0, 31
	s_and_b32 s1, s1, -8
	s_lshr_b32 s25, s25, 24
	s_or_b32 s1, s1, s24
	s_add_i32 s24, s1, s25
	s_ashr_i32 s24, s24, 8
	s_lshl_b32 s1, s1, 5
	s_lshl_b32 s25, s24, 13
	s_lshl_b32 s0, s0, 3
	s_sub_i32 s25, s1, s25
	global_load_dwordx4 v[192:195], v[36:37], off nt
	s_and_b32 s0, s0, 64
	s_lshl_b32 s24, s24, 7
	v_add_u32_e32 v37, s25, v169
	s_or_b32 s0, s24, s0
	v_or_b32_e32 v36, s25, v168
	v_readfirstlane_b32 s24, v37
	s_ashr_i32 s1, s0, 31
	s_mul_i32 s27, s0, 0x10900
	v_ashrrev_i32_e32 v37, 31, v36
	s_andn2_b32 s24, s24, 31
	s_mul_hi_i32 s26, s0, 0x10900
	v_lshlrev_b64 v[36:37], 11, v[36:37]
	s_add_u32 s27, s12, s27
	v_lshl_add_u64 v[36:37], s[2:3], 0, v[36:37]
	s_addc_u32 s26, s13, s26
	s_ashr_i32 s25, s24, 31
	v_lshl_add_u64 v[36:37], v[36:37], 0, s[0:1]
	s_lshl_b64 s[0:1], s[24:25], 2
	s_add_u32 s0, s27, s0
	s_addc_u32 s1, s26, s1
	s_mov_b64 s[24:25], s[0:1]
	s_add_u32 s26, s0, 0x84800
	s_addc_u32 s27, s1, 0
	v_lshl_add_u64 v[162:163], v[36:37], 0, v[156:157]
	v_lshl_add_u64 v[36:37], s[24:25], 0, v[2:3]
	s_add_u32 s24, s0, 0x109000
	global_load_dwordx4 v[56:59], v[36:37], off nt
	s_addc_u32 s25, s1, 0
	v_lshl_add_u64 v[36:37], s[26:27], 0, v[2:3]
	s_add_u32 s26, s0, 0x18d800
	global_load_dwordx4 v[68:71], v[36:37], off nt
	s_addc_u32 s27, s1, 0
	v_lshl_add_u64 v[36:37], s[24:25], 0, v[2:3]
	s_add_u32 s24, s0, 0x212000
	global_load_dwordx4 v[80:83], v[36:37], off nt
	s_addc_u32 s25, s1, 0
	v_lshl_add_u64 v[36:37], s[26:27], 0, v[2:3]
	s_add_u32 s26, s0, 0x296800
	global_load_dwordx4 v[96:99], v[36:37], off nt
	s_addc_u32 s27, s1, 0
	v_lshl_add_u64 v[36:37], s[24:25], 0, v[2:3]
	s_add_u32 s24, s0, 0x31b000
	s_addc_u32 s25, s1, 0
	global_load_dwordx4 v[112:115], v[36:37], off nt
	s_add_u32 s0, s0, 0x39f800
	v_lshl_add_u64 v[36:37], s[26:27], 0, v[2:3]
	global_load_dwordx4 v[124:127], v[36:37], off nt
	s_addc_u32 s1, s1, 0
	s_add_i32 s26, s5, 16
	v_lshl_add_u64 v[36:37], s[24:25], 0, v[2:3]
	s_ashr_i32 s24, s26, 31
	global_load_dwordx4 v[136:139], v[36:37], off nt
	s_lshr_b32 s24, s24, 19
	v_lshl_add_u64 v[36:37], s[0:1], 0, v[2:3]
	s_add_i32 s0, s26, s24
	s_and_b32 s0, s0, 0xffffe000
	s_sub_i32 s0, s26, s0
	s_ashr_i32 s1, s0, 1
	s_and_b32 s24, s0, 7
	s_ashr_i32 s25, s0, 31
	s_and_b32 s1, s1, -8
	s_lshr_b32 s25, s25, 24
	s_or_b32 s1, s1, s24
	s_add_i32 s24, s1, s25
	s_ashr_i32 s24, s24, 8
	s_lshl_b32 s1, s1, 5
	s_lshl_b32 s25, s24, 13
	s_lshl_b32 s0, s0, 3
	s_sub_i32 s25, s1, s25
	global_load_dwordx4 v[144:147], v[36:37], off nt
	s_and_b32 s0, s0, 64
	s_lshl_b32 s24, s24, 7
	v_add_u32_e32 v37, s25, v169
	s_or_b32 s0, s24, s0
	v_or_b32_e32 v36, s25, v168
	v_readfirstlane_b32 s24, v37
	s_ashr_i32 s1, s0, 31
	s_mul_i32 s27, s0, 0x10900
	v_ashrrev_i32_e32 v37, 31, v36
	s_andn2_b32 s24, s24, 31
	s_mul_hi_i32 s26, s0, 0x10900
	v_lshlrev_b64 v[36:37], 11, v[36:37]
	s_add_u32 s27, s12, s27
	v_lshl_add_u64 v[36:37], s[2:3], 0, v[36:37]
	s_addc_u32 s26, s13, s26
	s_ashr_i32 s25, s24, 31
	v_lshl_add_u64 v[36:37], v[36:37], 0, s[0:1]
	s_lshl_b64 s[0:1], s[24:25], 2
	s_add_u32 s0, s27, s0
	s_addc_u32 s1, s26, s1
	s_mov_b64 s[24:25], s[0:1]
	s_add_u32 s26, s0, 0x84800
	s_addc_u32 s27, s1, 0
	v_lshl_add_u64 v[158:159], v[36:37], 0, v[156:157]
	v_lshl_add_u64 v[36:37], s[24:25], 0, v[2:3]
	s_add_u32 s24, s0, 0x109000
	global_load_dwordx4 v[36:39], v[36:37], off nt
	s_addc_u32 s25, s1, 0
	v_lshl_add_u64 v[40:41], s[26:27], 0, v[2:3]
	s_add_u32 s26, s0, 0x18d800
	global_load_dwordx4 v[44:47], v[40:41], off nt
	s_addc_u32 s27, s1, 0
	v_lshl_add_u64 v[40:41], s[24:25], 0, v[2:3]
	s_add_u32 s24, s0, 0x212000
	global_load_dwordx4 v[52:55], v[40:41], off nt
	s_addc_u32 s25, s1, 0
	v_lshl_add_u64 v[40:41], s[26:27], 0, v[2:3]
	s_add_u32 s26, s0, 0x296800
	global_load_dwordx4 v[64:67], v[40:41], off nt
	s_addc_u32 s27, s1, 0
	v_lshl_add_u64 v[40:41], s[24:25], 0, v[2:3]
	s_add_u32 s24, s0, 0x31b000
	s_addc_u32 s25, s1, 0
	global_load_dwordx4 v[76:79], v[40:41], off nt
	s_add_u32 s0, s0, 0x39f800
	v_lshl_add_u64 v[40:41], s[26:27], 0, v[2:3]
	global_load_dwordx4 v[88:91], v[40:41], off nt
	s_addc_u32 s1, s1, 0
	s_add_i32 s26, s5, 24
	v_lshl_add_u64 v[40:41], s[24:25], 0, v[2:3]
	s_ashr_i32 s24, s26, 31
	global_load_dwordx4 v[116:119], v[40:41], off nt
	s_lshr_b32 s24, s24, 19
	v_lshl_add_u64 v[40:41], s[0:1], 0, v[2:3]
	s_add_i32 s0, s26, s24
	s_and_b32 s0, s0, 0xffffe000
	s_sub_i32 s0, s26, s0
	s_ashr_i32 s1, s0, 1
	s_and_b32 s24, s0, 7
	s_ashr_i32 s25, s0, 31
	s_and_b32 s1, s1, -8
	s_lshr_b32 s25, s25, 24
	s_or_b32 s1, s1, s24
	s_add_i32 s24, s1, s25
	s_ashr_i32 s24, s24, 8
	s_lshl_b32 s1, s1, 5
	s_lshl_b32 s25, s24, 13
	s_lshl_b32 s0, s0, 3
	s_sub_i32 s25, s1, s25
	global_load_dwordx4 v[128:131], v[40:41], off nt
	s_and_b32 s0, s0, 64
	s_lshl_b32 s24, s24, 7
	v_add_u32_e32 v41, s25, v169
	s_or_b32 s0, s24, s0
	v_or_b32_e32 v40, s25, v168
	v_readfirstlane_b32 s24, v41
	s_ashr_i32 s1, s0, 31
	s_mul_i32 s27, s0, 0x10900
	v_ashrrev_i32_e32 v41, 31, v40
	s_andn2_b32 s24, s24, 31
	s_mul_hi_i32 s26, s0, 0x10900
	v_lshlrev_b64 v[40:41], 11, v[40:41]
	s_add_u32 s27, s12, s27
	v_lshl_add_u64 v[40:41], s[2:3], 0, v[40:41]
	s_addc_u32 s26, s13, s26
	s_ashr_i32 s25, s24, 31
	v_lshl_add_u64 v[160:161], v[40:41], 0, s[0:1]
	s_lshl_b64 s[0:1], s[24:25], 2
	s_add_u32 s0, s27, s0
	s_addc_u32 s1, s26, s1
	s_mov_b64 s[24:25], s[0:1]
	s_add_u32 s26, s0, 0x84800
	s_addc_u32 s27, s1, 0
	v_lshl_add_u64 v[40:41], s[24:25], 0, v[2:3]
	global_load_dwordx4 v[40:43], v[40:41], off nt
	s_add_u32 s24, s0, 0x109000
	s_addc_u32 s25, s1, 0
	v_lshl_add_u64 v[48:49], s[26:27], 0, v[2:3]
	global_load_dwordx4 v[48:51], v[48:49], off nt
	s_add_u32 s26, s0, 0x18d800
	s_addc_u32 s27, s1, 0
	v_lshl_add_u64 v[60:61], s[24:25], 0, v[2:3]
	global_load_dwordx4 v[60:63], v[60:61], off nt
	s_add_u32 s24, s0, 0x212000
	s_addc_u32 s25, s1, 0
	v_lshl_add_u64 v[72:73], s[26:27], 0, v[2:3]
	global_load_dwordx4 v[72:75], v[72:73], off nt
	s_add_u32 s26, s0, 0x296800
	s_addc_u32 s27, s1, 0
	v_lshl_add_u64 v[84:85], s[24:25], 0, v[2:3]
	global_load_dwordx4 v[84:87], v[84:85], off nt
	s_add_u32 s24, s0, 0x31b000
	s_addc_u32 s25, s1, 0
	v_lshl_add_u64 v[100:101], s[26:27], 0, v[2:3]
	global_load_dwordx4 v[100:103], v[100:101], off nt
	s_add_u32 s0, s0, 0x39f800
	s_addc_u32 s1, s1, 0
	v_lshl_add_u64 v[104:105], s[24:25], 0, v[2:3]
	global_load_dwordx4 v[104:107], v[104:105], off nt
	v_add_u32_e32 v172, 0x420, v171
	v_add_u32_e32 v173, 0x428, v171
	v_add_u32_e32 v174, 0x840, v171
	v_add_u32_e32 v175, 0x848, v171
	v_add_u32_e32 v176, 0xc60, v171
	v_add_u32_e32 v177, 0xc68, v171
	v_add_u32_e32 v178, 0x1080, v171
	v_add_u32_e32 v179, 0x1088, v171
	v_add_u32_e32 v183, 0x14a0, v171
	v_add_u32_e32 v184, 0x14a8, v171
	v_add_u32_e32 v185, 0x18c0, v171
	v_add_u32_e32 v186, 0x18c8, v171
	v_add_u32_e32 v187, 0x1ce0, v171
	v_add_u32_e32 v189, 0x1ce8, v171
	s_waitcnt vmcnt(30)
	ds_write2_b32 v171, v92, v93 offset1:1
	ds_write2_b32 v171, v94, v95 offset0:2 offset1:3
	s_waitcnt vmcnt(29)
	ds_write2_b32 v172, v108, v109 offset1:1
	ds_write2_b32 v173, v110, v111 offset1:1
	s_waitcnt vmcnt(28)
	ds_write2_b32 v174, v120, v121 offset1:1
	ds_write2_b32 v175, v122, v123 offset1:1
	s_waitcnt vmcnt(27)
	ds_write2_b32 v176, v132, v133 offset1:1
	ds_write2_b32 v177, v134, v135 offset1:1
	s_waitcnt vmcnt(26)
	ds_write2_b32 v178, v140, v141 offset1:1
	ds_write2_b32 v179, v142, v143 offset1:1
	s_waitcnt vmcnt(25)
	ds_write2_b32 v183, v148, v149 offset1:1
	ds_write2_b32 v184, v150, v151 offset1:1
	s_waitcnt vmcnt(24)
	ds_write2_b32 v185, v152, v153 offset1:1
	ds_write2_b32 v186, v154, v155 offset1:1
	s_waitcnt vmcnt(23)
	ds_write2_b32 v187, v192, v193 offset1:1
	ds_write2_b32 v189, v194, v195 offset1:1
	v_lshl_add_u64 v[92:93], s[0:1], 0, v[2:3]
	global_load_dwordx4 v[92:95], v[92:93], off nt
	v_add_u32_e32 v188, 0x400, v170
	v_mov_b32_e32 v190, v170
	v_add_u32_e32 v191, 0x400, v170
	ds_read2_b32 v[108:109], v170 offset1:33
	ds_read2_b32 v[110:111], v170 offset0:66 offset1:99
	ds_read2_b32 v[120:121], v170 offset0:132 offset1:165
	ds_read2_b32 v[122:123], v170 offset0:198 offset1:231
	ds_read2_b32 v[132:133], v188 offset0:8 offset1:41
	ds_read2_b32 v[134:135], v188 offset0:74 offset1:107
	ds_read2_b32 v[140:141], v188 offset0:140 offset1:173
	ds_read2_b32 v[142:143], v188 offset0:206 offset1:239
	ds_read2_b32 v[148:149], v190 offset0:16 offset1:49
	ds_read2_b32 v[150:151], v190 offset0:82 offset1:115
	ds_read2_b32 v[152:153], v190 offset0:148 offset1:181
	ds_read2_b32 v[154:155], v190 offset0:214 offset1:247
	ds_read2_b32 v[192:193], v191 offset0:24 offset1:57
	ds_read2_b32 v[194:195], v191 offset0:90 offset1:123
	ds_read2_b32 v[196:197], v191 offset0:156 offset1:189
	ds_read2_b32 v[198:199], v191 offset0:222 offset1:255
	v_mov_b32_e32 v4, v3
	v_mov_b32_e32 v5, v3
	v_mov_b32_e32 v6, v3
	v_mov_b32_e32 v7, v3
	s_waitcnt lgkmcnt(14)
	v_mul_f32_e32 v108, 0x42800000, v108
	v_mul_f32_e32 v109, 0x42800000, v109
	s_waitcnt lgkmcnt(13)
	v_mul_f32_e32 v120, 0x42800000, v120
	v_mul_f32_e32 v121, 0x42800000, v121
	s_waitcnt lgkmcnt(11)
	v_mul_f32_e32 v132, 0x42800000, v132
	v_mul_f32_e32 v133, 0x42800000, v133
	s_waitcnt lgkmcnt(9)
	v_mul_f32_e32 v140, 0x42800000, v140
	v_mul_f32_e32 v141, 0x42800000, v141
	v_mov_b32_e32 v8, v3
	v_mov_b32_e32 v9, v3
	v_mov_b32_e32 v10, v3
	v_mov_b32_e32 v11, v3
	s_waitcnt lgkmcnt(7)
	v_mul_f32_e32 v148, 0x42800000, v148
	v_mul_f32_e32 v149, 0x42800000, v149
	s_waitcnt lgkmcnt(5)
	v_mul_f32_e32 v152, 0x42800000, v152
	v_mul_f32_e32 v153, 0x42800000, v153
	s_waitcnt lgkmcnt(3)
	v_mul_f32_e32 v192, 0x42800000, v192
	v_mul_f32_e32 v193, 0x42800000, v193
	s_waitcnt lgkmcnt(1)
	v_mul_f32_e32 v196, 0x42800000, v196
	v_mul_f32_e32 v197, 0x42800000, v197
	v_cvt_pk_fp8_f32 v4, v108, v109
	v_cvt_pk_fp8_f32 v5, v120, v121
	v_cvt_pk_fp8_f32 v6, v132, v133
	v_cvt_pk_fp8_f32 v7, v140, v141
	v_cvt_pk_fp8_f32 v8, v148, v149
	v_cvt_pk_fp8_f32 v9, v152, v153
	v_cvt_pk_fp8_f32 v10, v192, v193
	v_cvt_pk_fp8_f32 v11, v196, v197
	v_mul_f32_e32 v110, 0x42800000, v110
	v_mul_f32_e32 v111, 0x42800000, v111
	v_mul_f32_e32 v122, 0x42800000, v122
	v_mul_f32_e32 v123, 0x42800000, v123
	v_mul_f32_e32 v134, 0x42800000, v134
	v_mul_f32_e32 v135, 0x42800000, v135
	v_mul_f32_e32 v142, 0x42800000, v142
	v_mul_f32_e32 v143, 0x42800000, v143
	v_mul_f32_e32 v150, 0x42800000, v150
	v_mul_f32_e32 v151, 0x42800000, v151
	v_mul_f32_e32 v154, 0x42800000, v154
	v_mul_f32_e32 v155, 0x42800000, v155
	v_mul_f32_e32 v194, 0x42800000, v194
	v_mul_f32_e32 v195, 0x42800000, v195
	s_waitcnt lgkmcnt(0)
	v_mul_f32_e32 v198, 0x42800000, v198
	v_mul_f32_e32 v199, 0x42800000, v199
	v_cvt_pk_fp8_f32 v4, v110, v111 op_sel:[0,0,1]
	v_cvt_pk_fp8_f32 v5, v122, v123 op_sel:[0,0,1]
	v_cvt_pk_fp8_f32 v6, v134, v135 op_sel:[0,0,1]
	v_cvt_pk_fp8_f32 v7, v142, v143 op_sel:[0,0,1]
	v_cvt_pk_fp8_f32 v8, v150, v151 op_sel:[0,0,1]
	v_cvt_pk_fp8_f32 v9, v154, v155 op_sel:[0,0,1]
	v_cvt_pk_fp8_f32 v10, v194, v195 op_sel:[0,0,1]
	v_cvt_pk_fp8_f32 v11, v198, v199 op_sel:[0,0,1]
	global_store_dwordx4 v[164:165], v[4:7], off
	s_nop 1
	v_add_co_u32_e32 v164, vcc, 0x8000, v164
	s_nop 1
	v_addc_co_u32_e32 v165, vcc, 0, v165, vcc
	global_store_dwordx4 v[164:165], v[8:11], off
	s_waitcnt vmcnt(25)
	ds_write2_b32 v171, v56, v57 offset1:1
	ds_write2_b32 v171, v58, v59 offset0:2 offset1:3
	s_waitcnt vmcnt(24)
	ds_write2_b32 v172, v68, v69 offset1:1
	ds_write2_b32 v173, v70, v71 offset1:1
	s_waitcnt vmcnt(23)
	ds_write2_b32 v174, v80, v81 offset1:1
	ds_write2_b32 v175, v82, v83 offset1:1
	s_waitcnt vmcnt(22)
	ds_write2_b32 v176, v96, v97 offset1:1
	ds_write2_b32 v177, v98, v99 offset1:1
	s_waitcnt vmcnt(21)
	ds_write2_b32 v178, v112, v113 offset1:1
	ds_write2_b32 v179, v114, v115 offset1:1
	s_waitcnt vmcnt(20)
	ds_write2_b32 v183, v124, v125 offset1:1
	ds_write2_b32 v184, v126, v127 offset1:1
	s_waitcnt vmcnt(19)
	ds_write2_b32 v185, v136, v137 offset1:1
	ds_write2_b32 v186, v138, v139 offset1:1
	s_waitcnt vmcnt(18)
	ds_write2_b32 v187, v144, v145 offset1:1
	ds_write2_b32 v189, v146, v147 offset1:1
	ds_read2_b32 v[4:5], v170 offset1:33
	ds_read2_b32 v[6:7], v170 offset0:66 offset1:99
	ds_read2_b32 v[8:9], v170 offset0:132 offset1:165
	ds_read2_b32 v[10:11], v170 offset0:198 offset1:231
	ds_read2_b32 v[56:57], v188 offset0:8 offset1:41
	ds_read2_b32 v[58:59], v188 offset0:74 offset1:107
	ds_read2_b32 v[68:69], v188 offset0:140 offset1:173
	ds_read2_b32 v[70:71], v188 offset0:206 offset1:239
	ds_read2_b32 v[80:81], v190 offset0:16 offset1:49
	ds_read2_b32 v[82:83], v190 offset0:82 offset1:115
	ds_read2_b32 v[96:97], v190 offset0:148 offset1:181
	ds_read2_b32 v[98:99], v190 offset0:214 offset1:247
	ds_read2_b32 v[108:109], v191 offset0:24 offset1:57
	ds_read2_b32 v[110:111], v191 offset0:90 offset1:123
	ds_read2_b32 v[112:113], v191 offset0:156 offset1:189
	ds_read2_b32 v[114:115], v191 offset0:222 offset1:255
	v_mov_b32_e32 v12, v3
	v_mov_b32_e32 v13, v3
	v_mov_b32_e32 v14, v3
	v_mov_b32_e32 v15, v3
	s_waitcnt lgkmcnt(14)
	v_mul_f32_e32 v4, 0x42800000, v4
	v_mul_f32_e32 v5, 0x42800000, v5
	s_waitcnt lgkmcnt(13)
	v_mul_f32_e32 v8, 0x42800000, v8
	v_mul_f32_e32 v9, 0x42800000, v9
	s_waitcnt lgkmcnt(11)
	v_mul_f32_e32 v56, 0x42800000, v56
	v_mul_f32_e32 v57, 0x42800000, v57
	s_waitcnt lgkmcnt(9)
	v_mul_f32_e32 v68, 0x42800000, v68
	v_mul_f32_e32 v69, 0x42800000, v69
	v_mov_b32_e32 v16, v3
	v_mov_b32_e32 v17, v3
	v_mov_b32_e32 v18, v3
	v_mov_b32_e32 v19, v3
	s_waitcnt lgkmcnt(7)
	v_mul_f32_e32 v80, 0x42800000, v80
	v_mul_f32_e32 v81, 0x42800000, v81
	s_waitcnt lgkmcnt(5)
	v_mul_f32_e32 v96, 0x42800000, v96
	v_mul_f32_e32 v97, 0x42800000, v97
	s_waitcnt lgkmcnt(3)
	v_mul_f32_e32 v108, 0x42800000, v108
	v_mul_f32_e32 v109, 0x42800000, v109
	s_waitcnt lgkmcnt(1)
	v_mul_f32_e32 v112, 0x42800000, v112
	v_mul_f32_e32 v113, 0x42800000, v113
	v_cvt_pk_fp8_f32 v12, v4, v5
	v_cvt_pk_fp8_f32 v13, v8, v9
	v_cvt_pk_fp8_f32 v14, v56, v57
	v_cvt_pk_fp8_f32 v15, v68, v69
	v_cvt_pk_fp8_f32 v16, v80, v81
	v_cvt_pk_fp8_f32 v17, v96, v97
	v_cvt_pk_fp8_f32 v18, v108, v109
	v_cvt_pk_fp8_f32 v19, v112, v113
	v_mul_f32_e32 v6, 0x42800000, v6
	v_mul_f32_e32 v7, 0x42800000, v7
	v_mul_f32_e32 v10, 0x42800000, v10
	v_mul_f32_e32 v11, 0x42800000, v11
	v_mul_f32_e32 v58, 0x42800000, v58
	v_mul_f32_e32 v59, 0x42800000, v59
	v_mul_f32_e32 v70, 0x42800000, v70
	v_mul_f32_e32 v71, 0x42800000, v71
	v_mul_f32_e32 v82, 0x42800000, v82
	v_mul_f32_e32 v83, 0x42800000, v83
	v_mul_f32_e32 v98, 0x42800000, v98
	v_mul_f32_e32 v99, 0x42800000, v99
	v_mul_f32_e32 v110, 0x42800000, v110
	v_mul_f32_e32 v111, 0x42800000, v111
	s_waitcnt lgkmcnt(0)
	v_mul_f32_e32 v114, 0x42800000, v114
	v_mul_f32_e32 v115, 0x42800000, v115
	v_cvt_pk_fp8_f32 v12, v6, v7 op_sel:[0,0,1]
	v_cvt_pk_fp8_f32 v13, v10, v11 op_sel:[0,0,1]
	v_cvt_pk_fp8_f32 v14, v58, v59 op_sel:[0,0,1]
	v_cvt_pk_fp8_f32 v15, v70, v71 op_sel:[0,0,1]
	v_cvt_pk_fp8_f32 v16, v82, v83 op_sel:[0,0,1]
	v_cvt_pk_fp8_f32 v17, v98, v99 op_sel:[0,0,1]
	v_cvt_pk_fp8_f32 v18, v110, v111 op_sel:[0,0,1]
	v_cvt_pk_fp8_f32 v19, v114, v115 op_sel:[0,0,1]
	global_store_dwordx4 v[162:163], v[12:15], off
	s_nop 1
	v_add_co_u32_e32 v162, vcc, 0x8000, v162
	s_nop 1
	v_addc_co_u32_e32 v163, vcc, 0, v163, vcc
	global_store_dwordx4 v[162:163], v[16:19], off
	s_waitcnt vmcnt(19)
	ds_write2_b32 v171, v36, v37 offset1:1
	ds_write2_b32 v171, v38, v39 offset0:2 offset1:3
	s_waitcnt vmcnt(18)
	ds_write2_b32 v172, v44, v45 offset1:1
	ds_write2_b32 v173, v46, v47 offset1:1
	s_waitcnt vmcnt(17)
	ds_write2_b32 v174, v52, v53 offset1:1
	ds_write2_b32 v175, v54, v55 offset1:1
	s_waitcnt vmcnt(16)
	ds_write2_b32 v176, v64, v65 offset1:1
	ds_write2_b32 v177, v66, v67 offset1:1
	s_waitcnt vmcnt(15)
	ds_write2_b32 v178, v76, v77 offset1:1
	ds_write2_b32 v179, v78, v79 offset1:1
	s_waitcnt vmcnt(14)
	ds_write2_b32 v183, v88, v89 offset1:1
	ds_write2_b32 v184, v90, v91 offset1:1
	s_waitcnt vmcnt(13)
	ds_write2_b32 v185, v116, v117 offset1:1
	ds_write2_b32 v186, v118, v119 offset1:1
	s_waitcnt vmcnt(12)
	ds_write2_b32 v187, v128, v129 offset1:1
	ds_write2_b32 v189, v130, v131 offset1:1
	ds_read2_b32 v[4:5], v170 offset1:33
	ds_read2_b32 v[6:7], v170 offset0:66 offset1:99
	ds_read2_b32 v[8:9], v170 offset0:132 offset1:165
	ds_read2_b32 v[10:11], v170 offset0:198 offset1:231
	ds_read2_b32 v[12:13], v188 offset0:8 offset1:41
	ds_read2_b32 v[14:15], v188 offset0:74 offset1:107
	ds_read2_b32 v[16:17], v188 offset0:140 offset1:173
	ds_read2_b32 v[18:19], v188 offset0:206 offset1:239
	ds_read2_b32 v[36:37], v190 offset0:16 offset1:49
	ds_read2_b32 v[38:39], v190 offset0:82 offset1:115
	ds_read2_b32 v[44:45], v190 offset0:148 offset1:181
	ds_read2_b32 v[46:47], v190 offset0:214 offset1:247
	ds_read2_b32 v[52:53], v191 offset0:24 offset1:57
	ds_read2_b32 v[54:55], v191 offset0:90 offset1:123
	ds_read2_b32 v[56:57], v191 offset0:156 offset1:189
	ds_read2_b32 v[58:59], v191 offset0:222 offset1:255
	v_mov_b32_e32 v20, v3
	v_mov_b32_e32 v21, v3
	v_mov_b32_e32 v22, v3
	v_mov_b32_e32 v23, v3
	s_waitcnt lgkmcnt(14)
	v_mul_f32_e32 v4, 0x42800000, v4
	v_mul_f32_e32 v5, 0x42800000, v5
	s_waitcnt lgkmcnt(13)
	v_mul_f32_e32 v8, 0x42800000, v8
	v_mul_f32_e32 v9, 0x42800000, v9
	s_waitcnt lgkmcnt(11)
	v_mul_f32_e32 v12, 0x42800000, v12
	v_mul_f32_e32 v13, 0x42800000, v13
	s_waitcnt lgkmcnt(9)
	v_mul_f32_e32 v16, 0x42800000, v16
	v_mul_f32_e32 v17, 0x42800000, v17
	v_mov_b32_e32 v24, v3
	v_mov_b32_e32 v25, v3
	v_mov_b32_e32 v26, v3
	v_mov_b32_e32 v27, v3
	s_waitcnt lgkmcnt(7)
	v_mul_f32_e32 v36, 0x42800000, v36
	v_mul_f32_e32 v37, 0x42800000, v37
	s_waitcnt lgkmcnt(5)
	v_mul_f32_e32 v44, 0x42800000, v44
	v_mul_f32_e32 v45, 0x42800000, v45
	s_waitcnt lgkmcnt(3)
	v_mul_f32_e32 v52, 0x42800000, v52
	v_mul_f32_e32 v53, 0x42800000, v53
	s_waitcnt lgkmcnt(1)
	v_mul_f32_e32 v56, 0x42800000, v56
	v_mul_f32_e32 v57, 0x42800000, v57
	v_cvt_pk_fp8_f32 v20, v4, v5
	v_cvt_pk_fp8_f32 v21, v8, v9
	v_cvt_pk_fp8_f32 v22, v12, v13
	v_cvt_pk_fp8_f32 v23, v16, v17
	v_cvt_pk_fp8_f32 v24, v36, v37
	v_cvt_pk_fp8_f32 v25, v44, v45
	v_cvt_pk_fp8_f32 v26, v52, v53
	v_cvt_pk_fp8_f32 v27, v56, v57
	v_mul_f32_e32 v6, 0x42800000, v6
	v_mul_f32_e32 v7, 0x42800000, v7
	v_mul_f32_e32 v10, 0x42800000, v10
	v_mul_f32_e32 v11, 0x42800000, v11
	v_mul_f32_e32 v14, 0x42800000, v14
	v_mul_f32_e32 v15, 0x42800000, v15
	v_mul_f32_e32 v18, 0x42800000, v18
	v_mul_f32_e32 v19, 0x42800000, v19
	v_mul_f32_e32 v38, 0x42800000, v38
	v_mul_f32_e32 v39, 0x42800000, v39
	v_mul_f32_e32 v46, 0x42800000, v46
	v_mul_f32_e32 v47, 0x42800000, v47
	v_mul_f32_e32 v54, 0x42800000, v54
	v_mul_f32_e32 v55, 0x42800000, v55
	s_waitcnt lgkmcnt(0)
	v_mul_f32_e32 v58, 0x42800000, v58
	v_mul_f32_e32 v59, 0x42800000, v59
	v_cvt_pk_fp8_f32 v20, v6, v7 op_sel:[0,0,1]
	v_cvt_pk_fp8_f32 v21, v10, v11 op_sel:[0,0,1]
	v_cvt_pk_fp8_f32 v22, v14, v15 op_sel:[0,0,1]
	v_cvt_pk_fp8_f32 v23, v18, v19 op_sel:[0,0,1]
	v_cvt_pk_fp8_f32 v24, v38, v39 op_sel:[0,0,1]
	v_cvt_pk_fp8_f32 v25, v46, v47 op_sel:[0,0,1]
	v_cvt_pk_fp8_f32 v26, v54, v55 op_sel:[0,0,1]
	v_cvt_pk_fp8_f32 v27, v58, v59 op_sel:[0,0,1]
	global_store_dwordx4 v[158:159], v[20:23], off
	s_nop 1
	v_add_co_u32_e32 v158, vcc, 0x8000, v158
	s_nop 1
	v_addc_co_u32_e32 v159, vcc, 0, v159, vcc
	global_store_dwordx4 v[158:159], v[24:27], off
	s_waitcnt vmcnt(13)
	ds_write2_b32 v171, v40, v41 offset1:1
	ds_write2_b32 v171, v42, v43 offset0:2 offset1:3
	s_waitcnt vmcnt(12)
	ds_write2_b32 v172, v48, v49 offset1:1
	ds_write2_b32 v173, v50, v51 offset1:1
	s_waitcnt vmcnt(11)
	ds_write2_b32 v174, v60, v61 offset1:1
	ds_write2_b32 v175, v62, v63 offset1:1
	s_waitcnt vmcnt(10)
	ds_write2_b32 v176, v72, v73 offset1:1
	ds_write2_b32 v177, v74, v75 offset1:1
	s_waitcnt vmcnt(9)
	ds_write2_b32 v178, v84, v85 offset1:1
	ds_write2_b32 v179, v86, v87 offset1:1
	s_waitcnt vmcnt(8)
	ds_write2_b32 v183, v100, v101 offset1:1
	ds_write2_b32 v184, v102, v103 offset1:1
	s_waitcnt vmcnt(7)
	ds_write2_b32 v185, v104, v105 offset1:1
	ds_write2_b32 v186, v106, v107 offset1:1
	s_waitcnt vmcnt(6)
	ds_write2_b32 v187, v92, v93 offset1:1
	ds_write2_b32 v189, v94, v95 offset1:1
	ds_read2_b32 v[4:5], v170 offset1:33
	ds_read2_b32 v[6:7], v170 offset0:66 offset1:99
	ds_read2_b32 v[8:9], v170 offset0:132 offset1:165
	ds_read2_b32 v[10:11], v170 offset0:198 offset1:231
	ds_read2_b32 v[12:13], v188 offset0:8 offset1:41
	ds_read2_b32 v[14:15], v188 offset0:74 offset1:107
	ds_read2_b32 v[16:17], v188 offset0:140 offset1:173
	ds_read2_b32 v[18:19], v188 offset0:206 offset1:239
	ds_read2_b32 v[20:21], v190 offset0:16 offset1:49
	ds_read2_b32 v[22:23], v190 offset0:82 offset1:115
	ds_read2_b32 v[24:25], v190 offset0:148 offset1:181
	ds_read2_b32 v[26:27], v190 offset0:214 offset1:247
	ds_read2_b32 v[36:37], v191 offset0:24 offset1:57
	ds_read2_b32 v[38:39], v191 offset0:90 offset1:123
	ds_read2_b32 v[40:41], v191 offset0:156 offset1:189
	ds_read2_b32 v[42:43], v191 offset0:222 offset1:255
	v_mov_b32_e32 v28, v3
	v_mov_b32_e32 v29, v3
	v_mov_b32_e32 v30, v3
	v_mov_b32_e32 v31, v3
	s_waitcnt lgkmcnt(14)
	v_mul_f32_e32 v4, 0x42800000, v4
	v_mul_f32_e32 v5, 0x42800000, v5
	s_waitcnt lgkmcnt(13)
	v_mul_f32_e32 v8, 0x42800000, v8
	v_mul_f32_e32 v9, 0x42800000, v9
	s_waitcnt lgkmcnt(11)
	v_mul_f32_e32 v12, 0x42800000, v12
	v_mul_f32_e32 v13, 0x42800000, v13
	s_waitcnt lgkmcnt(9)
	v_mul_f32_e32 v16, 0x42800000, v16
	v_mul_f32_e32 v17, 0x42800000, v17
	v_mov_b32_e32 v32, v3
	v_mov_b32_e32 v33, v3
	v_mov_b32_e32 v34, v3
	v_mov_b32_e32 v35, v3
	s_waitcnt lgkmcnt(7)
	v_mul_f32_e32 v20, 0x42800000, v20
	v_mul_f32_e32 v21, 0x42800000, v21
	s_waitcnt lgkmcnt(5)
	v_mul_f32_e32 v24, 0x42800000, v24
	v_mul_f32_e32 v25, 0x42800000, v25
	s_waitcnt lgkmcnt(3)
	v_mul_f32_e32 v36, 0x42800000, v36
	v_mul_f32_e32 v37, 0x42800000, v37
	s_waitcnt lgkmcnt(1)
	v_mul_f32_e32 v40, 0x42800000, v40
	v_mul_f32_e32 v41, 0x42800000, v41
	v_cvt_pk_fp8_f32 v28, v4, v5
	v_cvt_pk_fp8_f32 v29, v8, v9
	v_cvt_pk_fp8_f32 v30, v12, v13
	v_cvt_pk_fp8_f32 v31, v16, v17
	v_cvt_pk_fp8_f32 v32, v20, v21
	v_cvt_pk_fp8_f32 v33, v24, v25
	v_cvt_pk_fp8_f32 v34, v36, v37
	v_cvt_pk_fp8_f32 v35, v40, v41
	v_mul_f32_e32 v6, 0x42800000, v6
	v_mul_f32_e32 v7, 0x42800000, v7
	v_mul_f32_e32 v10, 0x42800000, v10
	v_mul_f32_e32 v11, 0x42800000, v11
	v_mul_f32_e32 v14, 0x42800000, v14
	v_mul_f32_e32 v15, 0x42800000, v15
	v_mul_f32_e32 v18, 0x42800000, v18
	v_mul_f32_e32 v19, 0x42800000, v19
	v_mul_f32_e32 v22, 0x42800000, v22
	v_mul_f32_e32 v23, 0x42800000, v23
	v_mul_f32_e32 v26, 0x42800000, v26
	v_mul_f32_e32 v27, 0x42800000, v27
	v_mul_f32_e32 v38, 0x42800000, v38
	v_mul_f32_e32 v39, 0x42800000, v39
	s_waitcnt lgkmcnt(0)
	v_mul_f32_e32 v42, 0x42800000, v42
	v_mul_f32_e32 v43, 0x42800000, v43
	v_cvt_pk_fp8_f32 v28, v6, v7 op_sel:[0,0,1]
	v_cvt_pk_fp8_f32 v29, v10, v11 op_sel:[0,0,1]
	v_cvt_pk_fp8_f32 v30, v14, v15 op_sel:[0,0,1]
	v_cvt_pk_fp8_f32 v31, v18, v19 op_sel:[0,0,1]
	v_cvt_pk_fp8_f32 v32, v22, v23 op_sel:[0,0,1]
	v_cvt_pk_fp8_f32 v33, v26, v27 op_sel:[0,0,1]
	v_cvt_pk_fp8_f32 v34, v38, v39 op_sel:[0,0,1]
	v_cvt_pk_fp8_f32 v35, v42, v43 op_sel:[0,0,1]
	v_lshl_add_u64 v[4:5], v[160:161], 0, v[156:157]
	global_store_dwordx4 v[4:5], v[28:31], off
	s_nop 1
	v_add_co_u32_e32 v4, vcc, 0x8000, v4
	s_nop 1
	v_addc_co_u32_e32 v5, vcc, 0, v5, vcc
	global_store_dwordx4 v[4:5], v[32:35], off
	s_add_i32 s5, s5, 32
	s_cmp_lt_i32 s5, s4
	s_cbranch_scc1 .LBB6_1071

.LBB6_1198:
	s_max_i32 s0, s90, 0xa6c0
	s_min_i32 s34, s91, 0x12ac0
	s_cmp_le_i32 s34, s0
	s_cbranch_scc1 .LBB6_1204
	s_sub_i32 s1, s34, s0
	s_mov_b32 s2, 18
	s_cmp_lt_i32 s1, 32
	s_cbranch_scc1 .LBB6_1204
	s_add_i32 s0, s0, s95
	s_add_i32 s34, s34, 0xffff5940
	s_add_i32 s35, s0, 0xffff5940
	s_cmp_ge_i32 s35, s34
	s_cbranch_scc1 .LBB6_1204
	s_ashr_i32 s3, s2, 31
	s_lshl_b64 s[0:1], s[2:3], 3
	s_add_u32 s0, s76, s0
	s_addc_u32 s1, s77, s1
	s_load_dwordx2 s[2:3], s[0:1], 0x0
	s_waitcnt vmcnt(0)
	v_lshrrev_b32_e32 v4, 3, v166
	v_lshlrev_b32_e32 v5, 2, v166
	v_lshlrev_b32_e32 v6, 5, v166
	v_mul_u32_u24_e32 v2, 0x2c00, v4
	v_and_b32_e32 v5, 28, v5
	v_lshrrev_b32_e32 v135, 2, v166
	v_lshlrev_b32_e32 v132, 4, v166
	v_and_b32_e32 v132, 48, v132
	s_add_u32 s36, s6, 0x81080000
	v_or_b32_e32 v2, v2, v5
	v_lshl_add_u32 v5, v5, 2, s94
	v_mul_u32_u24_e32 v4, 0x84, v4
	v_mul_u32_u24_e32 v6, 0x84, v132
	v_lshlrev_b32_e32 v7, 2, v135
	s_addc_u32 s37, s7, 0
	v_and_b32_e32 v134, 31, v167
	v_lshlrev_b32_e32 v2, 2, v2
	v_add3_u32 v136, s94, v6, v7
	v_mov_b32_e32 v133, v3
	v_add_u32_e32 v137, v5, v4
.LBB6_1202:
	s_mul_hi_i32 s0, s35, 0x2e8ba2e9
	s_lshr_b32 s1, s0, 31
	s_ashr_i32 s30, s0, 11
	s_add_i32 s30, s30, s1
	s_mul_i32 s0, s30, 0xffffd400
	s_add_i32 s0, s0, s35
	s_ashr_i32 s0, s0, 1
	s_and_b32 s1, s0, -8
	s_and_b32 s0, s35, 7
	s_or_b32 s1, s1, s0
	s_waitcnt lgkmcnt(0)
	s_mul_hi_i32 s4, s1, 0x2e8ba2e9
	s_lshr_b32 s5, s4, 31
	s_ashr_i32 s4, s4, 6
	s_add_i32 s4, s4, s5
	s_mul_i32 s5, s4, 0xfffffea0
	s_add_i32 s5, s5, s1
	s_lshl_b32 s1, s4, 7
	s_lshl_b32 s4, s35, 3
	s_and_b32 s24, s4, 64
	s_lshl_b32 s62, s5, 5
	s_or_b32 s28, s1, s24
	s_mul_i32 s4, s30, 0x5800000
	s_mul_hi_i32 s1, s30, 0x5800000
	s_add_u32 s12, s2, s4
	s_addc_u32 s1, s3, s1
	s_and_b32 s4, s62, 0xe0
	s_cmpk_lt_u32 s4, 0x80
	v_or_b32_e32 v4, s4, v134
	s_cselect_b64 vcc, -1, 0
	s_lshl_b32 s4, s5, 4
	s_and_b32 s4, s4, 0xffffff80
	v_or_b32_e32 v5, s4, v4
	s_addk_i32 s4, 0x1580
	v_add_u32_e32 v4, s4, v4
	v_cndmask_b32_e32 v4, v4, v5, vcc
	s_ashr_i32 s29, s28, 31
	v_readfirstlane_b32 s4, v4
	s_andn2_b32 s4, s4, 31
	s_mul_i32 s13, s28, 0xb000
	s_mul_hi_i32 s5, s28, 0xb000
	s_add_u32 s12, s12, s13
	s_addc_u32 s1, s1, s5
	s_ashr_i32 s5, s4, 31
	s_lshl_b64 s[4:5], s[4:5], 2
	s_add_u32 s4, s12, s4
	s_addc_u32 s5, s1, s5
	s_mov_b64 s[12:13], s[4:5]
	v_mov_b32_e32 v138, v3
	v_lshl_add_u64 v[4:5], s[12:13], 0, v[2:3]
	s_add_u32 s12, s4, 0x58000
	s_addc_u32 s13, s5, 0
	global_load_dwordx4 v[128:131], v[4:5], off nt
	v_mov_b32_e32 v139, v3
	v_lshl_add_u64 v[4:5], s[12:13], 0, v[2:3]
	s_add_u32 s12, s4, 0xb0000
	s_addc_u32 s13, s5, 0
	global_load_dwordx4 v[124:127], v[4:5], off nt
	s_nop 0
	v_lshl_add_u64 v[4:5], s[12:13], 0, v[2:3]
	s_add_u32 s12, s4, 0x108000
	s_addc_u32 s13, s5, 0
	global_load_dwordx4 v[120:123], v[4:5], off nt
	s_nop 0
	v_lshl_add_u64 v[4:5], s[12:13], 0, v[2:3]
	s_add_u32 s12, s4, 0x160000
	s_addc_u32 s13, s5, 0
	global_load_dwordx4 v[116:119], v[4:5], off nt
	s_nop 0
	v_lshl_add_u64 v[4:5], s[12:13], 0, v[2:3]
	s_add_u32 s12, s4, 0x1b8000
	s_addc_u32 s13, s5, 0
	global_load_dwordx4 v[112:115], v[4:5], off nt
	s_nop 0
	v_lshl_add_u64 v[4:5], s[12:13], 0, v[2:3]
	s_add_u32 s12, s4, 0x210000
	s_addc_u32 s13, s5, 0
	s_add_u32 s4, s4, 0x268000
	global_load_dwordx4 v[108:111], v[4:5], off nt
	s_addc_u32 s5, s5, 0
	v_lshl_add_u64 v[4:5], s[12:13], 0, v[2:3]
	global_load_dwordx4 v[104:107], v[4:5], off nt
	s_add_i32 s1, s35, 8
	v_lshl_add_u64 v[4:5], s[4:5], 0, v[2:3]
	s_mul_hi_i32 s4, s1, 0x2e8ba2e9
	s_lshr_b32 s5, s4, 31
	s_ashr_i32 s51, s4, 11
	s_add_i32 s51, s51, s5
	s_mul_i32 s4, s51, 0xffffd400
	s_add_i32 s4, s4, s1
	s_ashr_i32 s4, s4, 1
	s_and_b32 s4, s4, -8
	s_or_b32 s4, s4, s0
	s_mul_hi_i32 s5, s4, 0x2e8ba2e9
	s_lshr_b32 s12, s5, 31
	s_ashr_i32 s5, s5, 6
	s_add_i32 s5, s5, s12
	s_mul_i32 s12, s5, 0xfffffea0
	s_lshl_b32 s1, s1, 3
	s_add_i32 s12, s12, s4
	s_lshl_b32 s4, s5, 7
	s_and_b32 s1, s1, 64
	s_lshl_b32 s58, s12, 5
	s_or_b32 s26, s4, s1
	s_mul_i32 s4, s51, 0x5800000
	s_mul_hi_i32 s1, s51, 0x5800000
	s_add_u32 s5, s2, s4
	s_addc_u32 s1, s3, s1
	s_and_b32 s4, s58, 0xe0
	s_cmpk_lt_u32 s4, 0x80
	global_load_dwordx4 v[100:103], v[4:5], off nt
	v_or_b32_e32 v4, s4, v134
	s_cselect_b64 vcc, -1, 0
	s_lshl_b32 s4, s12, 4
	s_and_b32 s4, s4, 0xffffff80
	v_or_b32_e32 v5, s4, v4
	s_addk_i32 s4, 0x1580
	v_add_u32_e32 v4, s4, v4
	v_cndmask_b32_e32 v4, v4, v5, vcc
	s_ashr_i32 s27, s26, 31
	v_readfirstlane_b32 s4, v4
	s_andn2_b32 s4, s4, 31
	s_mul_i32 s13, s26, 0xb000
	s_mul_hi_i32 s12, s26, 0xb000
	s_add_u32 s13, s5, s13
	s_addc_u32 s1, s1, s12
	s_ashr_i32 s5, s4, 31
	s_lshl_b64 s[4:5], s[4:5], 2
	s_add_u32 s4, s13, s4
	s_addc_u32 s5, s1, s5
	s_mov_b64 s[12:13], s[4:5]
	s_nop 0
	v_lshl_add_u64 v[4:5], s[12:13], 0, v[2:3]
	s_add_u32 s12, s4, 0x58000
	s_addc_u32 s13, s5, 0
	global_load_dwordx4 v[68:71], v[4:5], off nt
	s_nop 0
	v_lshl_add_u64 v[4:5], s[12:13], 0, v[2:3]
	s_add_u32 s12, s4, 0xb0000
	s_addc_u32 s13, s5, 0
	global_load_dwordx4 v[72:75], v[4:5], off nt
	s_nop 0
	v_lshl_add_u64 v[4:5], s[12:13], 0, v[2:3]
	s_add_u32 s12, s4, 0x108000
	s_addc_u32 s13, s5, 0
	global_load_dwordx4 v[76:79], v[4:5], off nt
	s_nop 0
	v_lshl_add_u64 v[4:5], s[12:13], 0, v[2:3]
	s_add_u32 s12, s4, 0x160000
	s_addc_u32 s13, s5, 0
	global_load_dwordx4 v[80:83], v[4:5], off nt
	s_nop 0
	v_lshl_add_u64 v[4:5], s[12:13], 0, v[2:3]
	s_add_u32 s12, s4, 0x1b8000
	s_addc_u32 s13, s5, 0
	global_load_dwordx4 v[84:87], v[4:5], off nt
	s_nop 0
	v_lshl_add_u64 v[4:5], s[12:13], 0, v[2:3]
	s_add_u32 s12, s4, 0x210000
	s_addc_u32 s13, s5, 0
	s_add_u32 s4, s4, 0x268000
	global_load_dwordx4 v[88:91], v[4:5], off nt
	s_addc_u32 s5, s5, 0
	v_lshl_add_u64 v[4:5], s[12:13], 0, v[2:3]
	global_load_dwordx4 v[92:95], v[4:5], off nt
	s_add_i32 s1, s35, 16
	v_lshl_add_u64 v[4:5], s[4:5], 0, v[2:3]
	s_mul_hi_i32 s4, s1, 0x2e8ba2e9
	s_lshr_b32 s5, s4, 31
	s_ashr_i32 s49, s4, 11
	s_add_i32 s49, s49, s5
	s_mul_i32 s4, s49, 0xffffd400
	s_add_i32 s4, s4, s1
	s_ashr_i32 s1, s4, 1
	s_and_b32 s1, s1, -8
	s_or_b32 s1, s1, s0
	s_mul_hi_i32 s4, s1, 0x2e8ba2e9
	s_lshr_b32 s5, s4, 31
	s_ashr_i32 s4, s4, 6
	s_add_i32 s4, s4, s5
	s_mul_i32 s5, s4, 0xfffffea0
	s_add_i32 s5, s5, s1
	s_lshl_b32 s1, s4, 7
	s_lshl_b32 s50, s5, 5
	s_or_b32 s24, s1, s24
	s_mul_i32 s4, s49, 0x5800000
	s_mul_hi_i32 s1, s49, 0x5800000
	s_add_u32 s12, s2, s4
	s_addc_u32 s1, s3, s1
	s_and_b32 s4, s50, 0xe0
	s_cmpk_lt_u32 s4, 0x80
	global_load_dwordx4 v[96:99], v[4:5], off nt
	v_or_b32_e32 v4, s4, v134
	s_cselect_b64 vcc, -1, 0
	s_lshl_b32 s4, s5, 4
	s_and_b32 s4, s4, 0xffffff80
	v_or_b32_e32 v5, s4, v4
	s_addk_i32 s4, 0x1580
	v_add_u32_e32 v4, s4, v4
	v_cndmask_b32_e32 v4, v4, v5, vcc
	s_ashr_i32 s25, s24, 31
	v_readfirstlane_b32 s4, v4
	s_andn2_b32 s4, s4, 31
	s_mul_i32 s13, s24, 0xb000
	s_mul_hi_i32 s5, s24, 0xb000
	s_add_u32 s12, s12, s13
	s_addc_u32 s1, s1, s5
	s_ashr_i32 s5, s4, 31
	s_lshl_b64 s[4:5], s[4:5], 2
	s_add_u32 s4, s12, s4
	s_addc_u32 s5, s1, s5
	s_mov_b64 s[12:13], s[4:5]
	s_nop 0
	v_lshl_add_u64 v[4:5], s[12:13], 0, v[2:3]
	s_add_u32 s12, s4, 0x58000
	s_addc_u32 s13, s5, 0
	global_load_dwordx4 v[36:39], v[4:5], off nt
	s_nop 0
	v_lshl_add_u64 v[4:5], s[12:13], 0, v[2:3]
	s_add_u32 s12, s4, 0xb0000
	s_addc_u32 s13, s5, 0
	global_load_dwordx4 v[40:43], v[4:5], off nt
	s_nop 0
	v_lshl_add_u64 v[4:5], s[12:13], 0, v[2:3]
	s_add_u32 s12, s4, 0x108000
	s_addc_u32 s13, s5, 0
	global_load_dwordx4 v[44:47], v[4:5], off nt
	s_nop 0
	v_lshl_add_u64 v[4:5], s[12:13], 0, v[2:3]
	s_add_u32 s12, s4, 0x160000
	s_addc_u32 s13, s5, 0
	global_load_dwordx4 v[48:51], v[4:5], off nt
	s_nop 0
	v_lshl_add_u64 v[4:5], s[12:13], 0, v[2:3]
	s_add_u32 s12, s4, 0x1b8000
	s_addc_u32 s13, s5, 0
	global_load_dwordx4 v[52:55], v[4:5], off nt
	s_nop 0
	v_lshl_add_u64 v[4:5], s[12:13], 0, v[2:3]
	s_add_u32 s12, s4, 0x210000
	s_addc_u32 s13, s5, 0
	s_add_u32 s4, s4, 0x268000
	global_load_dwordx4 v[56:59], v[4:5], off nt
	s_addc_u32 s5, s5, 0
	v_lshl_add_u64 v[4:5], s[12:13], 0, v[2:3]
	global_load_dwordx4 v[60:63], v[4:5], off nt
	s_add_i32 s1, s35, 24
	v_lshl_add_u64 v[4:5], s[4:5], 0, v[2:3]
	s_mul_hi_i32 s4, s1, 0x2e8ba2e9
	s_lshr_b32 s5, s4, 31
	s_ashr_i32 s47, s4, 11
	s_add_i32 s47, s47, s5
	s_mul_i32 s4, s47, 0xffffd400
	s_add_i32 s4, s4, s1
	s_ashr_i32 s4, s4, 1
	s_and_b32 s4, s4, -8
	s_or_b32 s0, s4, s0
	s_mul_hi_i32 s4, s0, 0x2e8ba2e9
	s_lshr_b32 s5, s4, 31
	s_ashr_i32 s4, s4, 6
	s_add_i32 s4, s4, s5
	s_mul_i32 s5, s4, 0xfffffea0
	s_lshl_b32 s1, s1, 3
	s_add_i32 s5, s5, s0
	s_lshl_b32 s0, s4, 7
	s_and_b32 s1, s1, 64
	s_lshl_b32 s48, s5, 5
	s_or_b32 s4, s0, s1
	s_mul_i32 s1, s47, 0x5800000
	s_mul_hi_i32 s0, s47, 0x5800000
	s_add_u32 s1, s2, s1
	s_addc_u32 s12, s3, s0
	s_and_b32 s0, s48, 0xe0
	s_cmpk_lt_u32 s0, 0x80
	global_load_dwordx4 v[64:67], v[4:5], off nt
	v_or_b32_e32 v4, s0, v134
	s_cselect_b64 vcc, -1, 0
	s_lshl_b32 s0, s5, 4
	s_and_b32 s0, s0, 0xffffff80
	v_or_b32_e32 v5, s0, v4
	s_addk_i32 s0, 0x1580
	v_add_u32_e32 v4, s0, v4
	v_cndmask_b32_e32 v4, v4, v5, vcc
	s_ashr_i32 s5, s4, 31
	v_readfirstlane_b32 s0, v4
	s_andn2_b32 s0, s0, 31
	s_mul_i32 s31, s4, 0xb000
	s_mul_hi_i32 s13, s4, 0xb000
	s_add_u32 s31, s1, s31
	s_addc_u32 s12, s12, s13
	s_ashr_i32 s1, s0, 31
	s_lshl_b64 s[0:1], s[0:1], 2
	s_add_u32 s0, s31, s0
	s_addc_u32 s1, s12, s1
	s_mov_b64 s[12:13], s[0:1]
	s_nop 0
	v_lshl_add_u64 v[4:5], s[12:13], 0, v[2:3]
	s_add_u32 s12, s0, 0x58000
	s_addc_u32 s13, s1, 0
	global_load_dwordx4 v[4:7], v[4:5], off nt
	s_nop 0
	v_lshl_add_u64 v[8:9], s[12:13], 0, v[2:3]
	s_add_u32 s12, s0, 0xb0000
	s_addc_u32 s13, s1, 0
	global_load_dwordx4 v[8:11], v[8:9], off nt
	s_nop 0
	v_lshl_add_u64 v[12:13], s[12:13], 0, v[2:3]
	s_add_u32 s12, s0, 0x108000
	s_addc_u32 s13, s1, 0
	global_load_dwordx4 v[12:15], v[12:13], off nt
	s_nop 0
	v_lshl_add_u64 v[16:17], s[12:13], 0, v[2:3]
	s_add_u32 s12, s0, 0x160000
	s_addc_u32 s13, s1, 0
	global_load_dwordx4 v[16:19], v[16:17], off nt
	s_nop 0
	v_lshl_add_u64 v[20:21], s[12:13], 0, v[2:3]
	s_add_u32 s12, s0, 0x1b8000
	s_addc_u32 s13, s1, 0
	global_load_dwordx4 v[20:23], v[20:21], off nt
	s_nop 0
	v_lshl_add_u64 v[24:25], s[12:13], 0, v[2:3]
	s_add_u32 s12, s0, 0x210000
	s_addc_u32 s13, s1, 0
	s_add_u32 s0, s0, 0x268000
	global_load_dwordx4 v[24:27], v[24:25], off nt
	s_addc_u32 s1, s1, 0
	v_lshl_add_u64 v[28:29], s[12:13], 0, v[2:3]
	global_load_dwordx4 v[28:31], v[28:29], off nt
	s_nop 0
	v_lshl_add_u64 v[32:33], s[0:1], 0, v[2:3]
	global_load_dwordx4 v[32:35], v[32:33], off nt
	s_waitcnt vmcnt(31)
	ds_write2_b32 v137, v128, v129 offset1:1
	ds_write2_b32 v137, v130, v131 offset0:2 offset1:3
	v_add_u32_e32 v128, 0x420, v137
	s_waitcnt vmcnt(30)
	ds_write2_b32 v128, v124, v125 offset1:1
	v_add_u32_e32 v125, 0x840, v137
	s_waitcnt vmcnt(29)
	ds_write2_b32 v125, v120, v121 offset1:1
	v_add_u32_e32 v121, 0xc60, v137
	s_waitcnt vmcnt(28)
	ds_write2_b32 v121, v116, v117 offset1:1
	v_add_u32_e32 v117, 0x1080, v137
	s_waitcnt vmcnt(27)
	ds_write2_b32 v117, v112, v113 offset1:1
	v_add_u32_e32 v113, 0x14a0, v137
	s_waitcnt vmcnt(26)
	ds_write2_b32 v113, v108, v109 offset1:1
	v_add_u32_e32 v109, 0x18c0, v137
	s_waitcnt vmcnt(25)
	ds_write2_b32 v109, v104, v105 offset1:1
	v_add_u32_e32 v104, 0x18c8, v137
	v_add_u32_e32 v124, 0x428, v137
	v_add_u32_e32 v120, 0x848, v137
	v_add_u32_e32 v116, 0xc68, v137
	v_add_u32_e32 v112, 0x1088, v137
	v_add_u32_e32 v108, 0x14a8, v137
	ds_write2_b32 v104, v106, v107 offset1:1
	v_add_u32_e32 v105, 0x1ce0, v137
	v_add_u32_e32 v106, 0x1ce8, v137
	ds_write2_b32 v124, v126, v127 offset1:1
	ds_write2_b32 v120, v122, v123 offset1:1
	ds_write2_b32 v116, v118, v119 offset1:1
	ds_write2_b32 v112, v114, v115 offset1:1
	ds_write2_b32 v108, v110, v111 offset1:1
	s_waitcnt vmcnt(24)
	ds_write2_b32 v105, v100, v101 offset1:1
	ds_write2_b32 v106, v102, v103 offset1:1
	ds_read2_b32 v[110:111], v136 offset1:33
	ds_read2_b32 v[114:115], v136 offset0:66 offset1:99
	ds_read2_b32 v[118:119], v136 offset0:132 offset1:165
	ds_read2_b32 v[122:123], v136 offset0:198 offset1:231
	v_add_u32_e32 v102, 0x400, v136
	s_waitcnt lgkmcnt(3)
	v_mul_f32_e32 v101, 0x42800000, v110
	v_mul_f32_e32 v110, 0x42800000, v111
	v_mov_b32_e32 v103, v136
	v_cvt_pk_fp8_f32 v138, v101, v110
	ds_read2_b32 v[126:127], v102 offset0:8 offset1:41
	ds_read2_b32 v[130:131], v102 offset0:74 offset1:107
	ds_read2_b32 v[146:147], v102 offset0:140 offset1:173
	ds_read2_b32 v[148:149], v102 offset0:206 offset1:239
	ds_read2_b32 v[140:141], v103 offset0:16 offset1:49
	ds_read2_b32 v[142:143], v103 offset0:82 offset1:115
	ds_read2_b32 v[144:145], v103 offset0:148 offset1:181
	ds_read2_b32 v[150:151], v103 offset0:214 offset1:247
	s_waitcnt lgkmcnt(10)
	v_mul_f32_e32 v111, 0x42800000, v114
	v_mul_f32_e32 v114, 0x42800000, v115
	v_cvt_pk_fp8_f32 v138, v111, v114 op_sel:[0,0,1]
	s_waitcnt lgkmcnt(3)
	v_mul_f32_e32 v101, 0x42800000, v140
	v_mul_f32_e32 v110, 0x42800000, v141
	s_waitcnt lgkmcnt(2)
	v_mul_f32_e32 v111, 0x42800000, v142
	v_mov_b32_e32 v142, v3
	v_add_u32_e32 v107, 0x400, v136
	v_cvt_pk_fp8_f32 v142, v101, v110
	v_mul_f32_e32 v101, 0x42800000, v118
	v_mul_f32_e32 v110, 0x42800000, v119
	ds_read2_b32 v[152:153], v107 offset0:24 offset1:57
	ds_read2_b32 v[154:155], v107 offset0:90 offset1:123
	ds_read2_b32 v[156:157], v107 offset0:156 offset1:189
	ds_read2_b32 v[158:159], v107 offset0:222 offset1:255
	v_mul_f32_e32 v114, 0x42800000, v143
	v_cvt_pk_fp8_f32 v139, v101, v110
	s_waitcnt lgkmcnt(5)
	v_mul_f32_e32 v101, 0x42800000, v144
	v_mul_f32_e32 v110, 0x42800000, v145
	v_mov_b32_e32 v143, v3
	v_cvt_pk_fp8_f32 v143, v101, v110
	v_mul_f32_e32 v101, 0x42800000, v126
	v_mul_f32_e32 v110, 0x42800000, v127
	v_mov_b32_e32 v140, v3
	v_cvt_pk_fp8_f32 v140, v101, v110
	s_waitcnt lgkmcnt(3)
	v_mul_f32_e32 v101, 0x42800000, v152
	v_mul_f32_e32 v110, 0x42800000, v153
	v_mov_b32_e32 v144, v3
	v_cvt_pk_fp8_f32 v142, v111, v114 op_sel:[0,0,1]
	v_mul_f32_e32 v111, 0x42800000, v122
	v_mul_f32_e32 v114, 0x42800000, v123
	v_cvt_pk_fp8_f32 v144, v101, v110
	v_mul_f32_e32 v101, 0x42800000, v146
	v_mul_f32_e32 v110, 0x42800000, v147
	v_mov_b32_e32 v141, v3
	v_cvt_pk_fp8_f32 v139, v111, v114 op_sel:[0,0,1]
	v_mul_f32_e32 v111, 0x42800000, v150
	v_mul_f32_e32 v114, 0x42800000, v151
	v_cvt_pk_fp8_f32 v141, v101, v110
	s_waitcnt lgkmcnt(1)
	v_mul_f32_e32 v101, 0x42800000, v156
	v_mul_f32_e32 v110, 0x42800000, v157
	v_mov_b32_e32 v145, v3
	v_cvt_pk_fp8_f32 v143, v111, v114 op_sel:[0,0,1]
	v_mul_f32_e32 v111, 0x42800000, v130
	v_mul_f32_e32 v114, 0x42800000, v131
	v_cvt_pk_fp8_f32 v145, v101, v110
	s_mul_hi_i32 s0, s30, 0x1600000
	s_mul_i32 s30, s30, 0x1600000
	v_or_b32_e32 v100, s62, v135
	v_cvt_pk_fp8_f32 v140, v111, v114 op_sel:[0,0,1]
	v_mul_f32_e32 v111, 0x42800000, v154
	v_mul_f32_e32 v114, 0x42800000, v155
	s_add_u32 s30, s36, s30
	v_cvt_pk_fp8_f32 v144, v111, v114 op_sel:[0,0,1]
	v_mul_f32_e32 v111, 0x42800000, v148
	v_mul_f32_e32 v114, 0x42800000, v149
	v_ashrrev_i32_e32 v101, 31, v100
	s_addc_u32 s31, s37, s0
	v_cvt_pk_fp8_f32 v141, v111, v114 op_sel:[0,0,1]
	s_waitcnt lgkmcnt(0)
	v_mul_f32_e32 v111, 0x42800000, v158
	v_mul_f32_e32 v114, 0x42800000, v159
	v_lshlrev_b64 v[100:101], 11, v[100:101]
	v_cvt_pk_fp8_f32 v145, v111, v114 op_sel:[0,0,1]
	v_lshl_add_u64 v[100:101], s[30:31], 0, v[100:101]
	v_lshl_add_u64 v[100:101], v[100:101], 0, s[28:29]
	v_lshl_add_u64 v[100:101], v[100:101], 0, v[132:133]
	global_store_dwordx4 v[100:101], v[138:141], off
	s_nop 1
	v_add_co_u32_e32 v100, vcc, 0x8000, v100
	s_nop 1
	v_addc_co_u32_e32 v101, vcc, 0, v101, vcc
	global_store_dwordx4 v[100:101], v[142:145], off
	s_waitcnt vmcnt(25)
	ds_write2_b32 v137, v68, v69 offset1:1
	ds_write2_b32 v137, v70, v71 offset0:2 offset1:3
	s_waitcnt vmcnt(24)
	ds_write2_b32 v128, v72, v73 offset1:1
	ds_write2_b32 v124, v74, v75 offset1:1
	s_waitcnt vmcnt(23)
	ds_write2_b32 v125, v76, v77 offset1:1
	ds_write2_b32 v120, v78, v79 offset1:1
	s_waitcnt vmcnt(22)
	ds_write2_b32 v121, v80, v81 offset1:1
	ds_write2_b32 v116, v82, v83 offset1:1
	s_waitcnt vmcnt(21)
	ds_write2_b32 v117, v84, v85 offset1:1
	ds_write2_b32 v112, v86, v87 offset1:1
	s_waitcnt vmcnt(20)
	ds_write2_b32 v113, v88, v89 offset1:1
	ds_write2_b32 v108, v90, v91 offset1:1
	s_waitcnt vmcnt(19)
	ds_write2_b32 v109, v92, v93 offset1:1
	ds_write2_b32 v104, v94, v95 offset1:1
	s_waitcnt vmcnt(18)
	ds_write2_b32 v105, v96, v97 offset1:1
	ds_write2_b32 v106, v98, v99 offset1:1
	ds_read2_b32 v[94:95], v136 offset1:33
	ds_read2_b32 v[96:97], v136 offset0:66 offset1:99
	ds_read2_b32 v[92:93], v136 offset0:132 offset1:165
	ds_read2_b32 v[90:91], v136 offset0:198 offset1:231
	ds_read2_b32 v[84:85], v102 offset0:8 offset1:41
	ds_read2_b32 v[82:83], v102 offset0:74 offset1:107
	ds_read2_b32 v[76:77], v102 offset0:140 offset1:173
	ds_read2_b32 v[74:75], v102 offset0:206 offset1:239
	ds_read2_b32 v[98:99], v103 offset0:16 offset1:49
	ds_read2_b32 v[100:101], v103 offset0:82 offset1:115
	ds_read2_b32 v[88:89], v103 offset0:148 offset1:181
	ds_read2_b32 v[86:87], v103 offset0:214 offset1:247
	ds_read2_b32 v[80:81], v107 offset0:24 offset1:57
	ds_read2_b32 v[78:79], v107 offset0:90 offset1:123
	ds_read2_b32 v[72:73], v107 offset0:156 offset1:189
	ds_read2_b32 v[70:71], v107 offset0:222 offset1:255
	s_waitcnt lgkmcnt(14)
	v_mul_f32_e32 v69, 0x42800000, v94
	v_mul_f32_e32 v95, 0x42800000, v95
	v_mov_b32_e32 v94, v3
	v_cvt_pk_fp8_f32 v94, v69, v95
	s_waitcnt lgkmcnt(7)
	v_mul_f32_e32 v69, 0x42800000, v98
	v_mul_f32_e32 v95, 0x42800000, v99
	v_mov_b32_e32 v98, v3
	v_cvt_pk_fp8_f32 v98, v69, v95
	v_mul_f32_e32 v96, 0x42800000, v96
	v_mul_f32_e32 v97, 0x42800000, v97
	v_mul_f32_e32 v69, 0x42800000, v92
	v_mul_f32_e32 v92, 0x42800000, v93
	v_mov_b32_e32 v95, v3
	v_cvt_pk_fp8_f32 v94, v96, v97 op_sel:[0,0,1]
	s_waitcnt lgkmcnt(6)
	v_mul_f32_e32 v96, 0x42800000, v100
	v_mul_f32_e32 v97, 0x42800000, v101
	v_cvt_pk_fp8_f32 v95, v69, v92
	s_waitcnt lgkmcnt(5)
	v_mul_f32_e32 v69, 0x42800000, v88
	v_mul_f32_e32 v88, 0x42800000, v89
	v_mov_b32_e32 v99, v3
	v_cvt_pk_fp8_f32 v98, v96, v97 op_sel:[0,0,1]
	v_cvt_pk_fp8_f32 v99, v69, v88
	v_mul_f32_e32 v69, 0x42800000, v84
	v_mul_f32_e32 v84, 0x42800000, v85
	v_mov_b32_e32 v96, v3
	v_cvt_pk_fp8_f32 v96, v69, v84
	s_waitcnt lgkmcnt(3)
	v_mul_f32_e32 v69, 0x42800000, v80
	v_mul_f32_e32 v80, 0x42800000, v81
	v_mov_b32_e32 v100, v3
	v_cvt_pk_fp8_f32 v100, v69, v80
	v_mul_f32_e32 v69, 0x42800000, v76
	v_mul_f32_e32 v76, 0x42800000, v77
	v_mov_b32_e32 v97, v3
	v_cvt_pk_fp8_f32 v97, v69, v76
	s_waitcnt lgkmcnt(1)
	v_mul_f32_e32 v69, 0x42800000, v72
	v_mul_f32_e32 v72, 0x42800000, v73
	v_mov_b32_e32 v101, v3
	v_cvt_pk_fp8_f32 v101, v69, v72
	s_mul_hi_i32 s0, s51, 0x1600000
	s_mul_i32 s51, s51, 0x1600000
	v_or_b32_e32 v68, s58, v135
	s_add_u32 s28, s36, s51
	v_mul_f32_e32 v90, 0x42800000, v90
	v_mul_f32_e32 v91, 0x42800000, v91
	v_mul_f32_e32 v82, 0x42800000, v82
	v_mul_f32_e32 v83, 0x42800000, v83
	v_mul_f32_e32 v74, 0x42800000, v74
	v_mul_f32_e32 v75, 0x42800000, v75
	v_ashrrev_i32_e32 v69, 31, v68
	s_addc_u32 s29, s37, s0
	v_cvt_pk_fp8_f32 v95, v90, v91 op_sel:[0,0,1]
	v_mul_f32_e32 v86, 0x42800000, v86
	v_mul_f32_e32 v87, 0x42800000, v87
	v_cvt_pk_fp8_f32 v96, v82, v83 op_sel:[0,0,1]
	v_mul_f32_e32 v78, 0x42800000, v78
	v_mul_f32_e32 v79, 0x42800000, v79
	v_cvt_pk_fp8_f32 v97, v74, v75 op_sel:[0,0,1]
	s_waitcnt lgkmcnt(0)
	v_mul_f32_e32 v70, 0x42800000, v70
	v_mul_f32_e32 v71, 0x42800000, v71
	v_lshlrev_b64 v[68:69], 11, v[68:69]
	v_cvt_pk_fp8_f32 v99, v86, v87 op_sel:[0,0,1]
	v_cvt_pk_fp8_f32 v100, v78, v79 op_sel:[0,0,1]
	v_cvt_pk_fp8_f32 v101, v70, v71 op_sel:[0,0,1]
	v_lshl_add_u64 v[68:69], s[28:29], 0, v[68:69]
	v_lshl_add_u64 v[68:69], v[68:69], 0, s[26:27]
	v_lshl_add_u64 v[68:69], v[68:69], 0, v[132:133]
	global_store_dwordx4 v[68:69], v[94:97], off
	s_nop 1
	v_add_co_u32_e32 v68, vcc, 0x8000, v68
	s_nop 1
	v_addc_co_u32_e32 v69, vcc, 0, v69, vcc
	global_store_dwordx4 v[68:69], v[98:101], off
	s_waitcnt vmcnt(19)
	ds_write2_b32 v137, v36, v37 offset1:1
	ds_write2_b32 v137, v38, v39 offset0:2 offset1:3
	s_waitcnt vmcnt(18)
	ds_write2_b32 v128, v40, v41 offset1:1
	ds_write2_b32 v124, v42, v43 offset1:1
	s_waitcnt vmcnt(17)
	ds_write2_b32 v125, v44, v45 offset1:1
	ds_write2_b32 v120, v46, v47 offset1:1
	s_waitcnt vmcnt(16)
	ds_write2_b32 v121, v48, v49 offset1:1
	ds_write2_b32 v116, v50, v51 offset1:1
	s_waitcnt vmcnt(15)
	ds_write2_b32 v117, v52, v53 offset1:1
	ds_write2_b32 v112, v54, v55 offset1:1
	s_waitcnt vmcnt(14)
	ds_write2_b32 v113, v56, v57 offset1:1
	ds_write2_b32 v108, v58, v59 offset1:1
	s_waitcnt vmcnt(13)
	ds_write2_b32 v109, v60, v61 offset1:1
	ds_write2_b32 v104, v62, v63 offset1:1
	s_waitcnt vmcnt(12)
	ds_write2_b32 v105, v64, v65 offset1:1
	ds_write2_b32 v106, v66, v67 offset1:1
	ds_read2_b32 v[62:63], v136 offset1:33
	ds_read2_b32 v[64:65], v136 offset0:66 offset1:99
	ds_read2_b32 v[60:61], v136 offset0:132 offset1:165
	ds_read2_b32 v[58:59], v136 offset0:198 offset1:231
	ds_read2_b32 v[52:53], v102 offset0:8 offset1:41
	ds_read2_b32 v[50:51], v102 offset0:74 offset1:107
	ds_read2_b32 v[44:45], v102 offset0:140 offset1:173
	ds_read2_b32 v[42:43], v102 offset0:206 offset1:239
	ds_read2_b32 v[66:67], v103 offset0:16 offset1:49
	ds_read2_b32 v[68:69], v103 offset0:82 offset1:115
	ds_read2_b32 v[56:57], v103 offset0:148 offset1:181
	ds_read2_b32 v[54:55], v103 offset0:214 offset1:247
	ds_read2_b32 v[48:49], v107 offset0:24 offset1:57
	ds_read2_b32 v[46:47], v107 offset0:90 offset1:123
	ds_read2_b32 v[40:41], v107 offset0:156 offset1:189
	ds_read2_b32 v[38:39], v107 offset0:222 offset1:255
	s_waitcnt lgkmcnt(14)
	v_mul_f32_e32 v37, 0x42800000, v62
	v_mul_f32_e32 v63, 0x42800000, v63
	v_mov_b32_e32 v62, v3
	v_cvt_pk_fp8_f32 v62, v37, v63
	s_waitcnt lgkmcnt(7)
	v_mul_f32_e32 v37, 0x42800000, v66
	v_mul_f32_e32 v63, 0x42800000, v67
	v_mov_b32_e32 v66, v3
	v_cvt_pk_fp8_f32 v66, v37, v63
	v_mul_f32_e32 v64, 0x42800000, v64
	v_mul_f32_e32 v65, 0x42800000, v65
	v_mul_f32_e32 v37, 0x42800000, v60
	v_mul_f32_e32 v60, 0x42800000, v61
	v_mov_b32_e32 v63, v3
	v_cvt_pk_fp8_f32 v62, v64, v65 op_sel:[0,0,1]
	s_waitcnt lgkmcnt(6)
	v_mul_f32_e32 v64, 0x42800000, v68
	v_mul_f32_e32 v65, 0x42800000, v69
	v_cvt_pk_fp8_f32 v63, v37, v60
	s_waitcnt lgkmcnt(5)
	v_mul_f32_e32 v37, 0x42800000, v56
	v_mul_f32_e32 v56, 0x42800000, v57
	v_mov_b32_e32 v67, v3
	v_cvt_pk_fp8_f32 v66, v64, v65 op_sel:[0,0,1]
	v_cvt_pk_fp8_f32 v67, v37, v56
	v_mul_f32_e32 v37, 0x42800000, v52
	v_mul_f32_e32 v52, 0x42800000, v53
	v_mov_b32_e32 v64, v3
	v_cvt_pk_fp8_f32 v64, v37, v52
	s_waitcnt lgkmcnt(3)
	v_mul_f32_e32 v37, 0x42800000, v48
	v_mul_f32_e32 v48, 0x42800000, v49
	v_mov_b32_e32 v68, v3
	v_cvt_pk_fp8_f32 v68, v37, v48
	v_mul_f32_e32 v37, 0x42800000, v44
	v_mul_f32_e32 v44, 0x42800000, v45
	v_mov_b32_e32 v65, v3
	v_cvt_pk_fp8_f32 v65, v37, v44
	s_waitcnt lgkmcnt(1)
	v_mul_f32_e32 v37, 0x42800000, v40
	v_mul_f32_e32 v40, 0x42800000, v41
	v_mov_b32_e32 v69, v3
	v_cvt_pk_fp8_f32 v69, v37, v40
	s_mul_hi_i32 s0, s49, 0x1600000
	s_mul_i32 s49, s49, 0x1600000
	v_or_b32_e32 v36, s50, v135
	s_add_u32 s26, s36, s49
	v_mul_f32_e32 v58, 0x42800000, v58
	v_mul_f32_e32 v59, 0x42800000, v59
	v_mul_f32_e32 v50, 0x42800000, v50
	v_mul_f32_e32 v51, 0x42800000, v51
	v_mul_f32_e32 v42, 0x42800000, v42
	v_mul_f32_e32 v43, 0x42800000, v43
	v_ashrrev_i32_e32 v37, 31, v36
	s_addc_u32 s27, s37, s0
	v_cvt_pk_fp8_f32 v63, v58, v59 op_sel:[0,0,1]
	v_mul_f32_e32 v54, 0x42800000, v54
	v_mul_f32_e32 v55, 0x42800000, v55
	v_cvt_pk_fp8_f32 v64, v50, v51 op_sel:[0,0,1]
	v_mul_f32_e32 v46, 0x42800000, v46
	v_mul_f32_e32 v47, 0x42800000, v47
	v_cvt_pk_fp8_f32 v65, v42, v43 op_sel:[0,0,1]
	s_waitcnt lgkmcnt(0)
	v_mul_f32_e32 v38, 0x42800000, v38
	v_mul_f32_e32 v39, 0x42800000, v39
	v_lshlrev_b64 v[36:37], 11, v[36:37]
	v_cvt_pk_fp8_f32 v67, v54, v55 op_sel:[0,0,1]
	v_cvt_pk_fp8_f32 v68, v46, v47 op_sel:[0,0,1]
	v_cvt_pk_fp8_f32 v69, v38, v39 op_sel:[0,0,1]
	v_lshl_add_u64 v[36:37], s[26:27], 0, v[36:37]
	v_lshl_add_u64 v[36:37], v[36:37], 0, s[24:25]
	v_lshl_add_u64 v[36:37], v[36:37], 0, v[132:133]
	global_store_dwordx4 v[36:37], v[62:65], off
	s_nop 1
	v_add_co_u32_e32 v36, vcc, 0x8000, v36
	s_nop 1
	v_addc_co_u32_e32 v37, vcc, 0, v37, vcc
	global_store_dwordx4 v[36:37], v[66:69], off
	s_waitcnt vmcnt(13)
	ds_write2_b32 v137, v4, v5 offset1:1
	ds_write2_b32 v137, v6, v7 offset0:2 offset1:3
	s_waitcnt vmcnt(12)
	ds_write2_b32 v128, v8, v9 offset1:1
	ds_write2_b32 v124, v10, v11 offset1:1
	s_waitcnt vmcnt(11)
	ds_write2_b32 v125, v12, v13 offset1:1
	ds_write2_b32 v120, v14, v15 offset1:1
	s_waitcnt vmcnt(10)
	ds_write2_b32 v121, v16, v17 offset1:1
	ds_write2_b32 v116, v18, v19 offset1:1
	s_waitcnt vmcnt(9)
	ds_write2_b32 v117, v20, v21 offset1:1
	ds_write2_b32 v112, v22, v23 offset1:1
	s_waitcnt vmcnt(8)
	ds_write2_b32 v113, v24, v25 offset1:1
	ds_write2_b32 v108, v26, v27 offset1:1
	s_waitcnt vmcnt(7)
	ds_write2_b32 v109, v28, v29 offset1:1
	ds_write2_b32 v104, v30, v31 offset1:1
	s_waitcnt vmcnt(6)
	ds_write2_b32 v105, v32, v33 offset1:1
	ds_write2_b32 v106, v34, v35 offset1:1
	ds_read2_b32 v[4:5], v136 offset1:33
	ds_read2_b32 v[8:9], v136 offset0:66 offset1:99
	ds_read2_b32 v[32:33], v136 offset0:132 offset1:165
	ds_read2_b32 v[30:31], v136 offset0:198 offset1:231
	ds_read2_b32 v[24:25], v102 offset0:8 offset1:41
	ds_read2_b32 v[6:7], v102 offset0:74 offset1:107
	ds_read2_b32 v[20:21], v102 offset0:140 offset1:173
	ds_read2_b32 v[18:19], v102 offset0:206 offset1:239
	ds_read2_b32 v[34:35], v103 offset0:16 offset1:49
	ds_read2_b32 v[36:37], v103 offset0:82 offset1:115
	ds_read2_b32 v[28:29], v103 offset0:148 offset1:181
	ds_read2_b32 v[26:27], v103 offset0:214 offset1:247
	ds_read2_b32 v[22:23], v107 offset0:24 offset1:57
	ds_read2_b32 v[10:11], v107 offset0:90 offset1:123
	ds_read2_b32 v[16:17], v107 offset0:156 offset1:189
	ds_read2_b32 v[14:15], v107 offset0:222 offset1:255
	s_waitcnt lgkmcnt(14)
	v_mul_f32_e32 v13, 0x42800000, v4
	v_mul_f32_e32 v5, 0x42800000, v5
	v_mov_b32_e32 v4, v3
	v_cvt_pk_fp8_f32 v4, v13, v5
	v_mul_f32_e32 v8, 0x42800000, v8
	v_mul_f32_e32 v9, 0x42800000, v9
	s_waitcnt lgkmcnt(7)
	v_mul_f32_e32 v5, 0x42800000, v34
	v_cvt_pk_fp8_f32 v4, v8, v9 op_sel:[0,0,1]
	v_mul_f32_e32 v9, 0x42800000, v35
	v_mov_b32_e32 v8, v3
	v_cvt_pk_fp8_f32 v8, v5, v9
	s_waitcnt lgkmcnt(6)
	v_mul_f32_e32 v13, 0x42800000, v36
	v_mul_f32_e32 v34, 0x42800000, v37
	v_mul_f32_e32 v9, 0x42800000, v32
	v_cvt_pk_fp8_f32 v8, v13, v34 op_sel:[0,0,1]
	v_mul_f32_e32 v13, 0x42800000, v33
	v_mov_b32_e32 v5, v3
	v_cvt_pk_fp8_f32 v5, v9, v13
	s_waitcnt lgkmcnt(5)
	v_mul_f32_e32 v13, 0x42800000, v28
	v_mul_f32_e32 v28, 0x42800000, v29
	v_mov_b32_e32 v9, v3
	v_cvt_pk_fp8_f32 v9, v13, v28
	v_mul_f32_e32 v13, 0x42800000, v24
	v_mul_f32_e32 v24, 0x42800000, v25
	v_mul_f32_e32 v25, 0x42800000, v6
	v_mov_b32_e32 v6, v3
	v_cvt_pk_fp8_f32 v6, v13, v24
	v_mul_f32_e32 v7, 0x42800000, v7
	s_waitcnt lgkmcnt(3)
	v_mul_f32_e32 v13, 0x42800000, v23
	s_waitcnt lgkmcnt(2)
	v_mul_f32_e32 v11, 0x42800000, v11
	v_cvt_pk_fp8_f32 v6, v25, v7 op_sel:[0,0,1]
	v_mul_f32_e32 v7, 0x42800000, v22
	v_mul_f32_e32 v22, 0x42800000, v10
	v_mov_b32_e32 v10, v3
	v_cvt_pk_fp8_f32 v10, v7, v13
	v_mul_f32_e32 v13, 0x42800000, v21
	v_mov_b32_e32 v7, v3
	s_mul_hi_i32 s0, s47, 0x1600000
	v_cvt_pk_fp8_f32 v10, v22, v11 op_sel:[0,0,1]
	v_mul_f32_e32 v11, 0x42800000, v20
	v_cvt_pk_fp8_f32 v7, v11, v13
	s_waitcnt lgkmcnt(1)
	v_mul_f32_e32 v13, 0x42800000, v16
	v_mul_f32_e32 v16, 0x42800000, v17
	v_mov_b32_e32 v11, v3
	v_cvt_pk_fp8_f32 v11, v13, v16
	s_mul_i32 s47, s47, 0x1600000
	v_or_b32_e32 v12, s48, v135
	s_add_u32 s24, s36, s47
	v_mul_f32_e32 v30, 0x42800000, v30
	v_mul_f32_e32 v31, 0x42800000, v31
	v_mul_f32_e32 v18, 0x42800000, v18
	v_mul_f32_e32 v19, 0x42800000, v19
	v_ashrrev_i32_e32 v13, 31, v12
	s_addc_u32 s25, s37, s0
	v_cvt_pk_fp8_f32 v5, v30, v31 op_sel:[0,0,1]
	v_mul_f32_e32 v26, 0x42800000, v26
	v_mul_f32_e32 v27, 0x42800000, v27
	v_cvt_pk_fp8_f32 v7, v18, v19 op_sel:[0,0,1]
	s_waitcnt lgkmcnt(0)
	v_mul_f32_e32 v14, 0x42800000, v14
	v_mul_f32_e32 v15, 0x42800000, v15
	v_lshlrev_b64 v[12:13], 11, v[12:13]
	v_cvt_pk_fp8_f32 v9, v26, v27 op_sel:[0,0,1]
	v_cvt_pk_fp8_f32 v11, v14, v15 op_sel:[0,0,1]
	v_lshl_add_u64 v[12:13], s[24:25], 0, v[12:13]
	v_lshl_add_u64 v[12:13], v[12:13], 0, s[4:5]
	v_lshl_add_u64 v[12:13], v[12:13], 0, v[132:133]
	global_store_dwordx4 v[12:13], v[4:7], off
	s_nop 1
	v_add_co_u32_e32 v12, vcc, 0x8000, v12
	s_nop 1
	v_addc_co_u32_e32 v13, vcc, 0, v13, vcc
	global_store_dwordx4 v[12:13], v[8:11], off
	s_add_i32 s35, s35, 32
	s_cmp_lt_i32 s35, s34
	s_cbranch_scc1 .LBB6_1202
	s_mov_b32 s58, 0x800000
.LBB6_1204:
	s_max_i32 s0, s90, 0x12ac0
	s_min_i32 s12, s91, 0x16cc0
	s_cmp_le_i32 s12, s0
	s_cbranch_scc1 .LBB6_1209
	s_sub_i32 s1, s12, s0
	s_mov_b32 s2, 19
	s_cmp_lt_i32 s1, 32
	s_cbranch_scc1 .LBB6_1209
	s_add_i32 s0, s0, s95
	s_add_i32 s12, s12, 0xfffed540
	s_add_i32 s13, s0, 0xfffed540
	s_cmp_ge_i32 s13, s12
	s_cbranch_scc1 .LBB6_1209
	s_ashr_i32 s3, s2, 31
	s_lshl_b64 s[0:1], s[2:3], 3
	s_add_u32 s0, s76, s0
	s_addc_u32 s1, s77, s1
	s_load_dwordx2 s[2:3], s[0:1], 0x0
	v_lshlrev_b32_e32 v2, 4, v166
	s_waitcnt vmcnt(0)
	v_lshlrev_b32_e32 v6, 5, v166
	v_lshrrev_b32_e32 v4, 3, v166
	v_and_b32_e32 v5, 0x70, v2
	v_lshrrev_b32_e32 v147, 2, v166
	v_lshlrev_b32_e32 v144, 4, v166
	v_and_b32_e32 v144, 48, v144
	s_add_u32 s47, s6, 0x97080000
	v_lshl_or_b32 v2, v4, 13, v5
	v_add_u32_e32 v5, s94, v5
	v_mul_u32_u24_e32 v4, 0x84, v4
	v_mul_u32_u24_e32 v6, 0x84, v144
	v_lshlrev_b32_e32 v7, 2, v147
	s_addc_u32 s48, s7, 0
	v_and_b32_e32 v146, 31, v167
	v_mov_b32_e32 v145, v3
	v_add3_u32 v148, s94, v6, v7
	v_add_u32_e32 v149, v5, v4
.LBB6_1208:
	s_mul_hi_i32 s1, s13, 0x2e8ba2e9
	s_waitcnt lgkmcnt(0)
	s_lshr_b32 s5, s1, 31
	s_ashr_i32 s1, s1, 10
	s_lshl_b32 s4, s13, 3
	s_add_i32 s1, s1, s5
	s_and_b32 s33, s4, 64
	s_mul_i32 s4, s1, 0xffffea00
	s_add_i32 s4, s4, s13
	s_mul_hi_i32 s7, s1, 0xb00000
	s_mul_i32 s6, s1, 0xb00000
	s_ashr_i32 s1, s4, 1
	s_and_b32 s0, s13, 7
	s_ashr_i32 s4, s4, 31
	s_and_b32 s1, s1, -8
	s_lshr_b32 s4, s4, 26
	s_or_b32 s1, s1, s0
	s_add_i32 s4, s1, s4
	s_ashr_i32 s4, s4, 6
	s_lshl_b32 s1, s1, 5
	s_lshl_b32 s5, s4, 11
	s_lshl_b32 s4, s4, 7
	s_lshl_b64 s[24:25], s[6:7], 2
	s_sub_i32 s1, s1, s5
	s_or_b32 s4, s4, s33
	s_add_u32 s28, s2, s24
	v_or_b32_e32 v36, s1, v146
	v_or_b32_e32 v167, s1, v147
	s_addc_u32 s1, s3, s25
	v_readfirstlane_b32 s24, v36
	s_ashr_i32 s5, s4, 31
	s_andn2_b32 s24, s24, 31
	s_lshl_b64 s[26:27], s[4:5], 13
	s_add_u32 s26, s28, s26
	s_addc_u32 s1, s1, s27
	s_ashr_i32 s25, s24, 31
	s_lshl_b64 s[24:25], s[24:25], 2
	s_add_u32 s24, s26, s24
	s_addc_u32 s25, s1, s25
	s_mov_b64 s[26:27], s[24:25]
	s_add_u32 s28, s24, 0x10000
	s_addc_u32 s29, s25, 0
	v_lshl_add_u64 v[36:37], s[26:27], 0, v[2:3]
	s_add_u32 s26, s24, 0x20000
	global_load_dwordx4 v[124:127], v[36:37], off nt
	s_addc_u32 s27, s25, 0
	v_lshl_add_u64 v[36:37], s[28:29], 0, v[2:3]
	s_add_u32 s28, s24, 0x30000
	global_load_dwordx4 v[132:135], v[36:37], off nt
	s_addc_u32 s29, s25, 0
	v_lshl_add_u64 v[36:37], s[26:27], 0, v[2:3]
	s_add_u32 s26, s24, 0x40000
	global_load_dwordx4 v[136:139], v[36:37], off nt
	s_addc_u32 s27, s25, 0
	v_lshl_add_u64 v[36:37], s[28:29], 0, v[2:3]
	s_add_u32 s28, s24, 0x50000
	global_load_dwordx4 v[140:143], v[36:37], off nt
	s_addc_u32 s29, s25, 0
	v_lshl_add_u64 v[36:37], s[26:27], 0, v[2:3]
	s_add_u32 s26, s24, 0x60000
	s_addc_u32 s27, s25, 0
	global_load_dwordx4 v[168:171], v[36:37], off nt
	s_add_u32 s24, s24, 0x70000
	v_lshl_add_u64 v[36:37], s[28:29], 0, v[2:3]
	global_load_dwordx4 v[172:175], v[36:37], off nt
	s_addc_u32 s25, s25, 0
	s_add_i32 s1, s13, 8
	v_lshl_add_u64 v[36:37], s[26:27], 0, v[2:3]
	s_mul_hi_i32 s26, s1, 0x2e8ba2e9
	global_load_dwordx4 v[176:179], v[36:37], off nt
	s_lshr_b32 s28, s26, 31
	s_ashr_i32 s26, s26, 10
	v_lshl_add_u64 v[36:37], s[24:25], 0, v[2:3]
	s_add_i32 s24, s26, s28
	s_mul_i32 s25, s24, 0xffffea00
	s_add_i32 s25, s25, s1
	s_lshl_b32 s27, s1, 3
	s_ashr_i32 s1, s25, 1
	s_and_b32 s30, s27, 64
	s_mul_hi_i32 s27, s24, 0xb00000
	s_mul_i32 s26, s24, 0xb00000
	s_ashr_i32 s24, s25, 31
	s_and_b32 s1, s1, -8
	s_lshr_b32 s24, s24, 26
	s_or_b32 s1, s1, s0
	s_add_i32 s24, s1, s24
	s_ashr_i32 s24, s24, 6
	s_lshl_b32 s1, s1, 5
	s_lshl_b32 s25, s24, 11
	s_lshl_b32 s24, s24, 7
	s_lshl_b64 s[28:29], s[26:27], 2
	s_sub_i32 s1, s1, s25
	s_or_b32 s24, s24, s30
	global_load_dwordx4 v[184:187], v[36:37], off nt
	s_add_u32 s34, s2, s28
	v_or_b32_e32 v36, s1, v146
	v_or_b32_e32 v183, s1, v147
	s_addc_u32 s1, s3, s29
	v_readfirstlane_b32 s28, v36
	s_ashr_i32 s25, s24, 31
	s_andn2_b32 s28, s28, 31
	s_lshl_b64 s[30:31], s[24:25], 13
	s_add_u32 s30, s34, s30
	s_addc_u32 s1, s1, s31
	s_ashr_i32 s29, s28, 31
	s_lshl_b64 s[28:29], s[28:29], 2
	s_add_u32 s28, s30, s28
	s_addc_u32 s29, s1, s29
	s_mov_b64 s[30:31], s[28:29]
	s_add_u32 s34, s28, 0x10000
	s_addc_u32 s35, s29, 0
	v_lshl_add_u64 v[36:37], s[30:31], 0, v[2:3]
	s_add_u32 s30, s28, 0x20000
	global_load_dwordx4 v[76:79], v[36:37], off nt
	s_addc_u32 s31, s29, 0
	v_lshl_add_u64 v[36:37], s[34:35], 0, v[2:3]
	s_add_u32 s34, s28, 0x30000
	global_load_dwordx4 v[88:91], v[36:37], off nt
	s_addc_u32 s35, s29, 0
	v_lshl_add_u64 v[36:37], s[30:31], 0, v[2:3]
	s_add_u32 s30, s28, 0x40000
	global_load_dwordx4 v[96:99], v[36:37], off nt
	s_addc_u32 s31, s29, 0
	v_lshl_add_u64 v[36:37], s[34:35], 0, v[2:3]
	s_add_u32 s34, s28, 0x50000
	global_load_dwordx4 v[100:103], v[36:37], off nt
	s_addc_u32 s35, s29, 0
	v_lshl_add_u64 v[36:37], s[30:31], 0, v[2:3]
	s_add_u32 s30, s28, 0x60000
	s_addc_u32 s31, s29, 0
	global_load_dwordx4 v[108:111], v[36:37], off nt
	s_add_u32 s28, s28, 0x70000
	v_lshl_add_u64 v[36:37], s[34:35], 0, v[2:3]
	global_load_dwordx4 v[112:115], v[36:37], off nt
	s_addc_u32 s29, s29, 0
	s_add_i32 s1, s13, 16
	v_lshl_add_u64 v[36:37], s[30:31], 0, v[2:3]
	s_mul_hi_i32 s30, s1, 0x2e8ba2e9
	global_load_dwordx4 v[120:123], v[36:37], off nt
	s_lshr_b32 s31, s30, 31
	s_ashr_i32 s30, s30, 10
	v_lshl_add_u64 v[36:37], s[28:29], 0, v[2:3]
	s_add_i32 s28, s30, s31
	s_mul_i32 s30, s28, 0xffffea00
	s_add_i32 s30, s30, s1
	s_ashr_i32 s1, s30, 1
	s_ashr_i32 s30, s30, 31
	s_and_b32 s1, s1, -8
	s_lshr_b32 s30, s30, 26
	s_or_b32 s1, s1, s0
	s_add_i32 s30, s1, s30
	s_ashr_i32 s30, s30, 6
	s_mul_hi_i32 s29, s28, 0xb00000
	s_mul_i32 s28, s28, 0xb00000
	s_lshl_b32 s1, s1, 5
	s_lshl_b32 s31, s30, 11
	s_lshl_b32 s30, s30, 7
	s_lshl_b64 s[34:35], s[28:29], 2
	s_sub_i32 s1, s1, s31
	s_or_b32 s30, s30, s33
	global_load_dwordx4 v[128:131], v[36:37], off nt
	s_add_u32 s33, s2, s34
	v_or_b32_e32 v36, s1, v146
	v_or_b32_e32 v200, s1, v147
	s_addc_u32 s1, s3, s35
	v_readfirstlane_b32 s34, v36
	s_ashr_i32 s31, s30, 31
	s_andn2_b32 s34, s34, 31
	s_lshl_b64 s[36:37], s[30:31], 13
	s_add_u32 s33, s33, s36
	s_addc_u32 s1, s1, s37
	s_ashr_i32 s35, s34, 31
	s_lshl_b64 s[34:35], s[34:35], 2
	s_add_u32 s34, s33, s34
	s_addc_u32 s35, s1, s35
	s_mov_b64 s[36:37], s[34:35]
	s_add_u32 s50, s34, 0x10000
	s_addc_u32 s51, s35, 0
	v_lshl_add_u64 v[36:37], s[36:37], 0, v[2:3]
	s_add_u32 s36, s34, 0x20000
	global_load_dwordx4 v[48:51], v[36:37], off nt
	s_addc_u32 s37, s35, 0
	v_lshl_add_u64 v[36:37], s[50:51], 0, v[2:3]
	s_add_u32 s50, s34, 0x30000
	global_load_dwordx4 v[56:59], v[36:37], off nt
	s_addc_u32 s51, s35, 0
	v_lshl_add_u64 v[36:37], s[36:37], 0, v[2:3]
	s_add_u32 s36, s34, 0x40000
	global_load_dwordx4 v[64:67], v[36:37], off nt
	s_addc_u32 s37, s35, 0
	v_lshl_add_u64 v[36:37], s[50:51], 0, v[2:3]
	s_add_u32 s50, s34, 0x50000
	global_load_dwordx4 v[72:75], v[36:37], off nt
	s_addc_u32 s51, s35, 0
	v_lshl_add_u64 v[36:37], s[36:37], 0, v[2:3]
	s_add_u32 s36, s34, 0x60000
	s_addc_u32 s37, s35, 0
	s_add_u32 s34, s34, 0x70000
	global_load_dwordx4 v[84:87], v[36:37], off nt
	s_addc_u32 s35, s35, 0
	v_lshl_add_u64 v[36:37], s[50:51], 0, v[2:3]
	s_add_i32 s1, s13, 24
	global_load_dwordx4 v[92:95], v[36:37], off nt
	s_mul_hi_i32 s33, s1, 0x2e8ba2e9
	v_lshl_add_u64 v[36:37], s[36:37], 0, v[2:3]
	s_lshr_b32 s37, s33, 31
	s_ashr_i32 s33, s33, 10
	global_load_dwordx4 v[104:107], v[36:37], off nt
	s_add_i32 s33, s33, s37
	v_lshl_add_u64 v[36:37], s[34:35], 0, v[2:3]
	s_mul_i32 s34, s33, 0xffffea00
	s_add_i32 s34, s34, s1
	s_lshl_b32 s36, s1, 3
	s_ashr_i32 s1, s34, 1
	s_and_b32 s45, s36, 64
	s_mul_hi_i32 s37, s33, 0xb00000
	s_mul_i32 s36, s33, 0xb00000
	s_ashr_i32 s33, s34, 31
	s_and_b32 s1, s1, -8
	s_lshr_b32 s33, s33, 26
	s_or_b32 s0, s1, s0
	s_add_i32 s1, s0, s33
	s_ashr_i32 s1, s1, 6
	s_lshl_b32 s0, s0, 5
	s_lshl_b32 s33, s1, 11
	s_lshl_b32 s1, s1, 7
	s_lshl_b64 s[50:51], s[36:37], 2
	s_sub_i32 s0, s0, s33
	s_or_b32 s34, s1, s45
	global_load_dwordx4 v[116:119], v[36:37], off nt
	s_add_u32 s1, s2, s50
	v_or_b32_e32 v36, s0, v146
	v_or_b32_e32 v201, s0, v147
	s_addc_u32 s33, s3, s51
	v_readfirstlane_b32 s0, v36
	s_ashr_i32 s35, s34, 31
	s_andn2_b32 s0, s0, 31
	s_lshl_b64 s[50:51], s[34:35], 13
	s_add_u32 s45, s1, s50
	s_addc_u32 s33, s33, s51
	s_ashr_i32 s1, s0, 31
	s_lshl_b64 s[0:1], s[0:1], 2
	s_add_u32 s0, s45, s0
	s_addc_u32 s1, s33, s1
	s_mov_b64 s[50:51], s[0:1]
	s_add_u32 s64, s0, 0x10000
	s_addc_u32 s65, s1, 0
	v_lshl_add_u64 v[36:37], s[50:51], 0, v[2:3]
	global_load_dwordx4 v[36:39], v[36:37], off nt
	s_add_u32 s50, s0, 0x20000
	s_addc_u32 s51, s1, 0
	v_lshl_add_u64 v[40:41], s[64:65], 0, v[2:3]
	global_load_dwordx4 v[40:43], v[40:41], off nt
	s_add_u32 s64, s0, 0x30000
	s_addc_u32 s65, s1, 0
	v_lshl_add_u64 v[44:45], s[50:51], 0, v[2:3]
	global_load_dwordx4 v[44:47], v[44:45], off nt
	s_add_u32 s50, s0, 0x40000
	s_addc_u32 s51, s1, 0
	v_lshl_add_u64 v[52:53], s[64:65], 0, v[2:3]
	global_load_dwordx4 v[52:55], v[52:53], off nt
	s_add_u32 s64, s0, 0x50000
	s_addc_u32 s65, s1, 0
	v_lshl_add_u64 v[60:61], s[50:51], 0, v[2:3]
	global_load_dwordx4 v[60:63], v[60:61], off nt
	s_add_u32 s50, s0, 0x60000
	s_addc_u32 s51, s1, 0
	v_lshl_add_u64 v[68:69], s[64:65], 0, v[2:3]
	global_load_dwordx4 v[68:71], v[68:69], off nt
	s_add_u32 s0, s0, 0x70000
	s_addc_u32 s1, s1, 0
	v_lshl_add_u64 v[80:81], s[50:51], 0, v[2:3]
	global_load_dwordx4 v[80:83], v[80:81], off nt
	v_add_u32_e32 v150, 0x420, v149
	v_add_u32_e32 v151, 0x428, v149
	v_add_u32_e32 v152, 0x840, v149
	v_add_u32_e32 v153, 0x848, v149
	v_add_u32_e32 v154, 0xc60, v149
	v_add_u32_e32 v155, 0xc68, v149
	v_add_u32_e32 v156, 0x1080, v149
	v_add_u32_e32 v157, 0x1088, v149
	v_add_u32_e32 v158, 0x14a0, v149
	v_add_u32_e32 v159, 0x14a8, v149
	v_add_u32_e32 v160, 0x18c0, v149
	v_add_u32_e32 v161, 0x18c8, v149
	v_add_u32_e32 v162, 0x1ce0, v149
	v_add_u32_e32 v163, 0x1ce8, v149
	s_waitcnt vmcnt(30)
	ds_write2_b32 v149, v124, v125 offset1:1
	ds_write2_b32 v149, v126, v127 offset0:2 offset1:3
	s_waitcnt vmcnt(29)
	ds_write2_b32 v150, v132, v133 offset1:1
	ds_write2_b32 v151, v134, v135 offset1:1
	s_waitcnt vmcnt(28)
	ds_write2_b32 v152, v136, v137 offset1:1
	ds_write2_b32 v153, v138, v139 offset1:1
	s_waitcnt vmcnt(27)
	ds_write2_b32 v154, v140, v141 offset1:1
	ds_write2_b32 v155, v142, v143 offset1:1
	s_waitcnt vmcnt(26)
	ds_write2_b32 v156, v168, v169 offset1:1
	ds_write2_b32 v157, v170, v171 offset1:1
	s_waitcnt vmcnt(25)
	ds_write2_b32 v158, v172, v173 offset1:1
	ds_write2_b32 v159, v174, v175 offset1:1
	s_waitcnt vmcnt(24)
	ds_write2_b32 v160, v176, v177 offset1:1
	ds_write2_b32 v161, v178, v179 offset1:1
	s_waitcnt vmcnt(23)
	ds_write2_b32 v162, v184, v185 offset1:1
	ds_write2_b32 v163, v186, v187 offset1:1
	v_lshl_add_u64 v[124:125], s[0:1], 0, v[2:3]
	global_load_dwordx4 v[124:127], v[124:125], off nt
	s_add_u32 s6, s47, s6
	s_addc_u32 s7, s48, s7
	v_add_u32_e32 v164, 0x400, v148
	v_mov_b32_e32 v165, v148
	v_add_u32_e32 v166, 0x400, v148
	v_mov_b64_e32 v[132:133], s[6:7]
	s_add_u32 s0, s47, s26
	ds_read2_b32 v[134:135], v148 offset1:33
	ds_read2_b32 v[136:137], v148 offset0:66 offset1:99
	ds_read2_b32 v[138:139], v148 offset0:132 offset1:165
	ds_read2_b32 v[140:141], v148 offset0:198 offset1:231
	ds_read2_b32 v[142:143], v164 offset0:8 offset1:41
	ds_read2_b32 v[168:169], v164 offset0:74 offset1:107
	ds_read2_b32 v[170:171], v164 offset0:140 offset1:173
	ds_read2_b32 v[172:173], v164 offset0:206 offset1:239
	ds_read2_b32 v[174:175], v165 offset0:16 offset1:49
	ds_read2_b32 v[176:177], v165 offset0:82 offset1:115
	ds_read2_b32 v[178:179], v165 offset0:148 offset1:181
	ds_read2_b32 v[184:185], v165 offset0:214 offset1:247
	ds_read2_b32 v[186:187], v166 offset0:24 offset1:57
	ds_read2_b32 v[188:189], v166 offset0:90 offset1:123
	ds_read2_b32 v[190:191], v166 offset0:156 offset1:189
	ds_read2_b32 v[192:193], v166 offset0:222 offset1:255
	v_mad_i64_i32 v[132:133], s[6:7], v167, s82, v[132:133]
	s_addc_u32 s1, s48, s27
	v_lshl_add_u64 v[132:133], v[132:133], 0, s[4:5]
	v_mov_b64_e32 v[194:195], s[0:1]
	v_mov_b32_e32 v4, v3
	v_mov_b32_e32 v5, v3
	v_mov_b32_e32 v6, v3
	v_mov_b32_e32 v7, v3
	v_lshl_add_u64 v[196:197], v[132:133], 0, v[144:145]
	v_mad_i64_i32 v[132:133], s[4:5], v183, s82, v[194:195]
	s_waitcnt lgkmcnt(14)
	v_mul_f32_e32 v167, 0x42800000, v134
	v_mul_f32_e32 v183, 0x42800000, v135
	s_waitcnt lgkmcnt(13)
	v_mul_f32_e32 v138, 0x42800000, v138
	v_mul_f32_e32 v139, 0x42800000, v139
	s_waitcnt lgkmcnt(11)
	v_mul_f32_e32 v142, 0x42800000, v142
	v_mul_f32_e32 v143, 0x42800000, v143
	s_waitcnt lgkmcnt(9)
	v_mul_f32_e32 v170, 0x42800000, v170
	v_mul_f32_e32 v171, 0x42800000, v171
	v_mov_b32_e32 v8, v3
	v_mov_b32_e32 v9, v3
	v_mov_b32_e32 v10, v3
	v_mov_b32_e32 v11, v3
	s_waitcnt lgkmcnt(7)
	v_mul_f32_e32 v174, 0x42800000, v174
	v_mul_f32_e32 v175, 0x42800000, v175
	s_waitcnt lgkmcnt(5)
	v_mul_f32_e32 v178, 0x42800000, v178
	v_mul_f32_e32 v179, 0x42800000, v179
	s_waitcnt lgkmcnt(3)
	v_mul_f32_e32 v186, 0x42800000, v186
	v_mul_f32_e32 v187, 0x42800000, v187
	s_waitcnt lgkmcnt(1)
	v_mul_f32_e32 v190, 0x42800000, v190
	v_mul_f32_e32 v191, 0x42800000, v191
	v_cvt_pk_fp8_f32 v4, v167, v183
	v_cvt_pk_fp8_f32 v5, v138, v139
	v_cvt_pk_fp8_f32 v6, v142, v143
	v_cvt_pk_fp8_f32 v7, v170, v171
	v_cvt_pk_fp8_f32 v8, v174, v175
	v_cvt_pk_fp8_f32 v9, v178, v179
	v_cvt_pk_fp8_f32 v10, v186, v187
	v_cvt_pk_fp8_f32 v11, v190, v191
	v_mul_f32_e32 v136, 0x42800000, v136
	v_mul_f32_e32 v137, 0x42800000, v137
	v_mul_f32_e32 v140, 0x42800000, v140
	v_mul_f32_e32 v141, 0x42800000, v141
	v_mul_f32_e32 v168, 0x42800000, v168
	v_mul_f32_e32 v169, 0x42800000, v169
	v_mul_f32_e32 v172, 0x42800000, v172
	v_mul_f32_e32 v173, 0x42800000, v173
	v_mul_f32_e32 v176, 0x42800000, v176
	v_mul_f32_e32 v177, 0x42800000, v177
	v_mul_f32_e32 v184, 0x42800000, v184
	v_mul_f32_e32 v185, 0x42800000, v185
	v_mul_f32_e32 v188, 0x42800000, v188
	v_mul_f32_e32 v189, 0x42800000, v189
	s_waitcnt lgkmcnt(0)
	v_mul_f32_e32 v192, 0x42800000, v192
	v_mul_f32_e32 v193, 0x42800000, v193
	v_cvt_pk_fp8_f32 v4, v136, v137 op_sel:[0,0,1]
	v_cvt_pk_fp8_f32 v5, v140, v141 op_sel:[0,0,1]
	v_cvt_pk_fp8_f32 v6, v168, v169 op_sel:[0,0,1]
	v_cvt_pk_fp8_f32 v7, v172, v173 op_sel:[0,0,1]
	v_cvt_pk_fp8_f32 v8, v176, v177 op_sel:[0,0,1]
	v_cvt_pk_fp8_f32 v9, v184, v185 op_sel:[0,0,1]
	v_cvt_pk_fp8_f32 v10, v188, v189 op_sel:[0,0,1]
	v_cvt_pk_fp8_f32 v11, v192, v193 op_sel:[0,0,1]
	global_store_dwordx4 v[196:197], v[4:7], off
	s_nop 1
	v_add_co_u32_e32 v196, vcc, 0x16000, v196
	s_nop 1
	v_addc_co_u32_e32 v197, vcc, 0, v197, vcc
	global_store_dwordx4 v[196:197], v[8:11], off
	s_waitcnt vmcnt(25)
	ds_write2_b32 v149, v76, v77 offset1:1
	ds_write2_b32 v149, v78, v79 offset0:2 offset1:3
	s_waitcnt vmcnt(24)
	ds_write2_b32 v150, v88, v89 offset1:1
	ds_write2_b32 v151, v90, v91 offset1:1
	s_waitcnt vmcnt(23)
	ds_write2_b32 v152, v96, v97 offset1:1
	ds_write2_b32 v153, v98, v99 offset1:1
	s_waitcnt vmcnt(22)
	ds_write2_b32 v154, v100, v101 offset1:1
	ds_write2_b32 v155, v102, v103 offset1:1
	s_waitcnt vmcnt(21)
	ds_write2_b32 v156, v108, v109 offset1:1
	ds_write2_b32 v157, v110, v111 offset1:1
	s_waitcnt vmcnt(20)
	ds_write2_b32 v158, v112, v113 offset1:1
	ds_write2_b32 v159, v114, v115 offset1:1
	s_waitcnt vmcnt(19)
	ds_write2_b32 v160, v120, v121 offset1:1
	ds_write2_b32 v161, v122, v123 offset1:1
	s_waitcnt vmcnt(18)
	ds_write2_b32 v162, v128, v129 offset1:1
	ds_write2_b32 v163, v130, v131 offset1:1
	ds_read2_b32 v[4:5], v148 offset1:33
	ds_read2_b32 v[6:7], v148 offset0:66 offset1:99
	ds_read2_b32 v[8:9], v148 offset0:132 offset1:165
	ds_read2_b32 v[10:11], v148 offset0:198 offset1:231
	ds_read2_b32 v[76:77], v164 offset0:8 offset1:41
	ds_read2_b32 v[78:79], v164 offset0:74 offset1:107
	ds_read2_b32 v[88:89], v164 offset0:140 offset1:173
	ds_read2_b32 v[90:91], v164 offset0:206 offset1:239
	ds_read2_b32 v[96:97], v165 offset0:16 offset1:49
	ds_read2_b32 v[98:99], v165 offset0:82 offset1:115
	ds_read2_b32 v[100:101], v165 offset0:148 offset1:181
	ds_read2_b32 v[102:103], v165 offset0:214 offset1:247
	ds_read2_b32 v[108:109], v166 offset0:24 offset1:57
	ds_read2_b32 v[110:111], v166 offset0:90 offset1:123
	ds_read2_b32 v[112:113], v166 offset0:156 offset1:189
	ds_read2_b32 v[114:115], v166 offset0:222 offset1:255
	v_mov_b32_e32 v12, v3
	v_mov_b32_e32 v13, v3
	v_mov_b32_e32 v14, v3
	v_mov_b32_e32 v15, v3
	s_waitcnt lgkmcnt(14)
	v_mul_f32_e32 v4, 0x42800000, v4
	v_mul_f32_e32 v5, 0x42800000, v5
	s_waitcnt lgkmcnt(13)
	v_mul_f32_e32 v8, 0x42800000, v8
	v_mul_f32_e32 v9, 0x42800000, v9
	s_waitcnt lgkmcnt(11)
	v_mul_f32_e32 v76, 0x42800000, v76
	v_mul_f32_e32 v77, 0x42800000, v77
	s_waitcnt lgkmcnt(9)
	v_mul_f32_e32 v88, 0x42800000, v88
	v_mul_f32_e32 v89, 0x42800000, v89
	v_mov_b32_e32 v16, v3
	v_mov_b32_e32 v17, v3
	v_mov_b32_e32 v18, v3
	v_mov_b32_e32 v19, v3
	s_waitcnt lgkmcnt(7)
	v_mul_f32_e32 v96, 0x42800000, v96
	v_mul_f32_e32 v97, 0x42800000, v97
	s_waitcnt lgkmcnt(5)
	v_mul_f32_e32 v100, 0x42800000, v100
	v_mul_f32_e32 v101, 0x42800000, v101
	s_waitcnt lgkmcnt(3)
	v_mul_f32_e32 v108, 0x42800000, v108
	v_mul_f32_e32 v109, 0x42800000, v109
	s_waitcnt lgkmcnt(1)
	v_mul_f32_e32 v112, 0x42800000, v112
	v_mul_f32_e32 v113, 0x42800000, v113
	v_cvt_pk_fp8_f32 v12, v4, v5
	v_cvt_pk_fp8_f32 v13, v8, v9
	v_cvt_pk_fp8_f32 v14, v76, v77
	v_cvt_pk_fp8_f32 v15, v88, v89
	v_cvt_pk_fp8_f32 v16, v96, v97
	v_cvt_pk_fp8_f32 v17, v100, v101
	v_cvt_pk_fp8_f32 v18, v108, v109
	v_cvt_pk_fp8_f32 v19, v112, v113
	v_mul_f32_e32 v6, 0x42800000, v6
	v_mul_f32_e32 v7, 0x42800000, v7
	v_mul_f32_e32 v10, 0x42800000, v10
	v_mul_f32_e32 v11, 0x42800000, v11
	v_mul_f32_e32 v78, 0x42800000, v78
	v_mul_f32_e32 v79, 0x42800000, v79
	v_mul_f32_e32 v90, 0x42800000, v90
	v_mul_f32_e32 v91, 0x42800000, v91
	v_mul_f32_e32 v98, 0x42800000, v98
	v_mul_f32_e32 v99, 0x42800000, v99
	v_mul_f32_e32 v102, 0x42800000, v102
	v_mul_f32_e32 v103, 0x42800000, v103
	v_mul_f32_e32 v110, 0x42800000, v110
	v_mul_f32_e32 v111, 0x42800000, v111
	s_waitcnt lgkmcnt(0)
	v_mul_f32_e32 v114, 0x42800000, v114
	v_mul_f32_e32 v115, 0x42800000, v115
	v_cvt_pk_fp8_f32 v12, v6, v7 op_sel:[0,0,1]
	v_cvt_pk_fp8_f32 v13, v10, v11 op_sel:[0,0,1]
	v_cvt_pk_fp8_f32 v14, v78, v79 op_sel:[0,0,1]
	v_cvt_pk_fp8_f32 v15, v90, v91 op_sel:[0,0,1]
	v_cvt_pk_fp8_f32 v16, v98, v99 op_sel:[0,0,1]
	v_cvt_pk_fp8_f32 v17, v102, v103 op_sel:[0,0,1]
	v_cvt_pk_fp8_f32 v18, v110, v111 op_sel:[0,0,1]
	v_cvt_pk_fp8_f32 v19, v114, v115 op_sel:[0,0,1]
	v_lshl_add_u64 v[132:133], v[132:133], 0, s[24:25]
	v_lshl_add_u64 v[198:199], v[132:133], 0, v[144:145]
	global_store_dwordx4 v[198:199], v[12:15], off
	s_nop 1
	v_add_co_u32_e32 v198, vcc, 0x16000, v198
	s_nop 1
	v_addc_co_u32_e32 v199, vcc, 0, v199, vcc
	global_store_dwordx4 v[198:199], v[16:19], off
	s_waitcnt vmcnt(19)
	ds_write2_b32 v149, v48, v49 offset1:1
	ds_write2_b32 v149, v50, v51 offset0:2 offset1:3
	s_waitcnt vmcnt(18)
	ds_write2_b32 v150, v56, v57 offset1:1
	ds_write2_b32 v151, v58, v59 offset1:1
	s_waitcnt vmcnt(17)
	ds_write2_b32 v152, v64, v65 offset1:1
	ds_write2_b32 v153, v66, v67 offset1:1
	s_waitcnt vmcnt(16)
	ds_write2_b32 v154, v72, v73 offset1:1
	ds_write2_b32 v155, v74, v75 offset1:1
	s_waitcnt vmcnt(15)
	ds_write2_b32 v156, v84, v85 offset1:1
	ds_write2_b32 v157, v86, v87 offset1:1
	s_waitcnt vmcnt(14)
	ds_write2_b32 v158, v92, v93 offset1:1
	ds_write2_b32 v159, v94, v95 offset1:1
	s_waitcnt vmcnt(13)
	ds_write2_b32 v160, v104, v105 offset1:1
	ds_write2_b32 v161, v106, v107 offset1:1
	s_waitcnt vmcnt(12)
	ds_write2_b32 v162, v116, v117 offset1:1
	ds_write2_b32 v163, v118, v119 offset1:1
	ds_read2_b32 v[4:5], v148 offset1:33
	ds_read2_b32 v[6:7], v148 offset0:66 offset1:99
	ds_read2_b32 v[8:9], v148 offset0:132 offset1:165
	ds_read2_b32 v[10:11], v148 offset0:198 offset1:231
	ds_read2_b32 v[12:13], v164 offset0:8 offset1:41
	ds_read2_b32 v[14:15], v164 offset0:74 offset1:107
	ds_read2_b32 v[16:17], v164 offset0:140 offset1:173
	ds_read2_b32 v[18:19], v164 offset0:206 offset1:239
	ds_read2_b32 v[48:49], v165 offset0:16 offset1:49
	ds_read2_b32 v[50:51], v165 offset0:82 offset1:115
	ds_read2_b32 v[56:57], v165 offset0:148 offset1:181
	ds_read2_b32 v[58:59], v165 offset0:214 offset1:247
	ds_read2_b32 v[64:65], v166 offset0:24 offset1:57
	ds_read2_b32 v[66:67], v166 offset0:90 offset1:123
	ds_read2_b32 v[72:73], v166 offset0:156 offset1:189
	ds_read2_b32 v[74:75], v166 offset0:222 offset1:255
	v_mov_b32_e32 v20, v3
	v_mov_b32_e32 v21, v3
	v_mov_b32_e32 v22, v3
	v_mov_b32_e32 v23, v3
	s_waitcnt lgkmcnt(14)
	v_mul_f32_e32 v4, 0x42800000, v4
	v_mul_f32_e32 v5, 0x42800000, v5
	s_waitcnt lgkmcnt(13)
	v_mul_f32_e32 v8, 0x42800000, v8
	v_mul_f32_e32 v9, 0x42800000, v9
	s_waitcnt lgkmcnt(11)
	v_mul_f32_e32 v12, 0x42800000, v12
	v_mul_f32_e32 v13, 0x42800000, v13
	s_waitcnt lgkmcnt(9)
	v_mul_f32_e32 v16, 0x42800000, v16
	v_mul_f32_e32 v17, 0x42800000, v17
	v_mov_b32_e32 v24, v3
	v_mov_b32_e32 v25, v3
	v_mov_b32_e32 v26, v3
	v_mov_b32_e32 v27, v3
	s_waitcnt lgkmcnt(7)
	v_mul_f32_e32 v48, 0x42800000, v48
	v_mul_f32_e32 v49, 0x42800000, v49
	s_waitcnt lgkmcnt(5)
	v_mul_f32_e32 v56, 0x42800000, v56
	v_mul_f32_e32 v57, 0x42800000, v57
	s_waitcnt lgkmcnt(3)
	v_mul_f32_e32 v64, 0x42800000, v64
	v_mul_f32_e32 v65, 0x42800000, v65
	s_waitcnt lgkmcnt(1)
	v_mul_f32_e32 v72, 0x42800000, v72
	v_mul_f32_e32 v73, 0x42800000, v73
	v_cvt_pk_fp8_f32 v20, v4, v5
	v_cvt_pk_fp8_f32 v21, v8, v9
	v_cvt_pk_fp8_f32 v22, v12, v13
	v_cvt_pk_fp8_f32 v23, v16, v17
	v_cvt_pk_fp8_f32 v24, v48, v49
	v_cvt_pk_fp8_f32 v25, v56, v57
	v_cvt_pk_fp8_f32 v26, v64, v65
	v_cvt_pk_fp8_f32 v27, v72, v73
	s_add_u32 s0, s47, s28
	s_addc_u32 s1, s48, s29
	v_mul_f32_e32 v6, 0x42800000, v6
	v_mul_f32_e32 v7, 0x42800000, v7
	v_mul_f32_e32 v10, 0x42800000, v10
	v_mul_f32_e32 v11, 0x42800000, v11
	v_mul_f32_e32 v14, 0x42800000, v14
	v_mul_f32_e32 v15, 0x42800000, v15
	v_mul_f32_e32 v18, 0x42800000, v18
	v_mul_f32_e32 v19, 0x42800000, v19
	v_mov_b64_e32 v[194:195], s[0:1]
	v_mul_f32_e32 v50, 0x42800000, v50
	v_mul_f32_e32 v51, 0x42800000, v51
	v_mul_f32_e32 v58, 0x42800000, v58
	v_mul_f32_e32 v59, 0x42800000, v59
	v_mul_f32_e32 v66, 0x42800000, v66
	v_mul_f32_e32 v67, 0x42800000, v67
	s_waitcnt lgkmcnt(0)
	v_mul_f32_e32 v74, 0x42800000, v74
	v_mul_f32_e32 v75, 0x42800000, v75
	v_cvt_pk_fp8_f32 v20, v6, v7 op_sel:[0,0,1]
	v_cvt_pk_fp8_f32 v21, v10, v11 op_sel:[0,0,1]
	v_cvt_pk_fp8_f32 v22, v14, v15 op_sel:[0,0,1]
	v_cvt_pk_fp8_f32 v23, v18, v19 op_sel:[0,0,1]
	v_mad_i64_i32 v[132:133], s[4:5], v200, s82, v[194:195]
	v_cvt_pk_fp8_f32 v24, v50, v51 op_sel:[0,0,1]
	v_cvt_pk_fp8_f32 v25, v58, v59 op_sel:[0,0,1]
	v_cvt_pk_fp8_f32 v26, v66, v67 op_sel:[0,0,1]
	v_cvt_pk_fp8_f32 v27, v74, v75 op_sel:[0,0,1]
	v_lshl_add_u64 v[132:133], v[132:133], 0, s[30:31]
	v_lshl_add_u64 v[134:135], v[132:133], 0, v[144:145]
	global_store_dwordx4 v[134:135], v[20:23], off
	s_nop 1
	v_add_co_u32_e32 v134, vcc, 0x16000, v134
	s_nop 1
	v_addc_co_u32_e32 v135, vcc, 0, v135, vcc
	global_store_dwordx4 v[134:135], v[24:27], off
	s_waitcnt vmcnt(13)
	ds_write2_b32 v149, v36, v37 offset1:1
	ds_write2_b32 v149, v38, v39 offset0:2 offset1:3
	s_waitcnt vmcnt(12)
	ds_write2_b32 v150, v40, v41 offset1:1
	ds_write2_b32 v151, v42, v43 offset1:1
	s_waitcnt vmcnt(11)
	ds_write2_b32 v152, v44, v45 offset1:1
	ds_write2_b32 v153, v46, v47 offset1:1
	s_waitcnt vmcnt(10)
	ds_write2_b32 v154, v52, v53 offset1:1
	ds_write2_b32 v155, v54, v55 offset1:1
	s_waitcnt vmcnt(9)
	ds_write2_b32 v156, v60, v61 offset1:1
	ds_write2_b32 v157, v62, v63 offset1:1
	s_waitcnt vmcnt(8)
	ds_write2_b32 v158, v68, v69 offset1:1
	ds_write2_b32 v159, v70, v71 offset1:1
	s_waitcnt vmcnt(7)
	ds_write2_b32 v160, v80, v81 offset1:1
	ds_write2_b32 v161, v82, v83 offset1:1
	s_waitcnt vmcnt(6)
	ds_write2_b32 v162, v124, v125 offset1:1
	ds_write2_b32 v163, v126, v127 offset1:1
	ds_read2_b32 v[4:5], v148 offset1:33
	ds_read2_b32 v[6:7], v148 offset0:66 offset1:99
	ds_read2_b32 v[8:9], v148 offset0:132 offset1:165
	ds_read2_b32 v[10:11], v148 offset0:198 offset1:231
	ds_read2_b32 v[12:13], v164 offset0:8 offset1:41
	ds_read2_b32 v[14:15], v164 offset0:74 offset1:107
	ds_read2_b32 v[16:17], v164 offset0:140 offset1:173
	ds_read2_b32 v[18:19], v164 offset0:206 offset1:239
	ds_read2_b32 v[20:21], v165 offset0:16 offset1:49
	ds_read2_b32 v[22:23], v165 offset0:82 offset1:115
	ds_read2_b32 v[24:25], v165 offset0:148 offset1:181
	ds_read2_b32 v[26:27], v165 offset0:214 offset1:247
	ds_read2_b32 v[36:37], v166 offset0:24 offset1:57
	ds_read2_b32 v[38:39], v166 offset0:90 offset1:123
	ds_read2_b32 v[40:41], v166 offset0:156 offset1:189
	ds_read2_b32 v[42:43], v166 offset0:222 offset1:255
	v_mov_b32_e32 v28, v3
	v_mov_b32_e32 v29, v3
	v_mov_b32_e32 v30, v3
	v_mov_b32_e32 v31, v3
	s_waitcnt lgkmcnt(14)
	v_mul_f32_e32 v4, 0x42800000, v4
	v_mul_f32_e32 v5, 0x42800000, v5
	s_waitcnt lgkmcnt(13)
	v_mul_f32_e32 v8, 0x42800000, v8
	v_mul_f32_e32 v9, 0x42800000, v9
	s_waitcnt lgkmcnt(11)
	v_mul_f32_e32 v12, 0x42800000, v12
	v_mul_f32_e32 v13, 0x42800000, v13
	s_waitcnt lgkmcnt(9)
	v_mul_f32_e32 v16, 0x42800000, v16
	v_mul_f32_e32 v17, 0x42800000, v17
	v_mov_b32_e32 v32, v3
	v_mov_b32_e32 v33, v3
	v_mov_b32_e32 v34, v3
	v_mov_b32_e32 v35, v3
	s_waitcnt lgkmcnt(7)
	v_mul_f32_e32 v20, 0x42800000, v20
	v_mul_f32_e32 v21, 0x42800000, v21
	s_waitcnt lgkmcnt(5)
	v_mul_f32_e32 v24, 0x42800000, v24
	v_mul_f32_e32 v25, 0x42800000, v25
	s_waitcnt lgkmcnt(3)
	v_mul_f32_e32 v36, 0x42800000, v36
	v_mul_f32_e32 v37, 0x42800000, v37
	s_waitcnt lgkmcnt(1)
	v_mul_f32_e32 v40, 0x42800000, v40
	v_mul_f32_e32 v41, 0x42800000, v41
	v_cvt_pk_fp8_f32 v28, v4, v5
	v_cvt_pk_fp8_f32 v29, v8, v9
	v_cvt_pk_fp8_f32 v30, v12, v13
	v_cvt_pk_fp8_f32 v31, v16, v17
	v_cvt_pk_fp8_f32 v32, v20, v21
	v_cvt_pk_fp8_f32 v33, v24, v25
	v_cvt_pk_fp8_f32 v34, v36, v37
	v_cvt_pk_fp8_f32 v35, v40, v41
	s_add_u32 s0, s47, s36
	s_addc_u32 s1, s48, s37
	v_mul_f32_e32 v6, 0x42800000, v6
	v_mul_f32_e32 v7, 0x42800000, v7
	v_mul_f32_e32 v10, 0x42800000, v10
	v_mul_f32_e32 v11, 0x42800000, v11
	v_mul_f32_e32 v14, 0x42800000, v14
	v_mul_f32_e32 v15, 0x42800000, v15
	v_mul_f32_e32 v18, 0x42800000, v18
	v_mul_f32_e32 v19, 0x42800000, v19
	v_mov_b64_e32 v[194:195], s[0:1]
	v_mul_f32_e32 v22, 0x42800000, v22
	v_mul_f32_e32 v23, 0x42800000, v23
	v_mul_f32_e32 v26, 0x42800000, v26
	v_mul_f32_e32 v27, 0x42800000, v27
	v_mul_f32_e32 v38, 0x42800000, v38
	v_mul_f32_e32 v39, 0x42800000, v39
	s_waitcnt lgkmcnt(0)
	v_mul_f32_e32 v42, 0x42800000, v42
	v_mul_f32_e32 v43, 0x42800000, v43
	v_cvt_pk_fp8_f32 v28, v6, v7 op_sel:[0,0,1]
	v_cvt_pk_fp8_f32 v29, v10, v11 op_sel:[0,0,1]
	v_cvt_pk_fp8_f32 v30, v14, v15 op_sel:[0,0,1]
	v_cvt_pk_fp8_f32 v31, v18, v19 op_sel:[0,0,1]
	v_mad_i64_i32 v[132:133], s[0:1], v201, s82, v[194:195]
	v_cvt_pk_fp8_f32 v32, v22, v23 op_sel:[0,0,1]
	v_cvt_pk_fp8_f32 v33, v26, v27 op_sel:[0,0,1]
	v_cvt_pk_fp8_f32 v34, v38, v39 op_sel:[0,0,1]
	v_cvt_pk_fp8_f32 v35, v42, v43 op_sel:[0,0,1]
	v_lshl_add_u64 v[132:133], v[132:133], 0, s[34:35]
	v_lshl_add_u64 v[4:5], v[132:133], 0, v[144:145]
	global_store_dwordx4 v[4:5], v[28:31], off
	s_nop 1
	v_add_co_u32_e32 v4, vcc, 0x16000, v4
	s_nop 1
	v_addc_co_u32_e32 v5, vcc, 0, v5, vcc
	global_store_dwordx4 v[4:5], v[32:35], off
	s_add_i32 s13, s13, 32
	s_cmp_ge_i32 s13, s12
	s_cbranch_scc0 .LBB6_1208

.LBB6_1307:
	v_readlane_b32 s6, v254, 13
	v_readlane_b32 s7, v254, 14
	s_waitcnt vmcnt(0)
	v_mov_b32_e32 v167, v0
	s_waitcnt lgkmcnt(0)
	s_barrier
	s_max_i32 s36, s90, 0
	v_readfirstlane_b32 s0, v167
	s_ashr_i32 s67, s0, 6
	v_readlane_b32 s0, v254, 60
	s_lshl_b32 s81, s67, 14
	v_readlane_b32 s1, v254, 61
	v_and_b32_e32 v166, 63, v167
	s_add_i32 s66, s81, 0
	s_mov_b64 s[2:3], -1
	s_and_b64 vcc, exec, s[0:1]
	s_cbranch_vccz .LBB6_1319
	s_min_i32 s28, s91, 0xdc00
	s_cmp_le_i32 s28, s36
	s_cbranch_scc1 .LBB6_1313
	s_sub_i32 s0, s28, s36
	s_mov_b32 s2, 18
	s_cmp_lt_i32 s0, 32
	s_cbranch_scc1 .LBB6_1313
	s_add_i32 s29, s67, s36
	s_cmp_ge_i32 s29, s28
	s_cbranch_scc1 .LBB6_1313
	s_ashr_i32 s3, s2, 31
	s_lshl_b64 s[0:1], s[2:3], 3
	s_add_u32 s0, s76, s0
	s_addc_u32 s1, s77, s1
	s_load_dwordx2 s[0:1], s[0:1], 0x0
	v_lshrrev_b32_e32 v4, 3, v166
	v_lshlrev_b32_e32 v2, 2, v166
	v_mul_u32_u24_e32 v5, 0x2c00, v4
	v_and_b32_e32 v6, 28, v2
	s_waitcnt lgkmcnt(0)
	s_add_u32 s30, s0, 0x10800000
	v_or_b32_e32 v2, v5, v6
	v_lshl_add_u32 v5, v6, 2, s66
	v_lshlrev_b32_e32 v6, 5, v166
	s_addc_u32 s31, s1, 0
	v_lshrrev_b32_e32 v135, 2, v166
	v_lshlrev_b32_e32 v132, 4, v166
	v_and_b32_e32 v132, 48, v132
	s_add_u32 s34, s6, 0x85280000
	v_mul_u32_u24_e32 v4, 0x84, v4
	v_mul_u32_u24_e32 v6, 0x84, v132
	v_lshlrev_b32_e32 v7, 2, v135
	v_and_b32_e32 v134, 31, v167
	s_addc_u32 s35, s7, 0
	v_lshlrev_b32_e32 v2, 2, v2
	v_add3_u32 v136, s66, v6, v7
	v_mov_b32_e32 v133, v3
	v_add_u32_e32 v137, v5, v4
.LBB6_1312:
	s_mul_hi_i32 s0, s29, 0x2e8ba2e9
	s_lshr_b32 s1, s0, 31
	s_ashr_i32 s26, s0, 11
	s_add_i32 s26, s26, s1
	s_mul_i32 s0, s26, 0xffffd400
	s_add_i32 s0, s0, s29
	s_ashr_i32 s0, s0, 1
	s_and_b32 s1, s0, -8
	s_and_b32 s0, s29, 7
	s_or_b32 s1, s1, s0
	s_mul_hi_i32 s2, s1, 0x2e8ba2e9
	s_lshr_b32 s3, s2, 31
	s_ashr_i32 s2, s2, 6
	s_add_i32 s2, s2, s3
	s_mul_i32 s3, s2, 0xfffffea0
	s_add_i32 s3, s3, s1
	s_lshl_b32 s1, s2, 7
	s_lshl_b32 s2, s29, 3
	s_and_b32 s12, s2, 64
	s_lshl_b32 s58, s3, 5
	s_or_b32 s24, s1, s12
	s_mul_i32 s2, s26, 0x5800000
	s_mul_hi_i32 s1, s26, 0x5800000
	s_add_u32 s4, s30, s2
	s_addc_u32 s1, s31, s1
	s_and_b32 s2, s58, 0xe0
	s_cmpk_lt_u32 s2, 0x80
	v_or_b32_e32 v4, s2, v134
	s_cselect_b64 vcc, -1, 0
	s_lshl_b32 s2, s3, 4
	s_and_b32 s2, s2, 0xffffff80
	v_or_b32_e32 v5, s2, v4
	s_addk_i32 s2, 0x1580
	v_add_u32_e32 v4, s2, v4
	v_cndmask_b32_e32 v4, v4, v5, vcc
	s_ashr_i32 s25, s24, 31
	v_readfirstlane_b32 s2, v4
	s_andn2_b32 s2, s2, 31
	s_mul_i32 s5, s24, 0xb000
	s_mul_hi_i32 s3, s24, 0xb000
	s_add_u32 s4, s4, s5
	s_addc_u32 s1, s1, s3
	s_ashr_i32 s3, s2, 31
	s_lshl_b64 s[2:3], s[2:3], 2
	s_add_u32 s2, s4, s2
	s_addc_u32 s3, s1, s3
	s_mov_b64 s[4:5], s[2:3]
	v_mov_b32_e32 v138, v3
	v_lshl_add_u64 v[4:5], s[4:5], 0, v[2:3]
	s_add_u32 s4, s2, 0x58000
	s_addc_u32 s5, s3, 0
	global_load_dwordx4 v[128:131], v[4:5], off nt
	v_mov_b32_e32 v139, v3
	v_lshl_add_u64 v[4:5], s[4:5], 0, v[2:3]
	s_add_u32 s4, s2, 0xb0000
	s_addc_u32 s5, s3, 0
	global_load_dwordx4 v[124:127], v[4:5], off nt
	s_nop 0
	v_lshl_add_u64 v[4:5], s[4:5], 0, v[2:3]
	s_add_u32 s4, s2, 0x108000
	s_addc_u32 s5, s3, 0
	global_load_dwordx4 v[120:123], v[4:5], off nt
	s_nop 0
	v_lshl_add_u64 v[4:5], s[4:5], 0, v[2:3]
	s_add_u32 s4, s2, 0x160000
	s_addc_u32 s5, s3, 0
	global_load_dwordx4 v[116:119], v[4:5], off nt
	s_nop 0
	v_lshl_add_u64 v[4:5], s[4:5], 0, v[2:3]
	s_add_u32 s4, s2, 0x1b8000
	s_addc_u32 s5, s3, 0
	global_load_dwordx4 v[112:115], v[4:5], off nt
	s_nop 0
	v_lshl_add_u64 v[4:5], s[4:5], 0, v[2:3]
	s_add_u32 s4, s2, 0x210000
	s_addc_u32 s5, s3, 0
	s_add_u32 s2, s2, 0x268000
	global_load_dwordx4 v[108:111], v[4:5], off nt
	s_addc_u32 s3, s3, 0
	v_lshl_add_u64 v[4:5], s[4:5], 0, v[2:3]
	global_load_dwordx4 v[104:107], v[4:5], off nt
	s_add_i32 s1, s29, 8
	v_lshl_add_u64 v[4:5], s[2:3], 0, v[2:3]
	s_mul_hi_i32 s2, s1, 0x2e8ba2e9
	s_lshr_b32 s3, s2, 31
	s_ashr_i32 s50, s2, 11
	s_add_i32 s50, s50, s3
	s_mul_i32 s2, s50, 0xffffd400
	s_add_i32 s2, s2, s1
	s_ashr_i32 s2, s2, 1
	s_and_b32 s2, s2, -8
	s_or_b32 s2, s2, s0
	s_mul_hi_i32 s3, s2, 0x2e8ba2e9
	s_lshr_b32 s4, s3, 31
	s_ashr_i32 s3, s3, 6
	s_add_i32 s3, s3, s4
	s_mul_i32 s4, s3, 0xfffffea0
	s_lshl_b32 s1, s1, 3
	s_add_i32 s4, s4, s2
	s_lshl_b32 s2, s3, 7
	s_and_b32 s1, s1, 64
	s_lshl_b32 s51, s4, 5
	s_or_b32 s22, s2, s1
	s_mul_i32 s2, s50, 0x5800000
	s_mul_hi_i32 s1, s50, 0x5800000
	s_add_u32 s3, s30, s2
	s_addc_u32 s1, s31, s1
	s_and_b32 s2, s51, 0xe0
	s_cmpk_lt_u32 s2, 0x80
	global_load_dwordx4 v[100:103], v[4:5], off nt
	v_or_b32_e32 v4, s2, v134
	s_cselect_b64 vcc, -1, 0
	s_lshl_b32 s2, s4, 4
	s_and_b32 s2, s2, 0xffffff80
	v_or_b32_e32 v5, s2, v4
	s_addk_i32 s2, 0x1580
	v_add_u32_e32 v4, s2, v4
	v_cndmask_b32_e32 v4, v4, v5, vcc
	s_ashr_i32 s23, s22, 31
	v_readfirstlane_b32 s2, v4
	s_andn2_b32 s2, s2, 31
	s_mul_i32 s5, s22, 0xb000
	s_mul_hi_i32 s4, s22, 0xb000
	s_add_u32 s5, s3, s5
	s_addc_u32 s1, s1, s4
	s_ashr_i32 s3, s2, 31
	s_lshl_b64 s[2:3], s[2:3], 2
	s_add_u32 s2, s5, s2
	s_addc_u32 s3, s1, s3
	s_mov_b64 s[4:5], s[2:3]
	s_nop 0
	v_lshl_add_u64 v[4:5], s[4:5], 0, v[2:3]
	s_add_u32 s4, s2, 0x58000
	s_addc_u32 s5, s3, 0
	global_load_dwordx4 v[68:71], v[4:5], off nt
	s_nop 0
	v_lshl_add_u64 v[4:5], s[4:5], 0, v[2:3]
	s_add_u32 s4, s2, 0xb0000
	s_addc_u32 s5, s3, 0
	global_load_dwordx4 v[72:75], v[4:5], off nt
	s_nop 0
	v_lshl_add_u64 v[4:5], s[4:5], 0, v[2:3]
	s_add_u32 s4, s2, 0x108000
	s_addc_u32 s5, s3, 0
	global_load_dwordx4 v[76:79], v[4:5], off nt
	s_nop 0
	v_lshl_add_u64 v[4:5], s[4:5], 0, v[2:3]
	s_add_u32 s4, s2, 0x160000
	s_addc_u32 s5, s3, 0
	global_load_dwordx4 v[80:83], v[4:5], off nt
	s_nop 0
	v_lshl_add_u64 v[4:5], s[4:5], 0, v[2:3]
	s_add_u32 s4, s2, 0x1b8000
	s_addc_u32 s5, s3, 0
	global_load_dwordx4 v[84:87], v[4:5], off nt
	s_nop 0
	v_lshl_add_u64 v[4:5], s[4:5], 0, v[2:3]
	s_add_u32 s4, s2, 0x210000
	s_addc_u32 s5, s3, 0
	s_add_u32 s2, s2, 0x268000
	global_load_dwordx4 v[88:91], v[4:5], off nt
	s_addc_u32 s3, s3, 0
	v_lshl_add_u64 v[4:5], s[4:5], 0, v[2:3]
	global_load_dwordx4 v[92:95], v[4:5], off nt
	s_add_i32 s1, s29, 16
	v_lshl_add_u64 v[4:5], s[2:3], 0, v[2:3]
	s_mul_hi_i32 s2, s1, 0x2e8ba2e9
	s_lshr_b32 s3, s2, 31
	s_ashr_i32 s48, s2, 11
	s_add_i32 s48, s48, s3
	s_mul_i32 s2, s48, 0xffffd400
	s_add_i32 s2, s2, s1
	s_ashr_i32 s1, s2, 1
	s_and_b32 s1, s1, -8
	s_or_b32 s1, s1, s0
	s_mul_hi_i32 s2, s1, 0x2e8ba2e9
	s_lshr_b32 s3, s2, 31
	s_ashr_i32 s2, s2, 6
	s_add_i32 s2, s2, s3
	s_mul_i32 s3, s2, 0xfffffea0
	s_add_i32 s3, s3, s1
	s_lshl_b32 s1, s2, 7
	s_lshl_b32 s49, s3, 5
	s_or_b32 s4, s1, s12
	s_mul_i32 s2, s48, 0x5800000
	s_mul_hi_i32 s1, s48, 0x5800000
	s_add_u32 s12, s30, s2
	s_addc_u32 s1, s31, s1
	s_and_b32 s2, s49, 0xe0
	s_cmpk_lt_u32 s2, 0x80
	global_load_dwordx4 v[96:99], v[4:5], off nt
	v_or_b32_e32 v4, s2, v134
	s_cselect_b64 vcc, -1, 0
	s_lshl_b32 s2, s3, 4
	s_and_b32 s2, s2, 0xffffff80
	v_or_b32_e32 v5, s2, v4
	s_addk_i32 s2, 0x1580
	v_add_u32_e32 v4, s2, v4
	v_cndmask_b32_e32 v4, v4, v5, vcc
	s_ashr_i32 s5, s4, 31
	v_readfirstlane_b32 s2, v4
	s_andn2_b32 s2, s2, 31
	s_mul_i32 s13, s4, 0xb000
	s_mul_hi_i32 s3, s4, 0xb000
	s_add_u32 s12, s12, s13
	s_addc_u32 s1, s1, s3
	s_ashr_i32 s3, s2, 31
	s_lshl_b64 s[2:3], s[2:3], 2
	s_add_u32 s2, s12, s2
	s_addc_u32 s3, s1, s3
	s_mov_b64 s[12:13], s[2:3]
	s_nop 0
	v_lshl_add_u64 v[4:5], s[12:13], 0, v[2:3]
	s_add_u32 s12, s2, 0x58000
	s_addc_u32 s13, s3, 0
	global_load_dwordx4 v[36:39], v[4:5], off nt
	s_nop 0
	v_lshl_add_u64 v[4:5], s[12:13], 0, v[2:3]
	s_add_u32 s12, s2, 0xb0000
	s_addc_u32 s13, s3, 0
	global_load_dwordx4 v[40:43], v[4:5], off nt
	s_nop 0
	v_lshl_add_u64 v[4:5], s[12:13], 0, v[2:3]
	s_add_u32 s12, s2, 0x108000
	s_addc_u32 s13, s3, 0
	global_load_dwordx4 v[44:47], v[4:5], off nt
	s_nop 0
	v_lshl_add_u64 v[4:5], s[12:13], 0, v[2:3]
	s_add_u32 s12, s2, 0x160000
	s_addc_u32 s13, s3, 0
	global_load_dwordx4 v[48:51], v[4:5], off nt
	s_nop 0
	v_lshl_add_u64 v[4:5], s[12:13], 0, v[2:3]
	s_add_u32 s12, s2, 0x1b8000
	s_addc_u32 s13, s3, 0
	global_load_dwordx4 v[52:55], v[4:5], off nt
	s_nop 0
	v_lshl_add_u64 v[4:5], s[12:13], 0, v[2:3]
	s_add_u32 s12, s2, 0x210000
	s_addc_u32 s13, s3, 0
	s_add_u32 s2, s2, 0x268000
	global_load_dwordx4 v[56:59], v[4:5], off nt
	s_addc_u32 s3, s3, 0
	v_lshl_add_u64 v[4:5], s[12:13], 0, v[2:3]
	global_load_dwordx4 v[60:63], v[4:5], off nt
	s_add_i32 s1, s29, 24
	v_lshl_add_u64 v[4:5], s[2:3], 0, v[2:3]
	s_mul_hi_i32 s2, s1, 0x2e8ba2e9
	s_lshr_b32 s3, s2, 31
	s_ashr_i32 s37, s2, 11
	s_add_i32 s37, s37, s3
	s_mul_i32 s2, s37, 0xffffd400
	s_add_i32 s2, s2, s1
	s_ashr_i32 s2, s2, 1
	s_and_b32 s2, s2, -8
	s_or_b32 s0, s2, s0
	s_mul_hi_i32 s2, s0, 0x2e8ba2e9
	s_lshr_b32 s3, s2, 31
	s_ashr_i32 s2, s2, 6
	s_add_i32 s2, s2, s3
	s_mul_i32 s3, s2, 0xfffffea0
	s_lshl_b32 s1, s1, 3
	s_add_i32 s3, s3, s0
	s_lshl_b32 s0, s2, 7
	s_and_b32 s1, s1, 64
	s_lshl_b32 s47, s3, 5
	s_or_b32 s2, s0, s1
	s_mul_i32 s1, s37, 0x5800000
	s_mul_hi_i32 s0, s37, 0x5800000
	s_add_u32 s1, s30, s1
	s_addc_u32 s12, s31, s0
	s_and_b32 s0, s47, 0xe0
	s_cmpk_lt_u32 s0, 0x80
	global_load_dwordx4 v[64:67], v[4:5], off nt
	v_or_b32_e32 v4, s0, v134
	s_cselect_b64 vcc, -1, 0
	s_lshl_b32 s0, s3, 4
	s_and_b32 s0, s0, 0xffffff80
	v_or_b32_e32 v5, s0, v4
	s_addk_i32 s0, 0x1580
	v_add_u32_e32 v4, s0, v4
	v_cndmask_b32_e32 v4, v4, v5, vcc
	s_ashr_i32 s3, s2, 31
	v_readfirstlane_b32 s0, v4
	s_andn2_b32 s0, s0, 31
	s_mul_i32 s27, s2, 0xb000
	s_mul_hi_i32 s13, s2, 0xb000
	s_add_u32 s27, s1, s27
	s_addc_u32 s12, s12, s13
	s_ashr_i32 s1, s0, 31
	s_lshl_b64 s[0:1], s[0:1], 2
	s_add_u32 s0, s27, s0
	s_addc_u32 s1, s12, s1
	s_mov_b64 s[12:13], s[0:1]
	s_nop 0
	v_lshl_add_u64 v[4:5], s[12:13], 0, v[2:3]
	s_add_u32 s12, s0, 0x58000
	s_addc_u32 s13, s1, 0
	global_load_dwordx4 v[4:7], v[4:5], off nt
	s_nop 0
	v_lshl_add_u64 v[8:9], s[12:13], 0, v[2:3]
	s_add_u32 s12, s0, 0xb0000
	s_addc_u32 s13, s1, 0
	global_load_dwordx4 v[8:11], v[8:9], off nt
	s_nop 0
	v_lshl_add_u64 v[12:13], s[12:13], 0, v[2:3]
	s_add_u32 s12, s0, 0x108000
	s_addc_u32 s13, s1, 0
	global_load_dwordx4 v[12:15], v[12:13], off nt
	s_nop 0
	v_lshl_add_u64 v[16:17], s[12:13], 0, v[2:3]
	s_add_u32 s12, s0, 0x160000
	s_addc_u32 s13, s1, 0
	global_load_dwordx4 v[16:19], v[16:17], off nt
	s_nop 0
	v_lshl_add_u64 v[20:21], s[12:13], 0, v[2:3]
	s_add_u32 s12, s0, 0x1b8000
	s_addc_u32 s13, s1, 0
	global_load_dwordx4 v[20:23], v[20:21], off nt
	s_nop 0
	v_lshl_add_u64 v[24:25], s[12:13], 0, v[2:3]
	s_add_u32 s12, s0, 0x210000
	s_addc_u32 s13, s1, 0
	s_add_u32 s0, s0, 0x268000
	global_load_dwordx4 v[24:27], v[24:25], off nt
	s_addc_u32 s1, s1, 0
	v_lshl_add_u64 v[28:29], s[12:13], 0, v[2:3]
	global_load_dwordx4 v[28:31], v[28:29], off nt
	s_nop 0
	v_lshl_add_u64 v[32:33], s[0:1], 0, v[2:3]
	global_load_dwordx4 v[32:35], v[32:33], off nt
	s_waitcnt vmcnt(31)
	ds_write2_b32 v137, v128, v129 offset1:1
	ds_write2_b32 v137, v130, v131 offset0:2 offset1:3
	v_add_u32_e32 v128, 0x420, v137
	s_waitcnt vmcnt(30)
	ds_write2_b32 v128, v124, v125 offset1:1
	v_add_u32_e32 v125, 0x840, v137
	s_waitcnt vmcnt(29)
	ds_write2_b32 v125, v120, v121 offset1:1
	v_add_u32_e32 v121, 0xc60, v137
	s_waitcnt vmcnt(28)
	ds_write2_b32 v121, v116, v117 offset1:1
	v_add_u32_e32 v117, 0x1080, v137
	s_waitcnt vmcnt(27)
	ds_write2_b32 v117, v112, v113 offset1:1
	v_add_u32_e32 v113, 0x14a0, v137
	s_waitcnt vmcnt(26)
	ds_write2_b32 v113, v108, v109 offset1:1
	v_add_u32_e32 v109, 0x18c0, v137
	s_waitcnt vmcnt(25)
	ds_write2_b32 v109, v104, v105 offset1:1
	v_add_u32_e32 v104, 0x18c8, v137
	v_add_u32_e32 v124, 0x428, v137
	v_add_u32_e32 v120, 0x848, v137
	v_add_u32_e32 v116, 0xc68, v137
	v_add_u32_e32 v112, 0x1088, v137
	v_add_u32_e32 v108, 0x14a8, v137
	ds_write2_b32 v104, v106, v107 offset1:1
	v_add_u32_e32 v105, 0x1ce0, v137
	v_add_u32_e32 v106, 0x1ce8, v137
	ds_write2_b32 v124, v126, v127 offset1:1
	ds_write2_b32 v120, v122, v123 offset1:1
	ds_write2_b32 v116, v118, v119 offset1:1
	ds_write2_b32 v112, v114, v115 offset1:1
	ds_write2_b32 v108, v110, v111 offset1:1
	s_waitcnt vmcnt(24)
	ds_write2_b32 v105, v100, v101 offset1:1
	ds_write2_b32 v106, v102, v103 offset1:1
	ds_read2_b32 v[110:111], v136 offset1:33
	ds_read2_b32 v[114:115], v136 offset0:66 offset1:99
	ds_read2_b32 v[118:119], v136 offset0:132 offset1:165
	ds_read2_b32 v[122:123], v136 offset0:198 offset1:231
	v_add_u32_e32 v102, 0x400, v136
	s_waitcnt lgkmcnt(3)
	v_mul_f32_e32 v101, 0x42800000, v110
	v_mul_f32_e32 v110, 0x42800000, v111
	v_mov_b32_e32 v103, v136
	v_cvt_pk_fp8_f32 v138, v101, v110
	ds_read2_b32 v[126:127], v102 offset0:8 offset1:41
	ds_read2_b32 v[130:131], v102 offset0:74 offset1:107
	ds_read2_b32 v[146:147], v102 offset0:140 offset1:173
	ds_read2_b32 v[148:149], v102 offset0:206 offset1:239
	ds_read2_b32 v[140:141], v103 offset0:16 offset1:49
	ds_read2_b32 v[142:143], v103 offset0:82 offset1:115
	ds_read2_b32 v[144:145], v103 offset0:148 offset1:181
	ds_read2_b32 v[150:151], v103 offset0:214 offset1:247
	s_waitcnt lgkmcnt(10)
	v_mul_f32_e32 v111, 0x42800000, v114
	v_mul_f32_e32 v114, 0x42800000, v115
	v_cvt_pk_fp8_f32 v138, v111, v114 op_sel:[0,0,1]
	s_waitcnt lgkmcnt(3)
	v_mul_f32_e32 v101, 0x42800000, v140
	v_mul_f32_e32 v110, 0x42800000, v141
	s_waitcnt lgkmcnt(2)
	v_mul_f32_e32 v111, 0x42800000, v142
	v_mov_b32_e32 v142, v3
	v_add_u32_e32 v107, 0x400, v136
	v_cvt_pk_fp8_f32 v142, v101, v110
	v_mul_f32_e32 v101, 0x42800000, v118
	v_mul_f32_e32 v110, 0x42800000, v119
	ds_read2_b32 v[152:153], v107 offset0:24 offset1:57
	ds_read2_b32 v[154:155], v107 offset0:90 offset1:123
	ds_read2_b32 v[156:157], v107 offset0:156 offset1:189
	ds_read2_b32 v[158:159], v107 offset0:222 offset1:255
	v_mul_f32_e32 v114, 0x42800000, v143
	v_cvt_pk_fp8_f32 v139, v101, v110
	s_waitcnt lgkmcnt(5)
	v_mul_f32_e32 v101, 0x42800000, v144
	v_mul_f32_e32 v110, 0x42800000, v145
	v_mov_b32_e32 v143, v3
	v_cvt_pk_fp8_f32 v143, v101, v110
	v_mul_f32_e32 v101, 0x42800000, v126
	v_mul_f32_e32 v110, 0x42800000, v127
	v_mov_b32_e32 v140, v3
	v_cvt_pk_fp8_f32 v140, v101, v110
	s_waitcnt lgkmcnt(3)
	v_mul_f32_e32 v101, 0x42800000, v152
	v_mul_f32_e32 v110, 0x42800000, v153
	v_mov_b32_e32 v144, v3
	v_cvt_pk_fp8_f32 v142, v111, v114 op_sel:[0,0,1]
	v_mul_f32_e32 v111, 0x42800000, v122
	v_mul_f32_e32 v114, 0x42800000, v123
	v_cvt_pk_fp8_f32 v144, v101, v110
	v_mul_f32_e32 v101, 0x42800000, v146
	v_mul_f32_e32 v110, 0x42800000, v147
	v_mov_b32_e32 v141, v3
	v_cvt_pk_fp8_f32 v139, v111, v114 op_sel:[0,0,1]
	v_mul_f32_e32 v111, 0x42800000, v150
	v_mul_f32_e32 v114, 0x42800000, v151
	v_cvt_pk_fp8_f32 v141, v101, v110
	s_waitcnt lgkmcnt(1)
	v_mul_f32_e32 v101, 0x42800000, v156
	v_mul_f32_e32 v110, 0x42800000, v157
	v_mov_b32_e32 v145, v3
	v_cvt_pk_fp8_f32 v143, v111, v114 op_sel:[0,0,1]
	v_mul_f32_e32 v111, 0x42800000, v130
	v_mul_f32_e32 v114, 0x42800000, v131
	v_cvt_pk_fp8_f32 v145, v101, v110
	s_mul_hi_i32 s0, s26, 0x1600000
	s_mul_i32 s26, s26, 0x1600000
	v_or_b32_e32 v100, s58, v135
	v_cvt_pk_fp8_f32 v140, v111, v114 op_sel:[0,0,1]
	v_mul_f32_e32 v111, 0x42800000, v154
	v_mul_f32_e32 v114, 0x42800000, v155
	s_add_u32 s26, s34, s26
	v_cvt_pk_fp8_f32 v144, v111, v114 op_sel:[0,0,1]
	v_mul_f32_e32 v111, 0x42800000, v148
	v_mul_f32_e32 v114, 0x42800000, v149
	v_ashrrev_i32_e32 v101, 31, v100
	s_addc_u32 s27, s35, s0
	v_cvt_pk_fp8_f32 v141, v111, v114 op_sel:[0,0,1]
	s_waitcnt lgkmcnt(0)
	v_mul_f32_e32 v111, 0x42800000, v158
	v_mul_f32_e32 v114, 0x42800000, v159
	v_lshlrev_b64 v[100:101], 11, v[100:101]
	v_cvt_pk_fp8_f32 v145, v111, v114 op_sel:[0,0,1]
	v_lshl_add_u64 v[100:101], s[26:27], 0, v[100:101]
	v_lshl_add_u64 v[100:101], v[100:101], 0, s[24:25]
	v_lshl_add_u64 v[100:101], v[100:101], 0, v[132:133]
	global_store_dwordx4 v[100:101], v[138:141], off
	s_nop 1
	v_add_co_u32_e32 v100, vcc, 0x8000, v100
	s_nop 1
	v_addc_co_u32_e32 v101, vcc, 0, v101, vcc
	global_store_dwordx4 v[100:101], v[142:145], off
	s_waitcnt vmcnt(25)
	ds_write2_b32 v137, v68, v69 offset1:1
	ds_write2_b32 v137, v70, v71 offset0:2 offset1:3
	s_waitcnt vmcnt(24)
	ds_write2_b32 v128, v72, v73 offset1:1
	ds_write2_b32 v124, v74, v75 offset1:1
	s_waitcnt vmcnt(23)
	ds_write2_b32 v125, v76, v77 offset1:1
	ds_write2_b32 v120, v78, v79 offset1:1
	s_waitcnt vmcnt(22)
	ds_write2_b32 v121, v80, v81 offset1:1
	ds_write2_b32 v116, v82, v83 offset1:1
	s_waitcnt vmcnt(21)
	ds_write2_b32 v117, v84, v85 offset1:1
	ds_write2_b32 v112, v86, v87 offset1:1
	s_waitcnt vmcnt(20)
	ds_write2_b32 v113, v88, v89 offset1:1
	ds_write2_b32 v108, v90, v91 offset1:1
	s_waitcnt vmcnt(19)
	ds_write2_b32 v109, v92, v93 offset1:1
	ds_write2_b32 v104, v94, v95 offset1:1
	s_waitcnt vmcnt(18)
	ds_write2_b32 v105, v96, v97 offset1:1
	ds_write2_b32 v106, v98, v99 offset1:1
	ds_read2_b32 v[94:95], v136 offset1:33
	ds_read2_b32 v[96:97], v136 offset0:66 offset1:99
	ds_read2_b32 v[92:93], v136 offset0:132 offset1:165
	ds_read2_b32 v[90:91], v136 offset0:198 offset1:231
	ds_read2_b32 v[84:85], v102 offset0:8 offset1:41
	ds_read2_b32 v[82:83], v102 offset0:74 offset1:107
	ds_read2_b32 v[76:77], v102 offset0:140 offset1:173
	ds_read2_b32 v[74:75], v102 offset0:206 offset1:239
	ds_read2_b32 v[98:99], v103 offset0:16 offset1:49
	ds_read2_b32 v[100:101], v103 offset0:82 offset1:115
	ds_read2_b32 v[88:89], v103 offset0:148 offset1:181
	ds_read2_b32 v[86:87], v103 offset0:214 offset1:247
	ds_read2_b32 v[80:81], v107 offset0:24 offset1:57
	ds_read2_b32 v[78:79], v107 offset0:90 offset1:123
	ds_read2_b32 v[72:73], v107 offset0:156 offset1:189
	ds_read2_b32 v[70:71], v107 offset0:222 offset1:255
	s_waitcnt lgkmcnt(14)
	v_mul_f32_e32 v69, 0x42800000, v94
	v_mul_f32_e32 v95, 0x42800000, v95
	v_mov_b32_e32 v94, v3
	v_cvt_pk_fp8_f32 v94, v69, v95
	s_waitcnt lgkmcnt(7)
	v_mul_f32_e32 v69, 0x42800000, v98
	v_mul_f32_e32 v95, 0x42800000, v99
	v_mov_b32_e32 v98, v3
	v_cvt_pk_fp8_f32 v98, v69, v95
	v_mul_f32_e32 v96, 0x42800000, v96
	v_mul_f32_e32 v97, 0x42800000, v97
	v_mul_f32_e32 v69, 0x42800000, v92
	v_mul_f32_e32 v92, 0x42800000, v93
	v_mov_b32_e32 v95, v3
	v_cvt_pk_fp8_f32 v94, v96, v97 op_sel:[0,0,1]
	s_waitcnt lgkmcnt(6)
	v_mul_f32_e32 v96, 0x42800000, v100
	v_mul_f32_e32 v97, 0x42800000, v101
	v_cvt_pk_fp8_f32 v95, v69, v92
	s_waitcnt lgkmcnt(5)
	v_mul_f32_e32 v69, 0x42800000, v88
	v_mul_f32_e32 v88, 0x42800000, v89
	v_mov_b32_e32 v99, v3
	v_cvt_pk_fp8_f32 v98, v96, v97 op_sel:[0,0,1]
	v_cvt_pk_fp8_f32 v99, v69, v88
	v_mul_f32_e32 v69, 0x42800000, v84
	v_mul_f32_e32 v84, 0x42800000, v85
	v_mov_b32_e32 v96, v3
	v_cvt_pk_fp8_f32 v96, v69, v84
	s_waitcnt lgkmcnt(3)
	v_mul_f32_e32 v69, 0x42800000, v80
	v_mul_f32_e32 v80, 0x42800000, v81
	v_mov_b32_e32 v100, v3
	v_cvt_pk_fp8_f32 v100, v69, v80
	v_mul_f32_e32 v69, 0x42800000, v76
	v_mul_f32_e32 v76, 0x42800000, v77
	v_mov_b32_e32 v97, v3
	v_cvt_pk_fp8_f32 v97, v69, v76
	s_waitcnt lgkmcnt(1)
	v_mul_f32_e32 v69, 0x42800000, v72
	v_mul_f32_e32 v72, 0x42800000, v73
	v_mov_b32_e32 v101, v3
	v_cvt_pk_fp8_f32 v101, v69, v72
	s_mul_hi_i32 s0, s50, 0x1600000
	s_mul_i32 s50, s50, 0x1600000
	v_or_b32_e32 v68, s51, v135
	s_add_u32 s24, s34, s50
	v_mul_f32_e32 v90, 0x42800000, v90
	v_mul_f32_e32 v91, 0x42800000, v91
	v_mul_f32_e32 v82, 0x42800000, v82
	v_mul_f32_e32 v83, 0x42800000, v83
	v_mul_f32_e32 v74, 0x42800000, v74
	v_mul_f32_e32 v75, 0x42800000, v75
	v_ashrrev_i32_e32 v69, 31, v68
	s_addc_u32 s25, s35, s0
	v_cvt_pk_fp8_f32 v95, v90, v91 op_sel:[0,0,1]
	v_mul_f32_e32 v86, 0x42800000, v86
	v_mul_f32_e32 v87, 0x42800000, v87
	v_cvt_pk_fp8_f32 v96, v82, v83 op_sel:[0,0,1]
	v_mul_f32_e32 v78, 0x42800000, v78
	v_mul_f32_e32 v79, 0x42800000, v79
	v_cvt_pk_fp8_f32 v97, v74, v75 op_sel:[0,0,1]
	s_waitcnt lgkmcnt(0)
	v_mul_f32_e32 v70, 0x42800000, v70
	v_mul_f32_e32 v71, 0x42800000, v71
	v_lshlrev_b64 v[68:69], 11, v[68:69]
	v_cvt_pk_fp8_f32 v99, v86, v87 op_sel:[0,0,1]
	v_cvt_pk_fp8_f32 v100, v78, v79 op_sel:[0,0,1]
	v_cvt_pk_fp8_f32 v101, v70, v71 op_sel:[0,0,1]
	v_lshl_add_u64 v[68:69], s[24:25], 0, v[68:69]
	v_lshl_add_u64 v[68:69], v[68:69], 0, s[22:23]
	v_lshl_add_u64 v[68:69], v[68:69], 0, v[132:133]
	global_store_dwordx4 v[68:69], v[94:97], off
	s_nop 1
	v_add_co_u32_e32 v68, vcc, 0x8000, v68
	s_nop 1
	v_addc_co_u32_e32 v69, vcc, 0, v69, vcc
	global_store_dwordx4 v[68:69], v[98:101], off
	s_waitcnt vmcnt(19)
	ds_write2_b32 v137, v36, v37 offset1:1
	ds_write2_b32 v137, v38, v39 offset0:2 offset1:3
	s_waitcnt vmcnt(18)
	ds_write2_b32 v128, v40, v41 offset1:1
	ds_write2_b32 v124, v42, v43 offset1:1
	s_waitcnt vmcnt(17)
	ds_write2_b32 v125, v44, v45 offset1:1
	ds_write2_b32 v120, v46, v47 offset1:1
	s_waitcnt vmcnt(16)
	ds_write2_b32 v121, v48, v49 offset1:1
	ds_write2_b32 v116, v50, v51 offset1:1
	s_waitcnt vmcnt(15)
	ds_write2_b32 v117, v52, v53 offset1:1
	ds_write2_b32 v112, v54, v55 offset1:1
	s_waitcnt vmcnt(14)
	ds_write2_b32 v113, v56, v57 offset1:1
	ds_write2_b32 v108, v58, v59 offset1:1
	s_waitcnt vmcnt(13)
	ds_write2_b32 v109, v60, v61 offset1:1
	ds_write2_b32 v104, v62, v63 offset1:1
	s_waitcnt vmcnt(12)
	ds_write2_b32 v105, v64, v65 offset1:1
	ds_write2_b32 v106, v66, v67 offset1:1
	ds_read2_b32 v[62:63], v136 offset1:33
	ds_read2_b32 v[64:65], v136 offset0:66 offset1:99
	ds_read2_b32 v[60:61], v136 offset0:132 offset1:165
	ds_read2_b32 v[58:59], v136 offset0:198 offset1:231
	ds_read2_b32 v[52:53], v102 offset0:8 offset1:41
	ds_read2_b32 v[50:51], v102 offset0:74 offset1:107
	ds_read2_b32 v[44:45], v102 offset0:140 offset1:173
	ds_read2_b32 v[42:43], v102 offset0:206 offset1:239
	ds_read2_b32 v[66:67], v103 offset0:16 offset1:49
	ds_read2_b32 v[68:69], v103 offset0:82 offset1:115
	ds_read2_b32 v[56:57], v103 offset0:148 offset1:181
	ds_read2_b32 v[54:55], v103 offset0:214 offset1:247
	ds_read2_b32 v[48:49], v107 offset0:24 offset1:57
	ds_read2_b32 v[46:47], v107 offset0:90 offset1:123
	ds_read2_b32 v[40:41], v107 offset0:156 offset1:189
	ds_read2_b32 v[38:39], v107 offset0:222 offset1:255
	s_waitcnt lgkmcnt(14)
	v_mul_f32_e32 v37, 0x42800000, v62
	v_mul_f32_e32 v63, 0x42800000, v63
	v_mov_b32_e32 v62, v3
	v_cvt_pk_fp8_f32 v62, v37, v63
	s_waitcnt lgkmcnt(7)
	v_mul_f32_e32 v37, 0x42800000, v66
	v_mul_f32_e32 v63, 0x42800000, v67
	v_mov_b32_e32 v66, v3
	v_cvt_pk_fp8_f32 v66, v37, v63
	v_mul_f32_e32 v64, 0x42800000, v64
	v_mul_f32_e32 v65, 0x42800000, v65
	v_mul_f32_e32 v37, 0x42800000, v60
	v_mul_f32_e32 v60, 0x42800000, v61
	v_mov_b32_e32 v63, v3
	v_cvt_pk_fp8_f32 v62, v64, v65 op_sel:[0,0,1]
	s_waitcnt lgkmcnt(6)
	v_mul_f32_e32 v64, 0x42800000, v68
	v_mul_f32_e32 v65, 0x42800000, v69
	v_cvt_pk_fp8_f32 v63, v37, v60
	s_waitcnt lgkmcnt(5)
	v_mul_f32_e32 v37, 0x42800000, v56
	v_mul_f32_e32 v56, 0x42800000, v57
	v_mov_b32_e32 v67, v3
	v_cvt_pk_fp8_f32 v66, v64, v65 op_sel:[0,0,1]
	v_cvt_pk_fp8_f32 v67, v37, v56
	v_mul_f32_e32 v37, 0x42800000, v52
	v_mul_f32_e32 v52, 0x42800000, v53
	v_mov_b32_e32 v64, v3
	v_cvt_pk_fp8_f32 v64, v37, v52
	s_waitcnt lgkmcnt(3)
	v_mul_f32_e32 v37, 0x42800000, v48
	v_mul_f32_e32 v48, 0x42800000, v49
	v_mov_b32_e32 v68, v3
	v_cvt_pk_fp8_f32 v68, v37, v48
	v_mul_f32_e32 v37, 0x42800000, v44
	v_mul_f32_e32 v44, 0x42800000, v45
	v_mov_b32_e32 v65, v3
	v_cvt_pk_fp8_f32 v65, v37, v44
	s_waitcnt lgkmcnt(1)
	v_mul_f32_e32 v37, 0x42800000, v40
	v_mul_f32_e32 v40, 0x42800000, v41
	v_mov_b32_e32 v69, v3
	v_cvt_pk_fp8_f32 v69, v37, v40
	s_mul_hi_i32 s0, s48, 0x1600000
	s_mul_i32 s48, s48, 0x1600000
	v_or_b32_e32 v36, s49, v135
	s_add_u32 s22, s34, s48
	v_mul_f32_e32 v58, 0x42800000, v58
	v_mul_f32_e32 v59, 0x42800000, v59
	v_mul_f32_e32 v50, 0x42800000, v50
	v_mul_f32_e32 v51, 0x42800000, v51
	v_mul_f32_e32 v42, 0x42800000, v42
	v_mul_f32_e32 v43, 0x42800000, v43
	v_ashrrev_i32_e32 v37, 31, v36
	s_addc_u32 s23, s35, s0
	v_cvt_pk_fp8_f32 v63, v58, v59 op_sel:[0,0,1]
	v_mul_f32_e32 v54, 0x42800000, v54
	v_mul_f32_e32 v55, 0x42800000, v55
	v_cvt_pk_fp8_f32 v64, v50, v51 op_sel:[0,0,1]
	v_mul_f32_e32 v46, 0x42800000, v46
	v_mul_f32_e32 v47, 0x42800000, v47
	v_cvt_pk_fp8_f32 v65, v42, v43 op_sel:[0,0,1]
	s_waitcnt lgkmcnt(0)
	v_mul_f32_e32 v38, 0x42800000, v38
	v_mul_f32_e32 v39, 0x42800000, v39
	v_lshlrev_b64 v[36:37], 11, v[36:37]
	v_cvt_pk_fp8_f32 v67, v54, v55 op_sel:[0,0,1]
	v_cvt_pk_fp8_f32 v68, v46, v47 op_sel:[0,0,1]
	v_cvt_pk_fp8_f32 v69, v38, v39 op_sel:[0,0,1]
	v_lshl_add_u64 v[36:37], s[22:23], 0, v[36:37]
	v_lshl_add_u64 v[36:37], v[36:37], 0, s[4:5]
	v_lshl_add_u64 v[36:37], v[36:37], 0, v[132:133]
	global_store_dwordx4 v[36:37], v[62:65], off
	s_nop 1
	v_add_co_u32_e32 v36, vcc, 0x8000, v36
	s_nop 1
	v_addc_co_u32_e32 v37, vcc, 0, v37, vcc
	global_store_dwordx4 v[36:37], v[66:69], off
	s_waitcnt vmcnt(13)
	ds_write2_b32 v137, v4, v5 offset1:1
	ds_write2_b32 v137, v6, v7 offset0:2 offset1:3
	s_waitcnt vmcnt(12)
	ds_write2_b32 v128, v8, v9 offset1:1
	ds_write2_b32 v124, v10, v11 offset1:1
	s_waitcnt vmcnt(11)
	ds_write2_b32 v125, v12, v13 offset1:1
	ds_write2_b32 v120, v14, v15 offset1:1
	s_waitcnt vmcnt(10)
	ds_write2_b32 v121, v16, v17 offset1:1
	ds_write2_b32 v116, v18, v19 offset1:1
	s_waitcnt vmcnt(9)
	ds_write2_b32 v117, v20, v21 offset1:1
	ds_write2_b32 v112, v22, v23 offset1:1
	s_waitcnt vmcnt(8)
	ds_write2_b32 v113, v24, v25 offset1:1
	ds_write2_b32 v108, v26, v27 offset1:1
	s_waitcnt vmcnt(7)
	ds_write2_b32 v109, v28, v29 offset1:1
	ds_write2_b32 v104, v30, v31 offset1:1
	s_waitcnt vmcnt(6)
	ds_write2_b32 v105, v32, v33 offset1:1
	ds_write2_b32 v106, v34, v35 offset1:1
	ds_read2_b32 v[4:5], v136 offset1:33
	ds_read2_b32 v[8:9], v136 offset0:66 offset1:99
	ds_read2_b32 v[32:33], v136 offset0:132 offset1:165
	ds_read2_b32 v[30:31], v136 offset0:198 offset1:231
	ds_read2_b32 v[24:25], v102 offset0:8 offset1:41
	ds_read2_b32 v[6:7], v102 offset0:74 offset1:107
	ds_read2_b32 v[20:21], v102 offset0:140 offset1:173
	ds_read2_b32 v[18:19], v102 offset0:206 offset1:239
	ds_read2_b32 v[34:35], v103 offset0:16 offset1:49
	ds_read2_b32 v[36:37], v103 offset0:82 offset1:115
	ds_read2_b32 v[28:29], v103 offset0:148 offset1:181
	ds_read2_b32 v[26:27], v103 offset0:214 offset1:247
	ds_read2_b32 v[22:23], v107 offset0:24 offset1:57
	ds_read2_b32 v[10:11], v107 offset0:90 offset1:123
	ds_read2_b32 v[16:17], v107 offset0:156 offset1:189
	ds_read2_b32 v[14:15], v107 offset0:222 offset1:255
	s_waitcnt lgkmcnt(14)
	v_mul_f32_e32 v13, 0x42800000, v4
	v_mul_f32_e32 v5, 0x42800000, v5
	v_mov_b32_e32 v4, v3
	v_cvt_pk_fp8_f32 v4, v13, v5
	v_mul_f32_e32 v8, 0x42800000, v8
	v_mul_f32_e32 v9, 0x42800000, v9
	s_waitcnt lgkmcnt(7)
	v_mul_f32_e32 v5, 0x42800000, v34
	v_cvt_pk_fp8_f32 v4, v8, v9 op_sel:[0,0,1]
	v_mul_f32_e32 v9, 0x42800000, v35
	v_mov_b32_e32 v8, v3
	v_cvt_pk_fp8_f32 v8, v5, v9
	s_waitcnt lgkmcnt(6)
	v_mul_f32_e32 v13, 0x42800000, v36
	v_mul_f32_e32 v34, 0x42800000, v37
	v_mul_f32_e32 v9, 0x42800000, v32
	v_cvt_pk_fp8_f32 v8, v13, v34 op_sel:[0,0,1]
	v_mul_f32_e32 v13, 0x42800000, v33
	v_mov_b32_e32 v5, v3
	v_cvt_pk_fp8_f32 v5, v9, v13
	s_waitcnt lgkmcnt(5)
	v_mul_f32_e32 v13, 0x42800000, v28
	v_mul_f32_e32 v28, 0x42800000, v29
	v_mov_b32_e32 v9, v3
	v_cvt_pk_fp8_f32 v9, v13, v28
	v_mul_f32_e32 v13, 0x42800000, v24
	v_mul_f32_e32 v24, 0x42800000, v25
	v_mul_f32_e32 v25, 0x42800000, v6
	v_mov_b32_e32 v6, v3
	v_cvt_pk_fp8_f32 v6, v13, v24
	v_mul_f32_e32 v7, 0x42800000, v7
	s_waitcnt lgkmcnt(3)
	v_mul_f32_e32 v13, 0x42800000, v23
	s_waitcnt lgkmcnt(2)
	v_mul_f32_e32 v11, 0x42800000, v11
	v_cvt_pk_fp8_f32 v6, v25, v7 op_sel:[0,0,1]
	v_mul_f32_e32 v7, 0x42800000, v22
	v_mul_f32_e32 v22, 0x42800000, v10
	v_mov_b32_e32 v10, v3
	v_cvt_pk_fp8_f32 v10, v7, v13
	v_mul_f32_e32 v13, 0x42800000, v21
	v_mov_b32_e32 v7, v3
	s_mul_hi_i32 s0, s37, 0x1600000
	v_cvt_pk_fp8_f32 v10, v22, v11 op_sel:[0,0,1]
	v_mul_f32_e32 v11, 0x42800000, v20
	v_cvt_pk_fp8_f32 v7, v11, v13
	s_waitcnt lgkmcnt(1)
	v_mul_f32_e32 v13, 0x42800000, v16
	v_mul_f32_e32 v16, 0x42800000, v17
	v_mov_b32_e32 v11, v3
	v_cvt_pk_fp8_f32 v11, v13, v16
	s_mul_i32 s37, s37, 0x1600000
	v_or_b32_e32 v12, s47, v135
	s_add_u32 s4, s34, s37
	v_mul_f32_e32 v30, 0x42800000, v30
	v_mul_f32_e32 v31, 0x42800000, v31
	v_mul_f32_e32 v18, 0x42800000, v18
	v_mul_f32_e32 v19, 0x42800000, v19
	v_ashrrev_i32_e32 v13, 31, v12
	s_addc_u32 s5, s35, s0
	v_cvt_pk_fp8_f32 v5, v30, v31 op_sel:[0,0,1]
	v_mul_f32_e32 v26, 0x42800000, v26
	v_mul_f32_e32 v27, 0x42800000, v27
	v_cvt_pk_fp8_f32 v7, v18, v19 op_sel:[0,0,1]
	s_waitcnt lgkmcnt(0)
	v_mul_f32_e32 v14, 0x42800000, v14
	v_mul_f32_e32 v15, 0x42800000, v15
	v_lshlrev_b64 v[12:13], 11, v[12:13]
	v_cvt_pk_fp8_f32 v9, v26, v27 op_sel:[0,0,1]
	v_cvt_pk_fp8_f32 v11, v14, v15 op_sel:[0,0,1]
	v_lshl_add_u64 v[12:13], s[4:5], 0, v[12:13]
	v_lshl_add_u64 v[12:13], v[12:13], 0, s[2:3]
	v_lshl_add_u64 v[12:13], v[12:13], 0, v[132:133]
	global_store_dwordx4 v[12:13], v[4:7], off
	s_nop 1
	v_add_co_u32_e32 v12, vcc, 0x8000, v12
	s_nop 1
	v_addc_co_u32_e32 v13, vcc, 0, v13, vcc
	global_store_dwordx4 v[12:13], v[8:11], off
	s_add_i32 s29, s29, 32
	s_cmp_lt_i32 s29, s28
	s_cbranch_scc1 .LBB6_1312
.LBB6_1313:
	s_max_i32 s0, s90, 0xdc00
	s_min_i32 s12, s91, 0x14a00
	s_cmp_le_i32 s12, s0
	s_mov_b32 s58, 0x800000
	s_cbranch_scc1 .LBB6_1318
	s_sub_i32 s1, s12, s0
	s_mov_b32 s2, 19
	s_cmp_lt_i32 s1, 32
	s_cbranch_scc1 .LBB6_1318
	s_add_i32 s0, s0, s67
	s_add_i32 s12, s12, 0xffff2400
	s_add_i32 s13, s0, 0xffff2400
	s_cmp_ge_i32 s13, s12
	s_cbranch_scc1 .LBB6_1318
	s_ashr_i32 s3, s2, 31
	s_lshl_b64 s[0:1], s[2:3], 3
	s_add_u32 s0, s76, s0
	s_addc_u32 s1, s77, s1
	s_load_dwordx2 s[0:1], s[0:1], 0x0
	v_lshlrev_b32_e32 v2, 4, v166
	v_lshlrev_b32_e32 v6, 5, v166
	v_lshrrev_b32_e32 v4, 3, v166
	v_and_b32_e32 v5, 0x70, v2
	s_waitcnt lgkmcnt(0)
	s_add_u32 s37, s0, 0x8400000
	s_addc_u32 s47, s1, 0
	v_lshrrev_b32_e32 v147, 2, v166
	v_lshlrev_b32_e32 v144, 4, v166
	v_and_b32_e32 v144, 48, v144
	s_add_u32 s48, s6, 0x99180000
	v_lshl_or_b32 v2, v4, 13, v5
	v_add_u32_e32 v5, s66, v5
	v_mul_u32_u24_e32 v4, 0x84, v4
	v_mul_u32_u24_e32 v6, 0x84, v144
	v_lshlrev_b32_e32 v7, 2, v147
	v_and_b32_e32 v146, 31, v167
	s_addc_u32 s49, s7, 0
	v_mov_b32_e32 v145, v3
	v_add3_u32 v148, s66, v6, v7
	v_add_u32_e32 v149, v5, v4
.LBB6_1317:
	s_mul_hi_i32 s1, s13, 0x2e8ba2e9
	s_lshr_b32 s3, s1, 31
	s_ashr_i32 s1, s1, 10
	s_lshl_b32 s2, s13, 3
	s_add_i32 s1, s1, s3
	s_and_b32 s33, s2, 64
	s_mul_i32 s2, s1, 0xffffea00
	s_add_i32 s2, s2, s13
	s_mul_hi_i32 s5, s1, 0xb00000
	s_mul_i32 s4, s1, 0xb00000
	s_ashr_i32 s1, s2, 1
	s_and_b32 s0, s13, 7
	s_ashr_i32 s2, s2, 31
	s_and_b32 s1, s1, -8
	s_lshr_b32 s2, s2, 26
	s_or_b32 s1, s1, s0
	s_add_i32 s2, s1, s2
	s_ashr_i32 s2, s2, 6
	s_lshl_b32 s1, s1, 5
	s_lshl_b32 s3, s2, 11
	s_lshl_b32 s2, s2, 7
	s_lshl_b64 s[22:23], s[4:5], 2
	s_sub_i32 s1, s1, s3
	s_or_b32 s2, s2, s33
	s_add_u32 s26, s37, s22
	v_or_b32_e32 v36, s1, v146
	v_or_b32_e32 v169, s1, v147
	s_addc_u32 s1, s47, s23
	v_readfirstlane_b32 s22, v36
	s_ashr_i32 s3, s2, 31
	s_andn2_b32 s22, s22, 31
	s_lshl_b64 s[24:25], s[2:3], 13
	s_add_u32 s24, s26, s24
	s_addc_u32 s1, s1, s25
	s_ashr_i32 s23, s22, 31
	s_lshl_b64 s[22:23], s[22:23], 2
	s_add_u32 s22, s24, s22
	s_addc_u32 s23, s1, s23
	s_mov_b64 s[24:25], s[22:23]
	s_add_u32 s26, s22, 0x10000
	s_addc_u32 s27, s23, 0
	v_lshl_add_u64 v[36:37], s[24:25], 0, v[2:3]
	s_add_u32 s24, s22, 0x20000
	global_load_dwordx4 v[124:127], v[36:37], off nt
	s_addc_u32 s25, s23, 0
	v_lshl_add_u64 v[36:37], s[26:27], 0, v[2:3]
	s_add_u32 s26, s22, 0x30000
	global_load_dwordx4 v[132:135], v[36:37], off nt
	s_addc_u32 s27, s23, 0
	v_lshl_add_u64 v[36:37], s[24:25], 0, v[2:3]
	s_add_u32 s24, s22, 0x40000
	global_load_dwordx4 v[136:139], v[36:37], off nt
	s_addc_u32 s25, s23, 0
	v_lshl_add_u64 v[36:37], s[26:27], 0, v[2:3]
	s_add_u32 s26, s22, 0x50000
	global_load_dwordx4 v[140:143], v[36:37], off nt
	s_addc_u32 s27, s23, 0
	v_lshl_add_u64 v[36:37], s[24:25], 0, v[2:3]
	s_add_u32 s24, s22, 0x60000
	s_addc_u32 s25, s23, 0
	global_load_dwordx4 v[170:173], v[36:37], off nt
	s_add_u32 s22, s22, 0x70000
	v_lshl_add_u64 v[36:37], s[26:27], 0, v[2:3]
	global_load_dwordx4 v[174:177], v[36:37], off nt
	s_addc_u32 s23, s23, 0
	s_add_i32 s1, s13, 8
	v_lshl_add_u64 v[36:37], s[24:25], 0, v[2:3]
	s_mul_hi_i32 s24, s1, 0x2e8ba2e9
	global_load_dwordx4 v[184:187], v[36:37], off nt
	s_lshr_b32 s26, s24, 31
	s_ashr_i32 s24, s24, 10
	v_lshl_add_u64 v[36:37], s[22:23], 0, v[2:3]
	s_add_i32 s22, s24, s26
	s_mul_i32 s23, s22, 0xffffea00
	s_add_i32 s23, s23, s1
	s_lshl_b32 s25, s1, 3
	s_ashr_i32 s1, s23, 1
	s_and_b32 s28, s25, 64
	s_mul_hi_i32 s25, s22, 0xb00000
	s_mul_i32 s24, s22, 0xb00000
	s_ashr_i32 s22, s23, 31
	s_and_b32 s1, s1, -8
	s_lshr_b32 s22, s22, 26
	s_or_b32 s1, s1, s0
	s_add_i32 s22, s1, s22
	s_ashr_i32 s22, s22, 6
	s_lshl_b32 s1, s1, 5
	s_lshl_b32 s23, s22, 11
	s_lshl_b32 s22, s22, 7
	s_lshl_b64 s[26:27], s[24:25], 2
	s_sub_i32 s1, s1, s23
	s_or_b32 s22, s22, s28
	global_load_dwordx4 v[188:191], v[36:37], off nt
	s_add_u32 s30, s37, s26
	v_or_b32_e32 v36, s1, v146
	v_or_b32_e32 v183, s1, v147
	s_addc_u32 s1, s47, s27
	v_readfirstlane_b32 s26, v36
	s_ashr_i32 s23, s22, 31
	s_andn2_b32 s26, s26, 31
	s_lshl_b64 s[28:29], s[22:23], 13
	s_add_u32 s28, s30, s28
	s_addc_u32 s1, s1, s29
	s_ashr_i32 s27, s26, 31
	s_lshl_b64 s[26:27], s[26:27], 2
	s_add_u32 s26, s28, s26
	s_addc_u32 s27, s1, s27
	s_mov_b64 s[28:29], s[26:27]
	s_add_u32 s30, s26, 0x10000
	s_addc_u32 s31, s27, 0
	v_lshl_add_u64 v[36:37], s[28:29], 0, v[2:3]
	s_add_u32 s28, s26, 0x20000
	global_load_dwordx4 v[76:79], v[36:37], off nt
	s_addc_u32 s29, s27, 0
	v_lshl_add_u64 v[36:37], s[30:31], 0, v[2:3]
	s_add_u32 s30, s26, 0x30000
	global_load_dwordx4 v[88:91], v[36:37], off nt
	s_addc_u32 s31, s27, 0
	v_lshl_add_u64 v[36:37], s[28:29], 0, v[2:3]
	s_add_u32 s28, s26, 0x40000
	global_load_dwordx4 v[96:99], v[36:37], off nt
	s_addc_u32 s29, s27, 0
	v_lshl_add_u64 v[36:37], s[30:31], 0, v[2:3]
	s_add_u32 s30, s26, 0x50000
	global_load_dwordx4 v[100:103], v[36:37], off nt
	s_addc_u32 s31, s27, 0
	v_lshl_add_u64 v[36:37], s[28:29], 0, v[2:3]
	s_add_u32 s28, s26, 0x60000
	s_addc_u32 s29, s27, 0
	global_load_dwordx4 v[108:111], v[36:37], off nt
	s_add_u32 s26, s26, 0x70000
	v_lshl_add_u64 v[36:37], s[30:31], 0, v[2:3]
	global_load_dwordx4 v[112:115], v[36:37], off nt
	s_addc_u32 s27, s27, 0
	s_add_i32 s1, s13, 16
	v_lshl_add_u64 v[36:37], s[28:29], 0, v[2:3]
	s_mul_hi_i32 s28, s1, 0x2e8ba2e9
	global_load_dwordx4 v[120:123], v[36:37], off nt
	s_lshr_b32 s29, s28, 31
	s_ashr_i32 s28, s28, 10
	v_lshl_add_u64 v[36:37], s[26:27], 0, v[2:3]
	s_add_i32 s26, s28, s29
	s_mul_i32 s28, s26, 0xffffea00
	s_add_i32 s28, s28, s1
	s_ashr_i32 s1, s28, 1
	s_ashr_i32 s28, s28, 31
	s_and_b32 s1, s1, -8
	s_lshr_b32 s28, s28, 26
	s_or_b32 s1, s1, s0
	s_add_i32 s28, s1, s28
	s_ashr_i32 s28, s28, 6
	s_mul_hi_i32 s27, s26, 0xb00000
	s_mul_i32 s26, s26, 0xb00000
	s_lshl_b32 s1, s1, 5
	s_lshl_b32 s29, s28, 11
	s_lshl_b32 s28, s28, 7
	s_lshl_b64 s[30:31], s[26:27], 2
	s_sub_i32 s1, s1, s29
	s_or_b32 s28, s28, s33
	global_load_dwordx4 v[128:131], v[36:37], off nt
	s_add_u32 s33, s37, s30
	v_or_b32_e32 v36, s1, v146
	v_or_b32_e32 v202, s1, v147
	s_addc_u32 s1, s47, s31
	v_readfirstlane_b32 s30, v36
	s_ashr_i32 s29, s28, 31
	s_andn2_b32 s30, s30, 31
	s_lshl_b64 s[34:35], s[28:29], 13
	s_add_u32 s33, s33, s34
	s_addc_u32 s1, s1, s35
	s_ashr_i32 s31, s30, 31
	s_lshl_b64 s[30:31], s[30:31], 2
	s_add_u32 s30, s33, s30
	s_addc_u32 s31, s1, s31
	s_mov_b64 s[34:35], s[30:31]
	s_add_u32 s50, s30, 0x10000
	s_addc_u32 s51, s31, 0
	v_lshl_add_u64 v[36:37], s[34:35], 0, v[2:3]
	s_add_u32 s34, s30, 0x20000
	global_load_dwordx4 v[48:51], v[36:37], off nt
	s_addc_u32 s35, s31, 0
	v_lshl_add_u64 v[36:37], s[50:51], 0, v[2:3]
	s_add_u32 s50, s30, 0x30000
	global_load_dwordx4 v[56:59], v[36:37], off nt
	s_addc_u32 s51, s31, 0
	v_lshl_add_u64 v[36:37], s[34:35], 0, v[2:3]
	s_add_u32 s34, s30, 0x40000
	global_load_dwordx4 v[64:67], v[36:37], off nt
	s_addc_u32 s35, s31, 0
	v_lshl_add_u64 v[36:37], s[50:51], 0, v[2:3]
	s_add_u32 s50, s30, 0x50000
	global_load_dwordx4 v[72:75], v[36:37], off nt
	s_addc_u32 s51, s31, 0
	v_lshl_add_u64 v[36:37], s[34:35], 0, v[2:3]
	s_add_u32 s34, s30, 0x60000
	s_addc_u32 s35, s31, 0
	s_add_u32 s30, s30, 0x70000
	global_load_dwordx4 v[84:87], v[36:37], off nt
	s_addc_u32 s31, s31, 0
	v_lshl_add_u64 v[36:37], s[50:51], 0, v[2:3]
	s_add_i32 s1, s13, 24
	global_load_dwordx4 v[92:95], v[36:37], off nt
	s_mul_hi_i32 s33, s1, 0x2e8ba2e9
	v_lshl_add_u64 v[36:37], s[34:35], 0, v[2:3]
	global_load_dwordx4 v[104:107], v[36:37], off nt
	s_lshr_b32 s35, s33, 31
	s_ashr_i32 s33, s33, 10
	v_lshl_add_u64 v[36:37], s[30:31], 0, v[2:3]
	s_add_i32 s30, s33, s35
	s_mul_i32 s31, s30, 0xffffea00
	s_add_i32 s31, s31, s1
	s_lshl_b32 s34, s1, 3
	s_ashr_i32 s1, s31, 1
	s_and_b32 s45, s34, 64
	s_mul_hi_i32 s35, s30, 0xb00000
	s_mul_i32 s34, s30, 0xb00000
	s_ashr_i32 s30, s31, 31
	s_and_b32 s1, s1, -8
	s_lshr_b32 s30, s30, 26
	s_or_b32 s0, s1, s0
	s_add_i32 s1, s0, s30
	s_ashr_i32 s1, s1, 6
	s_lshl_b32 s0, s0, 5
	s_lshl_b32 s30, s1, 11
	s_lshl_b32 s1, s1, 7
	s_lshl_b64 s[50:51], s[34:35], 2
	s_sub_i32 s0, s0, s30
	s_or_b32 s30, s1, s45
	global_load_dwordx4 v[116:119], v[36:37], off nt
	s_add_u32 s1, s37, s50
	v_or_b32_e32 v36, s0, v146
	v_or_b32_e32 v203, s0, v147
	s_addc_u32 s33, s47, s51
	v_readfirstlane_b32 s0, v36
	s_ashr_i32 s31, s30, 31
	s_andn2_b32 s0, s0, 31
	s_lshl_b64 s[50:51], s[30:31], 13
	s_add_u32 s45, s1, s50
	s_addc_u32 s33, s33, s51
	s_ashr_i32 s1, s0, 31
	s_lshl_b64 s[0:1], s[0:1], 2
	s_add_u32 s0, s45, s0
	s_addc_u32 s1, s33, s1
	s_mov_b64 s[50:51], s[0:1]
	s_add_u32 s64, s0, 0x10000
	s_addc_u32 s65, s1, 0
	v_lshl_add_u64 v[36:37], s[50:51], 0, v[2:3]
	global_load_dwordx4 v[36:39], v[36:37], off nt
	s_add_u32 s50, s0, 0x20000
	s_addc_u32 s51, s1, 0
	v_lshl_add_u64 v[40:41], s[64:65], 0, v[2:3]
	global_load_dwordx4 v[40:43], v[40:41], off nt
	s_add_u32 s64, s0, 0x30000
	s_addc_u32 s65, s1, 0
	v_lshl_add_u64 v[44:45], s[50:51], 0, v[2:3]
	global_load_dwordx4 v[44:47], v[44:45], off nt
	s_add_u32 s50, s0, 0x40000
	s_addc_u32 s51, s1, 0
	v_lshl_add_u64 v[52:53], s[64:65], 0, v[2:3]
	global_load_dwordx4 v[52:55], v[52:53], off nt
	s_add_u32 s64, s0, 0x50000
	s_addc_u32 s65, s1, 0
	v_lshl_add_u64 v[60:61], s[50:51], 0, v[2:3]
	global_load_dwordx4 v[60:63], v[60:61], off nt
	s_add_u32 s50, s0, 0x60000
	s_addc_u32 s51, s1, 0
	v_lshl_add_u64 v[68:69], s[64:65], 0, v[2:3]
	global_load_dwordx4 v[68:71], v[68:69], off nt
	s_add_u32 s0, s0, 0x70000
	s_addc_u32 s1, s1, 0
	v_lshl_add_u64 v[80:81], s[50:51], 0, v[2:3]
	global_load_dwordx4 v[80:83], v[80:81], off nt
	v_add_u32_e32 v150, 0x420, v149
	v_add_u32_e32 v151, 0x428, v149
	v_add_u32_e32 v152, 0x840, v149
	v_add_u32_e32 v153, 0x848, v149
	v_add_u32_e32 v154, 0xc60, v149
	v_add_u32_e32 v155, 0xc68, v149
	v_add_u32_e32 v156, 0x1080, v149
	v_add_u32_e32 v157, 0x1088, v149
	v_add_u32_e32 v158, 0x14a0, v149
	v_add_u32_e32 v159, 0x14a8, v149
	v_add_u32_e32 v160, 0x18c0, v149
	v_add_u32_e32 v161, 0x18c8, v149
	v_add_u32_e32 v162, 0x1ce0, v149
	v_add_u32_e32 v163, 0x1ce8, v149
	s_waitcnt vmcnt(30)
	ds_write2_b32 v149, v124, v125 offset1:1
	ds_write2_b32 v149, v126, v127 offset0:2 offset1:3
	s_waitcnt vmcnt(29)
	ds_write2_b32 v150, v132, v133 offset1:1
	ds_write2_b32 v151, v134, v135 offset1:1
	s_waitcnt vmcnt(28)
	ds_write2_b32 v152, v136, v137 offset1:1
	ds_write2_b32 v153, v138, v139 offset1:1
	s_waitcnt vmcnt(27)
	ds_write2_b32 v154, v140, v141 offset1:1
	ds_write2_b32 v155, v142, v143 offset1:1
	s_waitcnt vmcnt(26)
	ds_write2_b32 v156, v170, v171 offset1:1
	ds_write2_b32 v157, v172, v173 offset1:1
	s_waitcnt vmcnt(25)
	ds_write2_b32 v158, v174, v175 offset1:1
	ds_write2_b32 v159, v176, v177 offset1:1
	s_waitcnt vmcnt(24)
	ds_write2_b32 v160, v184, v185 offset1:1
	ds_write2_b32 v161, v186, v187 offset1:1
	s_waitcnt vmcnt(23)
	ds_write2_b32 v162, v188, v189 offset1:1
	ds_write2_b32 v163, v190, v191 offset1:1
	v_lshl_add_u64 v[124:125], s[0:1], 0, v[2:3]
	global_load_dwordx4 v[124:127], v[124:125], off nt
	s_add_u32 s4, s48, s4
	s_addc_u32 s5, s49, s5
	v_add_u32_e32 v164, 0x400, v148
	v_mov_b32_e32 v165, v148
	v_add_u32_e32 v168, 0x400, v148
	v_mov_b64_e32 v[132:133], s[4:5]
	s_add_u32 s0, s48, s24
	ds_read2_b32 v[134:135], v148 offset1:33
	ds_read2_b32 v[136:137], v148 offset0:66 offset1:99
	ds_read2_b32 v[138:139], v148 offset0:132 offset1:165
	ds_read2_b32 v[140:141], v148 offset0:198 offset1:231
	ds_read2_b32 v[142:143], v164 offset0:8 offset1:41
	ds_read2_b32 v[170:171], v164 offset0:74 offset1:107
	ds_read2_b32 v[172:173], v164 offset0:140 offset1:173
	ds_read2_b32 v[174:175], v164 offset0:206 offset1:239
	ds_read2_b32 v[176:177], v165 offset0:16 offset1:49
	ds_read2_b32 v[178:179], v165 offset0:82 offset1:115
	ds_read2_b32 v[184:185], v165 offset0:148 offset1:181
	ds_read2_b32 v[186:187], v165 offset0:214 offset1:247
	ds_read2_b32 v[188:189], v168 offset0:24 offset1:57
	ds_read2_b32 v[190:191], v168 offset0:90 offset1:123
	ds_read2_b32 v[192:193], v168 offset0:156 offset1:189
	ds_read2_b32 v[194:195], v168 offset0:222 offset1:255
	v_mad_i64_i32 v[132:133], s[4:5], v169, s82, v[132:133]
	s_addc_u32 s1, s49, s25
	v_lshl_add_u64 v[132:133], v[132:133], 0, s[2:3]
	v_mov_b64_e32 v[196:197], s[0:1]
	v_mov_b32_e32 v4, v3
	v_mov_b32_e32 v5, v3
	v_mov_b32_e32 v6, v3
	v_mov_b32_e32 v7, v3
	v_lshl_add_u64 v[198:199], v[132:133], 0, v[144:145]
	v_mad_i64_i32 v[132:133], s[2:3], v183, s82, v[196:197]
	s_waitcnt lgkmcnt(14)
	v_mul_f32_e32 v169, 0x42800000, v134
	v_mul_f32_e32 v183, 0x42800000, v135
	s_waitcnt lgkmcnt(13)
	v_mul_f32_e32 v138, 0x42800000, v138
	v_mul_f32_e32 v139, 0x42800000, v139
	s_waitcnt lgkmcnt(11)
	v_mul_f32_e32 v142, 0x42800000, v142
	v_mul_f32_e32 v143, 0x42800000, v143
	s_waitcnt lgkmcnt(9)
	v_mul_f32_e32 v172, 0x42800000, v172
	v_mul_f32_e32 v173, 0x42800000, v173
	v_mov_b32_e32 v8, v3
	v_mov_b32_e32 v9, v3
	v_mov_b32_e32 v10, v3
	v_mov_b32_e32 v11, v3
	s_waitcnt lgkmcnt(7)
	v_mul_f32_e32 v176, 0x42800000, v176
	v_mul_f32_e32 v177, 0x42800000, v177
	s_waitcnt lgkmcnt(5)
	v_mul_f32_e32 v184, 0x42800000, v184
	v_mul_f32_e32 v185, 0x42800000, v185
	s_waitcnt lgkmcnt(3)
	v_mul_f32_e32 v188, 0x42800000, v188
	v_mul_f32_e32 v189, 0x42800000, v189
	s_waitcnt lgkmcnt(1)
	v_mul_f32_e32 v192, 0x42800000, v192
	v_mul_f32_e32 v193, 0x42800000, v193
	v_cvt_pk_fp8_f32 v4, v169, v183
	v_cvt_pk_fp8_f32 v5, v138, v139
	v_cvt_pk_fp8_f32 v6, v142, v143
	v_cvt_pk_fp8_f32 v7, v172, v173
	v_cvt_pk_fp8_f32 v8, v176, v177
	v_cvt_pk_fp8_f32 v9, v184, v185
	v_cvt_pk_fp8_f32 v10, v188, v189
	v_cvt_pk_fp8_f32 v11, v192, v193
	v_mul_f32_e32 v136, 0x42800000, v136
	v_mul_f32_e32 v137, 0x42800000, v137
	v_mul_f32_e32 v140, 0x42800000, v140
	v_mul_f32_e32 v141, 0x42800000, v141
	v_mul_f32_e32 v170, 0x42800000, v170
	v_mul_f32_e32 v171, 0x42800000, v171
	v_mul_f32_e32 v174, 0x42800000, v174
	v_mul_f32_e32 v175, 0x42800000, v175
	v_mul_f32_e32 v178, 0x42800000, v178
	v_mul_f32_e32 v179, 0x42800000, v179
	v_mul_f32_e32 v186, 0x42800000, v186
	v_mul_f32_e32 v187, 0x42800000, v187
	v_mul_f32_e32 v190, 0x42800000, v190
	v_mul_f32_e32 v191, 0x42800000, v191
	s_waitcnt lgkmcnt(0)
	v_mul_f32_e32 v194, 0x42800000, v194
	v_mul_f32_e32 v195, 0x42800000, v195
	v_cvt_pk_fp8_f32 v4, v136, v137 op_sel:[0,0,1]
	v_cvt_pk_fp8_f32 v5, v140, v141 op_sel:[0,0,1]
	v_cvt_pk_fp8_f32 v6, v170, v171 op_sel:[0,0,1]
	v_cvt_pk_fp8_f32 v7, v174, v175 op_sel:[0,0,1]
	v_cvt_pk_fp8_f32 v8, v178, v179 op_sel:[0,0,1]
	v_cvt_pk_fp8_f32 v9, v186, v187 op_sel:[0,0,1]
	v_cvt_pk_fp8_f32 v10, v190, v191 op_sel:[0,0,1]
	v_cvt_pk_fp8_f32 v11, v194, v195 op_sel:[0,0,1]
	global_store_dwordx4 v[198:199], v[4:7], off
	s_nop 1
	v_add_co_u32_e32 v198, vcc, 0x16000, v198
	s_nop 1
	v_addc_co_u32_e32 v199, vcc, 0, v199, vcc
	global_store_dwordx4 v[198:199], v[8:11], off
	s_waitcnt vmcnt(25)
	ds_write2_b32 v149, v76, v77 offset1:1
	ds_write2_b32 v149, v78, v79 offset0:2 offset1:3
	s_waitcnt vmcnt(24)
	ds_write2_b32 v150, v88, v89 offset1:1
	ds_write2_b32 v151, v90, v91 offset1:1
	s_waitcnt vmcnt(23)
	ds_write2_b32 v152, v96, v97 offset1:1
	ds_write2_b32 v153, v98, v99 offset1:1
	s_waitcnt vmcnt(22)
	ds_write2_b32 v154, v100, v101 offset1:1
	ds_write2_b32 v155, v102, v103 offset1:1
	s_waitcnt vmcnt(21)
	ds_write2_b32 v156, v108, v109 offset1:1
	ds_write2_b32 v157, v110, v111 offset1:1
	s_waitcnt vmcnt(20)
	ds_write2_b32 v158, v112, v113 offset1:1
	ds_write2_b32 v159, v114, v115 offset1:1
	s_waitcnt vmcnt(19)
	ds_write2_b32 v160, v120, v121 offset1:1
	ds_write2_b32 v161, v122, v123 offset1:1
	s_waitcnt vmcnt(18)
	ds_write2_b32 v162, v128, v129 offset1:1
	ds_write2_b32 v163, v130, v131 offset1:1
	ds_read2_b32 v[4:5], v148 offset1:33
	ds_read2_b32 v[6:7], v148 offset0:66 offset1:99
	ds_read2_b32 v[8:9], v148 offset0:132 offset1:165
	ds_read2_b32 v[10:11], v148 offset0:198 offset1:231
	ds_read2_b32 v[76:77], v164 offset0:8 offset1:41
	ds_read2_b32 v[78:79], v164 offset0:74 offset1:107
	ds_read2_b32 v[88:89], v164 offset0:140 offset1:173
	ds_read2_b32 v[90:91], v164 offset0:206 offset1:239
	ds_read2_b32 v[96:97], v165 offset0:16 offset1:49
	ds_read2_b32 v[98:99], v165 offset0:82 offset1:115
	ds_read2_b32 v[100:101], v165 offset0:148 offset1:181
	ds_read2_b32 v[102:103], v165 offset0:214 offset1:247
	ds_read2_b32 v[108:109], v168 offset0:24 offset1:57
	ds_read2_b32 v[110:111], v168 offset0:90 offset1:123
	ds_read2_b32 v[112:113], v168 offset0:156 offset1:189
	ds_read2_b32 v[114:115], v168 offset0:222 offset1:255
	v_mov_b32_e32 v12, v3
	v_mov_b32_e32 v13, v3
	v_mov_b32_e32 v14, v3
	v_mov_b32_e32 v15, v3
	s_waitcnt lgkmcnt(14)
	v_mul_f32_e32 v4, 0x42800000, v4
	v_mul_f32_e32 v5, 0x42800000, v5
	s_waitcnt lgkmcnt(13)
	v_mul_f32_e32 v8, 0x42800000, v8
	v_mul_f32_e32 v9, 0x42800000, v9
	s_waitcnt lgkmcnt(11)
	v_mul_f32_e32 v76, 0x42800000, v76
	v_mul_f32_e32 v77, 0x42800000, v77
	s_waitcnt lgkmcnt(9)
	v_mul_f32_e32 v88, 0x42800000, v88
	v_mul_f32_e32 v89, 0x42800000, v89
	v_mov_b32_e32 v16, v3
	v_mov_b32_e32 v17, v3
	v_mov_b32_e32 v18, v3
	v_mov_b32_e32 v19, v3
	s_waitcnt lgkmcnt(7)
	v_mul_f32_e32 v96, 0x42800000, v96
	v_mul_f32_e32 v97, 0x42800000, v97
	s_waitcnt lgkmcnt(5)
	v_mul_f32_e32 v100, 0x42800000, v100
	v_mul_f32_e32 v101, 0x42800000, v101
	s_waitcnt lgkmcnt(3)
	v_mul_f32_e32 v108, 0x42800000, v108
	v_mul_f32_e32 v109, 0x42800000, v109
	s_waitcnt lgkmcnt(1)
	v_mul_f32_e32 v112, 0x42800000, v112
	v_mul_f32_e32 v113, 0x42800000, v113
	v_cvt_pk_fp8_f32 v12, v4, v5
	v_cvt_pk_fp8_f32 v13, v8, v9
	v_cvt_pk_fp8_f32 v14, v76, v77
	v_cvt_pk_fp8_f32 v15, v88, v89
	v_cvt_pk_fp8_f32 v16, v96, v97
	v_cvt_pk_fp8_f32 v17, v100, v101
	v_cvt_pk_fp8_f32 v18, v108, v109
	v_cvt_pk_fp8_f32 v19, v112, v113
	v_mul_f32_e32 v6, 0x42800000, v6
	v_mul_f32_e32 v7, 0x42800000, v7
	v_mul_f32_e32 v10, 0x42800000, v10
	v_mul_f32_e32 v11, 0x42800000, v11
	v_mul_f32_e32 v78, 0x42800000, v78
	v_mul_f32_e32 v79, 0x42800000, v79
	v_mul_f32_e32 v90, 0x42800000, v90
	v_mul_f32_e32 v91, 0x42800000, v91
	v_mul_f32_e32 v98, 0x42800000, v98
	v_mul_f32_e32 v99, 0x42800000, v99
	v_mul_f32_e32 v102, 0x42800000, v102
	v_mul_f32_e32 v103, 0x42800000, v103
	v_mul_f32_e32 v110, 0x42800000, v110
	v_mul_f32_e32 v111, 0x42800000, v111
	s_waitcnt lgkmcnt(0)
	v_mul_f32_e32 v114, 0x42800000, v114
	v_mul_f32_e32 v115, 0x42800000, v115
	v_cvt_pk_fp8_f32 v12, v6, v7 op_sel:[0,0,1]
	v_cvt_pk_fp8_f32 v13, v10, v11 op_sel:[0,0,1]
	v_cvt_pk_fp8_f32 v14, v78, v79 op_sel:[0,0,1]
	v_cvt_pk_fp8_f32 v15, v90, v91 op_sel:[0,0,1]
	v_cvt_pk_fp8_f32 v16, v98, v99 op_sel:[0,0,1]
	v_cvt_pk_fp8_f32 v17, v102, v103 op_sel:[0,0,1]
	v_cvt_pk_fp8_f32 v18, v110, v111 op_sel:[0,0,1]
	v_cvt_pk_fp8_f32 v19, v114, v115 op_sel:[0,0,1]
	v_lshl_add_u64 v[132:133], v[132:133], 0, s[22:23]
	v_lshl_add_u64 v[200:201], v[132:133], 0, v[144:145]
	global_store_dwordx4 v[200:201], v[12:15], off
	s_nop 1
	v_add_co_u32_e32 v200, vcc, 0x16000, v200
	s_nop 1
	v_addc_co_u32_e32 v201, vcc, 0, v201, vcc
	global_store_dwordx4 v[200:201], v[16:19], off
	s_waitcnt vmcnt(19)
	ds_write2_b32 v149, v48, v49 offset1:1
	ds_write2_b32 v149, v50, v51 offset0:2 offset1:3
	s_waitcnt vmcnt(18)
	ds_write2_b32 v150, v56, v57 offset1:1
	ds_write2_b32 v151, v58, v59 offset1:1
	s_waitcnt vmcnt(17)
	ds_write2_b32 v152, v64, v65 offset1:1
	ds_write2_b32 v153, v66, v67 offset1:1
	s_waitcnt vmcnt(16)
	ds_write2_b32 v154, v72, v73 offset1:1
	ds_write2_b32 v155, v74, v75 offset1:1
	s_waitcnt vmcnt(15)
	ds_write2_b32 v156, v84, v85 offset1:1
	ds_write2_b32 v157, v86, v87 offset1:1
	s_waitcnt vmcnt(14)
	ds_write2_b32 v158, v92, v93 offset1:1
	ds_write2_b32 v159, v94, v95 offset1:1
	s_waitcnt vmcnt(13)
	ds_write2_b32 v160, v104, v105 offset1:1
	ds_write2_b32 v161, v106, v107 offset1:1
	s_waitcnt vmcnt(12)
	ds_write2_b32 v162, v116, v117 offset1:1
	ds_write2_b32 v163, v118, v119 offset1:1
	ds_read2_b32 v[4:5], v148 offset1:33
	ds_read2_b32 v[6:7], v148 offset0:66 offset1:99
	ds_read2_b32 v[8:9], v148 offset0:132 offset1:165
	ds_read2_b32 v[10:11], v148 offset0:198 offset1:231
	ds_read2_b32 v[12:13], v164 offset0:8 offset1:41
	ds_read2_b32 v[14:15], v164 offset0:74 offset1:107
	ds_read2_b32 v[16:17], v164 offset0:140 offset1:173
	ds_read2_b32 v[18:19], v164 offset0:206 offset1:239
	ds_read2_b32 v[48:49], v165 offset0:16 offset1:49
	ds_read2_b32 v[50:51], v165 offset0:82 offset1:115
	ds_read2_b32 v[56:57], v165 offset0:148 offset1:181
	ds_read2_b32 v[58:59], v165 offset0:214 offset1:247
	ds_read2_b32 v[64:65], v168 offset0:24 offset1:57
	ds_read2_b32 v[66:67], v168 offset0:90 offset1:123
	ds_read2_b32 v[72:73], v168 offset0:156 offset1:189
	ds_read2_b32 v[74:75], v168 offset0:222 offset1:255
	v_mov_b32_e32 v20, v3
	v_mov_b32_e32 v21, v3
	v_mov_b32_e32 v22, v3
	v_mov_b32_e32 v23, v3
	s_waitcnt lgkmcnt(14)
	v_mul_f32_e32 v4, 0x42800000, v4
	v_mul_f32_e32 v5, 0x42800000, v5
	s_waitcnt lgkmcnt(13)
	v_mul_f32_e32 v8, 0x42800000, v8
	v_mul_f32_e32 v9, 0x42800000, v9
	s_waitcnt lgkmcnt(11)
	v_mul_f32_e32 v12, 0x42800000, v12
	v_mul_f32_e32 v13, 0x42800000, v13
	s_waitcnt lgkmcnt(9)
	v_mul_f32_e32 v16, 0x42800000, v16
	v_mul_f32_e32 v17, 0x42800000, v17
	v_mov_b32_e32 v24, v3
	v_mov_b32_e32 v25, v3
	v_mov_b32_e32 v26, v3
	v_mov_b32_e32 v27, v3
	s_waitcnt lgkmcnt(7)
	v_mul_f32_e32 v48, 0x42800000, v48
	v_mul_f32_e32 v49, 0x42800000, v49
	s_waitcnt lgkmcnt(5)
	v_mul_f32_e32 v56, 0x42800000, v56
	v_mul_f32_e32 v57, 0x42800000, v57
	s_waitcnt lgkmcnt(3)
	v_mul_f32_e32 v64, 0x42800000, v64
	v_mul_f32_e32 v65, 0x42800000, v65
	s_waitcnt lgkmcnt(1)
	v_mul_f32_e32 v72, 0x42800000, v72
	v_mul_f32_e32 v73, 0x42800000, v73
	v_cvt_pk_fp8_f32 v20, v4, v5
	v_cvt_pk_fp8_f32 v21, v8, v9
	v_cvt_pk_fp8_f32 v22, v12, v13
	v_cvt_pk_fp8_f32 v23, v16, v17
	v_cvt_pk_fp8_f32 v24, v48, v49
	v_cvt_pk_fp8_f32 v25, v56, v57
	v_cvt_pk_fp8_f32 v26, v64, v65
	v_cvt_pk_fp8_f32 v27, v72, v73
	s_add_u32 s0, s48, s26
	s_addc_u32 s1, s49, s27
	v_mul_f32_e32 v6, 0x42800000, v6
	v_mul_f32_e32 v7, 0x42800000, v7
	v_mul_f32_e32 v10, 0x42800000, v10
	v_mul_f32_e32 v11, 0x42800000, v11
	v_mul_f32_e32 v14, 0x42800000, v14
	v_mul_f32_e32 v15, 0x42800000, v15
	v_mul_f32_e32 v18, 0x42800000, v18
	v_mul_f32_e32 v19, 0x42800000, v19
	v_mov_b64_e32 v[196:197], s[0:1]
	v_mul_f32_e32 v50, 0x42800000, v50
	v_mul_f32_e32 v51, 0x42800000, v51
	v_mul_f32_e32 v58, 0x42800000, v58
	v_mul_f32_e32 v59, 0x42800000, v59
	v_mul_f32_e32 v66, 0x42800000, v66
	v_mul_f32_e32 v67, 0x42800000, v67
	s_waitcnt lgkmcnt(0)
	v_mul_f32_e32 v74, 0x42800000, v74
	v_mul_f32_e32 v75, 0x42800000, v75
	v_cvt_pk_fp8_f32 v20, v6, v7 op_sel:[0,0,1]
	v_cvt_pk_fp8_f32 v21, v10, v11 op_sel:[0,0,1]
	v_cvt_pk_fp8_f32 v22, v14, v15 op_sel:[0,0,1]
	v_cvt_pk_fp8_f32 v23, v18, v19 op_sel:[0,0,1]
	v_mad_i64_i32 v[132:133], s[2:3], v202, s82, v[196:197]
	v_cvt_pk_fp8_f32 v24, v50, v51 op_sel:[0,0,1]
	v_cvt_pk_fp8_f32 v25, v58, v59 op_sel:[0,0,1]
	v_cvt_pk_fp8_f32 v26, v66, v67 op_sel:[0,0,1]
	v_cvt_pk_fp8_f32 v27, v74, v75 op_sel:[0,0,1]
	v_lshl_add_u64 v[132:133], v[132:133], 0, s[28:29]
	v_lshl_add_u64 v[134:135], v[132:133], 0, v[144:145]
	global_store_dwordx4 v[134:135], v[20:23], off
	s_nop 1
	v_add_co_u32_e32 v134, vcc, 0x16000, v134
	s_nop 1
	v_addc_co_u32_e32 v135, vcc, 0, v135, vcc
	global_store_dwordx4 v[134:135], v[24:27], off
	s_waitcnt vmcnt(13)
	ds_write2_b32 v149, v36, v37 offset1:1
	ds_write2_b32 v149, v38, v39 offset0:2 offset1:3
	s_waitcnt vmcnt(12)
	ds_write2_b32 v150, v40, v41 offset1:1
	ds_write2_b32 v151, v42, v43 offset1:1
	s_waitcnt vmcnt(11)
	ds_write2_b32 v152, v44, v45 offset1:1
	ds_write2_b32 v153, v46, v47 offset1:1
	s_waitcnt vmcnt(10)
	ds_write2_b32 v154, v52, v53 offset1:1
	ds_write2_b32 v155, v54, v55 offset1:1
	s_waitcnt vmcnt(9)
	ds_write2_b32 v156, v60, v61 offset1:1
	ds_write2_b32 v157, v62, v63 offset1:1
	s_waitcnt vmcnt(8)
	ds_write2_b32 v158, v68, v69 offset1:1
	ds_write2_b32 v159, v70, v71 offset1:1
	s_waitcnt vmcnt(7)
	ds_write2_b32 v160, v80, v81 offset1:1
	ds_write2_b32 v161, v82, v83 offset1:1
	s_waitcnt vmcnt(6)
	ds_write2_b32 v162, v124, v125 offset1:1
	ds_write2_b32 v163, v126, v127 offset1:1
	ds_read2_b32 v[4:5], v148 offset1:33
	ds_read2_b32 v[6:7], v148 offset0:66 offset1:99
	ds_read2_b32 v[8:9], v148 offset0:132 offset1:165
	ds_read2_b32 v[10:11], v148 offset0:198 offset1:231
	ds_read2_b32 v[12:13], v164 offset0:8 offset1:41
	ds_read2_b32 v[14:15], v164 offset0:74 offset1:107
	ds_read2_b32 v[16:17], v164 offset0:140 offset1:173
	ds_read2_b32 v[18:19], v164 offset0:206 offset1:239
	ds_read2_b32 v[20:21], v165 offset0:16 offset1:49
	ds_read2_b32 v[22:23], v165 offset0:82 offset1:115
	ds_read2_b32 v[24:25], v165 offset0:148 offset1:181
	ds_read2_b32 v[26:27], v165 offset0:214 offset1:247
	ds_read2_b32 v[36:37], v168 offset0:24 offset1:57
	ds_read2_b32 v[38:39], v168 offset0:90 offset1:123
	ds_read2_b32 v[40:41], v168 offset0:156 offset1:189
	ds_read2_b32 v[42:43], v168 offset0:222 offset1:255
	v_mov_b32_e32 v28, v3
	v_mov_b32_e32 v29, v3
	v_mov_b32_e32 v30, v3
	v_mov_b32_e32 v31, v3
	s_waitcnt lgkmcnt(14)
	v_mul_f32_e32 v4, 0x42800000, v4
	v_mul_f32_e32 v5, 0x42800000, v5
	s_waitcnt lgkmcnt(13)
	v_mul_f32_e32 v8, 0x42800000, v8
	v_mul_f32_e32 v9, 0x42800000, v9
	s_waitcnt lgkmcnt(11)
	v_mul_f32_e32 v12, 0x42800000, v12
	v_mul_f32_e32 v13, 0x42800000, v13
	s_waitcnt lgkmcnt(9)
	v_mul_f32_e32 v16, 0x42800000, v16
	v_mul_f32_e32 v17, 0x42800000, v17
	v_mov_b32_e32 v32, v3
	v_mov_b32_e32 v33, v3
	v_mov_b32_e32 v34, v3
	v_mov_b32_e32 v35, v3
	s_waitcnt lgkmcnt(7)
	v_mul_f32_e32 v20, 0x42800000, v20
	v_mul_f32_e32 v21, 0x42800000, v21
	s_waitcnt lgkmcnt(5)
	v_mul_f32_e32 v24, 0x42800000, v24
	v_mul_f32_e32 v25, 0x42800000, v25
	s_waitcnt lgkmcnt(3)
	v_mul_f32_e32 v36, 0x42800000, v36
	v_mul_f32_e32 v37, 0x42800000, v37
	s_waitcnt lgkmcnt(1)
	v_mul_f32_e32 v40, 0x42800000, v40
	v_mul_f32_e32 v41, 0x42800000, v41
	v_cvt_pk_fp8_f32 v28, v4, v5
	v_cvt_pk_fp8_f32 v29, v8, v9
	v_cvt_pk_fp8_f32 v30, v12, v13
	v_cvt_pk_fp8_f32 v31, v16, v17
	v_cvt_pk_fp8_f32 v32, v20, v21
	v_cvt_pk_fp8_f32 v33, v24, v25
	v_cvt_pk_fp8_f32 v34, v36, v37
	v_cvt_pk_fp8_f32 v35, v40, v41
	s_add_u32 s0, s48, s34
	s_addc_u32 s1, s49, s35
	v_mul_f32_e32 v6, 0x42800000, v6
	v_mul_f32_e32 v7, 0x42800000, v7
	v_mul_f32_e32 v10, 0x42800000, v10
	v_mul_f32_e32 v11, 0x42800000, v11
	v_mul_f32_e32 v14, 0x42800000, v14
	v_mul_f32_e32 v15, 0x42800000, v15
	v_mul_f32_e32 v18, 0x42800000, v18
	v_mul_f32_e32 v19, 0x42800000, v19
	v_mov_b64_e32 v[196:197], s[0:1]
	v_mul_f32_e32 v22, 0x42800000, v22
	v_mul_f32_e32 v23, 0x42800000, v23
	v_mul_f32_e32 v26, 0x42800000, v26
	v_mul_f32_e32 v27, 0x42800000, v27
	v_mul_f32_e32 v38, 0x42800000, v38
	v_mul_f32_e32 v39, 0x42800000, v39
	s_waitcnt lgkmcnt(0)
	v_mul_f32_e32 v42, 0x42800000, v42
	v_mul_f32_e32 v43, 0x42800000, v43
	v_cvt_pk_fp8_f32 v28, v6, v7 op_sel:[0,0,1]
	v_cvt_pk_fp8_f32 v29, v10, v11 op_sel:[0,0,1]
	v_cvt_pk_fp8_f32 v30, v14, v15 op_sel:[0,0,1]
	v_cvt_pk_fp8_f32 v31, v18, v19 op_sel:[0,0,1]
	v_mad_i64_i32 v[132:133], s[0:1], v203, s82, v[196:197]
	v_cvt_pk_fp8_f32 v32, v22, v23 op_sel:[0,0,1]
	v_cvt_pk_fp8_f32 v33, v26, v27 op_sel:[0,0,1]
	v_cvt_pk_fp8_f32 v34, v38, v39 op_sel:[0,0,1]
	v_cvt_pk_fp8_f32 v35, v42, v43 op_sel:[0,0,1]
	v_lshl_add_u64 v[132:133], v[132:133], 0, s[30:31]
	v_lshl_add_u64 v[4:5], v[132:133], 0, v[144:145]
	global_store_dwordx4 v[4:5], v[28:31], off
	s_nop 1
	v_add_co_u32_e32 v4, vcc, 0x16000, v4
	s_nop 1
	v_addc_co_u32_e32 v5, vcc, 0, v5, vcc
	global_store_dwordx4 v[4:5], v[32:35], off
	s_add_i32 s13, s13, 32
	s_cmp_ge_i32 s13, s12
	s_cbranch_scc0 .LBB6_1317

.LBB6_1471:
	s_max_i32 s0, s90, 0x7b00
	s_min_i32 s4, s91, 0x9b00
	s_cmp_le_i32 s4, s0
	s_cbranch_scc1 .LBB6_1476
	s_sub_i32 s1, s4, s0
	s_mov_b32 s2, 2
	s_cmp_lt_i32 s1, 32
	s_cbranch_scc1 .LBB6_1476
	s_add_i32 s0, s0, s67
	s_addk_i32 s4, 0x8500
	s_add_i32 s5, s0, 0xffff8500
	s_cmp_ge_i32 s5, s4
	s_cbranch_scc1 .LBB6_1476
	s_ashr_i32 s3, s2, 31
	s_lshl_b64 s[0:1], s[2:3], 3
	s_add_u32 s0, s76, s0
	s_addc_u32 s1, s77, s1
	s_load_dwordx2 s[0:1], s[0:1], 0x0
	s_waitcnt vmcnt(0)
	v_lshrrev_b32_e32 v4, 3, v166
	v_lshlrev_b32_e32 v2, 2, v166
	v_mul_u32_u24_e32 v5, 0x4240, v4
	v_and_b32_e32 v6, 28, v2
	s_waitcnt lgkmcnt(0)
	s_add_u32 s12, s0, 0x8480000
	v_or_b32_e32 v2, v5, v6
	v_lshl_add_u32 v5, v6, 2, s66
	v_lshlrev_b32_e32 v6, 5, v166
	s_addc_u32 s13, s1, 0
	v_lshrrev_b32_e32 v168, 2, v166
	v_lshlrev_b32_e32 v156, 4, v166
	v_and_b32_e32 v156, 48, v156
	v_mov_b32_e32 v7, 0x2240
	s_add_u32 s2, s6, 0x8d080000
	v_mul_u32_u24_e32 v4, 0x84, v4
	v_mul_u32_u24_e32 v6, 0x84, v156
	v_and_or_b32 v169, v167, 31, v7
	v_lshlrev_b32_e32 v7, 2, v168
	s_addc_u32 s3, s7, 0
	v_lshlrev_b32_e32 v2, 2, v2
	v_mov_b32_e32 v157, v3
	v_add3_u32 v170, s66, v6, v7
	v_add_u32_e32 v171, v5, v4
.LBB6_1475:
	s_ashr_i32 s0, s5, 31
	s_lshr_b32 s0, s0, 19
	s_add_i32 s0, s5, s0
	s_and_b32 s0, s0, 0xffffe000
	s_sub_i32 s0, s5, s0
	s_ashr_i32 s1, s0, 1
	s_and_b32 s22, s0, 7
	s_ashr_i32 s23, s0, 31
	s_and_b32 s1, s1, -8
	s_lshr_b32 s23, s23, 24
	s_or_b32 s1, s1, s22
	s_add_i32 s22, s1, s23
	s_ashr_i32 s22, s22, 8
	s_lshl_b32 s1, s1, 5
	s_lshl_b32 s23, s22, 13
	s_lshl_b32 s0, s0, 3
	s_sub_i32 s23, s1, s23
	s_and_b32 s0, s0, 64
	s_lshl_b32 s22, s22, 7
	v_add_u32_e32 v37, s23, v169
	s_or_b32 s0, s22, s0
	v_or_b32_e32 v36, s23, v168
	v_readfirstlane_b32 s22, v37
	s_ashr_i32 s1, s0, 31
	s_mul_i32 s25, s0, 0x10900
	v_ashrrev_i32_e32 v37, 31, v36
	s_andn2_b32 s22, s22, 31
	s_mul_hi_i32 s24, s0, 0x10900
	v_lshlrev_b64 v[36:37], 11, v[36:37]
	s_add_u32 s25, s12, s25
	v_lshl_add_u64 v[36:37], s[2:3], 0, v[36:37]
	s_addc_u32 s24, s13, s24
	s_ashr_i32 s23, s22, 31
	v_lshl_add_u64 v[36:37], v[36:37], 0, s[0:1]
	s_lshl_b64 s[0:1], s[22:23], 2
	s_add_u32 s0, s25, s0
	s_addc_u32 s1, s24, s1
	s_mov_b64 s[22:23], s[0:1]
	s_add_u32 s24, s0, 0x84800
	s_addc_u32 s25, s1, 0
	v_lshl_add_u64 v[164:165], v[36:37], 0, v[156:157]
	v_lshl_add_u64 v[36:37], s[22:23], 0, v[2:3]
	s_add_u32 s22, s0, 0x109000
	global_load_dwordx4 v[92:95], v[36:37], off nt
	s_addc_u32 s23, s1, 0
	v_lshl_add_u64 v[36:37], s[24:25], 0, v[2:3]
	s_add_u32 s24, s0, 0x18d800
	global_load_dwordx4 v[108:111], v[36:37], off nt
	s_addc_u32 s25, s1, 0
	v_lshl_add_u64 v[36:37], s[22:23], 0, v[2:3]
	s_add_u32 s22, s0, 0x212000
	global_load_dwordx4 v[120:123], v[36:37], off nt
	s_addc_u32 s23, s1, 0
	v_lshl_add_u64 v[36:37], s[24:25], 0, v[2:3]
	s_add_u32 s24, s0, 0x296800
	global_load_dwordx4 v[132:135], v[36:37], off nt
	s_addc_u32 s25, s1, 0
	v_lshl_add_u64 v[36:37], s[22:23], 0, v[2:3]
	s_add_u32 s22, s0, 0x31b000
	s_addc_u32 s23, s1, 0
	global_load_dwordx4 v[140:143], v[36:37], off nt
	s_add_u32 s0, s0, 0x39f800
	v_lshl_add_u64 v[36:37], s[24:25], 0, v[2:3]
	global_load_dwordx4 v[148:151], v[36:37], off nt
	s_addc_u32 s1, s1, 0
	s_add_i32 s24, s5, 8
	v_lshl_add_u64 v[36:37], s[22:23], 0, v[2:3]
	s_ashr_i32 s22, s24, 31
	global_load_dwordx4 v[152:155], v[36:37], off nt
	s_lshr_b32 s22, s22, 19
	v_lshl_add_u64 v[36:37], s[0:1], 0, v[2:3]
	s_add_i32 s0, s24, s22
	s_and_b32 s0, s0, 0xffffe000
	s_sub_i32 s0, s24, s0
	s_ashr_i32 s1, s0, 1
	s_and_b32 s22, s0, 7
	s_ashr_i32 s23, s0, 31
	s_and_b32 s1, s1, -8
	s_lshr_b32 s23, s23, 24
	s_or_b32 s1, s1, s22
	s_add_i32 s22, s1, s23
	s_ashr_i32 s22, s22, 8
	s_lshl_b32 s1, s1, 5
	s_lshl_b32 s23, s22, 13
	s_lshl_b32 s0, s0, 3
	s_sub_i32 s23, s1, s23
	global_load_dwordx4 v[192:195], v[36:37], off nt
	s_and_b32 s0, s0, 64
	s_lshl_b32 s22, s22, 7
	v_add_u32_e32 v37, s23, v169
	s_or_b32 s0, s22, s0
	v_or_b32_e32 v36, s23, v168
	v_readfirstlane_b32 s22, v37
	s_ashr_i32 s1, s0, 31
	s_mul_i32 s25, s0, 0x10900
	v_ashrrev_i32_e32 v37, 31, v36
	s_andn2_b32 s22, s22, 31
	s_mul_hi_i32 s24, s0, 0x10900
	v_lshlrev_b64 v[36:37], 11, v[36:37]
	s_add_u32 s25, s12, s25
	v_lshl_add_u64 v[36:37], s[2:3], 0, v[36:37]
	s_addc_u32 s24, s13, s24
	s_ashr_i32 s23, s22, 31
	v_lshl_add_u64 v[36:37], v[36:37], 0, s[0:1]
	s_lshl_b64 s[0:1], s[22:23], 2
	s_add_u32 s0, s25, s0
	s_addc_u32 s1, s24, s1
	s_mov_b64 s[22:23], s[0:1]
	s_add_u32 s24, s0, 0x84800
	s_addc_u32 s25, s1, 0
	v_lshl_add_u64 v[162:163], v[36:37], 0, v[156:157]
	v_lshl_add_u64 v[36:37], s[22:23], 0, v[2:3]
	s_add_u32 s22, s0, 0x109000
	global_load_dwordx4 v[56:59], v[36:37], off nt
	s_addc_u32 s23, s1, 0
	v_lshl_add_u64 v[36:37], s[24:25], 0, v[2:3]
	s_add_u32 s24, s0, 0x18d800
	global_load_dwordx4 v[68:71], v[36:37], off nt
	s_addc_u32 s25, s1, 0
	v_lshl_add_u64 v[36:37], s[22:23], 0, v[2:3]
	s_add_u32 s22, s0, 0x212000
	global_load_dwordx4 v[80:83], v[36:37], off nt
	s_addc_u32 s23, s1, 0
	v_lshl_add_u64 v[36:37], s[24:25], 0, v[2:3]
	s_add_u32 s24, s0, 0x296800
	global_load_dwordx4 v[96:99], v[36:37], off nt
	s_addc_u32 s25, s1, 0
	v_lshl_add_u64 v[36:37], s[22:23], 0, v[2:3]
	s_add_u32 s22, s0, 0x31b000
	s_addc_u32 s23, s1, 0
	global_load_dwordx4 v[112:115], v[36:37], off nt
	s_add_u32 s0, s0, 0x39f800
	v_lshl_add_u64 v[36:37], s[24:25], 0, v[2:3]
	global_load_dwordx4 v[124:127], v[36:37], off nt
	s_addc_u32 s1, s1, 0
	s_add_i32 s24, s5, 16
	v_lshl_add_u64 v[36:37], s[22:23], 0, v[2:3]
	s_ashr_i32 s22, s24, 31
	global_load_dwordx4 v[136:139], v[36:37], off nt
	s_lshr_b32 s22, s22, 19
	v_lshl_add_u64 v[36:37], s[0:1], 0, v[2:3]
	s_add_i32 s0, s24, s22
	s_and_b32 s0, s0, 0xffffe000
	s_sub_i32 s0, s24, s0
	s_ashr_i32 s1, s0, 1
	s_and_b32 s22, s0, 7
	s_ashr_i32 s23, s0, 31
	s_and_b32 s1, s1, -8
	s_lshr_b32 s23, s23, 24
	s_or_b32 s1, s1, s22
	s_add_i32 s22, s1, s23
	s_ashr_i32 s22, s22, 8
	s_lshl_b32 s1, s1, 5
	s_lshl_b32 s23, s22, 13
	s_lshl_b32 s0, s0, 3
	s_sub_i32 s23, s1, s23
	global_load_dwordx4 v[144:147], v[36:37], off nt
	s_and_b32 s0, s0, 64
	s_lshl_b32 s22, s22, 7
	v_add_u32_e32 v37, s23, v169
	s_or_b32 s0, s22, s0
	v_or_b32_e32 v36, s23, v168
	v_readfirstlane_b32 s22, v37
	s_ashr_i32 s1, s0, 31
	s_mul_i32 s25, s0, 0x10900
	v_ashrrev_i32_e32 v37, 31, v36
	s_andn2_b32 s22, s22, 31
	s_mul_hi_i32 s24, s0, 0x10900
	v_lshlrev_b64 v[36:37], 11, v[36:37]
	s_add_u32 s25, s12, s25
	v_lshl_add_u64 v[36:37], s[2:3], 0, v[36:37]
	s_addc_u32 s24, s13, s24
	s_ashr_i32 s23, s22, 31
	v_lshl_add_u64 v[36:37], v[36:37], 0, s[0:1]
	s_lshl_b64 s[0:1], s[22:23], 2
	s_add_u32 s0, s25, s0
	s_addc_u32 s1, s24, s1
	s_mov_b64 s[22:23], s[0:1]
	s_add_u32 s24, s0, 0x84800
	s_addc_u32 s25, s1, 0
	v_lshl_add_u64 v[158:159], v[36:37], 0, v[156:157]
	v_lshl_add_u64 v[36:37], s[22:23], 0, v[2:3]
	s_add_u32 s22, s0, 0x109000
	global_load_dwordx4 v[36:39], v[36:37], off nt
	s_addc_u32 s23, s1, 0
	v_lshl_add_u64 v[40:41], s[24:25], 0, v[2:3]
	s_add_u32 s24, s0, 0x18d800
	global_load_dwordx4 v[44:47], v[40:41], off nt
	s_addc_u32 s25, s1, 0
	v_lshl_add_u64 v[40:41], s[22:23], 0, v[2:3]
	s_add_u32 s22, s0, 0x212000
	global_load_dwordx4 v[52:55], v[40:41], off nt
	s_addc_u32 s23, s1, 0
	v_lshl_add_u64 v[40:41], s[24:25], 0, v[2:3]
	s_add_u32 s24, s0, 0x296800
	global_load_dwordx4 v[64:67], v[40:41], off nt
	s_addc_u32 s25, s1, 0
	v_lshl_add_u64 v[40:41], s[22:23], 0, v[2:3]
	s_add_u32 s22, s0, 0x31b000
	s_addc_u32 s23, s1, 0
	global_load_dwordx4 v[76:79], v[40:41], off nt
	s_add_u32 s0, s0, 0x39f800
	v_lshl_add_u64 v[40:41], s[24:25], 0, v[2:3]
	global_load_dwordx4 v[88:91], v[40:41], off nt
	s_addc_u32 s1, s1, 0
	s_add_i32 s24, s5, 24
	v_lshl_add_u64 v[40:41], s[22:23], 0, v[2:3]
	s_ashr_i32 s22, s24, 31
	global_load_dwordx4 v[116:119], v[40:41], off nt
	s_lshr_b32 s22, s22, 19
	v_lshl_add_u64 v[40:41], s[0:1], 0, v[2:3]
	s_add_i32 s0, s24, s22
	s_and_b32 s0, s0, 0xffffe000
	s_sub_i32 s0, s24, s0
	s_ashr_i32 s1, s0, 1
	s_and_b32 s22, s0, 7
	s_ashr_i32 s23, s0, 31
	s_and_b32 s1, s1, -8
	s_lshr_b32 s23, s23, 24
	s_or_b32 s1, s1, s22
	s_add_i32 s22, s1, s23
	s_ashr_i32 s22, s22, 8
	s_lshl_b32 s1, s1, 5
	s_lshl_b32 s23, s22, 13
	s_lshl_b32 s0, s0, 3
	s_sub_i32 s23, s1, s23
	global_load_dwordx4 v[128:131], v[40:41], off nt
	s_and_b32 s0, s0, 64
	s_lshl_b32 s22, s22, 7
	v_add_u32_e32 v41, s23, v169
	s_or_b32 s0, s22, s0
	v_or_b32_e32 v40, s23, v168
	v_readfirstlane_b32 s22, v41
	s_ashr_i32 s1, s0, 31
	s_mul_i32 s25, s0, 0x10900
	v_ashrrev_i32_e32 v41, 31, v40
	s_andn2_b32 s22, s22, 31
	s_mul_hi_i32 s24, s0, 0x10900
	v_lshlrev_b64 v[40:41], 11, v[40:41]
	s_add_u32 s25, s12, s25
	v_lshl_add_u64 v[40:41], s[2:3], 0, v[40:41]
	s_addc_u32 s24, s13, s24
	s_ashr_i32 s23, s22, 31
	v_lshl_add_u64 v[160:161], v[40:41], 0, s[0:1]
	s_lshl_b64 s[0:1], s[22:23], 2
	s_add_u32 s0, s25, s0
	s_addc_u32 s1, s24, s1
	s_mov_b64 s[22:23], s[0:1]
	s_add_u32 s24, s0, 0x84800
	s_addc_u32 s25, s1, 0
	v_lshl_add_u64 v[40:41], s[22:23], 0, v[2:3]
	global_load_dwordx4 v[40:43], v[40:41], off nt
	s_add_u32 s22, s0, 0x109000
	s_addc_u32 s23, s1, 0
	v_lshl_add_u64 v[48:49], s[24:25], 0, v[2:3]
	global_load_dwordx4 v[48:51], v[48:49], off nt
	s_add_u32 s24, s0, 0x18d800
	s_addc_u32 s25, s1, 0
	v_lshl_add_u64 v[60:61], s[22:23], 0, v[2:3]
	global_load_dwordx4 v[60:63], v[60:61], off nt
	s_add_u32 s22, s0, 0x212000
	s_addc_u32 s23, s1, 0
	v_lshl_add_u64 v[72:73], s[24:25], 0, v[2:3]
	global_load_dwordx4 v[72:75], v[72:73], off nt
	s_add_u32 s24, s0, 0x296800
	s_addc_u32 s25, s1, 0
	v_lshl_add_u64 v[84:85], s[22:23], 0, v[2:3]
	global_load_dwordx4 v[84:87], v[84:85], off nt
	s_add_u32 s22, s0, 0x31b000
	s_addc_u32 s23, s1, 0
	v_lshl_add_u64 v[100:101], s[24:25], 0, v[2:3]
	global_load_dwordx4 v[100:103], v[100:101], off nt
	s_add_u32 s0, s0, 0x39f800
	s_addc_u32 s1, s1, 0
	v_lshl_add_u64 v[104:105], s[22:23], 0, v[2:3]
	global_load_dwordx4 v[104:107], v[104:105], off nt
	v_add_u32_e32 v172, 0x420, v171
	v_add_u32_e32 v173, 0x428, v171
	v_add_u32_e32 v174, 0x840, v171
	v_add_u32_e32 v175, 0x848, v171
	v_add_u32_e32 v176, 0xc60, v171
	v_add_u32_e32 v177, 0xc68, v171
	v_add_u32_e32 v178, 0x1080, v171
	v_add_u32_e32 v179, 0x1088, v171
	v_add_u32_e32 v183, 0x14a0, v171
	v_add_u32_e32 v184, 0x14a8, v171
	v_add_u32_e32 v185, 0x18c0, v171
	v_add_u32_e32 v186, 0x18c8, v171
	v_add_u32_e32 v187, 0x1ce0, v171
	v_add_u32_e32 v189, 0x1ce8, v171
	s_waitcnt vmcnt(30)
	ds_write2_b32 v171, v92, v93 offset1:1
	ds_write2_b32 v171, v94, v95 offset0:2 offset1:3
	s_waitcnt vmcnt(29)
	ds_write2_b32 v172, v108, v109 offset1:1
	ds_write2_b32 v173, v110, v111 offset1:1
	s_waitcnt vmcnt(28)
	ds_write2_b32 v174, v120, v121 offset1:1
	ds_write2_b32 v175, v122, v123 offset1:1
	s_waitcnt vmcnt(27)
	ds_write2_b32 v176, v132, v133 offset1:1
	ds_write2_b32 v177, v134, v135 offset1:1
	s_waitcnt vmcnt(26)
	ds_write2_b32 v178, v140, v141 offset1:1
	ds_write2_b32 v179, v142, v143 offset1:1
	s_waitcnt vmcnt(25)
	ds_write2_b32 v183, v148, v149 offset1:1
	ds_write2_b32 v184, v150, v151 offset1:1
	s_waitcnt vmcnt(24)
	ds_write2_b32 v185, v152, v153 offset1:1
	ds_write2_b32 v186, v154, v155 offset1:1
	s_waitcnt vmcnt(23)
	ds_write2_b32 v187, v192, v193 offset1:1
	ds_write2_b32 v189, v194, v195 offset1:1
	v_lshl_add_u64 v[92:93], s[0:1], 0, v[2:3]
	global_load_dwordx4 v[92:95], v[92:93], off nt
	v_add_u32_e32 v188, 0x400, v170
	v_mov_b32_e32 v190, v170
	v_add_u32_e32 v191, 0x400, v170
	ds_read2_b32 v[108:109], v170 offset1:33
	ds_read2_b32 v[110:111], v170 offset0:66 offset1:99
	ds_read2_b32 v[120:121], v170 offset0:132 offset1:165
	ds_read2_b32 v[122:123], v170 offset0:198 offset1:231
	ds_read2_b32 v[132:133], v188 offset0:8 offset1:41
	ds_read2_b32 v[134:135], v188 offset0:74 offset1:107
	ds_read2_b32 v[140:141], v188 offset0:140 offset1:173
	ds_read2_b32 v[142:143], v188 offset0:206 offset1:239
	ds_read2_b32 v[148:149], v190 offset0:16 offset1:49
	ds_read2_b32 v[150:151], v190 offset0:82 offset1:115
	ds_read2_b32 v[152:153], v190 offset0:148 offset1:181
	ds_read2_b32 v[154:155], v190 offset0:214 offset1:247
	ds_read2_b32 v[192:193], v191 offset0:24 offset1:57
	ds_read2_b32 v[194:195], v191 offset0:90 offset1:123
	ds_read2_b32 v[196:197], v191 offset0:156 offset1:189
	ds_read2_b32 v[198:199], v191 offset0:222 offset1:255
	v_mov_b32_e32 v4, v3
	v_mov_b32_e32 v5, v3
	v_mov_b32_e32 v6, v3
	v_mov_b32_e32 v7, v3
	s_waitcnt lgkmcnt(14)
	v_mul_f32_e32 v108, 0x42800000, v108
	v_mul_f32_e32 v109, 0x42800000, v109
	s_waitcnt lgkmcnt(13)
	v_mul_f32_e32 v120, 0x42800000, v120
	v_mul_f32_e32 v121, 0x42800000, v121
	s_waitcnt lgkmcnt(11)
	v_mul_f32_e32 v132, 0x42800000, v132
	v_mul_f32_e32 v133, 0x42800000, v133
	s_waitcnt lgkmcnt(9)
	v_mul_f32_e32 v140, 0x42800000, v140
	v_mul_f32_e32 v141, 0x42800000, v141
	v_mov_b32_e32 v8, v3
	v_mov_b32_e32 v9, v3
	v_mov_b32_e32 v10, v3
	v_mov_b32_e32 v11, v3
	s_waitcnt lgkmcnt(7)
	v_mul_f32_e32 v148, 0x42800000, v148
	v_mul_f32_e32 v149, 0x42800000, v149
	s_waitcnt lgkmcnt(5)
	v_mul_f32_e32 v152, 0x42800000, v152
	v_mul_f32_e32 v153, 0x42800000, v153
	s_waitcnt lgkmcnt(3)
	v_mul_f32_e32 v192, 0x42800000, v192
	v_mul_f32_e32 v193, 0x42800000, v193
	s_waitcnt lgkmcnt(1)
	v_mul_f32_e32 v196, 0x42800000, v196
	v_mul_f32_e32 v197, 0x42800000, v197
	v_cvt_pk_fp8_f32 v4, v108, v109
	v_cvt_pk_fp8_f32 v5, v120, v121
	v_cvt_pk_fp8_f32 v6, v132, v133
	v_cvt_pk_fp8_f32 v7, v140, v141
	v_cvt_pk_fp8_f32 v8, v148, v149
	v_cvt_pk_fp8_f32 v9, v152, v153
	v_cvt_pk_fp8_f32 v10, v192, v193
	v_cvt_pk_fp8_f32 v11, v196, v197
	v_mul_f32_e32 v110, 0x42800000, v110
	v_mul_f32_e32 v111, 0x42800000, v111
	v_mul_f32_e32 v122, 0x42800000, v122
	v_mul_f32_e32 v123, 0x42800000, v123
	v_mul_f32_e32 v134, 0x42800000, v134
	v_mul_f32_e32 v135, 0x42800000, v135
	v_mul_f32_e32 v142, 0x42800000, v142
	v_mul_f32_e32 v143, 0x42800000, v143
	v_mul_f32_e32 v150, 0x42800000, v150
	v_mul_f32_e32 v151, 0x42800000, v151
	v_mul_f32_e32 v154, 0x42800000, v154
	v_mul_f32_e32 v155, 0x42800000, v155
	v_mul_f32_e32 v194, 0x42800000, v194
	v_mul_f32_e32 v195, 0x42800000, v195
	s_waitcnt lgkmcnt(0)
	v_mul_f32_e32 v198, 0x42800000, v198
	v_mul_f32_e32 v199, 0x42800000, v199
	v_cvt_pk_fp8_f32 v4, v110, v111 op_sel:[0,0,1]
	v_cvt_pk_fp8_f32 v5, v122, v123 op_sel:[0,0,1]
	v_cvt_pk_fp8_f32 v6, v134, v135 op_sel:[0,0,1]
	v_cvt_pk_fp8_f32 v7, v142, v143 op_sel:[0,0,1]
	v_cvt_pk_fp8_f32 v8, v150, v151 op_sel:[0,0,1]
	v_cvt_pk_fp8_f32 v9, v154, v155 op_sel:[0,0,1]
	v_cvt_pk_fp8_f32 v10, v194, v195 op_sel:[0,0,1]
	v_cvt_pk_fp8_f32 v11, v198, v199 op_sel:[0,0,1]
	global_store_dwordx4 v[164:165], v[4:7], off
	s_nop 1
	v_add_co_u32_e32 v164, vcc, 0x8000, v164
	s_nop 1
	v_addc_co_u32_e32 v165, vcc, 0, v165, vcc
	global_store_dwordx4 v[164:165], v[8:11], off
	s_waitcnt vmcnt(25)
	ds_write2_b32 v171, v56, v57 offset1:1
	ds_write2_b32 v171, v58, v59 offset0:2 offset1:3
	s_waitcnt vmcnt(24)
	ds_write2_b32 v172, v68, v69 offset1:1
	ds_write2_b32 v173, v70, v71 offset1:1
	s_waitcnt vmcnt(23)
	ds_write2_b32 v174, v80, v81 offset1:1
	ds_write2_b32 v175, v82, v83 offset1:1
	s_waitcnt vmcnt(22)
	ds_write2_b32 v176, v96, v97 offset1:1
	ds_write2_b32 v177, v98, v99 offset1:1
	s_waitcnt vmcnt(21)
	ds_write2_b32 v178, v112, v113 offset1:1
	ds_write2_b32 v179, v114, v115 offset1:1
	s_waitcnt vmcnt(20)
	ds_write2_b32 v183, v124, v125 offset1:1
	ds_write2_b32 v184, v126, v127 offset1:1
	s_waitcnt vmcnt(19)
	ds_write2_b32 v185, v136, v137 offset1:1
	ds_write2_b32 v186, v138, v139 offset1:1
	s_waitcnt vmcnt(18)
	ds_write2_b32 v187, v144, v145 offset1:1
	ds_write2_b32 v189, v146, v147 offset1:1
	ds_read2_b32 v[4:5], v170 offset1:33
	ds_read2_b32 v[6:7], v170 offset0:66 offset1:99
	ds_read2_b32 v[8:9], v170 offset0:132 offset1:165
	ds_read2_b32 v[10:11], v170 offset0:198 offset1:231
	ds_read2_b32 v[56:57], v188 offset0:8 offset1:41
	ds_read2_b32 v[58:59], v188 offset0:74 offset1:107
	ds_read2_b32 v[68:69], v188 offset0:140 offset1:173
	ds_read2_b32 v[70:71], v188 offset0:206 offset1:239
	ds_read2_b32 v[80:81], v190 offset0:16 offset1:49
	ds_read2_b32 v[82:83], v190 offset0:82 offset1:115
	ds_read2_b32 v[96:97], v190 offset0:148 offset1:181
	ds_read2_b32 v[98:99], v190 offset0:214 offset1:247
	ds_read2_b32 v[108:109], v191 offset0:24 offset1:57
	ds_read2_b32 v[110:111], v191 offset0:90 offset1:123
	ds_read2_b32 v[112:113], v191 offset0:156 offset1:189
	ds_read2_b32 v[114:115], v191 offset0:222 offset1:255
	v_mov_b32_e32 v12, v3
	v_mov_b32_e32 v13, v3
	v_mov_b32_e32 v14, v3
	v_mov_b32_e32 v15, v3
	s_waitcnt lgkmcnt(14)
	v_mul_f32_e32 v4, 0x42800000, v4
	v_mul_f32_e32 v5, 0x42800000, v5
	s_waitcnt lgkmcnt(13)
	v_mul_f32_e32 v8, 0x42800000, v8
	v_mul_f32_e32 v9, 0x42800000, v9
	s_waitcnt lgkmcnt(11)
	v_mul_f32_e32 v56, 0x42800000, v56
	v_mul_f32_e32 v57, 0x42800000, v57
	s_waitcnt lgkmcnt(9)
	v_mul_f32_e32 v68, 0x42800000, v68
	v_mul_f32_e32 v69, 0x42800000, v69
	v_mov_b32_e32 v16, v3
	v_mov_b32_e32 v17, v3
	v_mov_b32_e32 v18, v3
	v_mov_b32_e32 v19, v3
	s_waitcnt lgkmcnt(7)
	v_mul_f32_e32 v80, 0x42800000, v80
	v_mul_f32_e32 v81, 0x42800000, v81
	s_waitcnt lgkmcnt(5)
	v_mul_f32_e32 v96, 0x42800000, v96
	v_mul_f32_e32 v97, 0x42800000, v97
	s_waitcnt lgkmcnt(3)
	v_mul_f32_e32 v108, 0x42800000, v108
	v_mul_f32_e32 v109, 0x42800000, v109
	s_waitcnt lgkmcnt(1)
	v_mul_f32_e32 v112, 0x42800000, v112
	v_mul_f32_e32 v113, 0x42800000, v113
	v_cvt_pk_fp8_f32 v12, v4, v5
	v_cvt_pk_fp8_f32 v13, v8, v9
	v_cvt_pk_fp8_f32 v14, v56, v57
	v_cvt_pk_fp8_f32 v15, v68, v69
	v_cvt_pk_fp8_f32 v16, v80, v81
	v_cvt_pk_fp8_f32 v17, v96, v97
	v_cvt_pk_fp8_f32 v18, v108, v109
	v_cvt_pk_fp8_f32 v19, v112, v113
	v_mul_f32_e32 v6, 0x42800000, v6
	v_mul_f32_e32 v7, 0x42800000, v7
	v_mul_f32_e32 v10, 0x42800000, v10
	v_mul_f32_e32 v11, 0x42800000, v11
	v_mul_f32_e32 v58, 0x42800000, v58
	v_mul_f32_e32 v59, 0x42800000, v59
	v_mul_f32_e32 v70, 0x42800000, v70
	v_mul_f32_e32 v71, 0x42800000, v71
	v_mul_f32_e32 v82, 0x42800000, v82
	v_mul_f32_e32 v83, 0x42800000, v83
	v_mul_f32_e32 v98, 0x42800000, v98
	v_mul_f32_e32 v99, 0x42800000, v99
	v_mul_f32_e32 v110, 0x42800000, v110
	v_mul_f32_e32 v111, 0x42800000, v111
	s_waitcnt lgkmcnt(0)
	v_mul_f32_e32 v114, 0x42800000, v114
	v_mul_f32_e32 v115, 0x42800000, v115
	v_cvt_pk_fp8_f32 v12, v6, v7 op_sel:[0,0,1]
	v_cvt_pk_fp8_f32 v13, v10, v11 op_sel:[0,0,1]
	v_cvt_pk_fp8_f32 v14, v58, v59 op_sel:[0,0,1]
	v_cvt_pk_fp8_f32 v15, v70, v71 op_sel:[0,0,1]
	v_cvt_pk_fp8_f32 v16, v82, v83 op_sel:[0,0,1]
	v_cvt_pk_fp8_f32 v17, v98, v99 op_sel:[0,0,1]
	v_cvt_pk_fp8_f32 v18, v110, v111 op_sel:[0,0,1]
	v_cvt_pk_fp8_f32 v19, v114, v115 op_sel:[0,0,1]
	global_store_dwordx4 v[162:163], v[12:15], off
	s_nop 1
	v_add_co_u32_e32 v162, vcc, 0x8000, v162
	s_nop 1
	v_addc_co_u32_e32 v163, vcc, 0, v163, vcc
	global_store_dwordx4 v[162:163], v[16:19], off
	s_waitcnt vmcnt(19)
	ds_write2_b32 v171, v36, v37 offset1:1
	ds_write2_b32 v171, v38, v39 offset0:2 offset1:3
	s_waitcnt vmcnt(18)
	ds_write2_b32 v172, v44, v45 offset1:1
	ds_write2_b32 v173, v46, v47 offset1:1
	s_waitcnt vmcnt(17)
	ds_write2_b32 v174, v52, v53 offset1:1
	ds_write2_b32 v175, v54, v55 offset1:1
	s_waitcnt vmcnt(16)
	ds_write2_b32 v176, v64, v65 offset1:1
	ds_write2_b32 v177, v66, v67 offset1:1
	s_waitcnt vmcnt(15)
	ds_write2_b32 v178, v76, v77 offset1:1
	ds_write2_b32 v179, v78, v79 offset1:1
	s_waitcnt vmcnt(14)
	ds_write2_b32 v183, v88, v89 offset1:1
	ds_write2_b32 v184, v90, v91 offset1:1
	s_waitcnt vmcnt(13)
	ds_write2_b32 v185, v116, v117 offset1:1
	ds_write2_b32 v186, v118, v119 offset1:1
	s_waitcnt vmcnt(12)
	ds_write2_b32 v187, v128, v129 offset1:1
	ds_write2_b32 v189, v130, v131 offset1:1
	ds_read2_b32 v[4:5], v170 offset1:33
	ds_read2_b32 v[6:7], v170 offset0:66 offset1:99
	ds_read2_b32 v[8:9], v170 offset0:132 offset1:165
	ds_read2_b32 v[10:11], v170 offset0:198 offset1:231
	ds_read2_b32 v[12:13], v188 offset0:8 offset1:41
	ds_read2_b32 v[14:15], v188 offset0:74 offset1:107
	ds_read2_b32 v[16:17], v188 offset0:140 offset1:173
	ds_read2_b32 v[18:19], v188 offset0:206 offset1:239
	ds_read2_b32 v[36:37], v190 offset0:16 offset1:49
	ds_read2_b32 v[38:39], v190 offset0:82 offset1:115
	ds_read2_b32 v[44:45], v190 offset0:148 offset1:181
	ds_read2_b32 v[46:47], v190 offset0:214 offset1:247
	ds_read2_b32 v[52:53], v191 offset0:24 offset1:57
	ds_read2_b32 v[54:55], v191 offset0:90 offset1:123
	ds_read2_b32 v[56:57], v191 offset0:156 offset1:189
	ds_read2_b32 v[58:59], v191 offset0:222 offset1:255
	v_mov_b32_e32 v20, v3
	v_mov_b32_e32 v21, v3
	v_mov_b32_e32 v22, v3
	v_mov_b32_e32 v23, v3
	s_waitcnt lgkmcnt(14)
	v_mul_f32_e32 v4, 0x42800000, v4
	v_mul_f32_e32 v5, 0x42800000, v5
	s_waitcnt lgkmcnt(13)
	v_mul_f32_e32 v8, 0x42800000, v8
	v_mul_f32_e32 v9, 0x42800000, v9
	s_waitcnt lgkmcnt(11)
	v_mul_f32_e32 v12, 0x42800000, v12
	v_mul_f32_e32 v13, 0x42800000, v13
	s_waitcnt lgkmcnt(9)
	v_mul_f32_e32 v16, 0x42800000, v16
	v_mul_f32_e32 v17, 0x42800000, v17
	v_mov_b32_e32 v24, v3
	v_mov_b32_e32 v25, v3
	v_mov_b32_e32 v26, v3
	v_mov_b32_e32 v27, v3
	s_waitcnt lgkmcnt(7)
	v_mul_f32_e32 v36, 0x42800000, v36
	v_mul_f32_e32 v37, 0x42800000, v37
	s_waitcnt lgkmcnt(5)
	v_mul_f32_e32 v44, 0x42800000, v44
	v_mul_f32_e32 v45, 0x42800000, v45
	s_waitcnt lgkmcnt(3)
	v_mul_f32_e32 v52, 0x42800000, v52
	v_mul_f32_e32 v53, 0x42800000, v53
	s_waitcnt lgkmcnt(1)
	v_mul_f32_e32 v56, 0x42800000, v56
	v_mul_f32_e32 v57, 0x42800000, v57
	v_cvt_pk_fp8_f32 v20, v4, v5
	v_cvt_pk_fp8_f32 v21, v8, v9
	v_cvt_pk_fp8_f32 v22, v12, v13
	v_cvt_pk_fp8_f32 v23, v16, v17
	v_cvt_pk_fp8_f32 v24, v36, v37
	v_cvt_pk_fp8_f32 v25, v44, v45
	v_cvt_pk_fp8_f32 v26, v52, v53
	v_cvt_pk_fp8_f32 v27, v56, v57
	v_mul_f32_e32 v6, 0x42800000, v6
	v_mul_f32_e32 v7, 0x42800000, v7
	v_mul_f32_e32 v10, 0x42800000, v10
	v_mul_f32_e32 v11, 0x42800000, v11
	v_mul_f32_e32 v14, 0x42800000, v14
	v_mul_f32_e32 v15, 0x42800000, v15
	v_mul_f32_e32 v18, 0x42800000, v18
	v_mul_f32_e32 v19, 0x42800000, v19
	v_mul_f32_e32 v38, 0x42800000, v38
	v_mul_f32_e32 v39, 0x42800000, v39
	v_mul_f32_e32 v46, 0x42800000, v46
	v_mul_f32_e32 v47, 0x42800000, v47
	v_mul_f32_e32 v54, 0x42800000, v54
	v_mul_f32_e32 v55, 0x42800000, v55
	s_waitcnt lgkmcnt(0)
	v_mul_f32_e32 v58, 0x42800000, v58
	v_mul_f32_e32 v59, 0x42800000, v59
	v_cvt_pk_fp8_f32 v20, v6, v7 op_sel:[0,0,1]
	v_cvt_pk_fp8_f32 v21, v10, v11 op_sel:[0,0,1]
	v_cvt_pk_fp8_f32 v22, v14, v15 op_sel:[0,0,1]
	v_cvt_pk_fp8_f32 v23, v18, v19 op_sel:[0,0,1]
	v_cvt_pk_fp8_f32 v24, v38, v39 op_sel:[0,0,1]
	v_cvt_pk_fp8_f32 v25, v46, v47 op_sel:[0,0,1]
	v_cvt_pk_fp8_f32 v26, v54, v55 op_sel:[0,0,1]
	v_cvt_pk_fp8_f32 v27, v58, v59 op_sel:[0,0,1]
	global_store_dwordx4 v[158:159], v[20:23], off
	s_nop 1
	v_add_co_u32_e32 v158, vcc, 0x8000, v158
	s_nop 1
	v_addc_co_u32_e32 v159, vcc, 0, v159, vcc
	global_store_dwordx4 v[158:159], v[24:27], off
	s_waitcnt vmcnt(13)
	ds_write2_b32 v171, v40, v41 offset1:1
	ds_write2_b32 v171, v42, v43 offset0:2 offset1:3
	s_waitcnt vmcnt(12)
	ds_write2_b32 v172, v48, v49 offset1:1
	ds_write2_b32 v173, v50, v51 offset1:1
	s_waitcnt vmcnt(11)
	ds_write2_b32 v174, v60, v61 offset1:1
	ds_write2_b32 v175, v62, v63 offset1:1
	s_waitcnt vmcnt(10)
	ds_write2_b32 v176, v72, v73 offset1:1
	ds_write2_b32 v177, v74, v75 offset1:1
	s_waitcnt vmcnt(9)
	ds_write2_b32 v178, v84, v85 offset1:1
	ds_write2_b32 v179, v86, v87 offset1:1
	s_waitcnt vmcnt(8)
	ds_write2_b32 v183, v100, v101 offset1:1
	ds_write2_b32 v184, v102, v103 offset1:1
	s_waitcnt vmcnt(7)
	ds_write2_b32 v185, v104, v105 offset1:1
	ds_write2_b32 v186, v106, v107 offset1:1
	s_waitcnt vmcnt(6)
	ds_write2_b32 v187, v92, v93 offset1:1
	ds_write2_b32 v189, v94, v95 offset1:1
	ds_read2_b32 v[4:5], v170 offset1:33
	ds_read2_b32 v[6:7], v170 offset0:66 offset1:99
	ds_read2_b32 v[8:9], v170 offset0:132 offset1:165
	ds_read2_b32 v[10:11], v170 offset0:198 offset1:231
	ds_read2_b32 v[12:13], v188 offset0:8 offset1:41
	ds_read2_b32 v[14:15], v188 offset0:74 offset1:107
	ds_read2_b32 v[16:17], v188 offset0:140 offset1:173
	ds_read2_b32 v[18:19], v188 offset0:206 offset1:239
	ds_read2_b32 v[20:21], v190 offset0:16 offset1:49
	ds_read2_b32 v[22:23], v190 offset0:82 offset1:115
	ds_read2_b32 v[24:25], v190 offset0:148 offset1:181
	ds_read2_b32 v[26:27], v190 offset0:214 offset1:247
	ds_read2_b32 v[36:37], v191 offset0:24 offset1:57
	ds_read2_b32 v[38:39], v191 offset0:90 offset1:123
	ds_read2_b32 v[40:41], v191 offset0:156 offset1:189
	ds_read2_b32 v[42:43], v191 offset0:222 offset1:255
	v_mov_b32_e32 v28, v3
	v_mov_b32_e32 v29, v3
	v_mov_b32_e32 v30, v3
	v_mov_b32_e32 v31, v3
	s_waitcnt lgkmcnt(14)
	v_mul_f32_e32 v4, 0x42800000, v4
	v_mul_f32_e32 v5, 0x42800000, v5
	s_waitcnt lgkmcnt(13)
	v_mul_f32_e32 v8, 0x42800000, v8
	v_mul_f32_e32 v9, 0x42800000, v9
	s_waitcnt lgkmcnt(11)
	v_mul_f32_e32 v12, 0x42800000, v12
	v_mul_f32_e32 v13, 0x42800000, v13
	s_waitcnt lgkmcnt(9)
	v_mul_f32_e32 v16, 0x42800000, v16
	v_mul_f32_e32 v17, 0x42800000, v17
	v_mov_b32_e32 v32, v3
	v_mov_b32_e32 v33, v3
	v_mov_b32_e32 v34, v3
	v_mov_b32_e32 v35, v3
	s_waitcnt lgkmcnt(7)
	v_mul_f32_e32 v20, 0x42800000, v20
	v_mul_f32_e32 v21, 0x42800000, v21
	s_waitcnt lgkmcnt(5)
	v_mul_f32_e32 v24, 0x42800000, v24
	v_mul_f32_e32 v25, 0x42800000, v25
	s_waitcnt lgkmcnt(3)
	v_mul_f32_e32 v36, 0x42800000, v36
	v_mul_f32_e32 v37, 0x42800000, v37
	s_waitcnt lgkmcnt(1)
	v_mul_f32_e32 v40, 0x42800000, v40
	v_mul_f32_e32 v41, 0x42800000, v41
	v_cvt_pk_fp8_f32 v28, v4, v5
	v_cvt_pk_fp8_f32 v29, v8, v9
	v_cvt_pk_fp8_f32 v30, v12, v13
	v_cvt_pk_fp8_f32 v31, v16, v17
	v_cvt_pk_fp8_f32 v32, v20, v21
	v_cvt_pk_fp8_f32 v33, v24, v25
	v_cvt_pk_fp8_f32 v34, v36, v37
	v_cvt_pk_fp8_f32 v35, v40, v41
	v_mul_f32_e32 v6, 0x42800000, v6
	v_mul_f32_e32 v7, 0x42800000, v7
	v_mul_f32_e32 v10, 0x42800000, v10
	v_mul_f32_e32 v11, 0x42800000, v11
	v_mul_f32_e32 v14, 0x42800000, v14
	v_mul_f32_e32 v15, 0x42800000, v15
	v_mul_f32_e32 v18, 0x42800000, v18
	v_mul_f32_e32 v19, 0x42800000, v19
	v_mul_f32_e32 v22, 0x42800000, v22
	v_mul_f32_e32 v23, 0x42800000, v23
	v_mul_f32_e32 v26, 0x42800000, v26
	v_mul_f32_e32 v27, 0x42800000, v27
	v_mul_f32_e32 v38, 0x42800000, v38
	v_mul_f32_e32 v39, 0x42800000, v39
	s_waitcnt lgkmcnt(0)
	v_mul_f32_e32 v42, 0x42800000, v42
	v_mul_f32_e32 v43, 0x42800000, v43
	v_cvt_pk_fp8_f32 v28, v6, v7 op_sel:[0,0,1]
	v_cvt_pk_fp8_f32 v29, v10, v11 op_sel:[0,0,1]
	v_cvt_pk_fp8_f32 v30, v14, v15 op_sel:[0,0,1]
	v_cvt_pk_fp8_f32 v31, v18, v19 op_sel:[0,0,1]
	v_cvt_pk_fp8_f32 v32, v22, v23 op_sel:[0,0,1]
	v_cvt_pk_fp8_f32 v33, v26, v27 op_sel:[0,0,1]
	v_cvt_pk_fp8_f32 v34, v38, v39 op_sel:[0,0,1]
	v_cvt_pk_fp8_f32 v35, v42, v43 op_sel:[0,0,1]
	v_lshl_add_u64 v[4:5], v[160:161], 0, v[156:157]
	global_store_dwordx4 v[4:5], v[28:31], off
	s_nop 1
	v_add_co_u32_e32 v4, vcc, 0x8000, v4
	s_nop 1
	v_addc_co_u32_e32 v5, vcc, 0, v5, vcc
	global_store_dwordx4 v[4:5], v[32:35], off
	s_add_i32 s5, s5, 32
	s_cmp_lt_i32 s5, s4
	s_cbranch_scc1 .LBB6_1475

.LBB6_1602:
	s_max_i32 s0, s90, 0xa6c0
	s_min_i32 s30, s91, 0x12ac0
	s_cmp_le_i32 s30, s0
	s_cbranch_scc1 .LBB6_1607
	s_sub_i32 s1, s30, s0
	s_mov_b32 s2, 18
	s_cmp_lt_i32 s1, 32
	s_cbranch_scc1 .LBB6_1607
	s_add_i32 s0, s0, s67
	s_add_i32 s30, s30, 0xffff5940
	s_add_i32 s31, s0, 0xffff5940
	s_cmp_ge_i32 s31, s30
	s_cbranch_scc1 .LBB6_1607
	s_ashr_i32 s3, s2, 31
	s_lshl_b64 s[0:1], s[2:3], 3
	s_add_u32 s0, s76, s0
	s_addc_u32 s1, s77, s1
	s_load_dwordx2 s[2:3], s[0:1], 0x0
	s_waitcnt vmcnt(0)
	v_lshrrev_b32_e32 v4, 3, v166
	v_lshlrev_b32_e32 v5, 2, v166
	v_lshlrev_b32_e32 v6, 5, v166
	v_mul_u32_u24_e32 v2, 0x2c00, v4
	v_and_b32_e32 v5, 28, v5
	v_lshrrev_b32_e32 v135, 2, v166
	v_lshlrev_b32_e32 v132, 4, v166
	v_and_b32_e32 v132, 48, v132
	s_add_u32 s34, s6, 0x81080000
	v_or_b32_e32 v2, v2, v5
	v_lshl_add_u32 v5, v5, 2, s66
	v_mul_u32_u24_e32 v4, 0x84, v4
	v_mul_u32_u24_e32 v6, 0x84, v132
	v_lshlrev_b32_e32 v7, 2, v135
	s_addc_u32 s35, s7, 0
	v_and_b32_e32 v134, 31, v167
	v_lshlrev_b32_e32 v2, 2, v2
	v_add3_u32 v136, s66, v6, v7
	v_mov_b32_e32 v133, v3
	v_add_u32_e32 v137, v5, v4
.LBB6_1606:
	s_mul_hi_i32 s0, s31, 0x2e8ba2e9
	s_lshr_b32 s1, s0, 31
	s_ashr_i32 s28, s0, 11
	s_add_i32 s28, s28, s1
	s_mul_i32 s0, s28, 0xffffd400
	s_add_i32 s0, s0, s31
	s_ashr_i32 s0, s0, 1
	s_and_b32 s1, s0, -8
	s_and_b32 s0, s31, 7
	s_or_b32 s1, s1, s0
	s_waitcnt lgkmcnt(0)
	s_mul_hi_i32 s4, s1, 0x2e8ba2e9
	s_lshr_b32 s5, s4, 31
	s_ashr_i32 s4, s4, 6
	s_add_i32 s4, s4, s5
	s_mul_i32 s5, s4, 0xfffffea0
	s_add_i32 s5, s5, s1
	s_lshl_b32 s1, s4, 7
	s_lshl_b32 s4, s31, 3
	s_and_b32 s22, s4, 64
	s_lshl_b32 s51, s5, 5
	s_or_b32 s26, s1, s22
	s_mul_i32 s4, s28, 0x5800000
	s_mul_hi_i32 s1, s28, 0x5800000
	s_add_u32 s12, s2, s4
	s_addc_u32 s1, s3, s1
	s_and_b32 s4, s51, 0xe0
	s_cmpk_lt_u32 s4, 0x80
	v_or_b32_e32 v4, s4, v134
	s_cselect_b64 vcc, -1, 0
	s_lshl_b32 s4, s5, 4
	s_and_b32 s4, s4, 0xffffff80
	v_or_b32_e32 v5, s4, v4
	s_addk_i32 s4, 0x1580
	v_add_u32_e32 v4, s4, v4
	v_cndmask_b32_e32 v4, v4, v5, vcc
	s_ashr_i32 s27, s26, 31
	v_readfirstlane_b32 s4, v4
	s_andn2_b32 s4, s4, 31
	s_mul_i32 s13, s26, 0xb000
	s_mul_hi_i32 s5, s26, 0xb000
	s_add_u32 s12, s12, s13
	s_addc_u32 s1, s1, s5
	s_ashr_i32 s5, s4, 31
	s_lshl_b64 s[4:5], s[4:5], 2
	s_add_u32 s4, s12, s4
	s_addc_u32 s5, s1, s5
	s_mov_b64 s[12:13], s[4:5]
	v_mov_b32_e32 v138, v3
	v_lshl_add_u64 v[4:5], s[12:13], 0, v[2:3]
	s_add_u32 s12, s4, 0x58000
	s_addc_u32 s13, s5, 0
	global_load_dwordx4 v[128:131], v[4:5], off nt
	v_mov_b32_e32 v139, v3
	v_lshl_add_u64 v[4:5], s[12:13], 0, v[2:3]
	s_add_u32 s12, s4, 0xb0000
	s_addc_u32 s13, s5, 0
	global_load_dwordx4 v[124:127], v[4:5], off nt
	s_nop 0
	v_lshl_add_u64 v[4:5], s[12:13], 0, v[2:3]
	s_add_u32 s12, s4, 0x108000
	s_addc_u32 s13, s5, 0
	global_load_dwordx4 v[120:123], v[4:5], off nt
	s_nop 0
	v_lshl_add_u64 v[4:5], s[12:13], 0, v[2:3]
	s_add_u32 s12, s4, 0x160000
	s_addc_u32 s13, s5, 0
	global_load_dwordx4 v[116:119], v[4:5], off nt
	s_nop 0
	v_lshl_add_u64 v[4:5], s[12:13], 0, v[2:3]
	s_add_u32 s12, s4, 0x1b8000
	s_addc_u32 s13, s5, 0
	global_load_dwordx4 v[112:115], v[4:5], off nt
	s_nop 0
	v_lshl_add_u64 v[4:5], s[12:13], 0, v[2:3]
	s_add_u32 s12, s4, 0x210000
	s_addc_u32 s13, s5, 0
	s_add_u32 s4, s4, 0x268000
	global_load_dwordx4 v[108:111], v[4:5], off nt
	s_addc_u32 s5, s5, 0
	v_lshl_add_u64 v[4:5], s[12:13], 0, v[2:3]
	global_load_dwordx4 v[104:107], v[4:5], off nt
	s_add_i32 s1, s31, 8
	v_lshl_add_u64 v[4:5], s[4:5], 0, v[2:3]
	s_mul_hi_i32 s4, s1, 0x2e8ba2e9
	s_lshr_b32 s5, s4, 31
	s_ashr_i32 s49, s4, 11
	s_add_i32 s49, s49, s5
	s_mul_i32 s4, s49, 0xffffd400
	s_add_i32 s4, s4, s1
	s_ashr_i32 s4, s4, 1
	s_and_b32 s4, s4, -8
	s_or_b32 s4, s4, s0
	s_mul_hi_i32 s5, s4, 0x2e8ba2e9
	s_lshr_b32 s12, s5, 31
	s_ashr_i32 s5, s5, 6
	s_add_i32 s5, s5, s12
	s_mul_i32 s12, s5, 0xfffffea0
	s_lshl_b32 s1, s1, 3
	s_add_i32 s12, s12, s4
	s_lshl_b32 s4, s5, 7
	s_and_b32 s1, s1, 64
	s_lshl_b32 s50, s12, 5
	s_or_b32 s24, s4, s1
	s_mul_i32 s4, s49, 0x5800000
	s_mul_hi_i32 s1, s49, 0x5800000
	s_add_u32 s5, s2, s4
	s_addc_u32 s1, s3, s1
	s_and_b32 s4, s50, 0xe0
	s_cmpk_lt_u32 s4, 0x80
	global_load_dwordx4 v[100:103], v[4:5], off nt
	v_or_b32_e32 v4, s4, v134
	s_cselect_b64 vcc, -1, 0
	s_lshl_b32 s4, s12, 4
	s_and_b32 s4, s4, 0xffffff80
	v_or_b32_e32 v5, s4, v4
	s_addk_i32 s4, 0x1580
	v_add_u32_e32 v4, s4, v4
	v_cndmask_b32_e32 v4, v4, v5, vcc
	s_ashr_i32 s25, s24, 31
	v_readfirstlane_b32 s4, v4
	s_andn2_b32 s4, s4, 31
	s_mul_i32 s13, s24, 0xb000
	s_mul_hi_i32 s12, s24, 0xb000
	s_add_u32 s13, s5, s13
	s_addc_u32 s1, s1, s12
	s_ashr_i32 s5, s4, 31
	s_lshl_b64 s[4:5], s[4:5], 2
	s_add_u32 s4, s13, s4
	s_addc_u32 s5, s1, s5
	s_mov_b64 s[12:13], s[4:5]
	s_nop 0
	v_lshl_add_u64 v[4:5], s[12:13], 0, v[2:3]
	s_add_u32 s12, s4, 0x58000
	s_addc_u32 s13, s5, 0
	global_load_dwordx4 v[68:71], v[4:5], off nt
	s_nop 0
	v_lshl_add_u64 v[4:5], s[12:13], 0, v[2:3]
	s_add_u32 s12, s4, 0xb0000
	s_addc_u32 s13, s5, 0
	global_load_dwordx4 v[72:75], v[4:5], off nt
	s_nop 0
	v_lshl_add_u64 v[4:5], s[12:13], 0, v[2:3]
	s_add_u32 s12, s4, 0x108000
	s_addc_u32 s13, s5, 0
	global_load_dwordx4 v[76:79], v[4:5], off nt
	s_nop 0
	v_lshl_add_u64 v[4:5], s[12:13], 0, v[2:3]
	s_add_u32 s12, s4, 0x160000
	s_addc_u32 s13, s5, 0
	global_load_dwordx4 v[80:83], v[4:5], off nt
	s_nop 0
	v_lshl_add_u64 v[4:5], s[12:13], 0, v[2:3]
	s_add_u32 s12, s4, 0x1b8000
	s_addc_u32 s13, s5, 0
	global_load_dwordx4 v[84:87], v[4:5], off nt
	s_nop 0
	v_lshl_add_u64 v[4:5], s[12:13], 0, v[2:3]
	s_add_u32 s12, s4, 0x210000
	s_addc_u32 s13, s5, 0
	s_add_u32 s4, s4, 0x268000
	global_load_dwordx4 v[88:91], v[4:5], off nt
	s_addc_u32 s5, s5, 0
	v_lshl_add_u64 v[4:5], s[12:13], 0, v[2:3]
	global_load_dwordx4 v[92:95], v[4:5], off nt
	s_add_i32 s1, s31, 16
	v_lshl_add_u64 v[4:5], s[4:5], 0, v[2:3]
	s_mul_hi_i32 s4, s1, 0x2e8ba2e9
	s_lshr_b32 s5, s4, 31
	s_ashr_i32 s47, s4, 11
	s_add_i32 s47, s47, s5
	s_mul_i32 s4, s47, 0xffffd400
	s_add_i32 s4, s4, s1
	s_ashr_i32 s1, s4, 1
	s_and_b32 s1, s1, -8
	s_or_b32 s1, s1, s0
	s_mul_hi_i32 s4, s1, 0x2e8ba2e9
	s_lshr_b32 s5, s4, 31
	s_ashr_i32 s4, s4, 6
	s_add_i32 s4, s4, s5
	s_mul_i32 s5, s4, 0xfffffea0
	s_add_i32 s5, s5, s1
	s_lshl_b32 s1, s4, 7
	s_lshl_b32 s48, s5, 5
	s_or_b32 s22, s1, s22
	s_mul_i32 s4, s47, 0x5800000
	s_mul_hi_i32 s1, s47, 0x5800000
	s_add_u32 s12, s2, s4
	s_addc_u32 s1, s3, s1
	s_and_b32 s4, s48, 0xe0
	s_cmpk_lt_u32 s4, 0x80
	global_load_dwordx4 v[96:99], v[4:5], off nt
	v_or_b32_e32 v4, s4, v134
	s_cselect_b64 vcc, -1, 0
	s_lshl_b32 s4, s5, 4
	s_and_b32 s4, s4, 0xffffff80
	v_or_b32_e32 v5, s4, v4
	s_addk_i32 s4, 0x1580
	v_add_u32_e32 v4, s4, v4
	v_cndmask_b32_e32 v4, v4, v5, vcc
	s_ashr_i32 s23, s22, 31
	v_readfirstlane_b32 s4, v4
	s_andn2_b32 s4, s4, 31
	s_mul_i32 s13, s22, 0xb000
	s_mul_hi_i32 s5, s22, 0xb000
	s_add_u32 s12, s12, s13
	s_addc_u32 s1, s1, s5
	s_ashr_i32 s5, s4, 31
	s_lshl_b64 s[4:5], s[4:5], 2
	s_add_u32 s4, s12, s4
	s_addc_u32 s5, s1, s5
	s_mov_b64 s[12:13], s[4:5]
	s_nop 0
	v_lshl_add_u64 v[4:5], s[12:13], 0, v[2:3]
	s_add_u32 s12, s4, 0x58000
	s_addc_u32 s13, s5, 0
	global_load_dwordx4 v[36:39], v[4:5], off nt
	s_nop 0
	v_lshl_add_u64 v[4:5], s[12:13], 0, v[2:3]
	s_add_u32 s12, s4, 0xb0000
	s_addc_u32 s13, s5, 0
	global_load_dwordx4 v[40:43], v[4:5], off nt
	s_nop 0
	v_lshl_add_u64 v[4:5], s[12:13], 0, v[2:3]
	s_add_u32 s12, s4, 0x108000
	s_addc_u32 s13, s5, 0
	global_load_dwordx4 v[44:47], v[4:5], off nt
	s_nop 0
	v_lshl_add_u64 v[4:5], s[12:13], 0, v[2:3]
	s_add_u32 s12, s4, 0x160000
	s_addc_u32 s13, s5, 0
	global_load_dwordx4 v[48:51], v[4:5], off nt
	s_nop 0
	v_lshl_add_u64 v[4:5], s[12:13], 0, v[2:3]
	s_add_u32 s12, s4, 0x1b8000
	s_addc_u32 s13, s5, 0
	global_load_dwordx4 v[52:55], v[4:5], off nt
	s_nop 0
	v_lshl_add_u64 v[4:5], s[12:13], 0, v[2:3]
	s_add_u32 s12, s4, 0x210000
	s_addc_u32 s13, s5, 0
	s_add_u32 s4, s4, 0x268000
	global_load_dwordx4 v[56:59], v[4:5], off nt
	s_addc_u32 s5, s5, 0
	v_lshl_add_u64 v[4:5], s[12:13], 0, v[2:3]
	global_load_dwordx4 v[60:63], v[4:5], off nt
	s_add_i32 s1, s31, 24
	v_lshl_add_u64 v[4:5], s[4:5], 0, v[2:3]
	s_mul_hi_i32 s4, s1, 0x2e8ba2e9
	s_lshr_b32 s5, s4, 31
	s_ashr_i32 s36, s4, 11
	s_add_i32 s36, s36, s5
	s_mul_i32 s4, s36, 0xffffd400
	s_add_i32 s4, s4, s1
	s_ashr_i32 s4, s4, 1
	s_and_b32 s4, s4, -8
	s_or_b32 s0, s4, s0
	s_mul_hi_i32 s4, s0, 0x2e8ba2e9
	s_lshr_b32 s5, s4, 31
	s_ashr_i32 s4, s4, 6
	s_add_i32 s4, s4, s5
	s_mul_i32 s5, s4, 0xfffffea0
	s_lshl_b32 s1, s1, 3
	s_add_i32 s5, s5, s0
	s_lshl_b32 s0, s4, 7
	s_and_b32 s1, s1, 64
	s_lshl_b32 s37, s5, 5
	s_or_b32 s4, s0, s1
	s_mul_i32 s1, s36, 0x5800000
	s_mul_hi_i32 s0, s36, 0x5800000
	s_add_u32 s1, s2, s1
	s_addc_u32 s12, s3, s0
	s_and_b32 s0, s37, 0xe0
	s_cmpk_lt_u32 s0, 0x80
	global_load_dwordx4 v[64:67], v[4:5], off nt
	v_or_b32_e32 v4, s0, v134
	s_cselect_b64 vcc, -1, 0
	s_lshl_b32 s0, s5, 4
	s_and_b32 s0, s0, 0xffffff80
	v_or_b32_e32 v5, s0, v4
	s_addk_i32 s0, 0x1580
	v_add_u32_e32 v4, s0, v4
	v_cndmask_b32_e32 v4, v4, v5, vcc
	s_ashr_i32 s5, s4, 31
	v_readfirstlane_b32 s0, v4
	s_andn2_b32 s0, s0, 31
	s_mul_i32 s29, s4, 0xb000
	s_mul_hi_i32 s13, s4, 0xb000
	s_add_u32 s29, s1, s29
	s_addc_u32 s12, s12, s13
	s_ashr_i32 s1, s0, 31
	s_lshl_b64 s[0:1], s[0:1], 2
	s_add_u32 s0, s29, s0
	s_addc_u32 s1, s12, s1
	s_mov_b64 s[12:13], s[0:1]
	s_nop 0
	v_lshl_add_u64 v[4:5], s[12:13], 0, v[2:3]
	s_add_u32 s12, s0, 0x58000
	s_addc_u32 s13, s1, 0
	global_load_dwordx4 v[4:7], v[4:5], off nt
	s_nop 0
	v_lshl_add_u64 v[8:9], s[12:13], 0, v[2:3]
	s_add_u32 s12, s0, 0xb0000
	s_addc_u32 s13, s1, 0
	global_load_dwordx4 v[8:11], v[8:9], off nt
	s_nop 0
	v_lshl_add_u64 v[12:13], s[12:13], 0, v[2:3]
	s_add_u32 s12, s0, 0x108000
	s_addc_u32 s13, s1, 0
	global_load_dwordx4 v[12:15], v[12:13], off nt
	s_nop 0
	v_lshl_add_u64 v[16:17], s[12:13], 0, v[2:3]
	s_add_u32 s12, s0, 0x160000
	s_addc_u32 s13, s1, 0
	global_load_dwordx4 v[16:19], v[16:17], off nt
	s_nop 0
	v_lshl_add_u64 v[20:21], s[12:13], 0, v[2:3]
	s_add_u32 s12, s0, 0x1b8000
	s_addc_u32 s13, s1, 0
	global_load_dwordx4 v[20:23], v[20:21], off nt
	s_nop 0
	v_lshl_add_u64 v[24:25], s[12:13], 0, v[2:3]
	s_add_u32 s12, s0, 0x210000
	s_addc_u32 s13, s1, 0
	s_add_u32 s0, s0, 0x268000
	global_load_dwordx4 v[24:27], v[24:25], off nt
	s_addc_u32 s1, s1, 0
	v_lshl_add_u64 v[28:29], s[12:13], 0, v[2:3]
	global_load_dwordx4 v[28:31], v[28:29], off nt
	s_nop 0
	v_lshl_add_u64 v[32:33], s[0:1], 0, v[2:3]
	global_load_dwordx4 v[32:35], v[32:33], off nt
	s_waitcnt vmcnt(31)
	ds_write2_b32 v137, v128, v129 offset1:1
	ds_write2_b32 v137, v130, v131 offset0:2 offset1:3
	v_add_u32_e32 v128, 0x420, v137
	s_waitcnt vmcnt(30)
	ds_write2_b32 v128, v124, v125 offset1:1
	v_add_u32_e32 v125, 0x840, v137
	s_waitcnt vmcnt(29)
	ds_write2_b32 v125, v120, v121 offset1:1
	v_add_u32_e32 v121, 0xc60, v137
	s_waitcnt vmcnt(28)
	ds_write2_b32 v121, v116, v117 offset1:1
	v_add_u32_e32 v117, 0x1080, v137
	s_waitcnt vmcnt(27)
	ds_write2_b32 v117, v112, v113 offset1:1
	v_add_u32_e32 v113, 0x14a0, v137
	s_waitcnt vmcnt(26)
	ds_write2_b32 v113, v108, v109 offset1:1
	v_add_u32_e32 v109, 0x18c0, v137
	s_waitcnt vmcnt(25)
	ds_write2_b32 v109, v104, v105 offset1:1
	v_add_u32_e32 v104, 0x18c8, v137
	v_add_u32_e32 v124, 0x428, v137
	v_add_u32_e32 v120, 0x848, v137
	v_add_u32_e32 v116, 0xc68, v137
	v_add_u32_e32 v112, 0x1088, v137
	v_add_u32_e32 v108, 0x14a8, v137
	ds_write2_b32 v104, v106, v107 offset1:1
	v_add_u32_e32 v105, 0x1ce0, v137
	v_add_u32_e32 v106, 0x1ce8, v137
	ds_write2_b32 v124, v126, v127 offset1:1
	ds_write2_b32 v120, v122, v123 offset1:1
	ds_write2_b32 v116, v118, v119 offset1:1
	ds_write2_b32 v112, v114, v115 offset1:1
	ds_write2_b32 v108, v110, v111 offset1:1
	s_waitcnt vmcnt(24)
	ds_write2_b32 v105, v100, v101 offset1:1
	ds_write2_b32 v106, v102, v103 offset1:1
	ds_read2_b32 v[110:111], v136 offset1:33
	ds_read2_b32 v[114:115], v136 offset0:66 offset1:99
	ds_read2_b32 v[118:119], v136 offset0:132 offset1:165
	ds_read2_b32 v[122:123], v136 offset0:198 offset1:231
	v_add_u32_e32 v102, 0x400, v136
	s_waitcnt lgkmcnt(3)
	v_mul_f32_e32 v101, 0x42800000, v110
	v_mul_f32_e32 v110, 0x42800000, v111
	v_mov_b32_e32 v103, v136
	v_cvt_pk_fp8_f32 v138, v101, v110
	ds_read2_b32 v[126:127], v102 offset0:8 offset1:41
	ds_read2_b32 v[130:131], v102 offset0:74 offset1:107
	ds_read2_b32 v[146:147], v102 offset0:140 offset1:173
	ds_read2_b32 v[148:149], v102 offset0:206 offset1:239
	ds_read2_b32 v[140:141], v103 offset0:16 offset1:49
	ds_read2_b32 v[142:143], v103 offset0:82 offset1:115
	ds_read2_b32 v[144:145], v103 offset0:148 offset1:181
	ds_read2_b32 v[150:151], v103 offset0:214 offset1:247
	s_waitcnt lgkmcnt(10)
	v_mul_f32_e32 v111, 0x42800000, v114
	v_mul_f32_e32 v114, 0x42800000, v115
	v_cvt_pk_fp8_f32 v138, v111, v114 op_sel:[0,0,1]
	s_waitcnt lgkmcnt(3)
	v_mul_f32_e32 v101, 0x42800000, v140
	v_mul_f32_e32 v110, 0x42800000, v141
	s_waitcnt lgkmcnt(2)
	v_mul_f32_e32 v111, 0x42800000, v142
	v_mov_b32_e32 v142, v3
	v_add_u32_e32 v107, 0x400, v136
	v_cvt_pk_fp8_f32 v142, v101, v110
	v_mul_f32_e32 v101, 0x42800000, v118
	v_mul_f32_e32 v110, 0x42800000, v119
	ds_read2_b32 v[152:153], v107 offset0:24 offset1:57
	ds_read2_b32 v[154:155], v107 offset0:90 offset1:123
	ds_read2_b32 v[156:157], v107 offset0:156 offset1:189
	ds_read2_b32 v[158:159], v107 offset0:222 offset1:255
	v_mul_f32_e32 v114, 0x42800000, v143
	v_cvt_pk_fp8_f32 v139, v101, v110
	s_waitcnt lgkmcnt(5)
	v_mul_f32_e32 v101, 0x42800000, v144
	v_mul_f32_e32 v110, 0x42800000, v145
	v_mov_b32_e32 v143, v3
	v_cvt_pk_fp8_f32 v143, v101, v110
	v_mul_f32_e32 v101, 0x42800000, v126
	v_mul_f32_e32 v110, 0x42800000, v127
	v_mov_b32_e32 v140, v3
	v_cvt_pk_fp8_f32 v140, v101, v110
	s_waitcnt lgkmcnt(3)
	v_mul_f32_e32 v101, 0x42800000, v152
	v_mul_f32_e32 v110, 0x42800000, v153
	v_mov_b32_e32 v144, v3
	v_cvt_pk_fp8_f32 v142, v111, v114 op_sel:[0,0,1]
	v_mul_f32_e32 v111, 0x42800000, v122
	v_mul_f32_e32 v114, 0x42800000, v123
	v_cvt_pk_fp8_f32 v144, v101, v110
	v_mul_f32_e32 v101, 0x42800000, v146
	v_mul_f32_e32 v110, 0x42800000, v147
	v_mov_b32_e32 v141, v3
	v_cvt_pk_fp8_f32 v139, v111, v114 op_sel:[0,0,1]
	v_mul_f32_e32 v111, 0x42800000, v150
	v_mul_f32_e32 v114, 0x42800000, v151
	v_cvt_pk_fp8_f32 v141, v101, v110
	s_waitcnt lgkmcnt(1)
	v_mul_f32_e32 v101, 0x42800000, v156
	v_mul_f32_e32 v110, 0x42800000, v157
	v_mov_b32_e32 v145, v3
	v_cvt_pk_fp8_f32 v143, v111, v114 op_sel:[0,0,1]
	v_mul_f32_e32 v111, 0x42800000, v130
	v_mul_f32_e32 v114, 0x42800000, v131
	v_cvt_pk_fp8_f32 v145, v101, v110
	s_mul_hi_i32 s0, s28, 0x1600000
	s_mul_i32 s28, s28, 0x1600000
	v_or_b32_e32 v100, s51, v135
	v_cvt_pk_fp8_f32 v140, v111, v114 op_sel:[0,0,1]
	v_mul_f32_e32 v111, 0x42800000, v154
	v_mul_f32_e32 v114, 0x42800000, v155
	s_add_u32 s28, s34, s28
	v_cvt_pk_fp8_f32 v144, v111, v114 op_sel:[0,0,1]
	v_mul_f32_e32 v111, 0x42800000, v148
	v_mul_f32_e32 v114, 0x42800000, v149
	v_ashrrev_i32_e32 v101, 31, v100
	s_addc_u32 s29, s35, s0
	v_cvt_pk_fp8_f32 v141, v111, v114 op_sel:[0,0,1]
	s_waitcnt lgkmcnt(0)
	v_mul_f32_e32 v111, 0x42800000, v158
	v_mul_f32_e32 v114, 0x42800000, v159
	v_lshlrev_b64 v[100:101], 11, v[100:101]
	v_cvt_pk_fp8_f32 v145, v111, v114 op_sel:[0,0,1]
	v_lshl_add_u64 v[100:101], s[28:29], 0, v[100:101]
	v_lshl_add_u64 v[100:101], v[100:101], 0, s[26:27]
	v_lshl_add_u64 v[100:101], v[100:101], 0, v[132:133]
	global_store_dwordx4 v[100:101], v[138:141], off
	s_nop 1
	v_add_co_u32_e32 v100, vcc, 0x8000, v100
	s_nop 1
	v_addc_co_u32_e32 v101, vcc, 0, v101, vcc
	global_store_dwordx4 v[100:101], v[142:145], off
	s_waitcnt vmcnt(25)
	ds_write2_b32 v137, v68, v69 offset1:1
	ds_write2_b32 v137, v70, v71 offset0:2 offset1:3
	s_waitcnt vmcnt(24)
	ds_write2_b32 v128, v72, v73 offset1:1
	ds_write2_b32 v124, v74, v75 offset1:1
	s_waitcnt vmcnt(23)
	ds_write2_b32 v125, v76, v77 offset1:1
	ds_write2_b32 v120, v78, v79 offset1:1
	s_waitcnt vmcnt(22)
	ds_write2_b32 v121, v80, v81 offset1:1
	ds_write2_b32 v116, v82, v83 offset1:1
	s_waitcnt vmcnt(21)
	ds_write2_b32 v117, v84, v85 offset1:1
	ds_write2_b32 v112, v86, v87 offset1:1
	s_waitcnt vmcnt(20)
	ds_write2_b32 v113, v88, v89 offset1:1
	ds_write2_b32 v108, v90, v91 offset1:1
	s_waitcnt vmcnt(19)
	ds_write2_b32 v109, v92, v93 offset1:1
	ds_write2_b32 v104, v94, v95 offset1:1
	s_waitcnt vmcnt(18)
	ds_write2_b32 v105, v96, v97 offset1:1
	ds_write2_b32 v106, v98, v99 offset1:1
	ds_read2_b32 v[94:95], v136 offset1:33
	ds_read2_b32 v[96:97], v136 offset0:66 offset1:99
	ds_read2_b32 v[92:93], v136 offset0:132 offset1:165
	ds_read2_b32 v[90:91], v136 offset0:198 offset1:231
	ds_read2_b32 v[84:85], v102 offset0:8 offset1:41
	ds_read2_b32 v[82:83], v102 offset0:74 offset1:107
	ds_read2_b32 v[76:77], v102 offset0:140 offset1:173
	ds_read2_b32 v[74:75], v102 offset0:206 offset1:239
	ds_read2_b32 v[98:99], v103 offset0:16 offset1:49
	ds_read2_b32 v[100:101], v103 offset0:82 offset1:115
	ds_read2_b32 v[88:89], v103 offset0:148 offset1:181
	ds_read2_b32 v[86:87], v103 offset0:214 offset1:247
	ds_read2_b32 v[80:81], v107 offset0:24 offset1:57
	ds_read2_b32 v[78:79], v107 offset0:90 offset1:123
	ds_read2_b32 v[72:73], v107 offset0:156 offset1:189
	ds_read2_b32 v[70:71], v107 offset0:222 offset1:255
	s_waitcnt lgkmcnt(14)
	v_mul_f32_e32 v69, 0x42800000, v94
	v_mul_f32_e32 v95, 0x42800000, v95
	v_mov_b32_e32 v94, v3
	v_cvt_pk_fp8_f32 v94, v69, v95
	s_waitcnt lgkmcnt(7)
	v_mul_f32_e32 v69, 0x42800000, v98
	v_mul_f32_e32 v95, 0x42800000, v99
	v_mov_b32_e32 v98, v3
	v_cvt_pk_fp8_f32 v98, v69, v95
	v_mul_f32_e32 v96, 0x42800000, v96
	v_mul_f32_e32 v97, 0x42800000, v97
	v_mul_f32_e32 v69, 0x42800000, v92
	v_mul_f32_e32 v92, 0x42800000, v93
	v_mov_b32_e32 v95, v3
	v_cvt_pk_fp8_f32 v94, v96, v97 op_sel:[0,0,1]
	s_waitcnt lgkmcnt(6)
	v_mul_f32_e32 v96, 0x42800000, v100
	v_mul_f32_e32 v97, 0x42800000, v101
	v_cvt_pk_fp8_f32 v95, v69, v92
	s_waitcnt lgkmcnt(5)
	v_mul_f32_e32 v69, 0x42800000, v88
	v_mul_f32_e32 v88, 0x42800000, v89
	v_mov_b32_e32 v99, v3
	v_cvt_pk_fp8_f32 v98, v96, v97 op_sel:[0,0,1]
	v_cvt_pk_fp8_f32 v99, v69, v88
	v_mul_f32_e32 v69, 0x42800000, v84
	v_mul_f32_e32 v84, 0x42800000, v85
	v_mov_b32_e32 v96, v3
	v_cvt_pk_fp8_f32 v96, v69, v84
	s_waitcnt lgkmcnt(3)
	v_mul_f32_e32 v69, 0x42800000, v80
	v_mul_f32_e32 v80, 0x42800000, v81
	v_mov_b32_e32 v100, v3
	v_cvt_pk_fp8_f32 v100, v69, v80
	v_mul_f32_e32 v69, 0x42800000, v76
	v_mul_f32_e32 v76, 0x42800000, v77
	v_mov_b32_e32 v97, v3
	v_cvt_pk_fp8_f32 v97, v69, v76
	s_waitcnt lgkmcnt(1)
	v_mul_f32_e32 v69, 0x42800000, v72
	v_mul_f32_e32 v72, 0x42800000, v73
	v_mov_b32_e32 v101, v3
	v_cvt_pk_fp8_f32 v101, v69, v72
	s_mul_hi_i32 s0, s49, 0x1600000
	s_mul_i32 s49, s49, 0x1600000
	v_or_b32_e32 v68, s50, v135
	s_add_u32 s26, s34, s49
	v_mul_f32_e32 v90, 0x42800000, v90
	v_mul_f32_e32 v91, 0x42800000, v91
	v_mul_f32_e32 v82, 0x42800000, v82
	v_mul_f32_e32 v83, 0x42800000, v83
	v_mul_f32_e32 v74, 0x42800000, v74
	v_mul_f32_e32 v75, 0x42800000, v75
	v_ashrrev_i32_e32 v69, 31, v68
	s_addc_u32 s27, s35, s0
	v_cvt_pk_fp8_f32 v95, v90, v91 op_sel:[0,0,1]
	v_mul_f32_e32 v86, 0x42800000, v86
	v_mul_f32_e32 v87, 0x42800000, v87
	v_cvt_pk_fp8_f32 v96, v82, v83 op_sel:[0,0,1]
	v_mul_f32_e32 v78, 0x42800000, v78
	v_mul_f32_e32 v79, 0x42800000, v79
	v_cvt_pk_fp8_f32 v97, v74, v75 op_sel:[0,0,1]
	s_waitcnt lgkmcnt(0)
	v_mul_f32_e32 v70, 0x42800000, v70
	v_mul_f32_e32 v71, 0x42800000, v71
	v_lshlrev_b64 v[68:69], 11, v[68:69]
	v_cvt_pk_fp8_f32 v99, v86, v87 op_sel:[0,0,1]
	v_cvt_pk_fp8_f32 v100, v78, v79 op_sel:[0,0,1]
	v_cvt_pk_fp8_f32 v101, v70, v71 op_sel:[0,0,1]
	v_lshl_add_u64 v[68:69], s[26:27], 0, v[68:69]
	v_lshl_add_u64 v[68:69], v[68:69], 0, s[24:25]
	v_lshl_add_u64 v[68:69], v[68:69], 0, v[132:133]
	global_store_dwordx4 v[68:69], v[94:97], off
	s_nop 1
	v_add_co_u32_e32 v68, vcc, 0x8000, v68
	s_nop 1
	v_addc_co_u32_e32 v69, vcc, 0, v69, vcc
	global_store_dwordx4 v[68:69], v[98:101], off
	s_waitcnt vmcnt(19)
	ds_write2_b32 v137, v36, v37 offset1:1
	ds_write2_b32 v137, v38, v39 offset0:2 offset1:3
	s_waitcnt vmcnt(18)
	ds_write2_b32 v128, v40, v41 offset1:1
	ds_write2_b32 v124, v42, v43 offset1:1
	s_waitcnt vmcnt(17)
	ds_write2_b32 v125, v44, v45 offset1:1
	ds_write2_b32 v120, v46, v47 offset1:1
	s_waitcnt vmcnt(16)
	ds_write2_b32 v121, v48, v49 offset1:1
	ds_write2_b32 v116, v50, v51 offset1:1
	s_waitcnt vmcnt(15)
	ds_write2_b32 v117, v52, v53 offset1:1
	ds_write2_b32 v112, v54, v55 offset1:1
	s_waitcnt vmcnt(14)
	ds_write2_b32 v113, v56, v57 offset1:1
	ds_write2_b32 v108, v58, v59 offset1:1
	s_waitcnt vmcnt(13)
	ds_write2_b32 v109, v60, v61 offset1:1
	ds_write2_b32 v104, v62, v63 offset1:1
	s_waitcnt vmcnt(12)
	ds_write2_b32 v105, v64, v65 offset1:1
	ds_write2_b32 v106, v66, v67 offset1:1
	ds_read2_b32 v[62:63], v136 offset1:33
	ds_read2_b32 v[64:65], v136 offset0:66 offset1:99
	ds_read2_b32 v[60:61], v136 offset0:132 offset1:165
	ds_read2_b32 v[58:59], v136 offset0:198 offset1:231
	ds_read2_b32 v[52:53], v102 offset0:8 offset1:41
	ds_read2_b32 v[50:51], v102 offset0:74 offset1:107
	ds_read2_b32 v[44:45], v102 offset0:140 offset1:173
	ds_read2_b32 v[42:43], v102 offset0:206 offset1:239
	ds_read2_b32 v[66:67], v103 offset0:16 offset1:49
	ds_read2_b32 v[68:69], v103 offset0:82 offset1:115
	ds_read2_b32 v[56:57], v103 offset0:148 offset1:181
	ds_read2_b32 v[54:55], v103 offset0:214 offset1:247
	ds_read2_b32 v[48:49], v107 offset0:24 offset1:57
	ds_read2_b32 v[46:47], v107 offset0:90 offset1:123
	ds_read2_b32 v[40:41], v107 offset0:156 offset1:189
	ds_read2_b32 v[38:39], v107 offset0:222 offset1:255
	s_waitcnt lgkmcnt(14)
	v_mul_f32_e32 v37, 0x42800000, v62
	v_mul_f32_e32 v63, 0x42800000, v63
	v_mov_b32_e32 v62, v3
	v_cvt_pk_fp8_f32 v62, v37, v63
	s_waitcnt lgkmcnt(7)
	v_mul_f32_e32 v37, 0x42800000, v66
	v_mul_f32_e32 v63, 0x42800000, v67
	v_mov_b32_e32 v66, v3
	v_cvt_pk_fp8_f32 v66, v37, v63
	v_mul_f32_e32 v64, 0x42800000, v64
	v_mul_f32_e32 v65, 0x42800000, v65
	v_mul_f32_e32 v37, 0x42800000, v60
	v_mul_f32_e32 v60, 0x42800000, v61
	v_mov_b32_e32 v63, v3
	v_cvt_pk_fp8_f32 v62, v64, v65 op_sel:[0,0,1]
	s_waitcnt lgkmcnt(6)
	v_mul_f32_e32 v64, 0x42800000, v68
	v_mul_f32_e32 v65, 0x42800000, v69
	v_cvt_pk_fp8_f32 v63, v37, v60
	s_waitcnt lgkmcnt(5)
	v_mul_f32_e32 v37, 0x42800000, v56
	v_mul_f32_e32 v56, 0x42800000, v57
	v_mov_b32_e32 v67, v3
	v_cvt_pk_fp8_f32 v66, v64, v65 op_sel:[0,0,1]
	v_cvt_pk_fp8_f32 v67, v37, v56
	v_mul_f32_e32 v37, 0x42800000, v52
	v_mul_f32_e32 v52, 0x42800000, v53
	v_mov_b32_e32 v64, v3
	v_cvt_pk_fp8_f32 v64, v37, v52
	s_waitcnt lgkmcnt(3)
	v_mul_f32_e32 v37, 0x42800000, v48
	v_mul_f32_e32 v48, 0x42800000, v49
	v_mov_b32_e32 v68, v3
	v_cvt_pk_fp8_f32 v68, v37, v48
	v_mul_f32_e32 v37, 0x42800000, v44
	v_mul_f32_e32 v44, 0x42800000, v45
	v_mov_b32_e32 v65, v3
	v_cvt_pk_fp8_f32 v65, v37, v44
	s_waitcnt lgkmcnt(1)
	v_mul_f32_e32 v37, 0x42800000, v40
	v_mul_f32_e32 v40, 0x42800000, v41
	v_mov_b32_e32 v69, v3
	v_cvt_pk_fp8_f32 v69, v37, v40
	s_mul_hi_i32 s0, s47, 0x1600000
	s_mul_i32 s47, s47, 0x1600000
	v_or_b32_e32 v36, s48, v135
	s_add_u32 s24, s34, s47
	v_mul_f32_e32 v58, 0x42800000, v58
	v_mul_f32_e32 v59, 0x42800000, v59
	v_mul_f32_e32 v50, 0x42800000, v50
	v_mul_f32_e32 v51, 0x42800000, v51
	v_mul_f32_e32 v42, 0x42800000, v42
	v_mul_f32_e32 v43, 0x42800000, v43
	v_ashrrev_i32_e32 v37, 31, v36
	s_addc_u32 s25, s35, s0
	v_cvt_pk_fp8_f32 v63, v58, v59 op_sel:[0,0,1]
	v_mul_f32_e32 v54, 0x42800000, v54
	v_mul_f32_e32 v55, 0x42800000, v55
	v_cvt_pk_fp8_f32 v64, v50, v51 op_sel:[0,0,1]
	v_mul_f32_e32 v46, 0x42800000, v46
	v_mul_f32_e32 v47, 0x42800000, v47
	v_cvt_pk_fp8_f32 v65, v42, v43 op_sel:[0,0,1]
	s_waitcnt lgkmcnt(0)
	v_mul_f32_e32 v38, 0x42800000, v38
	v_mul_f32_e32 v39, 0x42800000, v39
	v_lshlrev_b64 v[36:37], 11, v[36:37]
	v_cvt_pk_fp8_f32 v67, v54, v55 op_sel:[0,0,1]
	v_cvt_pk_fp8_f32 v68, v46, v47 op_sel:[0,0,1]
	v_cvt_pk_fp8_f32 v69, v38, v39 op_sel:[0,0,1]
	v_lshl_add_u64 v[36:37], s[24:25], 0, v[36:37]
	v_lshl_add_u64 v[36:37], v[36:37], 0, s[22:23]
	v_lshl_add_u64 v[36:37], v[36:37], 0, v[132:133]
	global_store_dwordx4 v[36:37], v[62:65], off
	s_nop 1
	v_add_co_u32_e32 v36, vcc, 0x8000, v36
	s_nop 1
	v_addc_co_u32_e32 v37, vcc, 0, v37, vcc
	global_store_dwordx4 v[36:37], v[66:69], off
	s_waitcnt vmcnt(13)
	ds_write2_b32 v137, v4, v5 offset1:1
	ds_write2_b32 v137, v6, v7 offset0:2 offset1:3
	s_waitcnt vmcnt(12)
	ds_write2_b32 v128, v8, v9 offset1:1
	ds_write2_b32 v124, v10, v11 offset1:1
	s_waitcnt vmcnt(11)
	ds_write2_b32 v125, v12, v13 offset1:1
	ds_write2_b32 v120, v14, v15 offset1:1
	s_waitcnt vmcnt(10)
	ds_write2_b32 v121, v16, v17 offset1:1
	ds_write2_b32 v116, v18, v19 offset1:1
	s_waitcnt vmcnt(9)
	ds_write2_b32 v117, v20, v21 offset1:1
	ds_write2_b32 v112, v22, v23 offset1:1
	s_waitcnt vmcnt(8)
	ds_write2_b32 v113, v24, v25 offset1:1
	ds_write2_b32 v108, v26, v27 offset1:1
	s_waitcnt vmcnt(7)
	ds_write2_b32 v109, v28, v29 offset1:1
	ds_write2_b32 v104, v30, v31 offset1:1
	s_waitcnt vmcnt(6)
	ds_write2_b32 v105, v32, v33 offset1:1
	ds_write2_b32 v106, v34, v35 offset1:1
	ds_read2_b32 v[4:5], v136 offset1:33
	ds_read2_b32 v[8:9], v136 offset0:66 offset1:99
	ds_read2_b32 v[32:33], v136 offset0:132 offset1:165
	ds_read2_b32 v[30:31], v136 offset0:198 offset1:231
	ds_read2_b32 v[24:25], v102 offset0:8 offset1:41
	ds_read2_b32 v[6:7], v102 offset0:74 offset1:107
	ds_read2_b32 v[20:21], v102 offset0:140 offset1:173
	ds_read2_b32 v[18:19], v102 offset0:206 offset1:239
	ds_read2_b32 v[34:35], v103 offset0:16 offset1:49
	ds_read2_b32 v[36:37], v103 offset0:82 offset1:115
	ds_read2_b32 v[28:29], v103 offset0:148 offset1:181
	ds_read2_b32 v[26:27], v103 offset0:214 offset1:247
	ds_read2_b32 v[22:23], v107 offset0:24 offset1:57
	ds_read2_b32 v[10:11], v107 offset0:90 offset1:123
	ds_read2_b32 v[16:17], v107 offset0:156 offset1:189
	ds_read2_b32 v[14:15], v107 offset0:222 offset1:255
	s_waitcnt lgkmcnt(14)
	v_mul_f32_e32 v13, 0x42800000, v4
	v_mul_f32_e32 v5, 0x42800000, v5
	v_mov_b32_e32 v4, v3
	v_cvt_pk_fp8_f32 v4, v13, v5
	v_mul_f32_e32 v8, 0x42800000, v8
	v_mul_f32_e32 v9, 0x42800000, v9
	s_waitcnt lgkmcnt(7)
	v_mul_f32_e32 v5, 0x42800000, v34
	v_cvt_pk_fp8_f32 v4, v8, v9 op_sel:[0,0,1]
	v_mul_f32_e32 v9, 0x42800000, v35
	v_mov_b32_e32 v8, v3
	v_cvt_pk_fp8_f32 v8, v5, v9
	s_waitcnt lgkmcnt(6)
	v_mul_f32_e32 v13, 0x42800000, v36
	v_mul_f32_e32 v34, 0x42800000, v37
	v_mul_f32_e32 v9, 0x42800000, v32
	v_cvt_pk_fp8_f32 v8, v13, v34 op_sel:[0,0,1]
	v_mul_f32_e32 v13, 0x42800000, v33
	v_mov_b32_e32 v5, v3
	v_cvt_pk_fp8_f32 v5, v9, v13
	s_waitcnt lgkmcnt(5)
	v_mul_f32_e32 v13, 0x42800000, v28
	v_mul_f32_e32 v28, 0x42800000, v29
	v_mov_b32_e32 v9, v3
	v_cvt_pk_fp8_f32 v9, v13, v28
	v_mul_f32_e32 v13, 0x42800000, v24
	v_mul_f32_e32 v24, 0x42800000, v25
	v_mul_f32_e32 v25, 0x42800000, v6
	v_mov_b32_e32 v6, v3
	v_cvt_pk_fp8_f32 v6, v13, v24
	v_mul_f32_e32 v7, 0x42800000, v7
	s_waitcnt lgkmcnt(3)
	v_mul_f32_e32 v13, 0x42800000, v23
	s_waitcnt lgkmcnt(2)
	v_mul_f32_e32 v11, 0x42800000, v11
	v_cvt_pk_fp8_f32 v6, v25, v7 op_sel:[0,0,1]
	v_mul_f32_e32 v7, 0x42800000, v22
	v_mul_f32_e32 v22, 0x42800000, v10
	v_mov_b32_e32 v10, v3
	v_cvt_pk_fp8_f32 v10, v7, v13
	v_mul_f32_e32 v13, 0x42800000, v21
	v_mov_b32_e32 v7, v3
	s_mul_hi_i32 s0, s36, 0x1600000
	v_cvt_pk_fp8_f32 v10, v22, v11 op_sel:[0,0,1]
	v_mul_f32_e32 v11, 0x42800000, v20
	v_cvt_pk_fp8_f32 v7, v11, v13
	s_waitcnt lgkmcnt(1)
	v_mul_f32_e32 v13, 0x42800000, v16
	v_mul_f32_e32 v16, 0x42800000, v17
	v_mov_b32_e32 v11, v3
	v_cvt_pk_fp8_f32 v11, v13, v16
	s_mul_i32 s36, s36, 0x1600000
	v_or_b32_e32 v12, s37, v135
	s_add_u32 s22, s34, s36
	v_mul_f32_e32 v30, 0x42800000, v30
	v_mul_f32_e32 v31, 0x42800000, v31
	v_mul_f32_e32 v18, 0x42800000, v18
	v_mul_f32_e32 v19, 0x42800000, v19
	v_ashrrev_i32_e32 v13, 31, v12
	s_addc_u32 s23, s35, s0
	v_cvt_pk_fp8_f32 v5, v30, v31 op_sel:[0,0,1]
	v_mul_f32_e32 v26, 0x42800000, v26
	v_mul_f32_e32 v27, 0x42800000, v27
	v_cvt_pk_fp8_f32 v7, v18, v19 op_sel:[0,0,1]
	s_waitcnt lgkmcnt(0)
	v_mul_f32_e32 v14, 0x42800000, v14
	v_mul_f32_e32 v15, 0x42800000, v15
	v_lshlrev_b64 v[12:13], 11, v[12:13]
	v_cvt_pk_fp8_f32 v9, v26, v27 op_sel:[0,0,1]
	v_cvt_pk_fp8_f32 v11, v14, v15 op_sel:[0,0,1]
	v_lshl_add_u64 v[12:13], s[22:23], 0, v[12:13]
	v_lshl_add_u64 v[12:13], v[12:13], 0, s[4:5]
	v_lshl_add_u64 v[12:13], v[12:13], 0, v[132:133]
	global_store_dwordx4 v[12:13], v[4:7], off
	s_nop 1
	v_add_co_u32_e32 v12, vcc, 0x8000, v12
	s_nop 1
	v_addc_co_u32_e32 v13, vcc, 0, v13, vcc
	global_store_dwordx4 v[12:13], v[8:11], off
	s_add_i32 s31, s31, 32
	s_cmp_lt_i32 s31, s30
	s_cbranch_scc1 .LBB6_1606

.LBB6_1610:
	s_ashr_i32 s3, s2, 31
	s_lshl_b64 s[0:1], s[2:3], 3
	s_add_u32 s0, s76, s0
	s_addc_u32 s1, s77, s1
	s_load_dwordx2 s[2:3], s[0:1], 0x0
	v_lshlrev_b32_e32 v2, 4, v166
	s_waitcnt vmcnt(0)
	v_lshlrev_b32_e32 v6, 5, v166
	v_lshrrev_b32_e32 v4, 3, v166
	v_and_b32_e32 v5, 0x70, v2
	v_lshrrev_b32_e32 v147, 2, v166
	v_lshlrev_b32_e32 v144, 4, v166
	v_and_b32_e32 v144, 48, v144
	s_add_u32 s36, s6, 0x97080000
	v_lshl_or_b32 v2, v4, 13, v5
	v_add_u32_e32 v5, s66, v5
	v_mul_u32_u24_e32 v4, 0x84, v4
	v_mul_u32_u24_e32 v6, 0x84, v144
	v_lshlrev_b32_e32 v7, 2, v147
	s_addc_u32 s37, s7, 0
	v_and_b32_e32 v146, 31, v167
	v_mov_b32_e32 v145, v3
	v_add3_u32 v148, s66, v6, v7
	v_add_u32_e32 v149, v5, v4
.LBB6_1611:
	s_mul_hi_i32 s1, s13, 0x2e8ba2e9
	s_waitcnt lgkmcnt(0)
	s_lshr_b32 s5, s1, 31
	s_ashr_i32 s1, s1, 10
	s_lshl_b32 s4, s13, 3
	s_add_i32 s1, s1, s5
	s_and_b32 s33, s4, 64
	s_mul_i32 s4, s1, 0xffffea00
	s_add_i32 s4, s4, s13
	s_mul_hi_i32 s7, s1, 0xb00000
	s_mul_i32 s6, s1, 0xb00000
	s_ashr_i32 s1, s4, 1
	s_and_b32 s0, s13, 7
	s_ashr_i32 s4, s4, 31
	s_and_b32 s1, s1, -8
	s_lshr_b32 s4, s4, 26
	s_or_b32 s1, s1, s0
	s_add_i32 s4, s1, s4
	s_ashr_i32 s4, s4, 6
	s_lshl_b32 s1, s1, 5
	s_lshl_b32 s5, s4, 11
	s_lshl_b32 s4, s4, 7
	s_lshl_b64 s[22:23], s[6:7], 2
	s_sub_i32 s1, s1, s5
	s_or_b32 s4, s4, s33
	s_add_u32 s26, s2, s22
	v_or_b32_e32 v36, s1, v146
	v_or_b32_e32 v167, s1, v147
	s_addc_u32 s1, s3, s23
	v_readfirstlane_b32 s22, v36
	s_ashr_i32 s5, s4, 31
	s_andn2_b32 s22, s22, 31
	s_lshl_b64 s[24:25], s[4:5], 13
	s_add_u32 s24, s26, s24
	s_addc_u32 s1, s1, s25
	s_ashr_i32 s23, s22, 31
	s_lshl_b64 s[22:23], s[22:23], 2
	s_add_u32 s22, s24, s22
	s_addc_u32 s23, s1, s23
	s_mov_b64 s[24:25], s[22:23]
	s_add_u32 s26, s22, 0x10000
	s_addc_u32 s27, s23, 0
	v_lshl_add_u64 v[36:37], s[24:25], 0, v[2:3]
	s_add_u32 s24, s22, 0x20000
	global_load_dwordx4 v[124:127], v[36:37], off nt
	s_addc_u32 s25, s23, 0
	v_lshl_add_u64 v[36:37], s[26:27], 0, v[2:3]
	s_add_u32 s26, s22, 0x30000
	global_load_dwordx4 v[132:135], v[36:37], off nt
	s_addc_u32 s27, s23, 0
	v_lshl_add_u64 v[36:37], s[24:25], 0, v[2:3]
	s_add_u32 s24, s22, 0x40000
	global_load_dwordx4 v[136:139], v[36:37], off nt
	s_addc_u32 s25, s23, 0
	v_lshl_add_u64 v[36:37], s[26:27], 0, v[2:3]
	s_add_u32 s26, s22, 0x50000
	global_load_dwordx4 v[140:143], v[36:37], off nt
	s_addc_u32 s27, s23, 0
	v_lshl_add_u64 v[36:37], s[24:25], 0, v[2:3]
	s_add_u32 s24, s22, 0x60000
	s_addc_u32 s25, s23, 0
	global_load_dwordx4 v[168:171], v[36:37], off nt
	s_add_u32 s22, s22, 0x70000
	v_lshl_add_u64 v[36:37], s[26:27], 0, v[2:3]
	global_load_dwordx4 v[172:175], v[36:37], off nt
	s_addc_u32 s23, s23, 0
	s_add_i32 s1, s13, 8
	v_lshl_add_u64 v[36:37], s[24:25], 0, v[2:3]
	s_mul_hi_i32 s24, s1, 0x2e8ba2e9
	global_load_dwordx4 v[176:179], v[36:37], off nt
	s_lshr_b32 s26, s24, 31
	s_ashr_i32 s24, s24, 10
	v_lshl_add_u64 v[36:37], s[22:23], 0, v[2:3]
	s_add_i32 s22, s24, s26
	s_mul_i32 s23, s22, 0xffffea00
	s_add_i32 s23, s23, s1
	s_lshl_b32 s25, s1, 3
	s_ashr_i32 s1, s23, 1
	s_and_b32 s28, s25, 64
	s_mul_hi_i32 s25, s22, 0xb00000
	s_mul_i32 s24, s22, 0xb00000
	s_ashr_i32 s22, s23, 31
	s_and_b32 s1, s1, -8
	s_lshr_b32 s22, s22, 26
	s_or_b32 s1, s1, s0
	s_add_i32 s22, s1, s22
	s_ashr_i32 s22, s22, 6
	s_lshl_b32 s1, s1, 5
	s_lshl_b32 s23, s22, 11
	s_lshl_b32 s22, s22, 7
	s_lshl_b64 s[26:27], s[24:25], 2
	s_sub_i32 s1, s1, s23
	s_or_b32 s22, s22, s28
	global_load_dwordx4 v[184:187], v[36:37], off nt
	s_add_u32 s30, s2, s26
	v_or_b32_e32 v36, s1, v146
	v_or_b32_e32 v183, s1, v147
	s_addc_u32 s1, s3, s27
	v_readfirstlane_b32 s26, v36
	s_ashr_i32 s23, s22, 31
	s_andn2_b32 s26, s26, 31
	s_lshl_b64 s[28:29], s[22:23], 13
	s_add_u32 s28, s30, s28
	s_addc_u32 s1, s1, s29
	s_ashr_i32 s27, s26, 31
	s_lshl_b64 s[26:27], s[26:27], 2
	s_add_u32 s26, s28, s26
	s_addc_u32 s27, s1, s27
	s_mov_b64 s[28:29], s[26:27]
	s_add_u32 s30, s26, 0x10000
	s_addc_u32 s31, s27, 0
	v_lshl_add_u64 v[36:37], s[28:29], 0, v[2:3]
	s_add_u32 s28, s26, 0x20000
	global_load_dwordx4 v[76:79], v[36:37], off nt
	s_addc_u32 s29, s27, 0
	v_lshl_add_u64 v[36:37], s[30:31], 0, v[2:3]
	s_add_u32 s30, s26, 0x30000
	global_load_dwordx4 v[88:91], v[36:37], off nt
	s_addc_u32 s31, s27, 0
	v_lshl_add_u64 v[36:37], s[28:29], 0, v[2:3]
	s_add_u32 s28, s26, 0x40000
	global_load_dwordx4 v[96:99], v[36:37], off nt
	s_addc_u32 s29, s27, 0
	v_lshl_add_u64 v[36:37], s[30:31], 0, v[2:3]
	s_add_u32 s30, s26, 0x50000
	global_load_dwordx4 v[100:103], v[36:37], off nt
	s_addc_u32 s31, s27, 0
	v_lshl_add_u64 v[36:37], s[28:29], 0, v[2:3]
	s_add_u32 s28, s26, 0x60000
	s_addc_u32 s29, s27, 0
	global_load_dwordx4 v[108:111], v[36:37], off nt
	s_add_u32 s26, s26, 0x70000
	v_lshl_add_u64 v[36:37], s[30:31], 0, v[2:3]
	global_load_dwordx4 v[112:115], v[36:37], off nt
	s_addc_u32 s27, s27, 0
	s_add_i32 s1, s13, 16
	v_lshl_add_u64 v[36:37], s[28:29], 0, v[2:3]
	s_mul_hi_i32 s28, s1, 0x2e8ba2e9
	global_load_dwordx4 v[120:123], v[36:37], off nt
	s_lshr_b32 s29, s28, 31
	s_ashr_i32 s28, s28, 10
	v_lshl_add_u64 v[36:37], s[26:27], 0, v[2:3]
	s_add_i32 s26, s28, s29
	s_mul_i32 s28, s26, 0xffffea00
	s_add_i32 s28, s28, s1
	s_ashr_i32 s1, s28, 1
	s_ashr_i32 s28, s28, 31
	s_and_b32 s1, s1, -8
	s_lshr_b32 s28, s28, 26
	s_or_b32 s1, s1, s0
	s_add_i32 s28, s1, s28
	s_ashr_i32 s28, s28, 6
	s_mul_hi_i32 s27, s26, 0xb00000
	s_mul_i32 s26, s26, 0xb00000
	s_lshl_b32 s1, s1, 5
	s_lshl_b32 s29, s28, 11
	s_lshl_b32 s28, s28, 7
	s_lshl_b64 s[30:31], s[26:27], 2
	s_sub_i32 s1, s1, s29
	s_or_b32 s28, s28, s33
	global_load_dwordx4 v[128:131], v[36:37], off nt
	s_add_u32 s33, s2, s30
	v_or_b32_e32 v36, s1, v146
	v_or_b32_e32 v200, s1, v147
	s_addc_u32 s1, s3, s31
	v_readfirstlane_b32 s30, v36
	s_ashr_i32 s29, s28, 31
	s_andn2_b32 s30, s30, 31
	s_lshl_b64 s[34:35], s[28:29], 13
	s_add_u32 s33, s33, s34
	s_addc_u32 s1, s1, s35
	s_ashr_i32 s31, s30, 31
	s_lshl_b64 s[30:31], s[30:31], 2
	s_add_u32 s30, s33, s30
	s_addc_u32 s31, s1, s31
	s_mov_b64 s[34:35], s[30:31]
	s_add_u32 s48, s30, 0x10000
	s_addc_u32 s49, s31, 0
	v_lshl_add_u64 v[36:37], s[34:35], 0, v[2:3]
	s_add_u32 s34, s30, 0x20000
	global_load_dwordx4 v[48:51], v[36:37], off nt
	s_addc_u32 s35, s31, 0
	v_lshl_add_u64 v[36:37], s[48:49], 0, v[2:3]
	s_add_u32 s48, s30, 0x30000
	global_load_dwordx4 v[56:59], v[36:37], off nt
	s_addc_u32 s49, s31, 0
	v_lshl_add_u64 v[36:37], s[34:35], 0, v[2:3]
	s_add_u32 s34, s30, 0x40000
	global_load_dwordx4 v[64:67], v[36:37], off nt
	s_addc_u32 s35, s31, 0
	v_lshl_add_u64 v[36:37], s[48:49], 0, v[2:3]
	s_add_u32 s48, s30, 0x50000
	global_load_dwordx4 v[72:75], v[36:37], off nt
	s_addc_u32 s49, s31, 0
	v_lshl_add_u64 v[36:37], s[34:35], 0, v[2:3]
	s_add_u32 s34, s30, 0x60000
	s_addc_u32 s35, s31, 0
	s_add_u32 s30, s30, 0x70000
	global_load_dwordx4 v[84:87], v[36:37], off nt
	s_addc_u32 s31, s31, 0
	v_lshl_add_u64 v[36:37], s[48:49], 0, v[2:3]
	s_add_i32 s1, s13, 24
	global_load_dwordx4 v[92:95], v[36:37], off nt
	s_mul_hi_i32 s33, s1, 0x2e8ba2e9
	v_lshl_add_u64 v[36:37], s[34:35], 0, v[2:3]
	global_load_dwordx4 v[104:107], v[36:37], off nt
	s_lshr_b32 s35, s33, 31
	s_ashr_i32 s33, s33, 10
	v_lshl_add_u64 v[36:37], s[30:31], 0, v[2:3]
	s_add_i32 s30, s33, s35
	s_mul_i32 s31, s30, 0xffffea00
	s_add_i32 s31, s31, s1
	s_lshl_b32 s34, s1, 3
	s_ashr_i32 s1, s31, 1
	s_and_b32 s45, s34, 64
	s_mul_hi_i32 s35, s30, 0xb00000
	s_mul_i32 s34, s30, 0xb00000
	s_ashr_i32 s30, s31, 31
	s_and_b32 s1, s1, -8
	s_lshr_b32 s30, s30, 26
	s_or_b32 s0, s1, s0
	s_add_i32 s1, s0, s30
	s_ashr_i32 s1, s1, 6
	s_lshl_b32 s0, s0, 5
	s_lshl_b32 s30, s1, 11
	s_lshl_b32 s1, s1, 7
	s_lshl_b64 s[48:49], s[34:35], 2
	s_sub_i32 s0, s0, s30
	s_or_b32 s30, s1, s45
	global_load_dwordx4 v[116:119], v[36:37], off nt
	s_add_u32 s1, s2, s48
	v_or_b32_e32 v36, s0, v146
	v_or_b32_e32 v201, s0, v147
	s_addc_u32 s33, s3, s49
	v_readfirstlane_b32 s0, v36
	s_ashr_i32 s31, s30, 31
	s_andn2_b32 s0, s0, 31
	s_lshl_b64 s[48:49], s[30:31], 13
	s_add_u32 s45, s1, s48
	s_addc_u32 s33, s33, s49
	s_ashr_i32 s1, s0, 31
	s_lshl_b64 s[0:1], s[0:1], 2
	s_add_u32 s0, s45, s0
	s_addc_u32 s1, s33, s1
	s_mov_b64 s[48:49], s[0:1]
	s_add_u32 s50, s0, 0x10000
	s_addc_u32 s51, s1, 0
	v_lshl_add_u64 v[36:37], s[48:49], 0, v[2:3]
	global_load_dwordx4 v[36:39], v[36:37], off nt
	s_add_u32 s48, s0, 0x20000
	s_addc_u32 s49, s1, 0
	v_lshl_add_u64 v[40:41], s[50:51], 0, v[2:3]
	global_load_dwordx4 v[40:43], v[40:41], off nt
	s_add_u32 s50, s0, 0x30000
	s_addc_u32 s51, s1, 0
	v_lshl_add_u64 v[44:45], s[48:49], 0, v[2:3]
	global_load_dwordx4 v[44:47], v[44:45], off nt
	s_add_u32 s48, s0, 0x40000
	s_addc_u32 s49, s1, 0
	v_lshl_add_u64 v[52:53], s[50:51], 0, v[2:3]
	global_load_dwordx4 v[52:55], v[52:53], off nt
	s_add_u32 s50, s0, 0x50000
	s_addc_u32 s51, s1, 0
	v_lshl_add_u64 v[60:61], s[48:49], 0, v[2:3]
	global_load_dwordx4 v[60:63], v[60:61], off nt
	s_add_u32 s48, s0, 0x60000
	s_addc_u32 s49, s1, 0
	v_lshl_add_u64 v[68:69], s[50:51], 0, v[2:3]
	global_load_dwordx4 v[68:71], v[68:69], off nt
	s_add_u32 s0, s0, 0x70000
	s_addc_u32 s1, s1, 0
	v_lshl_add_u64 v[80:81], s[48:49], 0, v[2:3]
	global_load_dwordx4 v[80:83], v[80:81], off nt
	v_add_u32_e32 v150, 0x420, v149
	v_add_u32_e32 v151, 0x428, v149
	v_add_u32_e32 v152, 0x840, v149
	v_add_u32_e32 v153, 0x848, v149
	v_add_u32_e32 v154, 0xc60, v149
	v_add_u32_e32 v155, 0xc68, v149
	v_add_u32_e32 v156, 0x1080, v149
	v_add_u32_e32 v157, 0x1088, v149
	v_add_u32_e32 v158, 0x14a0, v149
	v_add_u32_e32 v159, 0x14a8, v149
	v_add_u32_e32 v160, 0x18c0, v149
	v_add_u32_e32 v161, 0x18c8, v149
	v_add_u32_e32 v162, 0x1ce0, v149
	v_add_u32_e32 v163, 0x1ce8, v149
	s_waitcnt vmcnt(30)
	ds_write2_b32 v149, v124, v125 offset1:1
	ds_write2_b32 v149, v126, v127 offset0:2 offset1:3
	s_waitcnt vmcnt(29)
	ds_write2_b32 v150, v132, v133 offset1:1
	ds_write2_b32 v151, v134, v135 offset1:1
	s_waitcnt vmcnt(28)
	ds_write2_b32 v152, v136, v137 offset1:1
	ds_write2_b32 v153, v138, v139 offset1:1
	s_waitcnt vmcnt(27)
	ds_write2_b32 v154, v140, v141 offset1:1
	ds_write2_b32 v155, v142, v143 offset1:1
	s_waitcnt vmcnt(26)
	ds_write2_b32 v156, v168, v169 offset1:1
	ds_write2_b32 v157, v170, v171 offset1:1
	s_waitcnt vmcnt(25)
	ds_write2_b32 v158, v172, v173 offset1:1
	ds_write2_b32 v159, v174, v175 offset1:1
	s_waitcnt vmcnt(24)
	ds_write2_b32 v160, v176, v177 offset1:1
	ds_write2_b32 v161, v178, v179 offset1:1
	s_waitcnt vmcnt(23)
	ds_write2_b32 v162, v184, v185 offset1:1
	ds_write2_b32 v163, v186, v187 offset1:1
	v_lshl_add_u64 v[124:125], s[0:1], 0, v[2:3]
	global_load_dwordx4 v[124:127], v[124:125], off nt
	s_add_u32 s6, s36, s6
	s_addc_u32 s7, s37, s7
	v_add_u32_e32 v164, 0x400, v148
	v_mov_b32_e32 v165, v148
	v_add_u32_e32 v166, 0x400, v148
	v_mov_b64_e32 v[132:133], s[6:7]
	s_add_u32 s0, s36, s24
	ds_read2_b32 v[134:135], v148 offset1:33
	ds_read2_b32 v[136:137], v148 offset0:66 offset1:99
	ds_read2_b32 v[138:139], v148 offset0:132 offset1:165
	ds_read2_b32 v[140:141], v148 offset0:198 offset1:231
	ds_read2_b32 v[142:143], v164 offset0:8 offset1:41
	ds_read2_b32 v[168:169], v164 offset0:74 offset1:107
	ds_read2_b32 v[170:171], v164 offset0:140 offset1:173
	ds_read2_b32 v[172:173], v164 offset0:206 offset1:239
	ds_read2_b32 v[174:175], v165 offset0:16 offset1:49
	ds_read2_b32 v[176:177], v165 offset0:82 offset1:115
	ds_read2_b32 v[178:179], v165 offset0:148 offset1:181
	ds_read2_b32 v[184:185], v165 offset0:214 offset1:247
	ds_read2_b32 v[186:187], v166 offset0:24 offset1:57
	ds_read2_b32 v[188:189], v166 offset0:90 offset1:123
	ds_read2_b32 v[190:191], v166 offset0:156 offset1:189
	ds_read2_b32 v[192:193], v166 offset0:222 offset1:255
	v_mad_i64_i32 v[132:133], s[6:7], v167, s82, v[132:133]
	s_addc_u32 s1, s37, s25
	v_lshl_add_u64 v[132:133], v[132:133], 0, s[4:5]
	v_mov_b64_e32 v[194:195], s[0:1]
	v_mov_b32_e32 v4, v3
	v_mov_b32_e32 v5, v3
	v_mov_b32_e32 v6, v3
	v_mov_b32_e32 v7, v3
	v_lshl_add_u64 v[196:197], v[132:133], 0, v[144:145]
	v_mad_i64_i32 v[132:133], s[4:5], v183, s82, v[194:195]
	s_waitcnt lgkmcnt(14)
	v_mul_f32_e32 v167, 0x42800000, v134
	v_mul_f32_e32 v183, 0x42800000, v135
	s_waitcnt lgkmcnt(13)
	v_mul_f32_e32 v138, 0x42800000, v138
	v_mul_f32_e32 v139, 0x42800000, v139
	s_waitcnt lgkmcnt(11)
	v_mul_f32_e32 v142, 0x42800000, v142
	v_mul_f32_e32 v143, 0x42800000, v143
	s_waitcnt lgkmcnt(9)
	v_mul_f32_e32 v170, 0x42800000, v170
	v_mul_f32_e32 v171, 0x42800000, v171
	v_mov_b32_e32 v8, v3
	v_mov_b32_e32 v9, v3
	v_mov_b32_e32 v10, v3
	v_mov_b32_e32 v11, v3
	s_waitcnt lgkmcnt(7)
	v_mul_f32_e32 v174, 0x42800000, v174
	v_mul_f32_e32 v175, 0x42800000, v175
	s_waitcnt lgkmcnt(5)
	v_mul_f32_e32 v178, 0x42800000, v178
	v_mul_f32_e32 v179, 0x42800000, v179
	s_waitcnt lgkmcnt(3)
	v_mul_f32_e32 v186, 0x42800000, v186
	v_mul_f32_e32 v187, 0x42800000, v187
	s_waitcnt lgkmcnt(1)
	v_mul_f32_e32 v190, 0x42800000, v190
	v_mul_f32_e32 v191, 0x42800000, v191
	v_cvt_pk_fp8_f32 v4, v167, v183
	v_cvt_pk_fp8_f32 v5, v138, v139
	v_cvt_pk_fp8_f32 v6, v142, v143
	v_cvt_pk_fp8_f32 v7, v170, v171
	v_cvt_pk_fp8_f32 v8, v174, v175
	v_cvt_pk_fp8_f32 v9, v178, v179
	v_cvt_pk_fp8_f32 v10, v186, v187
	v_cvt_pk_fp8_f32 v11, v190, v191
	v_mul_f32_e32 v136, 0x42800000, v136
	v_mul_f32_e32 v137, 0x42800000, v137
	v_mul_f32_e32 v140, 0x42800000, v140
	v_mul_f32_e32 v141, 0x42800000, v141
	v_mul_f32_e32 v168, 0x42800000, v168
	v_mul_f32_e32 v169, 0x42800000, v169
	v_mul_f32_e32 v172, 0x42800000, v172
	v_mul_f32_e32 v173, 0x42800000, v173
	v_mul_f32_e32 v176, 0x42800000, v176
	v_mul_f32_e32 v177, 0x42800000, v177
	v_mul_f32_e32 v184, 0x42800000, v184
	v_mul_f32_e32 v185, 0x42800000, v185
	v_mul_f32_e32 v188, 0x42800000, v188
	v_mul_f32_e32 v189, 0x42800000, v189
	s_waitcnt lgkmcnt(0)
	v_mul_f32_e32 v192, 0x42800000, v192
	v_mul_f32_e32 v193, 0x42800000, v193
	v_cvt_pk_fp8_f32 v4, v136, v137 op_sel:[0,0,1]
	v_cvt_pk_fp8_f32 v5, v140, v141 op_sel:[0,0,1]
	v_cvt_pk_fp8_f32 v6, v168, v169 op_sel:[0,0,1]
	v_cvt_pk_fp8_f32 v7, v172, v173 op_sel:[0,0,1]
	v_cvt_pk_fp8_f32 v8, v176, v177 op_sel:[0,0,1]
	v_cvt_pk_fp8_f32 v9, v184, v185 op_sel:[0,0,1]
	v_cvt_pk_fp8_f32 v10, v188, v189 op_sel:[0,0,1]
	v_cvt_pk_fp8_f32 v11, v192, v193 op_sel:[0,0,1]
	global_store_dwordx4 v[196:197], v[4:7], off
	s_nop 1
	v_add_co_u32_e32 v196, vcc, 0x16000, v196
	s_nop 1
	v_addc_co_u32_e32 v197, vcc, 0, v197, vcc
	global_store_dwordx4 v[196:197], v[8:11], off
	s_waitcnt vmcnt(25)
	ds_write2_b32 v149, v76, v77 offset1:1
	ds_write2_b32 v149, v78, v79 offset0:2 offset1:3
	s_waitcnt vmcnt(24)
	ds_write2_b32 v150, v88, v89 offset1:1
	ds_write2_b32 v151, v90, v91 offset1:1
	s_waitcnt vmcnt(23)
	ds_write2_b32 v152, v96, v97 offset1:1
	ds_write2_b32 v153, v98, v99 offset1:1
	s_waitcnt vmcnt(22)
	ds_write2_b32 v154, v100, v101 offset1:1
	ds_write2_b32 v155, v102, v103 offset1:1
	s_waitcnt vmcnt(21)
	ds_write2_b32 v156, v108, v109 offset1:1
	ds_write2_b32 v157, v110, v111 offset1:1
	s_waitcnt vmcnt(20)
	ds_write2_b32 v158, v112, v113 offset1:1
	ds_write2_b32 v159, v114, v115 offset1:1
	s_waitcnt vmcnt(19)
	ds_write2_b32 v160, v120, v121 offset1:1
	ds_write2_b32 v161, v122, v123 offset1:1
	s_waitcnt vmcnt(18)
	ds_write2_b32 v162, v128, v129 offset1:1
	ds_write2_b32 v163, v130, v131 offset1:1
	ds_read2_b32 v[4:5], v148 offset1:33
	ds_read2_b32 v[6:7], v148 offset0:66 offset1:99
	ds_read2_b32 v[8:9], v148 offset0:132 offset1:165
	ds_read2_b32 v[10:11], v148 offset0:198 offset1:231
	ds_read2_b32 v[76:77], v164 offset0:8 offset1:41
	ds_read2_b32 v[78:79], v164 offset0:74 offset1:107
	ds_read2_b32 v[88:89], v164 offset0:140 offset1:173
	ds_read2_b32 v[90:91], v164 offset0:206 offset1:239
	ds_read2_b32 v[96:97], v165 offset0:16 offset1:49
	ds_read2_b32 v[98:99], v165 offset0:82 offset1:115
	ds_read2_b32 v[100:101], v165 offset0:148 offset1:181
	ds_read2_b32 v[102:103], v165 offset0:214 offset1:247
	ds_read2_b32 v[108:109], v166 offset0:24 offset1:57
	ds_read2_b32 v[110:111], v166 offset0:90 offset1:123
	ds_read2_b32 v[112:113], v166 offset0:156 offset1:189
	ds_read2_b32 v[114:115], v166 offset0:222 offset1:255
	v_mov_b32_e32 v12, v3
	v_mov_b32_e32 v13, v3
	v_mov_b32_e32 v14, v3
	v_mov_b32_e32 v15, v3
	s_waitcnt lgkmcnt(14)
	v_mul_f32_e32 v4, 0x42800000, v4
	v_mul_f32_e32 v5, 0x42800000, v5
	s_waitcnt lgkmcnt(13)
	v_mul_f32_e32 v8, 0x42800000, v8
	v_mul_f32_e32 v9, 0x42800000, v9
	s_waitcnt lgkmcnt(11)
	v_mul_f32_e32 v76, 0x42800000, v76
	v_mul_f32_e32 v77, 0x42800000, v77
	s_waitcnt lgkmcnt(9)
	v_mul_f32_e32 v88, 0x42800000, v88
	v_mul_f32_e32 v89, 0x42800000, v89
	v_mov_b32_e32 v16, v3
	v_mov_b32_e32 v17, v3
	v_mov_b32_e32 v18, v3
	v_mov_b32_e32 v19, v3
	s_waitcnt lgkmcnt(7)
	v_mul_f32_e32 v96, 0x42800000, v96
	v_mul_f32_e32 v97, 0x42800000, v97
	s_waitcnt lgkmcnt(5)
	v_mul_f32_e32 v100, 0x42800000, v100
	v_mul_f32_e32 v101, 0x42800000, v101
	s_waitcnt lgkmcnt(3)
	v_mul_f32_e32 v108, 0x42800000, v108
	v_mul_f32_e32 v109, 0x42800000, v109
	s_waitcnt lgkmcnt(1)
	v_mul_f32_e32 v112, 0x42800000, v112
	v_mul_f32_e32 v113, 0x42800000, v113
	v_cvt_pk_fp8_f32 v12, v4, v5
	v_cvt_pk_fp8_f32 v13, v8, v9
	v_cvt_pk_fp8_f32 v14, v76, v77
	v_cvt_pk_fp8_f32 v15, v88, v89
	v_cvt_pk_fp8_f32 v16, v96, v97
	v_cvt_pk_fp8_f32 v17, v100, v101
	v_cvt_pk_fp8_f32 v18, v108, v109
	v_cvt_pk_fp8_f32 v19, v112, v113
	v_mul_f32_e32 v6, 0x42800000, v6
	v_mul_f32_e32 v7, 0x42800000, v7
	v_mul_f32_e32 v10, 0x42800000, v10
	v_mul_f32_e32 v11, 0x42800000, v11
	v_mul_f32_e32 v78, 0x42800000, v78
	v_mul_f32_e32 v79, 0x42800000, v79
	v_mul_f32_e32 v90, 0x42800000, v90
	v_mul_f32_e32 v91, 0x42800000, v91
	v_mul_f32_e32 v98, 0x42800000, v98
	v_mul_f32_e32 v99, 0x42800000, v99
	v_mul_f32_e32 v102, 0x42800000, v102
	v_mul_f32_e32 v103, 0x42800000, v103
	v_mul_f32_e32 v110, 0x42800000, v110
	v_mul_f32_e32 v111, 0x42800000, v111
	s_waitcnt lgkmcnt(0)
	v_mul_f32_e32 v114, 0x42800000, v114
	v_mul_f32_e32 v115, 0x42800000, v115
	v_cvt_pk_fp8_f32 v12, v6, v7 op_sel:[0,0,1]
	v_cvt_pk_fp8_f32 v13, v10, v11 op_sel:[0,0,1]
	v_cvt_pk_fp8_f32 v14, v78, v79 op_sel:[0,0,1]
	v_cvt_pk_fp8_f32 v15, v90, v91 op_sel:[0,0,1]
	v_cvt_pk_fp8_f32 v16, v98, v99 op_sel:[0,0,1]
	v_cvt_pk_fp8_f32 v17, v102, v103 op_sel:[0,0,1]
	v_cvt_pk_fp8_f32 v18, v110, v111 op_sel:[0,0,1]
	v_cvt_pk_fp8_f32 v19, v114, v115 op_sel:[0,0,1]
	v_lshl_add_u64 v[132:133], v[132:133], 0, s[22:23]
	v_lshl_add_u64 v[198:199], v[132:133], 0, v[144:145]
	global_store_dwordx4 v[198:199], v[12:15], off
	s_nop 1
	v_add_co_u32_e32 v198, vcc, 0x16000, v198
	s_nop 1
	v_addc_co_u32_e32 v199, vcc, 0, v199, vcc
	global_store_dwordx4 v[198:199], v[16:19], off
	s_waitcnt vmcnt(19)
	ds_write2_b32 v149, v48, v49 offset1:1
	ds_write2_b32 v149, v50, v51 offset0:2 offset1:3
	s_waitcnt vmcnt(18)
	ds_write2_b32 v150, v56, v57 offset1:1
	ds_write2_b32 v151, v58, v59 offset1:1
	s_waitcnt vmcnt(17)
	ds_write2_b32 v152, v64, v65 offset1:1
	ds_write2_b32 v153, v66, v67 offset1:1
	s_waitcnt vmcnt(16)
	ds_write2_b32 v154, v72, v73 offset1:1
	ds_write2_b32 v155, v74, v75 offset1:1
	s_waitcnt vmcnt(15)
	ds_write2_b32 v156, v84, v85 offset1:1
	ds_write2_b32 v157, v86, v87 offset1:1
	s_waitcnt vmcnt(14)
	ds_write2_b32 v158, v92, v93 offset1:1
	ds_write2_b32 v159, v94, v95 offset1:1
	s_waitcnt vmcnt(13)
	ds_write2_b32 v160, v104, v105 offset1:1
	ds_write2_b32 v161, v106, v107 offset1:1
	s_waitcnt vmcnt(12)
	ds_write2_b32 v162, v116, v117 offset1:1
	ds_write2_b32 v163, v118, v119 offset1:1
	ds_read2_b32 v[4:5], v148 offset1:33
	ds_read2_b32 v[6:7], v148 offset0:66 offset1:99
	ds_read2_b32 v[8:9], v148 offset0:132 offset1:165
	ds_read2_b32 v[10:11], v148 offset0:198 offset1:231
	ds_read2_b32 v[12:13], v164 offset0:8 offset1:41
	ds_read2_b32 v[14:15], v164 offset0:74 offset1:107
	ds_read2_b32 v[16:17], v164 offset0:140 offset1:173
	ds_read2_b32 v[18:19], v164 offset0:206 offset1:239
	ds_read2_b32 v[48:49], v165 offset0:16 offset1:49
	ds_read2_b32 v[50:51], v165 offset0:82 offset1:115
	ds_read2_b32 v[56:57], v165 offset0:148 offset1:181
	ds_read2_b32 v[58:59], v165 offset0:214 offset1:247
	ds_read2_b32 v[64:65], v166 offset0:24 offset1:57
	ds_read2_b32 v[66:67], v166 offset0:90 offset1:123
	ds_read2_b32 v[72:73], v166 offset0:156 offset1:189
	ds_read2_b32 v[74:75], v166 offset0:222 offset1:255
	v_mov_b32_e32 v20, v3
	v_mov_b32_e32 v21, v3
	v_mov_b32_e32 v22, v3
	v_mov_b32_e32 v23, v3
	s_waitcnt lgkmcnt(14)
	v_mul_f32_e32 v4, 0x42800000, v4
	v_mul_f32_e32 v5, 0x42800000, v5
	s_waitcnt lgkmcnt(13)
	v_mul_f32_e32 v8, 0x42800000, v8
	v_mul_f32_e32 v9, 0x42800000, v9
	s_waitcnt lgkmcnt(11)
	v_mul_f32_e32 v12, 0x42800000, v12
	v_mul_f32_e32 v13, 0x42800000, v13
	s_waitcnt lgkmcnt(9)
	v_mul_f32_e32 v16, 0x42800000, v16
	v_mul_f32_e32 v17, 0x42800000, v17
	v_mov_b32_e32 v24, v3
	v_mov_b32_e32 v25, v3
	v_mov_b32_e32 v26, v3
	v_mov_b32_e32 v27, v3
	s_waitcnt lgkmcnt(7)
	v_mul_f32_e32 v48, 0x42800000, v48
	v_mul_f32_e32 v49, 0x42800000, v49
	s_waitcnt lgkmcnt(5)
	v_mul_f32_e32 v56, 0x42800000, v56
	v_mul_f32_e32 v57, 0x42800000, v57
	s_waitcnt lgkmcnt(3)
	v_mul_f32_e32 v64, 0x42800000, v64
	v_mul_f32_e32 v65, 0x42800000, v65
	s_waitcnt lgkmcnt(1)
	v_mul_f32_e32 v72, 0x42800000, v72
	v_mul_f32_e32 v73, 0x42800000, v73
	v_cvt_pk_fp8_f32 v20, v4, v5
	v_cvt_pk_fp8_f32 v21, v8, v9
	v_cvt_pk_fp8_f32 v22, v12, v13
	v_cvt_pk_fp8_f32 v23, v16, v17
	v_cvt_pk_fp8_f32 v24, v48, v49
	v_cvt_pk_fp8_f32 v25, v56, v57
	v_cvt_pk_fp8_f32 v26, v64, v65
	v_cvt_pk_fp8_f32 v27, v72, v73
	s_add_u32 s0, s36, s26
	s_addc_u32 s1, s37, s27
	v_mul_f32_e32 v6, 0x42800000, v6
	v_mul_f32_e32 v7, 0x42800000, v7
	v_mul_f32_e32 v10, 0x42800000, v10
	v_mul_f32_e32 v11, 0x42800000, v11
	v_mul_f32_e32 v14, 0x42800000, v14
	v_mul_f32_e32 v15, 0x42800000, v15
	v_mul_f32_e32 v18, 0x42800000, v18
	v_mul_f32_e32 v19, 0x42800000, v19
	v_mov_b64_e32 v[194:195], s[0:1]
	v_mul_f32_e32 v50, 0x42800000, v50
	v_mul_f32_e32 v51, 0x42800000, v51
	v_mul_f32_e32 v58, 0x42800000, v58
	v_mul_f32_e32 v59, 0x42800000, v59
	v_mul_f32_e32 v66, 0x42800000, v66
	v_mul_f32_e32 v67, 0x42800000, v67
	s_waitcnt lgkmcnt(0)
	v_mul_f32_e32 v74, 0x42800000, v74
	v_mul_f32_e32 v75, 0x42800000, v75
	v_cvt_pk_fp8_f32 v20, v6, v7 op_sel:[0,0,1]
	v_cvt_pk_fp8_f32 v21, v10, v11 op_sel:[0,0,1]
	v_cvt_pk_fp8_f32 v22, v14, v15 op_sel:[0,0,1]
	v_cvt_pk_fp8_f32 v23, v18, v19 op_sel:[0,0,1]
	v_mad_i64_i32 v[132:133], s[4:5], v200, s82, v[194:195]
	v_cvt_pk_fp8_f32 v24, v50, v51 op_sel:[0,0,1]
	v_cvt_pk_fp8_f32 v25, v58, v59 op_sel:[0,0,1]
	v_cvt_pk_fp8_f32 v26, v66, v67 op_sel:[0,0,1]
	v_cvt_pk_fp8_f32 v27, v74, v75 op_sel:[0,0,1]
	v_lshl_add_u64 v[132:133], v[132:133], 0, s[28:29]
	v_lshl_add_u64 v[134:135], v[132:133], 0, v[144:145]
	global_store_dwordx4 v[134:135], v[20:23], off
	s_nop 1
	v_add_co_u32_e32 v134, vcc, 0x16000, v134
	s_nop 1
	v_addc_co_u32_e32 v135, vcc, 0, v135, vcc
	global_store_dwordx4 v[134:135], v[24:27], off
	s_waitcnt vmcnt(13)
	ds_write2_b32 v149, v36, v37 offset1:1
	ds_write2_b32 v149, v38, v39 offset0:2 offset1:3
	s_waitcnt vmcnt(12)
	ds_write2_b32 v150, v40, v41 offset1:1
	ds_write2_b32 v151, v42, v43 offset1:1
	s_waitcnt vmcnt(11)
	ds_write2_b32 v152, v44, v45 offset1:1
	ds_write2_b32 v153, v46, v47 offset1:1
	s_waitcnt vmcnt(10)
	ds_write2_b32 v154, v52, v53 offset1:1
	ds_write2_b32 v155, v54, v55 offset1:1
	s_waitcnt vmcnt(9)
	ds_write2_b32 v156, v60, v61 offset1:1
	ds_write2_b32 v157, v62, v63 offset1:1
	s_waitcnt vmcnt(8)
	ds_write2_b32 v158, v68, v69 offset1:1
	ds_write2_b32 v159, v70, v71 offset1:1
	s_waitcnt vmcnt(7)
	ds_write2_b32 v160, v80, v81 offset1:1
	ds_write2_b32 v161, v82, v83 offset1:1
	s_waitcnt vmcnt(6)
	ds_write2_b32 v162, v124, v125 offset1:1
	ds_write2_b32 v163, v126, v127 offset1:1
	ds_read2_b32 v[4:5], v148 offset1:33
	ds_read2_b32 v[6:7], v148 offset0:66 offset1:99
	ds_read2_b32 v[8:9], v148 offset0:132 offset1:165
	ds_read2_b32 v[10:11], v148 offset0:198 offset1:231
	ds_read2_b32 v[12:13], v164 offset0:8 offset1:41
	ds_read2_b32 v[14:15], v164 offset0:74 offset1:107
	ds_read2_b32 v[16:17], v164 offset0:140 offset1:173
	ds_read2_b32 v[18:19], v164 offset0:206 offset1:239
	ds_read2_b32 v[20:21], v165 offset0:16 offset1:49
	ds_read2_b32 v[22:23], v165 offset0:82 offset1:115
	ds_read2_b32 v[24:25], v165 offset0:148 offset1:181
	ds_read2_b32 v[26:27], v165 offset0:214 offset1:247
	ds_read2_b32 v[36:37], v166 offset0:24 offset1:57
	ds_read2_b32 v[38:39], v166 offset0:90 offset1:123
	ds_read2_b32 v[40:41], v166 offset0:156 offset1:189
	ds_read2_b32 v[42:43], v166 offset0:222 offset1:255
	v_mov_b32_e32 v28, v3
	v_mov_b32_e32 v29, v3
	v_mov_b32_e32 v30, v3
	v_mov_b32_e32 v31, v3
	s_waitcnt lgkmcnt(14)
	v_mul_f32_e32 v4, 0x42800000, v4
	v_mul_f32_e32 v5, 0x42800000, v5
	s_waitcnt lgkmcnt(13)
	v_mul_f32_e32 v8, 0x42800000, v8
	v_mul_f32_e32 v9, 0x42800000, v9
	s_waitcnt lgkmcnt(11)
	v_mul_f32_e32 v12, 0x42800000, v12
	v_mul_f32_e32 v13, 0x42800000, v13
	s_waitcnt lgkmcnt(9)
	v_mul_f32_e32 v16, 0x42800000, v16
	v_mul_f32_e32 v17, 0x42800000, v17
	v_mov_b32_e32 v32, v3
	v_mov_b32_e32 v33, v3
	v_mov_b32_e32 v34, v3
	v_mov_b32_e32 v35, v3
	s_waitcnt lgkmcnt(7)
	v_mul_f32_e32 v20, 0x42800000, v20
	v_mul_f32_e32 v21, 0x42800000, v21
	s_waitcnt lgkmcnt(5)
	v_mul_f32_e32 v24, 0x42800000, v24
	v_mul_f32_e32 v25, 0x42800000, v25
	s_waitcnt lgkmcnt(3)
	v_mul_f32_e32 v36, 0x42800000, v36
	v_mul_f32_e32 v37, 0x42800000, v37
	s_waitcnt lgkmcnt(1)
	v_mul_f32_e32 v40, 0x42800000, v40
	v_mul_f32_e32 v41, 0x42800000, v41
	v_cvt_pk_fp8_f32 v28, v4, v5
	v_cvt_pk_fp8_f32 v29, v8, v9
	v_cvt_pk_fp8_f32 v30, v12, v13
	v_cvt_pk_fp8_f32 v31, v16, v17
	v_cvt_pk_fp8_f32 v32, v20, v21
	v_cvt_pk_fp8_f32 v33, v24, v25
	v_cvt_pk_fp8_f32 v34, v36, v37
	v_cvt_pk_fp8_f32 v35, v40, v41
	s_add_u32 s0, s36, s34
	s_addc_u32 s1, s37, s35
	v_mul_f32_e32 v6, 0x42800000, v6
	v_mul_f32_e32 v7, 0x42800000, v7
	v_mul_f32_e32 v10, 0x42800000, v10
	v_mul_f32_e32 v11, 0x42800000, v11
	v_mul_f32_e32 v14, 0x42800000, v14
	v_mul_f32_e32 v15, 0x42800000, v15
	v_mul_f32_e32 v18, 0x42800000, v18
	v_mul_f32_e32 v19, 0x42800000, v19
	v_mov_b64_e32 v[194:195], s[0:1]
	v_mul_f32_e32 v22, 0x42800000, v22
	v_mul_f32_e32 v23, 0x42800000, v23
	v_mul_f32_e32 v26, 0x42800000, v26
	v_mul_f32_e32 v27, 0x42800000, v27
	v_mul_f32_e32 v38, 0x42800000, v38
	v_mul_f32_e32 v39, 0x42800000, v39
	s_waitcnt lgkmcnt(0)
	v_mul_f32_e32 v42, 0x42800000, v42
	v_mul_f32_e32 v43, 0x42800000, v43
	v_cvt_pk_fp8_f32 v28, v6, v7 op_sel:[0,0,1]
	v_cvt_pk_fp8_f32 v29, v10, v11 op_sel:[0,0,1]
	v_cvt_pk_fp8_f32 v30, v14, v15 op_sel:[0,0,1]
	v_cvt_pk_fp8_f32 v31, v18, v19 op_sel:[0,0,1]
	v_mad_i64_i32 v[132:133], s[0:1], v201, s82, v[194:195]
	v_cvt_pk_fp8_f32 v32, v22, v23 op_sel:[0,0,1]
	v_cvt_pk_fp8_f32 v33, v26, v27 op_sel:[0,0,1]
	v_cvt_pk_fp8_f32 v34, v38, v39 op_sel:[0,0,1]
	v_cvt_pk_fp8_f32 v35, v42, v43 op_sel:[0,0,1]
	v_lshl_add_u64 v[132:133], v[132:133], 0, s[30:31]
	v_lshl_add_u64 v[4:5], v[132:133], 0, v[144:145]
	global_store_dwordx4 v[4:5], v[28:31], off
	s_nop 1
	v_add_co_u32_e32 v4, vcc, 0x16000, v4
	s_nop 1
	v_addc_co_u32_e32 v5, vcc, 0, v5, vcc
	global_store_dwordx4 v[4:5], v[32:35], off
	s_add_i32 s13, s13, 32
	s_cmp_ge_i32 s13, s12
	s_cbranch_scc0 .LBB6_1611
	s_getpc_b64 s[98:99]

.LBB6_2087:
	s_mov_b32 s0, s96
	s_cmpk_lt_i32 s0, 0x80
	s_cbranch_scc1 .LBB6_2098
	v_readlane_b32 s2, v254, 13
	v_readlane_b32 s3, v254, 14
	v_mov_b32_e32 v135, v0
	s_waitcnt vmcnt(0) lgkmcnt(0)
	s_barrier
	s_mul_i32 s19, s0, 0xa0
	s_add_i32 s18, s19, 0xaa00
	v_readfirstlane_b32 s0, v135
	s_ashr_i32 s17, s0, 6
	s_add_i32 s19, s19, 0xaaa0
	s_lshl_b32 s0, s17, 14
	s_add_i32 s16, s0, 0
	s_max_i32 s0, s18, 0
	s_min_i32 s20, s19, 0xdc00
	s_cmp_le_i32 s20, s0
	v_and_b32_e32 v134, 63, v135
	s_cbranch_scc1 .LBB6_2093
	s_sub_i32 s1, s20, s0
	s_mov_b32 s4, 18
	s_cmp_lt_i32 s1, 32
	s_cbranch_scc1 .LBB6_2093
	s_add_i32 s21, s17, s0
	s_cmp_ge_i32 s21, s20
	s_cbranch_scc1 .LBB6_2093
	s_ashr_i32 s5, s4, 31
	s_lshl_b64 s[0:1], s[4:5], 3
	s_add_u32 s0, s76, s0
	s_addc_u32 s1, s77, s1
	s_load_dwordx2 s[0:1], s[0:1], 0x0
	v_lshrrev_b32_e32 v4, 3, v134
	v_lshlrev_b32_e32 v2, 2, v134
	v_mul_u32_u24_e32 v5, 0x2c00, v4
	v_and_b32_e32 v6, 28, v2
	s_waitcnt lgkmcnt(0)
	s_add_u32 s22, s0, 0x10800000
	v_or_b32_e32 v2, v5, v6
	v_lshl_add_u32 v5, v6, 2, s16
	v_lshlrev_b32_e32 v6, 5, v134
	s_addc_u32 s23, s1, 0
	v_lshrrev_b32_e32 v137, 2, v134
	v_lshlrev_b32_e32 v132, 4, v134
	v_and_b32_e32 v132, 48, v132
	s_add_u32 s24, s2, 0x85280000
	v_mul_u32_u24_e32 v4, 0x84, v4
	v_mul_u32_u24_e32 v6, 0x84, v132
	v_lshlrev_b32_e32 v7, 2, v137
	v_and_b32_e32 v136, 31, v135
	s_addc_u32 s25, s3, 0
	v_lshlrev_b32_e32 v2, 2, v2
	v_add3_u32 v138, s16, v6, v7
	v_mov_b32_e32 v133, v3
	v_add_u32_e32 v139, v5, v4
.LBB6_2092:
	s_mul_hi_i32 s0, s21, 0x2e8ba2e9
	s_lshr_b32 s1, s0, 31
	s_ashr_i32 s14, s0, 11
	s_add_i32 s14, s14, s1
	s_mul_i32 s0, s14, 0xffffd400
	s_add_i32 s0, s0, s21
	s_ashr_i32 s0, s0, 1
	s_and_b32 s1, s0, -8
	s_and_b32 s0, s21, 7
	s_or_b32 s1, s1, s0
	s_mul_hi_i32 s4, s1, 0x2e8ba2e9
	s_lshr_b32 s5, s4, 31
	s_ashr_i32 s4, s4, 6
	s_add_i32 s4, s4, s5
	s_mul_i32 s5, s4, 0xfffffea0
	s_add_i32 s5, s5, s1
	s_lshl_b32 s1, s4, 7
	s_lshl_b32 s4, s21, 3
	s_and_b32 s12, s4, 64
	s_lshl_b32 s34, s5, 5
	s_or_b32 s10, s1, s12
	s_mul_i32 s4, s14, 0x5800000
	s_mul_hi_i32 s1, s14, 0x5800000
	s_add_u32 s6, s22, s4
	s_addc_u32 s1, s23, s1
	s_and_b32 s4, s34, 0xe0
	s_cmpk_lt_u32 s4, 0x80
	v_or_b32_e32 v4, s4, v136
	s_cselect_b64 vcc, -1, 0
	s_lshl_b32 s4, s5, 4
	s_and_b32 s4, s4, 0xffffff80
	v_or_b32_e32 v5, s4, v4
	s_addk_i32 s4, 0x1580
	v_add_u32_e32 v4, s4, v4
	v_cndmask_b32_e32 v4, v4, v5, vcc
	s_ashr_i32 s11, s10, 31
	v_readfirstlane_b32 s4, v4
	s_andn2_b32 s4, s4, 31
	s_mul_i32 s7, s10, 0xb000
	s_mul_hi_i32 s5, s10, 0xb000
	s_add_u32 s6, s6, s7
	s_addc_u32 s1, s1, s5
	s_ashr_i32 s5, s4, 31
	s_lshl_b64 s[4:5], s[4:5], 2
	s_add_u32 s4, s6, s4
	s_addc_u32 s5, s1, s5
	s_mov_b64 s[6:7], s[4:5]
	v_mov_b32_e32 v140, v3
	v_lshl_add_u64 v[4:5], s[6:7], 0, v[2:3]
	s_add_u32 s6, s4, 0x58000
	s_addc_u32 s7, s5, 0
	global_load_dwordx4 v[128:131], v[4:5], off nt
	v_mov_b32_e32 v141, v3
	v_lshl_add_u64 v[4:5], s[6:7], 0, v[2:3]
	s_add_u32 s6, s4, 0xb0000
	s_addc_u32 s7, s5, 0
	global_load_dwordx4 v[124:127], v[4:5], off nt
	s_nop 0
	v_lshl_add_u64 v[4:5], s[6:7], 0, v[2:3]
	s_add_u32 s6, s4, 0x108000
	s_addc_u32 s7, s5, 0
	global_load_dwordx4 v[120:123], v[4:5], off nt
	s_nop 0
	v_lshl_add_u64 v[4:5], s[6:7], 0, v[2:3]
	s_add_u32 s6, s4, 0x160000
	s_addc_u32 s7, s5, 0
	global_load_dwordx4 v[116:119], v[4:5], off nt
	s_nop 0
	v_lshl_add_u64 v[4:5], s[6:7], 0, v[2:3]
	s_add_u32 s6, s4, 0x1b8000
	s_addc_u32 s7, s5, 0
	global_load_dwordx4 v[112:115], v[4:5], off nt
	s_nop 0
	v_lshl_add_u64 v[4:5], s[6:7], 0, v[2:3]
	s_add_u32 s6, s4, 0x210000
	s_addc_u32 s7, s5, 0
	s_add_u32 s4, s4, 0x268000
	global_load_dwordx4 v[108:111], v[4:5], off nt
	s_addc_u32 s5, s5, 0
	v_lshl_add_u64 v[4:5], s[6:7], 0, v[2:3]
	global_load_dwordx4 v[104:107], v[4:5], off nt
	s_add_i32 s1, s21, 8
	v_lshl_add_u64 v[4:5], s[4:5], 0, v[2:3]
	s_mul_hi_i32 s4, s1, 0x2e8ba2e9
	s_lshr_b32 s5, s4, 31
	s_ashr_i32 s30, s4, 11
	s_add_i32 s30, s30, s5
	s_mul_i32 s4, s30, 0xffffd400
	s_add_i32 s4, s4, s1
	s_ashr_i32 s4, s4, 1
	s_and_b32 s4, s4, -8
	s_or_b32 s4, s4, s0
	s_mul_hi_i32 s5, s4, 0x2e8ba2e9
	s_lshr_b32 s6, s5, 31
	s_ashr_i32 s5, s5, 6
	s_add_i32 s5, s5, s6
	s_mul_i32 s6, s5, 0xfffffea0
	s_lshl_b32 s1, s1, 3
	s_add_i32 s6, s6, s4
	s_lshl_b32 s4, s5, 7
	s_and_b32 s1, s1, 64
	s_lshl_b32 s31, s6, 5
	s_or_b32 s8, s4, s1
	s_mul_i32 s4, s30, 0x5800000
	s_mul_hi_i32 s1, s30, 0x5800000
	s_add_u32 s5, s22, s4
	s_addc_u32 s1, s23, s1
	s_and_b32 s4, s31, 0xe0
	s_cmpk_lt_u32 s4, 0x80
	global_load_dwordx4 v[100:103], v[4:5], off nt
	v_or_b32_e32 v4, s4, v136
	s_cselect_b64 vcc, -1, 0
	s_lshl_b32 s4, s6, 4
	s_and_b32 s4, s4, 0xffffff80
	v_or_b32_e32 v5, s4, v4
	s_addk_i32 s4, 0x1580
	v_add_u32_e32 v4, s4, v4
	v_cndmask_b32_e32 v4, v4, v5, vcc
	s_ashr_i32 s9, s8, 31
	v_readfirstlane_b32 s4, v4
	s_andn2_b32 s4, s4, 31
	s_mul_i32 s7, s8, 0xb000
	s_mul_hi_i32 s6, s8, 0xb000
	s_add_u32 s7, s5, s7
	s_addc_u32 s1, s1, s6
	s_ashr_i32 s5, s4, 31
	s_lshl_b64 s[4:5], s[4:5], 2
	s_add_u32 s4, s7, s4
	s_addc_u32 s5, s1, s5
	s_mov_b64 s[6:7], s[4:5]
	s_nop 0
	v_lshl_add_u64 v[4:5], s[6:7], 0, v[2:3]
	s_add_u32 s6, s4, 0x58000
	s_addc_u32 s7, s5, 0
	global_load_dwordx4 v[68:71], v[4:5], off nt
	s_nop 0
	v_lshl_add_u64 v[4:5], s[6:7], 0, v[2:3]
	s_add_u32 s6, s4, 0xb0000
	s_addc_u32 s7, s5, 0
	global_load_dwordx4 v[72:75], v[4:5], off nt
	s_nop 0
	v_lshl_add_u64 v[4:5], s[6:7], 0, v[2:3]
	s_add_u32 s6, s4, 0x108000
	s_addc_u32 s7, s5, 0
	global_load_dwordx4 v[76:79], v[4:5], off nt
	s_nop 0
	v_lshl_add_u64 v[4:5], s[6:7], 0, v[2:3]
	s_add_u32 s6, s4, 0x160000
	s_addc_u32 s7, s5, 0
	global_load_dwordx4 v[80:83], v[4:5], off nt
	s_nop 0
	v_lshl_add_u64 v[4:5], s[6:7], 0, v[2:3]
	s_add_u32 s6, s4, 0x1b8000
	s_addc_u32 s7, s5, 0
	global_load_dwordx4 v[84:87], v[4:5], off nt
	s_nop 0
	v_lshl_add_u64 v[4:5], s[6:7], 0, v[2:3]
	s_add_u32 s6, s4, 0x210000
	s_addc_u32 s7, s5, 0
	s_add_u32 s4, s4, 0x268000
	global_load_dwordx4 v[88:91], v[4:5], off nt
	s_addc_u32 s5, s5, 0
	v_lshl_add_u64 v[4:5], s[6:7], 0, v[2:3]
	global_load_dwordx4 v[92:95], v[4:5], off nt
	s_add_i32 s1, s21, 16
	v_lshl_add_u64 v[4:5], s[4:5], 0, v[2:3]
	s_mul_hi_i32 s4, s1, 0x2e8ba2e9
	s_lshr_b32 s5, s4, 31
	s_ashr_i32 s28, s4, 11
	s_add_i32 s28, s28, s5
	s_mul_i32 s4, s28, 0xffffd400
	s_add_i32 s4, s4, s1
	s_ashr_i32 s1, s4, 1
	s_and_b32 s1, s1, -8
	s_or_b32 s1, s1, s0
	s_mul_hi_i32 s4, s1, 0x2e8ba2e9
	s_lshr_b32 s5, s4, 31
	s_ashr_i32 s4, s4, 6
	s_add_i32 s4, s4, s5
	s_mul_i32 s5, s4, 0xfffffea0
	s_add_i32 s5, s5, s1
	s_lshl_b32 s1, s4, 7
	s_lshl_b32 s29, s5, 5
	s_or_b32 s6, s1, s12
	s_mul_i32 s4, s28, 0x5800000
	s_mul_hi_i32 s1, s28, 0x5800000
	s_add_u32 s12, s22, s4
	s_addc_u32 s1, s23, s1
	s_and_b32 s4, s29, 0xe0
	s_cmpk_lt_u32 s4, 0x80
	global_load_dwordx4 v[96:99], v[4:5], off nt
	v_or_b32_e32 v4, s4, v136
	s_cselect_b64 vcc, -1, 0
	s_lshl_b32 s4, s5, 4
	s_and_b32 s4, s4, 0xffffff80
	v_or_b32_e32 v5, s4, v4
	s_addk_i32 s4, 0x1580
	v_add_u32_e32 v4, s4, v4
	v_cndmask_b32_e32 v4, v4, v5, vcc
	s_ashr_i32 s7, s6, 31
	v_readfirstlane_b32 s4, v4
	s_andn2_b32 s4, s4, 31
	s_mul_i32 s13, s6, 0xb000
	s_mul_hi_i32 s5, s6, 0xb000
	s_add_u32 s12, s12, s13
	s_addc_u32 s1, s1, s5
	s_ashr_i32 s5, s4, 31
	s_lshl_b64 s[4:5], s[4:5], 2
	s_add_u32 s4, s12, s4
	s_addc_u32 s5, s1, s5
	s_mov_b64 s[12:13], s[4:5]
	s_nop 0
	v_lshl_add_u64 v[4:5], s[12:13], 0, v[2:3]
	s_add_u32 s12, s4, 0x58000
	s_addc_u32 s13, s5, 0
	global_load_dwordx4 v[36:39], v[4:5], off nt
	s_nop 0
	v_lshl_add_u64 v[4:5], s[12:13], 0, v[2:3]
	s_add_u32 s12, s4, 0xb0000
	s_addc_u32 s13, s5, 0
	global_load_dwordx4 v[40:43], v[4:5], off nt
	s_nop 0
	v_lshl_add_u64 v[4:5], s[12:13], 0, v[2:3]
	s_add_u32 s12, s4, 0x108000
	s_addc_u32 s13, s5, 0
	global_load_dwordx4 v[44:47], v[4:5], off nt
	s_nop 0
	v_lshl_add_u64 v[4:5], s[12:13], 0, v[2:3]
	s_add_u32 s12, s4, 0x160000
	s_addc_u32 s13, s5, 0
	global_load_dwordx4 v[48:51], v[4:5], off nt
	s_nop 0
	v_lshl_add_u64 v[4:5], s[12:13], 0, v[2:3]
	s_add_u32 s12, s4, 0x1b8000
	s_addc_u32 s13, s5, 0
	global_load_dwordx4 v[52:55], v[4:5], off nt
	s_nop 0
	v_lshl_add_u64 v[4:5], s[12:13], 0, v[2:3]
	s_add_u32 s12, s4, 0x210000
	s_addc_u32 s13, s5, 0
	s_add_u32 s4, s4, 0x268000
	global_load_dwordx4 v[56:59], v[4:5], off nt
	s_addc_u32 s5, s5, 0
	v_lshl_add_u64 v[4:5], s[12:13], 0, v[2:3]
	global_load_dwordx4 v[60:63], v[4:5], off nt
	s_add_i32 s1, s21, 24
	v_lshl_add_u64 v[4:5], s[4:5], 0, v[2:3]
	s_mul_hi_i32 s4, s1, 0x2e8ba2e9
	s_lshr_b32 s5, s4, 31
	s_ashr_i32 s26, s4, 11
	s_add_i32 s26, s26, s5
	s_mul_i32 s4, s26, 0xffffd400
	s_add_i32 s4, s4, s1
	s_ashr_i32 s4, s4, 1
	s_and_b32 s4, s4, -8
	s_or_b32 s0, s4, s0
	s_mul_hi_i32 s4, s0, 0x2e8ba2e9
	s_lshr_b32 s5, s4, 31
	s_ashr_i32 s4, s4, 6
	s_add_i32 s4, s4, s5
	s_mul_i32 s5, s4, 0xfffffea0
	s_lshl_b32 s1, s1, 3
	s_add_i32 s5, s5, s0
	s_lshl_b32 s0, s4, 7
	s_and_b32 s1, s1, 64
	s_lshl_b32 s27, s5, 5
	s_or_b32 s4, s0, s1
	s_mul_i32 s1, s26, 0x5800000
	s_mul_hi_i32 s0, s26, 0x5800000
	s_add_u32 s1, s22, s1
	s_addc_u32 s12, s23, s0
	s_and_b32 s0, s27, 0xe0
	s_cmpk_lt_u32 s0, 0x80
	global_load_dwordx4 v[64:67], v[4:5], off nt
	v_or_b32_e32 v4, s0, v136
	s_cselect_b64 vcc, -1, 0
	s_lshl_b32 s0, s5, 4
	s_and_b32 s0, s0, 0xffffff80
	v_or_b32_e32 v5, s0, v4
	s_addk_i32 s0, 0x1580
	v_add_u32_e32 v4, s0, v4
	v_cndmask_b32_e32 v4, v4, v5, vcc
	s_ashr_i32 s5, s4, 31
	v_readfirstlane_b32 s0, v4
	s_andn2_b32 s0, s0, 31
	s_mul_i32 s15, s4, 0xb000
	s_mul_hi_i32 s13, s4, 0xb000
	s_add_u32 s15, s1, s15
	s_addc_u32 s12, s12, s13
	s_ashr_i32 s1, s0, 31
	s_lshl_b64 s[0:1], s[0:1], 2
	s_add_u32 s0, s15, s0
	s_addc_u32 s1, s12, s1
	s_mov_b64 s[12:13], s[0:1]
	s_nop 0
	v_lshl_add_u64 v[4:5], s[12:13], 0, v[2:3]
	s_add_u32 s12, s0, 0x58000
	s_addc_u32 s13, s1, 0
	global_load_dwordx4 v[4:7], v[4:5], off nt
	s_nop 0
	v_lshl_add_u64 v[8:9], s[12:13], 0, v[2:3]
	s_add_u32 s12, s0, 0xb0000
	s_addc_u32 s13, s1, 0
	global_load_dwordx4 v[8:11], v[8:9], off nt
	s_nop 0
	v_lshl_add_u64 v[12:13], s[12:13], 0, v[2:3]
	s_add_u32 s12, s0, 0x108000
	s_addc_u32 s13, s1, 0
	global_load_dwordx4 v[12:15], v[12:13], off nt
	s_nop 0
	v_lshl_add_u64 v[16:17], s[12:13], 0, v[2:3]
	s_add_u32 s12, s0, 0x160000
	s_addc_u32 s13, s1, 0
	global_load_dwordx4 v[16:19], v[16:17], off nt
	s_nop 0
	v_lshl_add_u64 v[20:21], s[12:13], 0, v[2:3]
	s_add_u32 s12, s0, 0x1b8000
	s_addc_u32 s13, s1, 0
	global_load_dwordx4 v[20:23], v[20:21], off nt
	s_nop 0
	v_lshl_add_u64 v[24:25], s[12:13], 0, v[2:3]
	s_add_u32 s12, s0, 0x210000
	s_addc_u32 s13, s1, 0
	s_add_u32 s0, s0, 0x268000
	global_load_dwordx4 v[24:27], v[24:25], off nt
	s_addc_u32 s1, s1, 0
	v_lshl_add_u64 v[28:29], s[12:13], 0, v[2:3]
	global_load_dwordx4 v[28:31], v[28:29], off nt
	s_nop 0
	v_lshl_add_u64 v[32:33], s[0:1], 0, v[2:3]
	global_load_dwordx4 v[32:35], v[32:33], off nt
	s_waitcnt vmcnt(31)
	ds_write2_b32 v139, v128, v129 offset1:1
	ds_write2_b32 v139, v130, v131 offset0:2 offset1:3
	v_add_u32_e32 v128, 0x420, v139
	s_waitcnt vmcnt(30)
	ds_write2_b32 v128, v124, v125 offset1:1
	v_add_u32_e32 v125, 0x840, v139
	s_waitcnt vmcnt(29)
	ds_write2_b32 v125, v120, v121 offset1:1
	v_add_u32_e32 v121, 0xc60, v139
	s_waitcnt vmcnt(28)
	ds_write2_b32 v121, v116, v117 offset1:1
	v_add_u32_e32 v117, 0x1080, v139
	s_waitcnt vmcnt(27)
	ds_write2_b32 v117, v112, v113 offset1:1
	v_add_u32_e32 v113, 0x14a0, v139
	s_waitcnt vmcnt(26)
	ds_write2_b32 v113, v108, v109 offset1:1
	v_add_u32_e32 v109, 0x18c0, v139
	s_waitcnt vmcnt(25)
	ds_write2_b32 v109, v104, v105 offset1:1
	v_add_u32_e32 v104, 0x18c8, v139
	v_add_u32_e32 v124, 0x428, v139
	v_add_u32_e32 v120, 0x848, v139
	v_add_u32_e32 v116, 0xc68, v139
	v_add_u32_e32 v112, 0x1088, v139
	v_add_u32_e32 v108, 0x14a8, v139
	ds_write2_b32 v104, v106, v107 offset1:1
	v_add_u32_e32 v105, 0x1ce0, v139
	v_add_u32_e32 v106, 0x1ce8, v139
	ds_write2_b32 v124, v126, v127 offset1:1
	ds_write2_b32 v120, v122, v123 offset1:1
	ds_write2_b32 v116, v118, v119 offset1:1
	ds_write2_b32 v112, v114, v115 offset1:1
	ds_write2_b32 v108, v110, v111 offset1:1
	s_waitcnt vmcnt(24)
	ds_write2_b32 v105, v100, v101 offset1:1
	ds_write2_b32 v106, v102, v103 offset1:1
	ds_read2_b32 v[110:111], v138 offset1:33
	ds_read2_b32 v[114:115], v138 offset0:66 offset1:99
	ds_read2_b32 v[118:119], v138 offset0:132 offset1:165
	ds_read2_b32 v[122:123], v138 offset0:198 offset1:231
	v_add_u32_e32 v102, 0x400, v138
	s_waitcnt lgkmcnt(3)
	v_mul_f32_e32 v101, 0x42800000, v110
	v_mul_f32_e32 v110, 0x42800000, v111
	v_mov_b32_e32 v103, v138
	v_cvt_pk_fp8_f32 v140, v101, v110
	ds_read2_b32 v[126:127], v102 offset0:8 offset1:41
	ds_read2_b32 v[130:131], v102 offset0:74 offset1:107
	ds_read2_b32 v[148:149], v102 offset0:140 offset1:173
	ds_read2_b32 v[150:151], v102 offset0:206 offset1:239
	ds_read2_b32 v[142:143], v103 offset0:16 offset1:49
	ds_read2_b32 v[144:145], v103 offset0:82 offset1:115
	ds_read2_b32 v[146:147], v103 offset0:148 offset1:181
	ds_read2_b32 v[152:153], v103 offset0:214 offset1:247
	s_waitcnt lgkmcnt(10)
	v_mul_f32_e32 v111, 0x42800000, v114
	v_mul_f32_e32 v114, 0x42800000, v115
	v_cvt_pk_fp8_f32 v140, v111, v114 op_sel:[0,0,1]
	s_waitcnt lgkmcnt(3)
	v_mul_f32_e32 v101, 0x42800000, v142
	v_mul_f32_e32 v110, 0x42800000, v143
	s_waitcnt lgkmcnt(2)
	v_mul_f32_e32 v111, 0x42800000, v144
	v_mov_b32_e32 v144, v3
	v_add_u32_e32 v107, 0x400, v138
	v_cvt_pk_fp8_f32 v144, v101, v110
	v_mul_f32_e32 v101, 0x42800000, v118
	v_mul_f32_e32 v110, 0x42800000, v119
	ds_read2_b32 v[154:155], v107 offset0:24 offset1:57
	ds_read2_b32 v[156:157], v107 offset0:90 offset1:123
	ds_read2_b32 v[166:167], v107 offset0:156 offset1:189
	ds_read2_b32 v[168:169], v107 offset0:222 offset1:255
	v_mul_f32_e32 v114, 0x42800000, v145
	v_cvt_pk_fp8_f32 v141, v101, v110
	s_waitcnt lgkmcnt(5)
	v_mul_f32_e32 v101, 0x42800000, v146
	v_mul_f32_e32 v110, 0x42800000, v147
	v_mov_b32_e32 v145, v3
	v_cvt_pk_fp8_f32 v145, v101, v110
	v_mul_f32_e32 v101, 0x42800000, v126
	v_mul_f32_e32 v110, 0x42800000, v127
	v_mov_b32_e32 v142, v3
	v_cvt_pk_fp8_f32 v142, v101, v110
	s_waitcnt lgkmcnt(3)
	v_mul_f32_e32 v101, 0x42800000, v154
	v_mul_f32_e32 v110, 0x42800000, v155
	v_mov_b32_e32 v146, v3
	v_cvt_pk_fp8_f32 v144, v111, v114 op_sel:[0,0,1]
	v_mul_f32_e32 v111, 0x42800000, v122
	v_mul_f32_e32 v114, 0x42800000, v123
	v_cvt_pk_fp8_f32 v146, v101, v110
	v_mul_f32_e32 v101, 0x42800000, v148
	v_mul_f32_e32 v110, 0x42800000, v149
	v_mov_b32_e32 v143, v3
	v_cvt_pk_fp8_f32 v141, v111, v114 op_sel:[0,0,1]
	v_mul_f32_e32 v111, 0x42800000, v152
	v_mul_f32_e32 v114, 0x42800000, v153
	v_cvt_pk_fp8_f32 v143, v101, v110
	s_waitcnt lgkmcnt(1)
	v_mul_f32_e32 v101, 0x42800000, v166
	v_mul_f32_e32 v110, 0x42800000, v167
	v_mov_b32_e32 v147, v3
	v_cvt_pk_fp8_f32 v145, v111, v114 op_sel:[0,0,1]
	v_mul_f32_e32 v111, 0x42800000, v130
	v_mul_f32_e32 v114, 0x42800000, v131
	v_cvt_pk_fp8_f32 v147, v101, v110
	s_mul_hi_i32 s0, s14, 0x1600000
	s_mul_i32 s14, s14, 0x1600000
	v_or_b32_e32 v100, s34, v137
	v_cvt_pk_fp8_f32 v142, v111, v114 op_sel:[0,0,1]
	v_mul_f32_e32 v111, 0x42800000, v156
	v_mul_f32_e32 v114, 0x42800000, v157
	s_add_u32 s14, s24, s14
	v_cvt_pk_fp8_f32 v146, v111, v114 op_sel:[0,0,1]
	v_mul_f32_e32 v111, 0x42800000, v150
	v_mul_f32_e32 v114, 0x42800000, v151
	v_ashrrev_i32_e32 v101, 31, v100
	s_addc_u32 s15, s25, s0
	v_cvt_pk_fp8_f32 v143, v111, v114 op_sel:[0,0,1]
	s_waitcnt lgkmcnt(0)
	v_mul_f32_e32 v111, 0x42800000, v168
	v_mul_f32_e32 v114, 0x42800000, v169
	v_lshlrev_b64 v[100:101], 11, v[100:101]
	v_cvt_pk_fp8_f32 v147, v111, v114 op_sel:[0,0,1]
	v_lshl_add_u64 v[100:101], s[14:15], 0, v[100:101]
	v_lshl_add_u64 v[100:101], v[100:101], 0, s[10:11]
	v_lshl_add_u64 v[100:101], v[100:101], 0, v[132:133]
	global_store_dwordx4 v[100:101], v[140:143], off
	s_nop 1
	v_add_co_u32_e32 v100, vcc, 0x8000, v100
	s_nop 1
	v_addc_co_u32_e32 v101, vcc, 0, v101, vcc
	global_store_dwordx4 v[100:101], v[144:147], off
	s_waitcnt vmcnt(25)
	ds_write2_b32 v139, v68, v69 offset1:1
	ds_write2_b32 v139, v70, v71 offset0:2 offset1:3
	s_waitcnt vmcnt(24)
	ds_write2_b32 v128, v72, v73 offset1:1
	ds_write2_b32 v124, v74, v75 offset1:1
	s_waitcnt vmcnt(23)
	ds_write2_b32 v125, v76, v77 offset1:1
	ds_write2_b32 v120, v78, v79 offset1:1
	s_waitcnt vmcnt(22)
	ds_write2_b32 v121, v80, v81 offset1:1
	ds_write2_b32 v116, v82, v83 offset1:1
	s_waitcnt vmcnt(21)
	ds_write2_b32 v117, v84, v85 offset1:1
	ds_write2_b32 v112, v86, v87 offset1:1
	s_waitcnt vmcnt(20)
	ds_write2_b32 v113, v88, v89 offset1:1
	ds_write2_b32 v108, v90, v91 offset1:1
	s_waitcnt vmcnt(19)
	ds_write2_b32 v109, v92, v93 offset1:1
	ds_write2_b32 v104, v94, v95 offset1:1
	s_waitcnt vmcnt(18)
	ds_write2_b32 v105, v96, v97 offset1:1
	ds_write2_b32 v106, v98, v99 offset1:1
	ds_read2_b32 v[94:95], v138 offset1:33
	ds_read2_b32 v[96:97], v138 offset0:66 offset1:99
	ds_read2_b32 v[92:93], v138 offset0:132 offset1:165
	ds_read2_b32 v[90:91], v138 offset0:198 offset1:231
	ds_read2_b32 v[84:85], v102 offset0:8 offset1:41
	ds_read2_b32 v[82:83], v102 offset0:74 offset1:107
	ds_read2_b32 v[76:77], v102 offset0:140 offset1:173
	ds_read2_b32 v[74:75], v102 offset0:206 offset1:239
	ds_read2_b32 v[98:99], v103 offset0:16 offset1:49
	ds_read2_b32 v[100:101], v103 offset0:82 offset1:115
	ds_read2_b32 v[88:89], v103 offset0:148 offset1:181
	ds_read2_b32 v[86:87], v103 offset0:214 offset1:247
	ds_read2_b32 v[80:81], v107 offset0:24 offset1:57
	ds_read2_b32 v[78:79], v107 offset0:90 offset1:123
	ds_read2_b32 v[72:73], v107 offset0:156 offset1:189
	ds_read2_b32 v[70:71], v107 offset0:222 offset1:255
	s_waitcnt lgkmcnt(14)
	v_mul_f32_e32 v69, 0x42800000, v94
	v_mul_f32_e32 v95, 0x42800000, v95
	v_mov_b32_e32 v94, v3
	v_cvt_pk_fp8_f32 v94, v69, v95
	s_waitcnt lgkmcnt(7)
	v_mul_f32_e32 v69, 0x42800000, v98
	v_mul_f32_e32 v95, 0x42800000, v99
	v_mov_b32_e32 v98, v3
	v_cvt_pk_fp8_f32 v98, v69, v95
	v_mul_f32_e32 v96, 0x42800000, v96
	v_mul_f32_e32 v97, 0x42800000, v97
	v_mul_f32_e32 v69, 0x42800000, v92
	v_mul_f32_e32 v92, 0x42800000, v93
	v_mov_b32_e32 v95, v3
	v_cvt_pk_fp8_f32 v94, v96, v97 op_sel:[0,0,1]
	s_waitcnt lgkmcnt(6)
	v_mul_f32_e32 v96, 0x42800000, v100
	v_mul_f32_e32 v97, 0x42800000, v101
	v_cvt_pk_fp8_f32 v95, v69, v92
	s_waitcnt lgkmcnt(5)
	v_mul_f32_e32 v69, 0x42800000, v88
	v_mul_f32_e32 v88, 0x42800000, v89
	v_mov_b32_e32 v99, v3
	v_cvt_pk_fp8_f32 v98, v96, v97 op_sel:[0,0,1]
	v_cvt_pk_fp8_f32 v99, v69, v88
	v_mul_f32_e32 v69, 0x42800000, v84
	v_mul_f32_e32 v84, 0x42800000, v85
	v_mov_b32_e32 v96, v3
	v_cvt_pk_fp8_f32 v96, v69, v84
	s_waitcnt lgkmcnt(3)
	v_mul_f32_e32 v69, 0x42800000, v80
	v_mul_f32_e32 v80, 0x42800000, v81
	v_mov_b32_e32 v100, v3
	v_cvt_pk_fp8_f32 v100, v69, v80
	v_mul_f32_e32 v69, 0x42800000, v76
	v_mul_f32_e32 v76, 0x42800000, v77
	v_mov_b32_e32 v97, v3
	v_cvt_pk_fp8_f32 v97, v69, v76
	s_waitcnt lgkmcnt(1)
	v_mul_f32_e32 v69, 0x42800000, v72
	v_mul_f32_e32 v72, 0x42800000, v73
	v_mov_b32_e32 v101, v3
	v_cvt_pk_fp8_f32 v101, v69, v72
	s_mul_hi_i32 s0, s30, 0x1600000
	s_mul_i32 s30, s30, 0x1600000
	v_or_b32_e32 v68, s31, v137
	s_add_u32 s10, s24, s30
	v_mul_f32_e32 v90, 0x42800000, v90
	v_mul_f32_e32 v91, 0x42800000, v91
	v_mul_f32_e32 v82, 0x42800000, v82
	v_mul_f32_e32 v83, 0x42800000, v83
	v_mul_f32_e32 v74, 0x42800000, v74
	v_mul_f32_e32 v75, 0x42800000, v75
	v_ashrrev_i32_e32 v69, 31, v68
	s_addc_u32 s11, s25, s0
	v_cvt_pk_fp8_f32 v95, v90, v91 op_sel:[0,0,1]
	v_mul_f32_e32 v86, 0x42800000, v86
	v_mul_f32_e32 v87, 0x42800000, v87
	v_cvt_pk_fp8_f32 v96, v82, v83 op_sel:[0,0,1]
	v_mul_f32_e32 v78, 0x42800000, v78
	v_mul_f32_e32 v79, 0x42800000, v79
	v_cvt_pk_fp8_f32 v97, v74, v75 op_sel:[0,0,1]
	s_waitcnt lgkmcnt(0)
	v_mul_f32_e32 v70, 0x42800000, v70
	v_mul_f32_e32 v71, 0x42800000, v71
	v_lshlrev_b64 v[68:69], 11, v[68:69]
	v_cvt_pk_fp8_f32 v99, v86, v87 op_sel:[0,0,1]
	v_cvt_pk_fp8_f32 v100, v78, v79 op_sel:[0,0,1]
	v_cvt_pk_fp8_f32 v101, v70, v71 op_sel:[0,0,1]
	v_lshl_add_u64 v[68:69], s[10:11], 0, v[68:69]
	v_lshl_add_u64 v[68:69], v[68:69], 0, s[8:9]
	v_lshl_add_u64 v[68:69], v[68:69], 0, v[132:133]
	global_store_dwordx4 v[68:69], v[94:97], off
	s_nop 1
	v_add_co_u32_e32 v68, vcc, 0x8000, v68
	s_nop 1
	v_addc_co_u32_e32 v69, vcc, 0, v69, vcc
	global_store_dwordx4 v[68:69], v[98:101], off
	s_waitcnt vmcnt(19)
	ds_write2_b32 v139, v36, v37 offset1:1
	ds_write2_b32 v139, v38, v39 offset0:2 offset1:3
	s_waitcnt vmcnt(18)
	ds_write2_b32 v128, v40, v41 offset1:1
	ds_write2_b32 v124, v42, v43 offset1:1
	s_waitcnt vmcnt(17)
	ds_write2_b32 v125, v44, v45 offset1:1
	ds_write2_b32 v120, v46, v47 offset1:1
	s_waitcnt vmcnt(16)
	ds_write2_b32 v121, v48, v49 offset1:1
	ds_write2_b32 v116, v50, v51 offset1:1
	s_waitcnt vmcnt(15)
	ds_write2_b32 v117, v52, v53 offset1:1
	ds_write2_b32 v112, v54, v55 offset1:1
	s_waitcnt vmcnt(14)
	ds_write2_b32 v113, v56, v57 offset1:1
	ds_write2_b32 v108, v58, v59 offset1:1
	s_waitcnt vmcnt(13)
	ds_write2_b32 v109, v60, v61 offset1:1
	ds_write2_b32 v104, v62, v63 offset1:1
	s_waitcnt vmcnt(12)
	ds_write2_b32 v105, v64, v65 offset1:1
	ds_write2_b32 v106, v66, v67 offset1:1
	ds_read2_b32 v[62:63], v138 offset1:33
	ds_read2_b32 v[64:65], v138 offset0:66 offset1:99
	ds_read2_b32 v[60:61], v138 offset0:132 offset1:165
	ds_read2_b32 v[58:59], v138 offset0:198 offset1:231
	ds_read2_b32 v[52:53], v102 offset0:8 offset1:41
	ds_read2_b32 v[50:51], v102 offset0:74 offset1:107
	ds_read2_b32 v[44:45], v102 offset0:140 offset1:173
	ds_read2_b32 v[42:43], v102 offset0:206 offset1:239
	ds_read2_b32 v[66:67], v103 offset0:16 offset1:49
	ds_read2_b32 v[68:69], v103 offset0:82 offset1:115
	ds_read2_b32 v[56:57], v103 offset0:148 offset1:181
	ds_read2_b32 v[54:55], v103 offset0:214 offset1:247
	ds_read2_b32 v[48:49], v107 offset0:24 offset1:57
	ds_read2_b32 v[46:47], v107 offset0:90 offset1:123
	ds_read2_b32 v[40:41], v107 offset0:156 offset1:189
	ds_read2_b32 v[38:39], v107 offset0:222 offset1:255
	s_waitcnt lgkmcnt(14)
	v_mul_f32_e32 v37, 0x42800000, v62
	v_mul_f32_e32 v63, 0x42800000, v63
	v_mov_b32_e32 v62, v3
	v_cvt_pk_fp8_f32 v62, v37, v63
	s_waitcnt lgkmcnt(7)
	v_mul_f32_e32 v37, 0x42800000, v66
	v_mul_f32_e32 v63, 0x42800000, v67
	v_mov_b32_e32 v66, v3
	v_cvt_pk_fp8_f32 v66, v37, v63
	v_mul_f32_e32 v64, 0x42800000, v64
	v_mul_f32_e32 v65, 0x42800000, v65
	v_mul_f32_e32 v37, 0x42800000, v60
	v_mul_f32_e32 v60, 0x42800000, v61
	v_mov_b32_e32 v63, v3
	v_cvt_pk_fp8_f32 v62, v64, v65 op_sel:[0,0,1]
	s_waitcnt lgkmcnt(6)
	v_mul_f32_e32 v64, 0x42800000, v68
	v_mul_f32_e32 v65, 0x42800000, v69
	v_cvt_pk_fp8_f32 v63, v37, v60
	s_waitcnt lgkmcnt(5)
	v_mul_f32_e32 v37, 0x42800000, v56
	v_mul_f32_e32 v56, 0x42800000, v57
	v_mov_b32_e32 v67, v3
	v_cvt_pk_fp8_f32 v66, v64, v65 op_sel:[0,0,1]
	v_cvt_pk_fp8_f32 v67, v37, v56
	v_mul_f32_e32 v37, 0x42800000, v52
	v_mul_f32_e32 v52, 0x42800000, v53
	v_mov_b32_e32 v64, v3
	v_cvt_pk_fp8_f32 v64, v37, v52
	s_waitcnt lgkmcnt(3)
	v_mul_f32_e32 v37, 0x42800000, v48
	v_mul_f32_e32 v48, 0x42800000, v49
	v_mov_b32_e32 v68, v3
	v_cvt_pk_fp8_f32 v68, v37, v48
	v_mul_f32_e32 v37, 0x42800000, v44
	v_mul_f32_e32 v44, 0x42800000, v45
	v_mov_b32_e32 v65, v3
	v_cvt_pk_fp8_f32 v65, v37, v44
	s_waitcnt lgkmcnt(1)
	v_mul_f32_e32 v37, 0x42800000, v40
	v_mul_f32_e32 v40, 0x42800000, v41
	v_mov_b32_e32 v69, v3
	v_cvt_pk_fp8_f32 v69, v37, v40
	s_mul_hi_i32 s0, s28, 0x1600000
	s_mul_i32 s28, s28, 0x1600000
	v_or_b32_e32 v36, s29, v137
	s_add_u32 s8, s24, s28
	v_mul_f32_e32 v58, 0x42800000, v58
	v_mul_f32_e32 v59, 0x42800000, v59
	v_mul_f32_e32 v50, 0x42800000, v50
	v_mul_f32_e32 v51, 0x42800000, v51
	v_mul_f32_e32 v42, 0x42800000, v42
	v_mul_f32_e32 v43, 0x42800000, v43
	v_ashrrev_i32_e32 v37, 31, v36
	s_addc_u32 s9, s25, s0
	v_cvt_pk_fp8_f32 v63, v58, v59 op_sel:[0,0,1]
	v_mul_f32_e32 v54, 0x42800000, v54
	v_mul_f32_e32 v55, 0x42800000, v55
	v_cvt_pk_fp8_f32 v64, v50, v51 op_sel:[0,0,1]
	v_mul_f32_e32 v46, 0x42800000, v46
	v_mul_f32_e32 v47, 0x42800000, v47
	v_cvt_pk_fp8_f32 v65, v42, v43 op_sel:[0,0,1]
	s_waitcnt lgkmcnt(0)
	v_mul_f32_e32 v38, 0x42800000, v38
	v_mul_f32_e32 v39, 0x42800000, v39
	v_lshlrev_b64 v[36:37], 11, v[36:37]
	v_cvt_pk_fp8_f32 v67, v54, v55 op_sel:[0,0,1]
	v_cvt_pk_fp8_f32 v68, v46, v47 op_sel:[0,0,1]
	v_cvt_pk_fp8_f32 v69, v38, v39 op_sel:[0,0,1]
	v_lshl_add_u64 v[36:37], s[8:9], 0, v[36:37]
	v_lshl_add_u64 v[36:37], v[36:37], 0, s[6:7]
	v_lshl_add_u64 v[36:37], v[36:37], 0, v[132:133]
	global_store_dwordx4 v[36:37], v[62:65], off
	s_nop 1
	v_add_co_u32_e32 v36, vcc, 0x8000, v36
	s_nop 1
	v_addc_co_u32_e32 v37, vcc, 0, v37, vcc
	global_store_dwordx4 v[36:37], v[66:69], off
	s_waitcnt vmcnt(13)
	ds_write2_b32 v139, v4, v5 offset1:1
	ds_write2_b32 v139, v6, v7 offset0:2 offset1:3
	s_waitcnt vmcnt(12)
	ds_write2_b32 v128, v8, v9 offset1:1
	ds_write2_b32 v124, v10, v11 offset1:1
	s_waitcnt vmcnt(11)
	ds_write2_b32 v125, v12, v13 offset1:1
	ds_write2_b32 v120, v14, v15 offset1:1
	s_waitcnt vmcnt(10)
	ds_write2_b32 v121, v16, v17 offset1:1
	ds_write2_b32 v116, v18, v19 offset1:1
	s_waitcnt vmcnt(9)
	ds_write2_b32 v117, v20, v21 offset1:1
	ds_write2_b32 v112, v22, v23 offset1:1
	s_waitcnt vmcnt(8)
	ds_write2_b32 v113, v24, v25 offset1:1
	ds_write2_b32 v108, v26, v27 offset1:1
	s_waitcnt vmcnt(7)
	ds_write2_b32 v109, v28, v29 offset1:1
	ds_write2_b32 v104, v30, v31 offset1:1
	s_waitcnt vmcnt(6)
	ds_write2_b32 v105, v32, v33 offset1:1
	ds_write2_b32 v106, v34, v35 offset1:1
	ds_read2_b32 v[4:5], v138 offset1:33
	ds_read2_b32 v[8:9], v138 offset0:66 offset1:99
	ds_read2_b32 v[32:33], v138 offset0:132 offset1:165
	ds_read2_b32 v[30:31], v138 offset0:198 offset1:231
	ds_read2_b32 v[24:25], v102 offset0:8 offset1:41
	ds_read2_b32 v[6:7], v102 offset0:74 offset1:107
	ds_read2_b32 v[20:21], v102 offset0:140 offset1:173
	ds_read2_b32 v[18:19], v102 offset0:206 offset1:239
	ds_read2_b32 v[34:35], v103 offset0:16 offset1:49
	ds_read2_b32 v[36:37], v103 offset0:82 offset1:115
	ds_read2_b32 v[28:29], v103 offset0:148 offset1:181
	ds_read2_b32 v[26:27], v103 offset0:214 offset1:247
	ds_read2_b32 v[22:23], v107 offset0:24 offset1:57
	ds_read2_b32 v[10:11], v107 offset0:90 offset1:123
	ds_read2_b32 v[16:17], v107 offset0:156 offset1:189
	ds_read2_b32 v[14:15], v107 offset0:222 offset1:255
	s_waitcnt lgkmcnt(14)
	v_mul_f32_e32 v13, 0x42800000, v4
	v_mul_f32_e32 v5, 0x42800000, v5
	v_mov_b32_e32 v4, v3
	v_cvt_pk_fp8_f32 v4, v13, v5
	v_mul_f32_e32 v8, 0x42800000, v8
	v_mul_f32_e32 v9, 0x42800000, v9
	s_waitcnt lgkmcnt(7)
	v_mul_f32_e32 v5, 0x42800000, v34
	v_cvt_pk_fp8_f32 v4, v8, v9 op_sel:[0,0,1]
	v_mul_f32_e32 v9, 0x42800000, v35
	v_mov_b32_e32 v8, v3
	v_cvt_pk_fp8_f32 v8, v5, v9
	s_waitcnt lgkmcnt(6)
	v_mul_f32_e32 v13, 0x42800000, v36
	v_mul_f32_e32 v34, 0x42800000, v37
	v_mul_f32_e32 v9, 0x42800000, v32
	v_cvt_pk_fp8_f32 v8, v13, v34 op_sel:[0,0,1]
	v_mul_f32_e32 v13, 0x42800000, v33
	v_mov_b32_e32 v5, v3
	v_cvt_pk_fp8_f32 v5, v9, v13
	s_waitcnt lgkmcnt(5)
	v_mul_f32_e32 v13, 0x42800000, v28
	v_mul_f32_e32 v28, 0x42800000, v29
	v_mov_b32_e32 v9, v3
	v_cvt_pk_fp8_f32 v9, v13, v28
	v_mul_f32_e32 v13, 0x42800000, v24
	v_mul_f32_e32 v24, 0x42800000, v25
	v_mul_f32_e32 v25, 0x42800000, v6
	v_mov_b32_e32 v6, v3
	v_cvt_pk_fp8_f32 v6, v13, v24
	v_mul_f32_e32 v7, 0x42800000, v7
	s_waitcnt lgkmcnt(3)
	v_mul_f32_e32 v13, 0x42800000, v23
	s_waitcnt lgkmcnt(2)
	v_mul_f32_e32 v11, 0x42800000, v11
	v_cvt_pk_fp8_f32 v6, v25, v7 op_sel:[0,0,1]
	v_mul_f32_e32 v7, 0x42800000, v22
	v_mul_f32_e32 v22, 0x42800000, v10
	v_mov_b32_e32 v10, v3
	v_cvt_pk_fp8_f32 v10, v7, v13
	v_mul_f32_e32 v13, 0x42800000, v21
	v_mov_b32_e32 v7, v3
	s_mul_hi_i32 s0, s26, 0x1600000
	v_cvt_pk_fp8_f32 v10, v22, v11 op_sel:[0,0,1]
	v_mul_f32_e32 v11, 0x42800000, v20
	v_cvt_pk_fp8_f32 v7, v11, v13
	s_waitcnt lgkmcnt(1)
	v_mul_f32_e32 v13, 0x42800000, v16
	v_mul_f32_e32 v16, 0x42800000, v17
	v_mov_b32_e32 v11, v3
	v_cvt_pk_fp8_f32 v11, v13, v16
	s_mul_i32 s26, s26, 0x1600000
	v_or_b32_e32 v12, s27, v137
	s_add_u32 s6, s24, s26
	v_mul_f32_e32 v30, 0x42800000, v30
	v_mul_f32_e32 v31, 0x42800000, v31
	v_mul_f32_e32 v18, 0x42800000, v18
	v_mul_f32_e32 v19, 0x42800000, v19
	v_ashrrev_i32_e32 v13, 31, v12
	s_addc_u32 s7, s25, s0
	v_cvt_pk_fp8_f32 v5, v30, v31 op_sel:[0,0,1]
	v_mul_f32_e32 v26, 0x42800000, v26
	v_mul_f32_e32 v27, 0x42800000, v27
	v_cvt_pk_fp8_f32 v7, v18, v19 op_sel:[0,0,1]
	s_waitcnt lgkmcnt(0)
	v_mul_f32_e32 v14, 0x42800000, v14
	v_mul_f32_e32 v15, 0x42800000, v15
	v_lshlrev_b64 v[12:13], 11, v[12:13]
	v_cvt_pk_fp8_f32 v9, v26, v27 op_sel:[0,0,1]
	v_cvt_pk_fp8_f32 v11, v14, v15 op_sel:[0,0,1]
	v_lshl_add_u64 v[12:13], s[6:7], 0, v[12:13]
	v_lshl_add_u64 v[12:13], v[12:13], 0, s[4:5]
	v_lshl_add_u64 v[12:13], v[12:13], 0, v[132:133]
	global_store_dwordx4 v[12:13], v[4:7], off
	s_nop 1
	v_add_co_u32_e32 v12, vcc, 0x8000, v12
	s_nop 1
	v_addc_co_u32_e32 v13, vcc, 0, v13, vcc
	global_store_dwordx4 v[12:13], v[8:11], off
	s_add_i32 s21, s21, 32
	s_cmp_lt_i32 s21, s20
	s_cbranch_scc1 .LBB6_2092
.LBB6_2093:
	s_max_i32 s0, s18, 0xdc00
	s_min_i32 s12, s19, 0x14a00
	s_cmp_le_i32 s12, s0
	s_cbranch_scc1 .LBB6_2098
	s_sub_i32 s1, s12, s0
	s_mov_b32 s4, 19
	s_cmp_lt_i32 s1, 32
	s_cbranch_scc1 .LBB6_2098
	s_add_i32 s0, s0, s17
	s_add_i32 s12, s12, 0xffff2400
	s_add_i32 s13, s0, 0xffff2400
	s_cmp_ge_i32 s13, s12
	s_cbranch_scc1 .LBB6_2098
	s_ashr_i32 s5, s4, 31
	s_lshl_b64 s[0:1], s[4:5], 3
	s_add_u32 s0, s76, s0
	s_addc_u32 s1, s77, s1
	s_load_dwordx2 s[0:1], s[0:1], 0x0
	v_lshlrev_b32_e32 v2, 4, v134
	v_lshlrev_b32_e32 v6, 5, v134
	v_lshrrev_b32_e32 v4, 3, v134
	v_and_b32_e32 v5, 0x70, v2
	s_waitcnt lgkmcnt(0)
	s_add_u32 s20, s0, 0x8400000
	s_addc_u32 s21, s1, 0
	v_lshrrev_b32_e32 v147, 2, v134
	v_lshlrev_b32_e32 v144, 4, v134
	v_and_b32_e32 v144, 48, v144
	s_add_u32 s22, s2, 0x99180000
	v_lshl_or_b32 v2, v4, 13, v5
	v_add_u32_e32 v5, s16, v5
	v_mul_u32_u24_e32 v4, 0x84, v4
	v_mul_u32_u24_e32 v6, 0x84, v144
	v_lshlrev_b32_e32 v7, 2, v147
	v_and_b32_e32 v146, 31, v135
	s_addc_u32 s23, s3, 0
	v_mov_b32_e32 v145, v3
	v_add3_u32 v148, s16, v6, v7
	v_add_u32_e32 v149, v5, v4
.LBB6_2097:
	s_mul_hi_i32 s1, s13, 0x2e8ba2e9
	s_lshr_b32 s3, s1, 31
	s_ashr_i32 s1, s1, 10
	s_lshl_b32 s2, s13, 3
	s_add_i32 s1, s1, s3
	s_and_b32 s18, s2, 64
	s_mul_i32 s2, s1, 0xffffea00
	s_add_i32 s2, s2, s13
	s_mul_hi_i32 s5, s1, 0xb00000
	s_mul_i32 s4, s1, 0xb00000
	s_ashr_i32 s1, s2, 1
	s_and_b32 s0, s13, 7
	s_ashr_i32 s2, s2, 31
	s_and_b32 s1, s1, -8
	s_lshr_b32 s2, s2, 26
	s_or_b32 s1, s1, s0
	s_add_i32 s2, s1, s2
	s_ashr_i32 s2, s2, 6
	s_lshl_b32 s1, s1, 5
	s_lshl_b32 s3, s2, 11
	s_lshl_b32 s2, s2, 7
	s_lshl_b64 s[6:7], s[4:5], 2
	s_sub_i32 s1, s1, s3
	s_or_b32 s2, s2, s18
	s_add_u32 s10, s20, s6
	v_or_b32_e32 v36, s1, v146
	v_or_b32_e32 v178, s1, v147
	s_addc_u32 s1, s21, s7
	v_readfirstlane_b32 s6, v36
	s_ashr_i32 s3, s2, 31
	s_andn2_b32 s6, s6, 31
	s_lshl_b64 s[8:9], s[2:3], 13
	s_add_u32 s8, s10, s8
	s_addc_u32 s1, s1, s9
	s_ashr_i32 s7, s6, 31
	s_lshl_b64 s[6:7], s[6:7], 2
	s_add_u32 s6, s8, s6
	s_addc_u32 s7, s1, s7
	s_mov_b64 s[8:9], s[6:7]
	s_add_u32 s10, s6, 0x10000
	s_addc_u32 s11, s7, 0
	v_lshl_add_u64 v[36:37], s[8:9], 0, v[2:3]
	s_add_u32 s8, s6, 0x20000
	global_load_dwordx4 v[124:127], v[36:37], off nt
	s_addc_u32 s9, s7, 0
	v_lshl_add_u64 v[36:37], s[10:11], 0, v[2:3]
	s_add_u32 s10, s6, 0x30000
	global_load_dwordx4 v[132:135], v[36:37], off nt
	s_addc_u32 s11, s7, 0
	v_lshl_add_u64 v[36:37], s[8:9], 0, v[2:3]
	s_add_u32 s8, s6, 0x40000
	global_load_dwordx4 v[136:139], v[36:37], off nt
	s_addc_u32 s9, s7, 0
	v_lshl_add_u64 v[36:37], s[10:11], 0, v[2:3]
	s_add_u32 s10, s6, 0x50000
	global_load_dwordx4 v[140:143], v[36:37], off nt
	s_addc_u32 s11, s7, 0
	v_lshl_add_u64 v[36:37], s[8:9], 0, v[2:3]
	s_add_u32 s8, s6, 0x60000
	s_addc_u32 s9, s7, 0
	global_load_dwordx4 v[174:177], v[36:37], off nt
	s_add_u32 s6, s6, 0x70000
	v_lshl_add_u64 v[36:37], s[10:11], 0, v[2:3]
	global_load_dwordx4 v[182:185], v[36:37], off nt
	s_addc_u32 s7, s7, 0
	s_add_i32 s1, s13, 8
	v_lshl_add_u64 v[36:37], s[8:9], 0, v[2:3]
	s_mul_hi_i32 s8, s1, 0x2e8ba2e9
	global_load_dwordx4 v[186:189], v[36:37], off nt
	s_lshr_b32 s10, s8, 31
	s_ashr_i32 s8, s8, 10
	v_lshl_add_u64 v[36:37], s[6:7], 0, v[2:3]
	s_add_i32 s6, s8, s10
	s_mul_i32 s7, s6, 0xffffea00
	s_add_i32 s7, s7, s1
	s_lshl_b32 s9, s1, 3
	s_ashr_i32 s1, s7, 1
	s_and_b32 s14, s9, 64
	s_mul_hi_i32 s9, s6, 0xb00000
	s_mul_i32 s8, s6, 0xb00000
	s_ashr_i32 s6, s7, 31
	s_and_b32 s1, s1, -8
	s_lshr_b32 s6, s6, 26
	s_or_b32 s1, s1, s0
	s_add_i32 s6, s1, s6
	s_ashr_i32 s6, s6, 6
	s_lshl_b32 s1, s1, 5
	s_lshl_b32 s7, s6, 11
	s_lshl_b32 s6, s6, 7
	s_lshl_b64 s[10:11], s[8:9], 2
	s_sub_i32 s1, s1, s7
	s_or_b32 s6, s6, s14
	global_load_dwordx4 v[190:193], v[36:37], off nt
	s_add_u32 s16, s20, s10
	v_or_b32_e32 v36, s1, v146
	v_or_b32_e32 v202, s1, v147
	s_addc_u32 s1, s21, s11
	v_readfirstlane_b32 s10, v36
	s_ashr_i32 s7, s6, 31
	s_andn2_b32 s10, s10, 31
	s_lshl_b64 s[14:15], s[6:7], 13
	s_add_u32 s14, s16, s14
	s_addc_u32 s1, s1, s15
	s_ashr_i32 s11, s10, 31
	s_lshl_b64 s[10:11], s[10:11], 2
	s_add_u32 s10, s14, s10
	s_addc_u32 s11, s1, s11
	s_mov_b64 s[14:15], s[10:11]
	s_add_u32 s16, s10, 0x10000
	s_addc_u32 s17, s11, 0
	v_lshl_add_u64 v[36:37], s[14:15], 0, v[2:3]
	s_add_u32 s14, s10, 0x20000
	global_load_dwordx4 v[76:79], v[36:37], off nt
	s_addc_u32 s15, s11, 0
	v_lshl_add_u64 v[36:37], s[16:17], 0, v[2:3]
	s_add_u32 s16, s10, 0x30000
	global_load_dwordx4 v[88:91], v[36:37], off nt
	s_addc_u32 s17, s11, 0
	v_lshl_add_u64 v[36:37], s[14:15], 0, v[2:3]
	s_add_u32 s14, s10, 0x40000
	global_load_dwordx4 v[96:99], v[36:37], off nt
	s_addc_u32 s15, s11, 0
	v_lshl_add_u64 v[36:37], s[16:17], 0, v[2:3]
	s_add_u32 s16, s10, 0x50000
	global_load_dwordx4 v[100:103], v[36:37], off nt
	s_addc_u32 s17, s11, 0
	v_lshl_add_u64 v[36:37], s[14:15], 0, v[2:3]
	s_add_u32 s14, s10, 0x60000
	s_addc_u32 s15, s11, 0
	global_load_dwordx4 v[108:111], v[36:37], off nt
	s_add_u32 s10, s10, 0x70000
	v_lshl_add_u64 v[36:37], s[16:17], 0, v[2:3]
	global_load_dwordx4 v[112:115], v[36:37], off nt
	s_addc_u32 s11, s11, 0
	s_add_i32 s1, s13, 16
	v_lshl_add_u64 v[36:37], s[14:15], 0, v[2:3]
	s_mul_hi_i32 s14, s1, 0x2e8ba2e9
	global_load_dwordx4 v[120:123], v[36:37], off nt
	s_lshr_b32 s15, s14, 31
	s_ashr_i32 s14, s14, 10
	v_lshl_add_u64 v[36:37], s[10:11], 0, v[2:3]
	s_add_i32 s10, s14, s15
	s_mul_i32 s14, s10, 0xffffea00
	s_add_i32 s14, s14, s1
	s_ashr_i32 s1, s14, 1
	s_ashr_i32 s14, s14, 31
	s_and_b32 s1, s1, -8
	s_lshr_b32 s14, s14, 26
	s_or_b32 s1, s1, s0
	s_add_i32 s14, s1, s14
	s_ashr_i32 s14, s14, 6
	s_mul_hi_i32 s11, s10, 0xb00000
	s_mul_i32 s10, s10, 0xb00000
	s_lshl_b32 s1, s1, 5
	s_lshl_b32 s15, s14, 11
	s_lshl_b32 s14, s14, 7
	s_lshl_b64 s[16:17], s[10:11], 2
	s_sub_i32 s1, s1, s15
	s_or_b32 s14, s14, s18
	global_load_dwordx4 v[128:131], v[36:37], off nt
	s_add_u32 s24, s20, s16
	v_or_b32_e32 v36, s1, v146
	v_or_b32_e32 v204, s1, v147
	s_addc_u32 s1, s21, s17
	v_readfirstlane_b32 s16, v36
	s_ashr_i32 s15, s14, 31
	s_andn2_b32 s16, s16, 31
	s_lshl_b64 s[18:19], s[14:15], 13
	s_add_u32 s18, s24, s18
	s_addc_u32 s1, s1, s19
	s_ashr_i32 s17, s16, 31
	s_lshl_b64 s[16:17], s[16:17], 2
	s_add_u32 s16, s18, s16
	s_addc_u32 s17, s1, s17
	s_mov_b64 s[18:19], s[16:17]
	s_add_u32 s24, s16, 0x10000
	s_addc_u32 s25, s17, 0
	v_lshl_add_u64 v[36:37], s[18:19], 0, v[2:3]
	s_add_u32 s18, s16, 0x20000
	global_load_dwordx4 v[48:51], v[36:37], off nt
	s_addc_u32 s19, s17, 0
	v_lshl_add_u64 v[36:37], s[24:25], 0, v[2:3]
	s_add_u32 s24, s16, 0x30000
	global_load_dwordx4 v[56:59], v[36:37], off nt
	s_addc_u32 s25, s17, 0
	v_lshl_add_u64 v[36:37], s[18:19], 0, v[2:3]
	s_add_u32 s18, s16, 0x40000
	global_load_dwordx4 v[64:67], v[36:37], off nt
	s_addc_u32 s19, s17, 0
	v_lshl_add_u64 v[36:37], s[24:25], 0, v[2:3]
	s_add_u32 s24, s16, 0x50000
	global_load_dwordx4 v[72:75], v[36:37], off nt
	s_addc_u32 s25, s17, 0
	v_lshl_add_u64 v[36:37], s[18:19], 0, v[2:3]
	s_add_u32 s18, s16, 0x60000
	s_addc_u32 s19, s17, 0
	global_load_dwordx4 v[84:87], v[36:37], off nt
	s_add_u32 s16, s16, 0x70000
	v_lshl_add_u64 v[36:37], s[24:25], 0, v[2:3]
	global_load_dwordx4 v[92:95], v[36:37], off nt
	s_addc_u32 s17, s17, 0
	s_add_i32 s1, s13, 24
	v_lshl_add_u64 v[36:37], s[18:19], 0, v[2:3]
	s_mul_hi_i32 s18, s1, 0x2e8ba2e9
	global_load_dwordx4 v[104:107], v[36:37], off nt
	s_lshr_b32 s24, s18, 31
	s_ashr_i32 s18, s18, 10
	v_lshl_add_u64 v[36:37], s[16:17], 0, v[2:3]
	s_add_i32 s16, s18, s24
	s_mul_i32 s17, s16, 0xffffea00
	s_add_i32 s17, s17, s1
	s_lshl_b32 s19, s1, 3
	s_ashr_i32 s1, s17, 1
	s_and_b32 s26, s19, 64
	s_mul_hi_i32 s19, s16, 0xb00000
	s_mul_i32 s18, s16, 0xb00000
	s_ashr_i32 s16, s17, 31
	s_and_b32 s1, s1, -8
	s_lshr_b32 s16, s16, 26
	s_or_b32 s0, s1, s0
	s_add_i32 s1, s0, s16
	s_ashr_i32 s1, s1, 6
	s_lshl_b32 s0, s0, 5
	s_lshl_b32 s16, s1, 11
	s_lshl_b32 s1, s1, 7
	s_lshl_b64 s[24:25], s[18:19], 2
	s_sub_i32 s0, s0, s16
	s_or_b32 s16, s1, s26
	global_load_dwordx4 v[116:119], v[36:37], off nt
	s_add_u32 s1, s20, s24
	v_or_b32_e32 v36, s0, v146
	v_or_b32_e32 v205, s0, v147
	s_addc_u32 s26, s21, s25
	v_readfirstlane_b32 s0, v36
	s_ashr_i32 s17, s16, 31
	s_andn2_b32 s0, s0, 31
	s_lshl_b64 s[24:25], s[16:17], 13
	s_add_u32 s24, s1, s24
	s_addc_u32 s25, s26, s25
	s_ashr_i32 s1, s0, 31
	s_lshl_b64 s[0:1], s[0:1], 2
	s_add_u32 s0, s24, s0
	s_addc_u32 s1, s25, s1
	s_mov_b64 s[24:25], s[0:1]
	s_add_u32 s26, s0, 0x10000
	s_addc_u32 s27, s1, 0
	v_lshl_add_u64 v[36:37], s[24:25], 0, v[2:3]
	global_load_dwordx4 v[36:39], v[36:37], off nt
	s_add_u32 s24, s0, 0x20000
	s_addc_u32 s25, s1, 0
	v_lshl_add_u64 v[40:41], s[26:27], 0, v[2:3]
	global_load_dwordx4 v[40:43], v[40:41], off nt
	s_add_u32 s26, s0, 0x30000
	s_addc_u32 s27, s1, 0
	v_lshl_add_u64 v[44:45], s[24:25], 0, v[2:3]
	global_load_dwordx4 v[44:47], v[44:45], off nt
	s_add_u32 s24, s0, 0x40000
	s_addc_u32 s25, s1, 0
	v_lshl_add_u64 v[52:53], s[26:27], 0, v[2:3]
	global_load_dwordx4 v[52:55], v[52:53], off nt
	s_add_u32 s26, s0, 0x50000
	s_addc_u32 s27, s1, 0
	v_lshl_add_u64 v[60:61], s[24:25], 0, v[2:3]
	global_load_dwordx4 v[60:63], v[60:61], off nt
	s_add_u32 s24, s0, 0x60000
	s_addc_u32 s25, s1, 0
	v_lshl_add_u64 v[68:69], s[26:27], 0, v[2:3]
	global_load_dwordx4 v[68:71], v[68:69], off nt
	s_add_u32 s0, s0, 0x70000
	s_addc_u32 s1, s1, 0
	v_lshl_add_u64 v[80:81], s[24:25], 0, v[2:3]
	global_load_dwordx4 v[80:83], v[80:81], off nt
	v_add_u32_e32 v150, 0x420, v149
	v_add_u32_e32 v151, 0x428, v149
	v_add_u32_e32 v152, 0x840, v149
	v_add_u32_e32 v153, 0x848, v149
	v_add_u32_e32 v154, 0xc60, v149
	v_add_u32_e32 v155, 0xc68, v149
	v_add_u32_e32 v156, 0x1080, v149
	v_add_u32_e32 v157, 0x1088, v149
	v_add_u32_e32 v165, 0x14a0, v149
	v_add_u32_e32 v166, 0x14a8, v149
	v_add_u32_e32 v167, 0x18c0, v149
	v_add_u32_e32 v168, 0x18c8, v149
	v_add_u32_e32 v169, 0x1ce0, v149
	v_add_u32_e32 v170, 0x1ce8, v149
	s_waitcnt vmcnt(30)
	ds_write2_b32 v149, v124, v125 offset1:1
	ds_write2_b32 v149, v126, v127 offset0:2 offset1:3
	s_waitcnt vmcnt(29)
	ds_write2_b32 v150, v132, v133 offset1:1
	ds_write2_b32 v151, v134, v135 offset1:1
	s_waitcnt vmcnt(28)
	ds_write2_b32 v152, v136, v137 offset1:1
	ds_write2_b32 v153, v138, v139 offset1:1
	s_waitcnt vmcnt(27)
	ds_write2_b32 v154, v140, v141 offset1:1
	ds_write2_b32 v155, v142, v143 offset1:1
	s_waitcnt vmcnt(26)
	ds_write2_b32 v156, v174, v175 offset1:1
	ds_write2_b32 v157, v176, v177 offset1:1
	s_waitcnt vmcnt(25)
	ds_write2_b32 v165, v182, v183 offset1:1
	ds_write2_b32 v166, v184, v185 offset1:1
	s_waitcnt vmcnt(24)
	ds_write2_b32 v167, v186, v187 offset1:1
	ds_write2_b32 v168, v188, v189 offset1:1
	s_waitcnt vmcnt(23)
	ds_write2_b32 v169, v190, v191 offset1:1
	ds_write2_b32 v170, v192, v193 offset1:1
	v_lshl_add_u64 v[124:125], s[0:1], 0, v[2:3]
	global_load_dwordx4 v[124:127], v[124:125], off nt
	s_add_u32 s4, s22, s4
	s_addc_u32 s5, s23, s5
	v_mov_b64_e32 v[132:133], s[4:5]
	s_add_u32 s0, s22, s8
	v_mad_i64_i32 v[132:133], s[4:5], v178, s82, v[132:133]
	s_addc_u32 s1, s23, s9
	v_add_u32_e32 v171, 0x400, v148
	v_mov_b32_e32 v172, v148
	v_add_u32_e32 v173, 0x400, v148
	ds_read2_b32 v[134:135], v148 offset1:33
	ds_read2_b32 v[136:137], v148 offset0:66 offset1:99
	ds_read2_b32 v[138:139], v148 offset0:132 offset1:165
	ds_read2_b32 v[140:141], v148 offset0:198 offset1:231
	ds_read2_b32 v[142:143], v171 offset0:8 offset1:41
	ds_read2_b32 v[174:175], v171 offset0:74 offset1:107
	ds_read2_b32 v[176:177], v171 offset0:140 offset1:173
	ds_read2_b32 v[178:179], v171 offset0:206 offset1:239
	ds_read2_b32 v[182:183], v172 offset0:16 offset1:49
	ds_read2_b32 v[184:185], v172 offset0:82 offset1:115
	ds_read2_b32 v[186:187], v172 offset0:148 offset1:181
	ds_read2_b32 v[188:189], v172 offset0:214 offset1:247
	ds_read2_b32 v[190:191], v173 offset0:24 offset1:57
	ds_read2_b32 v[192:193], v173 offset0:90 offset1:123
	ds_read2_b32 v[194:195], v173 offset0:156 offset1:189
	ds_read2_b32 v[196:197], v173 offset0:222 offset1:255
	v_lshl_add_u64 v[132:133], v[132:133], 0, s[2:3]
	v_mov_b64_e32 v[198:199], s[0:1]
	s_add_u32 s0, s22, s10
	v_lshl_add_u64 v[200:201], v[132:133], 0, v[144:145]
	v_mad_i64_i32 v[132:133], s[2:3], v202, s82, v[198:199]
	s_addc_u32 s1, s23, s11
	v_lshl_add_u64 v[132:133], v[132:133], 0, s[6:7]
	v_mov_b64_e32 v[198:199], s[0:1]
	v_mov_b32_e32 v4, v3
	v_mov_b32_e32 v5, v3
	v_mov_b32_e32 v6, v3
	v_mov_b32_e32 v7, v3
	v_lshl_add_u64 v[202:203], v[132:133], 0, v[144:145]
	v_mad_i64_i32 v[132:133], s[2:3], v204, s82, v[198:199]
	s_waitcnt lgkmcnt(14)
	v_mul_f32_e32 v204, 0x42800000, v134
	v_mul_f32_e32 v206, 0x42800000, v135
	s_waitcnt lgkmcnt(13)
	v_mul_f32_e32 v138, 0x42800000, v138
	v_mul_f32_e32 v139, 0x42800000, v139
	s_waitcnt lgkmcnt(11)
	v_mul_f32_e32 v142, 0x42800000, v142
	v_mul_f32_e32 v143, 0x42800000, v143
	s_waitcnt lgkmcnt(9)
	v_mul_f32_e32 v176, 0x42800000, v176
	v_mul_f32_e32 v177, 0x42800000, v177
	v_mov_b32_e32 v8, v3
	v_mov_b32_e32 v9, v3
	v_mov_b32_e32 v10, v3
	v_mov_b32_e32 v11, v3
	s_waitcnt lgkmcnt(7)
	v_mul_f32_e32 v182, 0x42800000, v182
	v_mul_f32_e32 v183, 0x42800000, v183
	s_waitcnt lgkmcnt(5)
	v_mul_f32_e32 v186, 0x42800000, v186
	v_mul_f32_e32 v187, 0x42800000, v187
	s_waitcnt lgkmcnt(3)
	v_mul_f32_e32 v190, 0x42800000, v190
	v_mul_f32_e32 v191, 0x42800000, v191
	s_waitcnt lgkmcnt(1)
	v_mul_f32_e32 v194, 0x42800000, v194
	v_mul_f32_e32 v195, 0x42800000, v195
	v_cvt_pk_fp8_f32 v4, v204, v206
	v_cvt_pk_fp8_f32 v5, v138, v139
	v_cvt_pk_fp8_f32 v6, v142, v143
	v_cvt_pk_fp8_f32 v7, v176, v177
	v_cvt_pk_fp8_f32 v8, v182, v183
	v_cvt_pk_fp8_f32 v9, v186, v187
	v_cvt_pk_fp8_f32 v10, v190, v191
	v_cvt_pk_fp8_f32 v11, v194, v195
	v_mul_f32_e32 v136, 0x42800000, v136
	v_mul_f32_e32 v137, 0x42800000, v137
	v_mul_f32_e32 v140, 0x42800000, v140
	v_mul_f32_e32 v141, 0x42800000, v141
	v_mul_f32_e32 v174, 0x42800000, v174
	v_mul_f32_e32 v175, 0x42800000, v175
	v_mul_f32_e32 v178, 0x42800000, v178
	v_mul_f32_e32 v179, 0x42800000, v179
	v_mul_f32_e32 v184, 0x42800000, v184
	v_mul_f32_e32 v185, 0x42800000, v185
	v_mul_f32_e32 v188, 0x42800000, v188
	v_mul_f32_e32 v189, 0x42800000, v189
	v_mul_f32_e32 v192, 0x42800000, v192
	v_mul_f32_e32 v193, 0x42800000, v193
	s_waitcnt lgkmcnt(0)
	v_mul_f32_e32 v196, 0x42800000, v196
	v_mul_f32_e32 v197, 0x42800000, v197
	v_cvt_pk_fp8_f32 v4, v136, v137 op_sel:[0,0,1]
	v_cvt_pk_fp8_f32 v5, v140, v141 op_sel:[0,0,1]
	v_cvt_pk_fp8_f32 v6, v174, v175 op_sel:[0,0,1]
	v_cvt_pk_fp8_f32 v7, v178, v179 op_sel:[0,0,1]
	v_cvt_pk_fp8_f32 v8, v184, v185 op_sel:[0,0,1]
	v_cvt_pk_fp8_f32 v9, v188, v189 op_sel:[0,0,1]
	v_cvt_pk_fp8_f32 v10, v192, v193 op_sel:[0,0,1]
	v_cvt_pk_fp8_f32 v11, v196, v197 op_sel:[0,0,1]
	global_store_dwordx4 v[200:201], v[4:7], off
	s_nop 1
	v_add_co_u32_e32 v200, vcc, 0x16000, v200
	s_nop 1
	v_addc_co_u32_e32 v201, vcc, 0, v201, vcc
	global_store_dwordx4 v[200:201], v[8:11], off
	s_waitcnt vmcnt(25)
	ds_write2_b32 v149, v76, v77 offset1:1
	ds_write2_b32 v149, v78, v79 offset0:2 offset1:3
	s_waitcnt vmcnt(24)
	ds_write2_b32 v150, v88, v89 offset1:1
	ds_write2_b32 v151, v90, v91 offset1:1
	s_waitcnt vmcnt(23)
	ds_write2_b32 v152, v96, v97 offset1:1
	ds_write2_b32 v153, v98, v99 offset1:1
	s_waitcnt vmcnt(22)
	ds_write2_b32 v154, v100, v101 offset1:1
	ds_write2_b32 v155, v102, v103 offset1:1
	s_waitcnt vmcnt(21)
	ds_write2_b32 v156, v108, v109 offset1:1
	ds_write2_b32 v157, v110, v111 offset1:1
	s_waitcnt vmcnt(20)
	ds_write2_b32 v165, v112, v113 offset1:1
	ds_write2_b32 v166, v114, v115 offset1:1
	s_waitcnt vmcnt(19)
	ds_write2_b32 v167, v120, v121 offset1:1
	ds_write2_b32 v168, v122, v123 offset1:1
	s_waitcnt vmcnt(18)
	ds_write2_b32 v169, v128, v129 offset1:1
	ds_write2_b32 v170, v130, v131 offset1:1
	ds_read2_b32 v[4:5], v148 offset1:33
	ds_read2_b32 v[6:7], v148 offset0:66 offset1:99
	ds_read2_b32 v[8:9], v148 offset0:132 offset1:165
	ds_read2_b32 v[10:11], v148 offset0:198 offset1:231
	ds_read2_b32 v[76:77], v171 offset0:8 offset1:41
	ds_read2_b32 v[78:79], v171 offset0:74 offset1:107
	ds_read2_b32 v[88:89], v171 offset0:140 offset1:173
	ds_read2_b32 v[90:91], v171 offset0:206 offset1:239
	ds_read2_b32 v[96:97], v172 offset0:16 offset1:49
	ds_read2_b32 v[98:99], v172 offset0:82 offset1:115
	ds_read2_b32 v[100:101], v172 offset0:148 offset1:181
	ds_read2_b32 v[102:103], v172 offset0:214 offset1:247
	ds_read2_b32 v[108:109], v173 offset0:24 offset1:57
	ds_read2_b32 v[110:111], v173 offset0:90 offset1:123
	ds_read2_b32 v[112:113], v173 offset0:156 offset1:189
	ds_read2_b32 v[114:115], v173 offset0:222 offset1:255
	v_mov_b32_e32 v12, v3
	v_mov_b32_e32 v13, v3
	v_mov_b32_e32 v14, v3
	v_mov_b32_e32 v15, v3
	s_waitcnt lgkmcnt(14)
	v_mul_f32_e32 v4, 0x42800000, v4
	v_mul_f32_e32 v5, 0x42800000, v5
	s_waitcnt lgkmcnt(13)
	v_mul_f32_e32 v8, 0x42800000, v8
	v_mul_f32_e32 v9, 0x42800000, v9
	s_waitcnt lgkmcnt(11)
	v_mul_f32_e32 v76, 0x42800000, v76
	v_mul_f32_e32 v77, 0x42800000, v77
	s_waitcnt lgkmcnt(9)
	v_mul_f32_e32 v88, 0x42800000, v88
	v_mul_f32_e32 v89, 0x42800000, v89
	v_mov_b32_e32 v16, v3
	v_mov_b32_e32 v17, v3
	v_mov_b32_e32 v18, v3
	v_mov_b32_e32 v19, v3
	s_waitcnt lgkmcnt(7)
	v_mul_f32_e32 v96, 0x42800000, v96
	v_mul_f32_e32 v97, 0x42800000, v97
	s_waitcnt lgkmcnt(5)
	v_mul_f32_e32 v100, 0x42800000, v100
	v_mul_f32_e32 v101, 0x42800000, v101
	s_waitcnt lgkmcnt(3)
	v_mul_f32_e32 v108, 0x42800000, v108
	v_mul_f32_e32 v109, 0x42800000, v109
	s_waitcnt lgkmcnt(1)
	v_mul_f32_e32 v112, 0x42800000, v112
	v_mul_f32_e32 v113, 0x42800000, v113
	v_cvt_pk_fp8_f32 v12, v4, v5
	v_cvt_pk_fp8_f32 v13, v8, v9
	v_cvt_pk_fp8_f32 v14, v76, v77
	v_cvt_pk_fp8_f32 v15, v88, v89
	v_cvt_pk_fp8_f32 v16, v96, v97
	v_cvt_pk_fp8_f32 v17, v100, v101
	v_cvt_pk_fp8_f32 v18, v108, v109
	v_cvt_pk_fp8_f32 v19, v112, v113
	v_mul_f32_e32 v6, 0x42800000, v6
	v_mul_f32_e32 v7, 0x42800000, v7
	v_mul_f32_e32 v10, 0x42800000, v10
	v_mul_f32_e32 v11, 0x42800000, v11
	v_mul_f32_e32 v78, 0x42800000, v78
	v_mul_f32_e32 v79, 0x42800000, v79
	v_mul_f32_e32 v90, 0x42800000, v90
	v_mul_f32_e32 v91, 0x42800000, v91
	v_mul_f32_e32 v98, 0x42800000, v98
	v_mul_f32_e32 v99, 0x42800000, v99
	v_mul_f32_e32 v102, 0x42800000, v102
	v_mul_f32_e32 v103, 0x42800000, v103
	v_mul_f32_e32 v110, 0x42800000, v110
	v_mul_f32_e32 v111, 0x42800000, v111
	s_waitcnt lgkmcnt(0)
	v_mul_f32_e32 v114, 0x42800000, v114
	v_mul_f32_e32 v115, 0x42800000, v115
	v_cvt_pk_fp8_f32 v12, v6, v7 op_sel:[0,0,1]
	v_cvt_pk_fp8_f32 v13, v10, v11 op_sel:[0,0,1]
	v_cvt_pk_fp8_f32 v14, v78, v79 op_sel:[0,0,1]
	v_cvt_pk_fp8_f32 v15, v90, v91 op_sel:[0,0,1]
	v_cvt_pk_fp8_f32 v16, v98, v99 op_sel:[0,0,1]
	v_cvt_pk_fp8_f32 v17, v102, v103 op_sel:[0,0,1]
	v_cvt_pk_fp8_f32 v18, v110, v111 op_sel:[0,0,1]
	v_cvt_pk_fp8_f32 v19, v114, v115 op_sel:[0,0,1]
	global_store_dwordx4 v[202:203], v[12:15], off
	s_nop 1
	v_add_co_u32_e32 v202, vcc, 0x16000, v202
	s_nop 1
	v_addc_co_u32_e32 v203, vcc, 0, v203, vcc
	global_store_dwordx4 v[202:203], v[16:19], off
	s_waitcnt vmcnt(19)
	ds_write2_b32 v149, v48, v49 offset1:1
	ds_write2_b32 v149, v50, v51 offset0:2 offset1:3
	s_waitcnt vmcnt(18)
	ds_write2_b32 v150, v56, v57 offset1:1
	ds_write2_b32 v151, v58, v59 offset1:1
	s_waitcnt vmcnt(17)
	ds_write2_b32 v152, v64, v65 offset1:1
	ds_write2_b32 v153, v66, v67 offset1:1
	s_waitcnt vmcnt(16)
	ds_write2_b32 v154, v72, v73 offset1:1
	ds_write2_b32 v155, v74, v75 offset1:1
	s_waitcnt vmcnt(15)
	ds_write2_b32 v156, v84, v85 offset1:1
	ds_write2_b32 v157, v86, v87 offset1:1
	s_waitcnt vmcnt(14)
	ds_write2_b32 v165, v92, v93 offset1:1
	ds_write2_b32 v166, v94, v95 offset1:1
	s_waitcnt vmcnt(13)
	ds_write2_b32 v167, v104, v105 offset1:1
	ds_write2_b32 v168, v106, v107 offset1:1
	s_waitcnt vmcnt(12)
	ds_write2_b32 v169, v116, v117 offset1:1
	ds_write2_b32 v170, v118, v119 offset1:1
	ds_read2_b32 v[4:5], v148 offset1:33
	ds_read2_b32 v[6:7], v148 offset0:66 offset1:99
	ds_read2_b32 v[8:9], v148 offset0:132 offset1:165
	ds_read2_b32 v[10:11], v148 offset0:198 offset1:231
	ds_read2_b32 v[12:13], v171 offset0:8 offset1:41
	ds_read2_b32 v[14:15], v171 offset0:74 offset1:107
	ds_read2_b32 v[16:17], v171 offset0:140 offset1:173
	ds_read2_b32 v[18:19], v171 offset0:206 offset1:239
	ds_read2_b32 v[48:49], v172 offset0:16 offset1:49
	ds_read2_b32 v[50:51], v172 offset0:82 offset1:115
	ds_read2_b32 v[56:57], v172 offset0:148 offset1:181
	ds_read2_b32 v[58:59], v172 offset0:214 offset1:247
	ds_read2_b32 v[64:65], v173 offset0:24 offset1:57
	ds_read2_b32 v[66:67], v173 offset0:90 offset1:123
	ds_read2_b32 v[72:73], v173 offset0:156 offset1:189
	ds_read2_b32 v[74:75], v173 offset0:222 offset1:255
	v_mov_b32_e32 v20, v3
	v_mov_b32_e32 v21, v3
	v_mov_b32_e32 v22, v3
	v_mov_b32_e32 v23, v3
	s_waitcnt lgkmcnt(14)
	v_mul_f32_e32 v4, 0x42800000, v4
	v_mul_f32_e32 v5, 0x42800000, v5
	s_waitcnt lgkmcnt(13)
	v_mul_f32_e32 v8, 0x42800000, v8
	v_mul_f32_e32 v9, 0x42800000, v9
	s_waitcnt lgkmcnt(11)
	v_mul_f32_e32 v12, 0x42800000, v12
	v_mul_f32_e32 v13, 0x42800000, v13
	s_waitcnt lgkmcnt(9)
	v_mul_f32_e32 v16, 0x42800000, v16
	v_mul_f32_e32 v17, 0x42800000, v17
	v_mov_b32_e32 v24, v3
	v_mov_b32_e32 v25, v3
	v_mov_b32_e32 v26, v3
	v_mov_b32_e32 v27, v3
	s_waitcnt lgkmcnt(7)
	v_mul_f32_e32 v48, 0x42800000, v48
	v_mul_f32_e32 v49, 0x42800000, v49
	s_waitcnt lgkmcnt(5)
	v_mul_f32_e32 v56, 0x42800000, v56
	v_mul_f32_e32 v57, 0x42800000, v57
	s_waitcnt lgkmcnt(3)
	v_mul_f32_e32 v64, 0x42800000, v64
	v_mul_f32_e32 v65, 0x42800000, v65
	s_waitcnt lgkmcnt(1)
	v_mul_f32_e32 v72, 0x42800000, v72
	v_mul_f32_e32 v73, 0x42800000, v73
	v_cvt_pk_fp8_f32 v20, v4, v5
	v_cvt_pk_fp8_f32 v21, v8, v9
	v_cvt_pk_fp8_f32 v22, v12, v13
	v_cvt_pk_fp8_f32 v23, v16, v17
	v_cvt_pk_fp8_f32 v24, v48, v49
	v_cvt_pk_fp8_f32 v25, v56, v57
	v_cvt_pk_fp8_f32 v26, v64, v65
	v_cvt_pk_fp8_f32 v27, v72, v73
	v_mul_f32_e32 v6, 0x42800000, v6
	v_mul_f32_e32 v7, 0x42800000, v7
	v_mul_f32_e32 v10, 0x42800000, v10
	v_mul_f32_e32 v11, 0x42800000, v11
	v_mul_f32_e32 v14, 0x42800000, v14
	v_mul_f32_e32 v15, 0x42800000, v15
	v_mul_f32_e32 v18, 0x42800000, v18
	v_mul_f32_e32 v19, 0x42800000, v19
	v_mul_f32_e32 v50, 0x42800000, v50
	v_mul_f32_e32 v51, 0x42800000, v51
	v_mul_f32_e32 v58, 0x42800000, v58
	v_mul_f32_e32 v59, 0x42800000, v59
	v_mul_f32_e32 v66, 0x42800000, v66
	v_mul_f32_e32 v67, 0x42800000, v67
	s_waitcnt lgkmcnt(0)
	v_mul_f32_e32 v74, 0x42800000, v74
	v_mul_f32_e32 v75, 0x42800000, v75
	v_cvt_pk_fp8_f32 v20, v6, v7 op_sel:[0,0,1]
	v_cvt_pk_fp8_f32 v21, v10, v11 op_sel:[0,0,1]
	v_cvt_pk_fp8_f32 v22, v14, v15 op_sel:[0,0,1]
	v_cvt_pk_fp8_f32 v23, v18, v19 op_sel:[0,0,1]
	v_cvt_pk_fp8_f32 v24, v50, v51 op_sel:[0,0,1]
	v_cvt_pk_fp8_f32 v25, v58, v59 op_sel:[0,0,1]
	v_cvt_pk_fp8_f32 v26, v66, v67 op_sel:[0,0,1]
	v_cvt_pk_fp8_f32 v27, v74, v75 op_sel:[0,0,1]
	v_lshl_add_u64 v[132:133], v[132:133], 0, s[14:15]
	v_lshl_add_u64 v[134:135], v[132:133], 0, v[144:145]
	global_store_dwordx4 v[134:135], v[20:23], off
	s_nop 1
	v_add_co_u32_e32 v134, vcc, 0x16000, v134
	s_nop 1
	v_addc_co_u32_e32 v135, vcc, 0, v135, vcc
	global_store_dwordx4 v[134:135], v[24:27], off
	s_waitcnt vmcnt(13)
	ds_write2_b32 v149, v36, v37 offset1:1
	ds_write2_b32 v149, v38, v39 offset0:2 offset1:3
	s_waitcnt vmcnt(12)
	ds_write2_b32 v150, v40, v41 offset1:1
	ds_write2_b32 v151, v42, v43 offset1:1
	s_waitcnt vmcnt(11)
	ds_write2_b32 v152, v44, v45 offset1:1
	ds_write2_b32 v153, v46, v47 offset1:1
	s_waitcnt vmcnt(10)
	ds_write2_b32 v154, v52, v53 offset1:1
	ds_write2_b32 v155, v54, v55 offset1:1
	s_waitcnt vmcnt(9)
	ds_write2_b32 v156, v60, v61 offset1:1
	ds_write2_b32 v157, v62, v63 offset1:1
	s_waitcnt vmcnt(8)
	ds_write2_b32 v165, v68, v69 offset1:1
	ds_write2_b32 v166, v70, v71 offset1:1
	s_waitcnt vmcnt(7)
	ds_write2_b32 v167, v80, v81 offset1:1
	ds_write2_b32 v168, v82, v83 offset1:1
	s_waitcnt vmcnt(6)
	ds_write2_b32 v169, v124, v125 offset1:1
	ds_write2_b32 v170, v126, v127 offset1:1
	ds_read2_b32 v[4:5], v148 offset1:33
	ds_read2_b32 v[6:7], v148 offset0:66 offset1:99
	ds_read2_b32 v[8:9], v148 offset0:132 offset1:165
	ds_read2_b32 v[10:11], v148 offset0:198 offset1:231
	ds_read2_b32 v[12:13], v171 offset0:8 offset1:41
	ds_read2_b32 v[14:15], v171 offset0:74 offset1:107
	ds_read2_b32 v[16:17], v171 offset0:140 offset1:173
	ds_read2_b32 v[18:19], v171 offset0:206 offset1:239
	ds_read2_b32 v[20:21], v172 offset0:16 offset1:49
	ds_read2_b32 v[22:23], v172 offset0:82 offset1:115
	ds_read2_b32 v[24:25], v172 offset0:148 offset1:181
	ds_read2_b32 v[26:27], v172 offset0:214 offset1:247
	ds_read2_b32 v[36:37], v173 offset0:24 offset1:57
	ds_read2_b32 v[38:39], v173 offset0:90 offset1:123
	ds_read2_b32 v[40:41], v173 offset0:156 offset1:189
	ds_read2_b32 v[42:43], v173 offset0:222 offset1:255
	v_mov_b32_e32 v28, v3
	v_mov_b32_e32 v29, v3
	v_mov_b32_e32 v30, v3
	v_mov_b32_e32 v31, v3
	s_waitcnt lgkmcnt(14)
	v_mul_f32_e32 v4, 0x42800000, v4
	v_mul_f32_e32 v5, 0x42800000, v5
	s_waitcnt lgkmcnt(13)
	v_mul_f32_e32 v8, 0x42800000, v8
	v_mul_f32_e32 v9, 0x42800000, v9
	s_waitcnt lgkmcnt(11)
	v_mul_f32_e32 v12, 0x42800000, v12
	v_mul_f32_e32 v13, 0x42800000, v13
	s_waitcnt lgkmcnt(9)
	v_mul_f32_e32 v16, 0x42800000, v16
	v_mul_f32_e32 v17, 0x42800000, v17
	v_mov_b32_e32 v32, v3
	v_mov_b32_e32 v33, v3
	v_mov_b32_e32 v34, v3
	v_mov_b32_e32 v35, v3
	s_waitcnt lgkmcnt(7)
	v_mul_f32_e32 v20, 0x42800000, v20
	v_mul_f32_e32 v21, 0x42800000, v21
	s_waitcnt lgkmcnt(5)
	v_mul_f32_e32 v24, 0x42800000, v24
	v_mul_f32_e32 v25, 0x42800000, v25
	s_waitcnt lgkmcnt(3)
	v_mul_f32_e32 v36, 0x42800000, v36
	v_mul_f32_e32 v37, 0x42800000, v37
	s_waitcnt lgkmcnt(1)
	v_mul_f32_e32 v40, 0x42800000, v40
	v_mul_f32_e32 v41, 0x42800000, v41
	v_cvt_pk_fp8_f32 v28, v4, v5
	v_cvt_pk_fp8_f32 v29, v8, v9
	v_cvt_pk_fp8_f32 v30, v12, v13
	v_cvt_pk_fp8_f32 v31, v16, v17
	v_cvt_pk_fp8_f32 v32, v20, v21
	v_cvt_pk_fp8_f32 v33, v24, v25
	v_cvt_pk_fp8_f32 v34, v36, v37
	v_cvt_pk_fp8_f32 v35, v40, v41
	s_add_u32 s0, s22, s18
	s_addc_u32 s1, s23, s19
	v_mul_f32_e32 v6, 0x42800000, v6
	v_mul_f32_e32 v7, 0x42800000, v7
	v_mul_f32_e32 v10, 0x42800000, v10
	v_mul_f32_e32 v11, 0x42800000, v11
	v_mul_f32_e32 v14, 0x42800000, v14
	v_mul_f32_e32 v15, 0x42800000, v15
	v_mul_f32_e32 v18, 0x42800000, v18
	v_mul_f32_e32 v19, 0x42800000, v19
	v_mov_b64_e32 v[198:199], s[0:1]
	v_mul_f32_e32 v22, 0x42800000, v22
	v_mul_f32_e32 v23, 0x42800000, v23
	v_mul_f32_e32 v26, 0x42800000, v26
	v_mul_f32_e32 v27, 0x42800000, v27
	v_mul_f32_e32 v38, 0x42800000, v38
	v_mul_f32_e32 v39, 0x42800000, v39
	s_waitcnt lgkmcnt(0)
	v_mul_f32_e32 v42, 0x42800000, v42
	v_mul_f32_e32 v43, 0x42800000, v43
	v_cvt_pk_fp8_f32 v28, v6, v7 op_sel:[0,0,1]
	v_cvt_pk_fp8_f32 v29, v10, v11 op_sel:[0,0,1]
	v_cvt_pk_fp8_f32 v30, v14, v15 op_sel:[0,0,1]
	v_cvt_pk_fp8_f32 v31, v18, v19 op_sel:[0,0,1]
	v_mad_i64_i32 v[132:133], s[0:1], v205, s82, v[198:199]
	v_cvt_pk_fp8_f32 v32, v22, v23 op_sel:[0,0,1]
	v_cvt_pk_fp8_f32 v33, v26, v27 op_sel:[0,0,1]
	v_cvt_pk_fp8_f32 v34, v38, v39 op_sel:[0,0,1]
	v_cvt_pk_fp8_f32 v35, v42, v43 op_sel:[0,0,1]
	v_lshl_add_u64 v[132:133], v[132:133], 0, s[16:17]
	v_lshl_add_u64 v[4:5], v[132:133], 0, v[144:145]
	global_store_dwordx4 v[4:5], v[28:31], off
	s_nop 1
	v_add_co_u32_e32 v4, vcc, 0x16000, v4
	s_nop 1
	v_addc_co_u32_e32 v5, vcc, 0, v5, vcc
	global_store_dwordx4 v[4:5], v[32:35], off
	s_add_i32 s13, s13, 32
	s_cmp_lt_i32 s13, s12
	s_cbranch_scc1 .LBB6_2097
